# v64 + counted-wait cleanup in the GEMM K-loops: hipcc's second s_waitcnt lgkmcnt(0) at 67 MFMA-segment heads removed (the template's own wait precedes it)
# speedup vs baseline: 1.0027x; 1.0027x over previous
; #define LAS __attribute__((address_space(3)))
; #define G_GATHER_OFFS(tab_, rv_) do { _Pragma("unroll") for (int i = 0; i < 2; ++i) { int R_, C_; G_SRC(i, R_, C_); const int ra_ = (tab_)[R_], rb_ = (tab_)[HALF + R_];        \
;     vAc[0][i] = (unsigned)((R_ < (rv_) ? ra_ : 0) * KB + C_); vAc[1][i] = (unsigned)((HALF + R_ < (rv_) ? rb_ : 0) * KB + C_); } } while (0)
; #define G_STAGE(bufoff, gbase, voff) do { _Pragma("unroll") for (int _i = 0; _i < 2; ++_i) \
;     __builtin_amdgcn_global_load_lds((const unsigned*)((const char*)(gbase) + (voff)[_i]), (LAS unsigned*)(lds + (bufoff) + ldsw + _i * 8192), 16, 0, 0); } while (0)
; #define G_LDA(dst, b, h) do { _Pragma("unroll") for (int m = 0; m < 4; ++m) dst[m] = G_LD2(G_SA(b, h) + aoff + m * 2048, G_SA(b, h) + (P::FP8 ? aoff1 : aoff + 1024) + m * 2048); } while (0)
; #define G_LDB(dst, b, h) do { _Pragma("unroll") for (int n = 0; n < 2; ++n) dst[n] = G_LD2(G_SB(b, h) + boff + n * 2048, G_SB(b, h) + (P::FP8 ? boff1 : boff + 1024) + n * 2048); } while (0)
; #define WAIT_V(n) asm volatile("s_waitcnt vmcnt(" #n ")" ::: "memory")
; #define WAIT_L(n) asm volatile("s_waitcnt lgkmcnt(" #n ")" ::: "memory")
; #define BAR __builtin_amdgcn_s_barrier()
; #define SCHED __builtin_amdgcn_sched_barrier(0)
; template <class P>
; DEV void gemm_stream(const P& pol) {
;     ...
;     for (int t = 0; t < nt; t += 2) {
;       const bool last = (t == nt - 2);
;       const size_t k1 = (size_t)(t + 1) * kstep, k2 = (size_t)(t + 2) * kstep;
;       const char* a20 = last ? nA0 : cA0 + k2; const char* a21 = last ? nA1 : cA1 + k2; const char* b2 = last ? nB : cB + k2;
;       G_LDB(B0, 0, 0); SCHED; G_LDA(At, 0, 0); G_STAGE(G_SA(1, 1), cA1 + k1, vAc[1]);
;       WAIT_L(8); BAR; WAIT_L(0); G_MMA(0, 0, At, B0); BAR; SCHED;
;       if (P::GATHER && last && has_next) { LAS int* tab = arow + ((ui + 1) & 1) * 256; G_GATHER_OFFS(tab, nxt.rv); }
;       G_LDB(B1, 0, 1); G_STAGE(G_SB(0, 0), b2, voffB);
;       BAR; WAIT_L(0); G_MMA(0, 1, At, B1); BAR;
;       G_LDA(At, 0, 1); G_STAGE(G_SA(0, 0), a20, vAc[0]);
;       BAR; WAIT_L(0); G_MMA(1, 0, At, B0); BAR; SCHED;
;       G_STAGE(G_SB(0, 1), b2 + hstep, voffB);
;       WAIT_V(6); BAR; G_MMA(1, 1, At, B1); BAR;
.LBB0_320:
	s_add_u32 s38, s93, s36
	s_addc_u32 s39, s94, s37
	s_add_u32 s44, s34, s36
	ds_read_b128 v[150:153], v141
	ds_read_b128 v[154:157], v178
	ds_read_b128 v[158:161], v185
	ds_read_b128 v[162:165], v186
	s_addc_u32 s45, s35, s37
	s_add_u32 s44, s44, 0x100
	s_addc_u32 s45, s45, 0
	s_add_u32 vcc_lo, s91, s36
	s_addc_u32 vcc_hi, s92, s37
	s_add_i32 m0, s46, 0xc000
	s_add_i32 s96, s46, 0xe000
	s_cmpk_eq_i32 s36, 0xf00
	s_cselect_b32 s45, s87, s45
	s_cselect_b32 s44, s88, s44
	v_lshl_add_u64 v[214:215], v[148:149], 0, s[36:37]
	ds_read_b128 v[166:169], v193
	ds_read_b128 v[170:173], v193 offset:1024
	ds_read_b128 v[174:177], v193 offset:2048
	ds_read_b128 v[194:197], v193 offset:3072
	ds_read_b128 v[198:201], v193 offset:4096
	ds_read_b128 v[202:205], v193 offset:5120
	ds_read_b128 v[206:209], v193 offset:6144
	ds_read_b128 v[210:213], v193 offset:7168
	global_load_lds_dwordx4 v[214:215], off
	v_lshl_add_u64 v[214:215], v[146:147], 0, s[36:37]
	s_mov_b32 m0, s96
	s_cselect_b32 s97, s10, s39
	global_load_lds_dwordx4 v[214:215], off
	s_waitcnt lgkmcnt(8)
	s_barrier
	s_waitcnt lgkmcnt(0)
	s_cselect_b32 s96, s86, s38
	s_setprio 1
	v_mfma_f32_16x16x32_bf16 v[126:129], v[150:153], v[166:169], v[126:129]
	v_mfma_f32_16x16x32_bf16 v[122:125], v[158:161], v[166:169], v[122:125]
	v_mfma_f32_16x16x32_bf16 v[118:121], v[150:153], v[174:177], v[118:121]
	v_mfma_f32_16x16x32_bf16 v[114:117], v[158:161], v[174:177], v[114:117]
	v_mfma_f32_16x16x32_bf16 v[110:113], v[150:153], v[198:201], v[110:113]
	v_mfma_f32_16x16x32_bf16 v[106:109], v[158:161], v[198:201], v[106:109]
	v_mfma_f32_16x16x32_bf16 v[102:105], v[150:153], v[206:209], v[102:105]
	v_mfma_f32_16x16x32_bf16 v[98:101], v[158:161], v[206:209], v[98:101]
	v_mfma_f32_16x16x32_bf16 v[126:129], v[154:157], v[170:173], v[126:129]
	v_mfma_f32_16x16x32_bf16 v[122:125], v[162:165], v[170:173], v[122:125]
	v_mfma_f32_16x16x32_bf16 v[118:121], v[154:157], v[194:197], v[118:121]
	v_mfma_f32_16x16x32_bf16 v[114:117], v[162:165], v[194:197], v[114:117]
	v_mfma_f32_16x16x32_bf16 v[110:113], v[154:157], v[202:205], v[110:113]
	v_mfma_f32_16x16x32_bf16 v[106:109], v[162:165], v[202:205], v[106:109]
	v_mfma_f32_16x16x32_bf16 v[102:105], v[154:157], v[210:213], v[102:105]
	v_mfma_f32_16x16x32_bf16 v[98:101], v[162:165], v[210:213], v[98:101]
	s_setprio 0
	s_barrier
	s_cselect_b32 s39, s89, vcc_hi
	s_cselect_b32 s38, s90, vcc_lo
	s_mov_b32 m0, s47
	v_lshl_add_u64 v[232:233], s[38:39], 0, v[130:131]
	ds_read_b128 v[214:217], v179
	ds_read_b128 v[218:221], v180
	ds_read_b128 v[224:227], v187
	ds_read_b128 v[228:231], v188
	global_load_lds_dwordx4 v[232:233], off
	v_lshl_add_u64 v[234:235], s[38:39], 0, v[132:133]
	s_mov_b32 m0, s52
	s_nop 0
	global_load_lds_dwordx4 v[234:235], off
	s_barrier
	s_waitcnt lgkmcnt(0)
	s_setprio 1
	v_mfma_f32_16x16x32_bf16 v[94:97], v[214:217], v[166:169], v[94:97]
	v_mfma_f32_16x16x32_bf16 v[90:93], v[224:227], v[166:169], v[90:93]
	v_mfma_f32_16x16x32_bf16 v[86:89], v[214:217], v[174:177], v[86:89]
	v_mfma_f32_16x16x32_bf16 v[82:85], v[224:227], v[174:177], v[82:85]
	v_mfma_f32_16x16x32_bf16 v[78:81], v[214:217], v[198:201], v[78:81]
	v_mfma_f32_16x16x32_bf16 v[74:77], v[224:227], v[198:201], v[74:77]
	v_mfma_f32_16x16x32_bf16 v[70:73], v[214:217], v[206:209], v[70:73]
	v_mfma_f32_16x16x32_bf16 v[66:69], v[224:227], v[206:209], v[66:69]
	v_mfma_f32_16x16x32_bf16 v[94:97], v[218:221], v[170:173], v[94:97]
	v_mfma_f32_16x16x32_bf16 v[90:93], v[228:231], v[170:173], v[90:93]
	v_mfma_f32_16x16x32_bf16 v[86:89], v[218:221], v[194:197], v[86:89]
	v_mfma_f32_16x16x32_bf16 v[82:85], v[228:231], v[194:197], v[82:85]
	v_mfma_f32_16x16x32_bf16 v[78:81], v[218:221], v[202:205], v[78:81]
	v_mfma_f32_16x16x32_bf16 v[74:77], v[228:231], v[202:205], v[74:77]
	v_mfma_f32_16x16x32_bf16 v[70:73], v[218:221], v[210:213], v[70:73]
	v_mfma_f32_16x16x32_bf16 v[66:69], v[228:231], v[210:213], v[66:69]
	s_setprio 0
	s_mov_b32 m0, s46
	v_lshl_add_u64 v[236:237], s[96:97], 0, v[134:135]
	s_barrier
	ds_read_b128 v[166:169], v193 offset:16384
	ds_read_b128 v[170:173], v193 offset:17408
	ds_read_b128 v[174:177], v193 offset:18432
	ds_read_b128 v[194:197], v193 offset:19456
	ds_read_b128 v[198:201], v193 offset:20480
	ds_read_b128 v[202:205], v193 offset:21504
	ds_read_b128 v[206:209], v193 offset:22528
	ds_read_b128 v[210:213], v193 offset:23552
	global_load_lds_dwordx4 v[236:237], off
	v_lshl_add_u64 v[238:239], s[96:97], 0, v[136:137]
	s_mov_b32 m0, s53
	s_nop 0
	global_load_lds_dwordx4 v[238:239], off
	s_barrier
	s_waitcnt lgkmcnt(0)
	s_setprio 1
	v_mfma_f32_16x16x32_bf16 v[62:65], v[150:153], v[166:169], v[62:65]
	v_mfma_f32_16x16x32_bf16 v[58:61], v[158:161], v[166:169], v[58:61]
	v_mfma_f32_16x16x32_bf16 v[54:57], v[150:153], v[174:177], v[54:57]
	v_mfma_f32_16x16x32_bf16 v[50:53], v[158:161], v[174:177], v[50:53]
	v_mfma_f32_16x16x32_bf16 v[46:49], v[150:153], v[198:201], v[46:49]
	v_mfma_f32_16x16x32_bf16 v[42:45], v[158:161], v[198:201], v[42:45]
	v_mfma_f32_16x16x32_bf16 v[38:41], v[150:153], v[206:209], v[38:41]
	v_mfma_f32_16x16x32_bf16 v[34:37], v[158:161], v[206:209], v[34:37]
	v_mfma_f32_16x16x32_bf16 v[62:65], v[154:157], v[170:173], v[62:65]
	v_mfma_f32_16x16x32_bf16 v[58:61], v[162:165], v[170:173], v[58:61]
	v_mfma_f32_16x16x32_bf16 v[54:57], v[154:157], v[194:197], v[54:57]
	v_mfma_f32_16x16x32_bf16 v[50:53], v[162:165], v[194:197], v[50:53]
	v_mfma_f32_16x16x32_bf16 v[46:49], v[154:157], v[202:205], v[46:49]
	v_mfma_f32_16x16x32_bf16 v[42:45], v[162:165], v[202:205], v[42:45]
	v_mfma_f32_16x16x32_bf16 v[38:41], v[154:157], v[210:213], v[38:41]
	v_mfma_f32_16x16x32_bf16 v[34:37], v[162:165], v[210:213], v[34:37]
	s_setprio 0
	s_barrier
; #define G_STAGE(bufoff, gbase, voff) do { _Pragma("unroll") for (int _i = 0; _i < 2; ++_i) \
;     __builtin_amdgcn_global_load_lds((const unsigned*)((const char*)(gbase) + (voff)[_i]), (LAS unsigned*)(lds + (bufoff) + ldsw + _i * 8192), 16, 0, 0); } while (0)
; #define G_LDA(dst, b, h) do { _Pragma("unroll") for (int m = 0; m < 4; ++m) dst[m] = G_LD2(G_SA(b, h) + aoff + m * 2048, G_SA(b, h) + (P::FP8 ? aoff1 : aoff + 1024) + m * 2048); } while (0)
; #define G_LDB(dst, b, h) do { _Pragma("unroll") for (int n = 0; n < 2; ++n) dst[n] = G_LD2(G_SB(b, h) + boff + n * 2048, G_SB(b, h) + (P::FP8 ? boff1 : boff + 1024) + n * 2048); } while (0)
; #define WAIT_V(n) asm volatile("s_waitcnt vmcnt(" #n ")" ::: "memory")
; #define WAIT_L(n) asm volatile("s_waitcnt lgkmcnt(" #n ")" ::: "memory")
; #define BAR __builtin_amdgcn_s_barrier()
; #define SCHED __builtin_amdgcn_sched_barrier(0)
; template <class P>
; DEV void gemm_stream(const P& pol) {
;     ...
;       WAIT_V(6); BAR; G_MMA(1, 1, At, B1); BAR;
;       G_LDB(B0, 1, 0); SCHED; G_LDA(At, 1, 0); G_STAGE(G_SA(0, 1), a21, vAc[1]);
;       WAIT_L(8); BAR; WAIT_L(0); G_MMA(0, 0, At, B0); BAR; SCHED;
;       G_LDB(B1, 1, 1); G_STAGE(G_SB(1, 0), b2 + kstep, voffB);
;       BAR; WAIT_L(0); G_MMA(0, 1, At, B1); BAR;
;       G_LDA(At, 1, 1); G_STAGE(G_SA(1, 0), a20 + kstep, vAc[0]);
;       BAR; WAIT_L(0); G_MMA(1, 0, At, B0); BAR; SCHED;
	s_add_u32 s96, s38, 0x80000
	s_addc_u32 s97, s39, 0
	s_mov_b32 m0, s54
	v_lshl_add_u64 v[150:151], s[96:97], 0, v[130:131]
	global_load_lds_dwordx4 v[150:151], off
	v_lshl_add_u64 v[150:151], s[96:97], 0, v[132:133]
	s_mov_b32 m0, s55
	s_nop 0
	global_load_lds_dwordx4 v[150:151], off
	s_waitcnt vmcnt(6)
	s_barrier
	s_setprio 1
	v_mfma_f32_16x16x32_bf16 v[30:33], v[214:217], v[166:169], v[30:33]
	v_mfma_f32_16x16x32_bf16 v[26:29], v[224:227], v[166:169], v[26:29]
	v_mfma_f32_16x16x32_bf16 v[22:25], v[214:217], v[174:177], v[22:25]
	v_mfma_f32_16x16x32_bf16 v[18:21], v[224:227], v[174:177], v[18:21]
	v_mfma_f32_16x16x32_bf16 v[14:17], v[214:217], v[198:201], v[14:17]
	v_mfma_f32_16x16x32_bf16 v[10:13], v[224:227], v[198:201], v[10:13]
	v_mfma_f32_16x16x32_bf16 v[6:9], v[214:217], v[206:209], v[6:9]
	v_mfma_f32_16x16x32_bf16 v[2:5], v[224:227], v[206:209], v[2:5]
	v_mfma_f32_16x16x32_bf16 v[30:33], v[218:221], v[170:173], v[30:33]
	v_mfma_f32_16x16x32_bf16 v[26:29], v[228:231], v[170:173], v[26:29]
	v_mfma_f32_16x16x32_bf16 v[22:25], v[218:221], v[194:197], v[22:25]
	v_mfma_f32_16x16x32_bf16 v[18:21], v[228:231], v[194:197], v[18:21]
	v_mfma_f32_16x16x32_bf16 v[14:17], v[218:221], v[202:205], v[14:17]
	v_mfma_f32_16x16x32_bf16 v[10:13], v[228:231], v[202:205], v[10:13]
	v_mfma_f32_16x16x32_bf16 v[6:9], v[218:221], v[210:213], v[6:9]
	v_mfma_f32_16x16x32_bf16 v[2:5], v[228:231], v[210:213], v[2:5]
	s_setprio 0
	s_barrier
	ds_read_b128 v[150:153], v181
	ds_read_b128 v[154:157], v182
	ds_read_b128 v[158:161], v189
	ds_read_b128 v[162:165], v190
	s_mov_b32 m0, s56
	v_lshl_add_u64 v[214:215], s[44:45], 0, v[134:135]
	ds_read_b128 v[166:169], v193 offset:32768
	ds_read_b128 v[170:173], v193 offset:33792
	ds_read_b128 v[174:177], v193 offset:34816
	ds_read_b128 v[194:197], v193 offset:35840
	ds_read_b128 v[198:201], v193 offset:36864
	ds_read_b128 v[202:205], v193 offset:37888
	ds_read_b128 v[206:209], v193 offset:38912
	ds_read_b128 v[210:213], v193 offset:39936
	global_load_lds_dwordx4 v[214:215], off
	v_lshl_add_u64 v[214:215], s[44:45], 0, v[136:137]
	s_mov_b32 m0, s57
	s_nop 0
	global_load_lds_dwordx4 v[214:215], off
	s_waitcnt lgkmcnt(8)
	s_barrier
	s_waitcnt lgkmcnt(0)
	s_setprio 1
	v_mfma_f32_16x16x32_bf16 v[126:129], v[150:153], v[166:169], v[126:129]
	v_mfma_f32_16x16x32_bf16 v[122:125], v[158:161], v[166:169], v[122:125]
	v_mfma_f32_16x16x32_bf16 v[118:121], v[150:153], v[174:177], v[118:121]
	v_mfma_f32_16x16x32_bf16 v[114:117], v[158:161], v[174:177], v[114:117]
	v_mfma_f32_16x16x32_bf16 v[110:113], v[150:153], v[198:201], v[110:113]
	v_mfma_f32_16x16x32_bf16 v[106:109], v[158:161], v[198:201], v[106:109]
	v_mfma_f32_16x16x32_bf16 v[102:105], v[150:153], v[206:209], v[102:105]
	v_mfma_f32_16x16x32_bf16 v[98:101], v[158:161], v[206:209], v[98:101]
	v_mfma_f32_16x16x32_bf16 v[126:129], v[154:157], v[170:173], v[126:129]
	v_mfma_f32_16x16x32_bf16 v[122:125], v[162:165], v[170:173], v[122:125]
	v_mfma_f32_16x16x32_bf16 v[118:121], v[154:157], v[194:197], v[118:121]
	v_mfma_f32_16x16x32_bf16 v[114:117], v[162:165], v[194:197], v[114:117]
	v_mfma_f32_16x16x32_bf16 v[110:113], v[154:157], v[202:205], v[110:113]
	v_mfma_f32_16x16x32_bf16 v[106:109], v[162:165], v[202:205], v[106:109]
	v_mfma_f32_16x16x32_bf16 v[102:105], v[154:157], v[210:213], v[102:105]
	v_mfma_f32_16x16x32_bf16 v[98:101], v[162:165], v[210:213], v[98:101]
	s_setprio 0
	s_barrier
	s_mov_b32 m0, s62
	v_lshl_add_u64 v[232:233], v[232:233], 0, s[12:13]
	ds_read_b128 v[214:217], v183
	ds_read_b128 v[218:221], v184
	ds_read_b128 v[224:227], v191
	ds_read_b128 v[228:231], v192
	global_load_lds_dwordx4 v[232:233], off
	v_lshl_add_u64 v[232:233], v[234:235], 0, s[12:13]
	s_mov_b32 m0, s63
	s_nop 0
	global_load_lds_dwordx4 v[232:233], off
	s_barrier
	s_waitcnt lgkmcnt(0)
	s_setprio 1
	v_mfma_f32_16x16x32_bf16 v[94:97], v[214:217], v[166:169], v[94:97]
	v_mfma_f32_16x16x32_bf16 v[90:93], v[224:227], v[166:169], v[90:93]
	v_mfma_f32_16x16x32_bf16 v[86:89], v[214:217], v[174:177], v[86:89]
	v_mfma_f32_16x16x32_bf16 v[82:85], v[224:227], v[174:177], v[82:85]
	v_mfma_f32_16x16x32_bf16 v[78:81], v[214:217], v[198:201], v[78:81]
	v_mfma_f32_16x16x32_bf16 v[74:77], v[224:227], v[198:201], v[74:77]
	v_mfma_f32_16x16x32_bf16 v[70:73], v[214:217], v[206:209], v[70:73]
	v_mfma_f32_16x16x32_bf16 v[66:69], v[224:227], v[206:209], v[66:69]
	v_mfma_f32_16x16x32_bf16 v[94:97], v[218:221], v[170:173], v[94:97]
	v_mfma_f32_16x16x32_bf16 v[90:93], v[228:231], v[170:173], v[90:93]
	v_mfma_f32_16x16x32_bf16 v[86:89], v[218:221], v[194:197], v[86:89]
	v_mfma_f32_16x16x32_bf16 v[82:85], v[228:231], v[194:197], v[82:85]
	v_mfma_f32_16x16x32_bf16 v[78:81], v[218:221], v[202:205], v[78:81]
	v_mfma_f32_16x16x32_bf16 v[74:77], v[228:231], v[202:205], v[74:77]
	v_mfma_f32_16x16x32_bf16 v[70:73], v[218:221], v[210:213], v[70:73]
	v_mfma_f32_16x16x32_bf16 v[66:69], v[228:231], v[210:213], v[66:69]
	s_setprio 0
	s_mov_b32 m0, s64
	v_lshl_add_u64 v[232:233], v[236:237], 0, s[12:13]
	s_barrier
	ds_read_b128 v[166:169], v193 offset:49152
	ds_read_b128 v[170:173], v193 offset:50176
	ds_read_b128 v[174:177], v193 offset:51200
	ds_read_b128 v[194:197], v193 offset:52224
	ds_read_b128 v[198:201], v193 offset:53248
	ds_read_b128 v[202:205], v193 offset:54272
	ds_read_b128 v[206:209], v193 offset:55296
	ds_read_b128 v[210:213], v193 offset:56320
	global_load_lds_dwordx4 v[232:233], off
	v_lshl_add_u64 v[232:233], v[238:239], 0, s[12:13]
	s_mov_b32 m0, s65
	s_nop 0
	global_load_lds_dwordx4 v[232:233], off
	s_barrier
; DEV int ltid() { int t = threadIdx.x; asm volatile("" : "+v"(t)); return t; }
; #define G_STAGE(bufoff, gbase, voff) do { _Pragma("unroll") for (int _i = 0; _i < 2; ++_i) \
;     __builtin_amdgcn_global_load_lds((const unsigned*)((const char*)(gbase) + (voff)[_i]), (LAS unsigned*)(lds + (bufoff) + ldsw + _i * 8192), 16, 0, 0); } while (0)
; #define WAIT_V(n) asm volatile("s_waitcnt vmcnt(" #n ")" ::: "memory")
; #define BAR __builtin_amdgcn_s_barrier()
; template <class P>
; DEV void gemm_stream(const P& pol) {
;     ...
;       BAR; WAIT_L(0); G_MMA(1, 0, At, B0); BAR; SCHED;
;       G_STAGE(G_SB(1, 1), b2 + hstep + kstep, voffB);
;       WAIT_V(6); BAR; G_MMA(1, 1, At, B1); BAR;
;       if (P::HASBIAS && has_next && t == 0) pol.bias_dma(nxt, btab + ((ui + 1) & 1) * 256 + ((wid & 3) << 6));
;       if (P::GATHER && has_next && t == 0) pol.arow_dma(nxt, arow + ((ui + 1) & 1) * 256 + ((wid & 3) << 6));
;     }
; template <int LB> DEV void stage_store_block(const unsigned (&v)[4][LB / 4], unsigned char* dst, long row_stride) {
;   extern __shared__ __attribute__((aligned(16))) char shm[];
;   constexpr int MP = LB == 8 ? 4 : (LB == 16 ? 2 : 1), PITCH = 16 * LB + 16, ROWS = 16 * MP;
;   static_assert(ROWS * PITCH <= STG_HALF, "staging region");
;   const int tid = ltid(), wr = tid >> 8, wc = (tid >> 6) & 3, fr = tid & 15, fq = (tid >> 4) & 3;
;   char* stg = shm + STG_OFF + wr * STG_HALF;
;   const int t4 = tid & 255;
; #pragma unroll
;   for (int ps = 0; ps < 4 / MP; ++ps) {
; #pragma unroll
;     for (int mm = 0; mm < MP; ++mm) {
;       char* wp = stg + (16 * mm + fr) * PITCH + (4 * wc + fq) * LB; const int m = ps * MP + mm;
;       if (LB == 8) *(u32x2*)wp = (u32x2){v[m][0], v[m][1]};
;       else { *(u32x4*)wp = (u32x4){v[m][0], v[m][1], v[m][2], v[m][3]}; if (LB == 32) *(u32x4*)(wp + 16) = (u32x4){v[m][LB / 4 - 4], v[m][LB / 4 - 3], v[m][LB / 4 - 2], v[m][LB / 4 - 1]}; }
;     }
;     asm volatile("s_waitcnt lgkmcnt(0)" ::: "memory"); __builtin_amdgcn_s_barrier(); asm volatile("" ::: "memory");
; #pragma unroll
;     for (int k = 0; k < 2; ++k) { const int idx = k * 256 + t4, row = idx / LB, ch = idx % LB;
;       *(u32x4*)(dst + (long)(ps * ROWS + row) * row_stride + ch * 16) = *(const u32x4*)(stg + row * PITCH + ch * 16); }
;     asm volatile("s_waitcnt lgkmcnt(0)" ::: "memory"); __builtin_amdgcn_s_barrier(); asm volatile("" ::: "memory");
;   }
; }
	s_waitcnt lgkmcnt(0)
	s_setprio 1
	v_mfma_f32_16x16x32_bf16 v[62:65], v[150:153], v[166:169], v[62:65]
	v_mfma_f32_16x16x32_bf16 v[58:61], v[158:161], v[166:169], v[58:61]
	v_mfma_f32_16x16x32_bf16 v[54:57], v[150:153], v[174:177], v[54:57]
	v_mfma_f32_16x16x32_bf16 v[50:53], v[158:161], v[174:177], v[50:53]
	v_mfma_f32_16x16x32_bf16 v[46:49], v[150:153], v[198:201], v[46:49]
	v_mfma_f32_16x16x32_bf16 v[42:45], v[158:161], v[198:201], v[42:45]
	v_mfma_f32_16x16x32_bf16 v[38:41], v[150:153], v[206:209], v[38:41]
	v_mfma_f32_16x16x32_bf16 v[34:37], v[158:161], v[206:209], v[34:37]
	v_mfma_f32_16x16x32_bf16 v[62:65], v[154:157], v[170:173], v[62:65]
	v_mfma_f32_16x16x32_bf16 v[58:61], v[162:165], v[170:173], v[58:61]
	v_mfma_f32_16x16x32_bf16 v[54:57], v[154:157], v[194:197], v[54:57]
	v_mfma_f32_16x16x32_bf16 v[50:53], v[162:165], v[194:197], v[50:53]
	v_mfma_f32_16x16x32_bf16 v[46:49], v[154:157], v[202:205], v[46:49]
	v_mfma_f32_16x16x32_bf16 v[42:45], v[162:165], v[202:205], v[42:45]
	v_mfma_f32_16x16x32_bf16 v[38:41], v[154:157], v[210:213], v[38:41]
	v_mfma_f32_16x16x32_bf16 v[34:37], v[162:165], v[210:213], v[34:37]
	s_setprio 0
	s_barrier
	s_add_u32 s38, s38, 0x80080
	s_addc_u32 s39, s39, 0
	s_mov_b32 m0, s66
	v_lshl_add_u64 v[150:151], s[38:39], 0, v[130:131]
	global_load_lds_dwordx4 v[150:151], off
	v_lshl_add_u64 v[150:151], s[38:39], 0, v[132:133]
	s_mov_b32 m0, s67
	s_nop 0
	global_load_lds_dwordx4 v[150:151], off
	s_waitcnt vmcnt(6)
	s_barrier
	s_setprio 1
	v_mfma_f32_16x16x32_bf16 v[30:33], v[214:217], v[166:169], v[30:33]
	v_mfma_f32_16x16x32_bf16 v[26:29], v[224:227], v[166:169], v[26:29]
	v_mfma_f32_16x16x32_bf16 v[22:25], v[214:217], v[174:177], v[22:25]
	v_mfma_f32_16x16x32_bf16 v[18:21], v[224:227], v[174:177], v[18:21]
	v_mfma_f32_16x16x32_bf16 v[14:17], v[214:217], v[198:201], v[14:17]
	v_mfma_f32_16x16x32_bf16 v[10:13], v[224:227], v[198:201], v[10:13]
	v_mfma_f32_16x16x32_bf16 v[6:9], v[214:217], v[206:209], v[6:9]
	v_mfma_f32_16x16x32_bf16 v[2:5], v[224:227], v[206:209], v[2:5]
	v_mfma_f32_16x16x32_bf16 v[30:33], v[218:221], v[170:173], v[30:33]
	v_mfma_f32_16x16x32_bf16 v[26:29], v[228:231], v[170:173], v[26:29]
	v_mfma_f32_16x16x32_bf16 v[22:25], v[218:221], v[194:197], v[22:25]
	v_mfma_f32_16x16x32_bf16 v[18:21], v[228:231], v[194:197], v[18:21]
	v_mfma_f32_16x16x32_bf16 v[14:17], v[218:221], v[202:205], v[14:17]
	v_mfma_f32_16x16x32_bf16 v[10:13], v[228:231], v[202:205], v[10:13]
	v_mfma_f32_16x16x32_bf16 v[6:9], v[218:221], v[210:213], v[6:9]
	v_mfma_f32_16x16x32_bf16 v[2:5], v[228:231], v[210:213], v[2:5]
	s_setprio 0
	s_add_i32 s95, s95, 2
	s_add_u32 s36, s36, 0x100
	s_addc_u32 s37, s37, 0
	s_cmp_gt_u32 s95, 29
	s_barrier
	s_cbranch_scc0 .LBB0_320
	s_cmp_gt_i32 s84, 1
	s_mov_b64 s[34:35], -1
	s_cbranch_scc0 .LBB0_340
	s_cmp_lt_i32 s84, 3
	s_cbranch_scc1 .LBB0_337
	s_cmp_lg_u32 s84, 3
	s_cbranch_scc0 .LBB0_333
	s_sub_i32 s10, s84, 20
	s_cmp_gt_u32 s10, -13
	s_cbranch_scc0 .LBB0_330
	s_cmp_gt_u32 s84, 15
	s_cbranch_scc0 .LBB0_327
	s_mov_b64 s[34:35], s[4:5]
	s_load_dwordx2 s[34:35], s[34:35], 0x160
	v_mov_b32_e32 v162, v0
	s_lshl_b32 s10, s85, 8
	v_mov_b32_e32 v166, s71
	v_lshrrev_b32_e32 v138, 8, v162
	s_add_i32 s36, s10, s61
	v_and_b32_e32 v163, 15, v162
	v_mad_i32_i24 v164, v138, s72, v166
	v_and_b32_e32 v165, 0xf0, v162
	v_lshlrev_b32_e32 v138, 4, v162
	v_bfe_u32 v162, v162, 4, 4
	s_ashr_i32 s37, s36, 31
	v_and_b32_e32 v138, 0xf0, v138
	v_mul_u32_u24_e32 v162, 0x110, v162
	s_lshl_b64 s[36:37], s[36:37], 11
	v_add3_u32 v167, v164, v138, v162
	v_mul_u32_u24_e32 v162, 0x110, v163
	s_waitcnt lgkmcnt(0)
	s_add_u32 s36, s34, s36
	v_cvt_pk_bf16_f32 v146, v126, v127
	v_cvt_pk_bf16_f32 v147, v128, v129
	v_cvt_pk_bf16_f32 v148, v122, v123
	v_cvt_pk_bf16_f32 v149, v124, v125
	v_add3_u32 v168, v164, v165, v162
	s_addc_u32 s37, s35, s37
	v_cvt_pk_bf16_f32 v150, v118, v119
	v_cvt_pk_bf16_f32 v151, v120, v121
	v_cvt_pk_bf16_f32 v152, v114, v115
	v_cvt_pk_bf16_f32 v153, v116, v117
	s_lshl_b32 s10, s84, 8
	ds_write_b128 v168, v[146:149]
	ds_write_b128 v168, v[150:153] offset:4352
	s_addk_i32 s10, 0xf000
	s_waitcnt lgkmcnt(0)
	s_barrier
	s_lshl_b64 s[34:35], s[10:11], 1
	ds_read_b128 v[146:149], v167
	ds_read_b128 v[150:153], v167 offset:4352
	s_add_u32 s34, s36, s34
	s_addc_u32 s35, s37, s35
	v_lshl_add_u64 v[162:163], s[34:35], 0, v[138:139]
	v_lshlrev_b32_e32 v138, 7, v165
	v_lshl_add_u64 v[164:165], v[162:163], 0, v[138:139]
	v_or_b32_e32 v138, 0x8000, v138
	s_waitcnt lgkmcnt(0)
	global_store_dwordx4 v[164:165], v[146:149], off
	v_cvt_pk_bf16_f32 v154, v110, v111
	v_cvt_pk_bf16_f32 v155, v112, v113
	v_lshl_add_u64 v[146:147], v[162:163], 0, v[138:139]
	v_cvt_pk_bf16_f32 v156, v106, v107
	v_cvt_pk_bf16_f32 v157, v108, v109
	global_store_dwordx4 v[146:147], v[150:153], off
	v_cvt_pk_bf16_f32 v158, v102, v103
	v_cvt_pk_bf16_f32 v159, v104, v105
	v_cvt_pk_bf16_f32 v160, v98, v99
	v_cvt_pk_bf16_f32 v161, v100, v101
	s_waitcnt lgkmcnt(0)
	s_barrier
	ds_write_b128 v168, v[154:157]
	ds_write_b128 v168, v[158:161] offset:4352
	s_waitcnt lgkmcnt(0)
	s_barrier
	ds_read_b128 v[146:149], v167
	ds_read_b128 v[150:153], v167 offset:4352
	v_add_co_u32_e32 v154, vcc, s58, v164
	v_mov_b32_e32 v162, v0
	s_nop 0
	v_addc_co_u32_e32 v155, vcc, 0, v165, vcc
	s_waitcnt lgkmcnt(0)
	global_store_dwordx4 v[154:155], v[146:149], off
	v_cvt_pk_bf16_f32 v154, v78, v79
	v_cvt_pk_bf16_f32 v155, v80, v81
	v_add_co_u32_e32 v146, vcc, s68, v164
	v_cvt_pk_bf16_f32 v148, v90, v91
	s_nop 0
	v_addc_co_u32_e32 v147, vcc, 0, v165, vcc
	global_store_dwordx4 v[146:147], v[150:153], off
	s_waitcnt lgkmcnt(0)
	s_barrier
; template <int LB> DEV void stage_store_block(const unsigned (&v)[4][LB / 4], unsigned char* dst, long row_stride) {
;   extern __shared__ __attribute__((aligned(16))) char shm[];
;   constexpr int MP = LB == 8 ? 4 : (LB == 16 ? 2 : 1), PITCH = 16 * LB + 16, ROWS = 16 * MP;
;   static_assert(ROWS * PITCH <= STG_HALF, "staging region");
;   const int tid = ltid(), wr = tid >> 8, wc = (tid >> 6) & 3, fr = tid & 15, fq = (tid >> 4) & 3;
;   char* stg = shm + STG_OFF + wr * STG_HALF;
;   const int t4 = tid & 255;
; #pragma unroll
;   for (int ps = 0; ps < 4 / MP; ++ps) {
; #pragma unroll
;     for (int mm = 0; mm < MP; ++mm) {
;       char* wp = stg + (16 * mm + fr) * PITCH + (4 * wc + fq) * LB; const int m = ps * MP + mm;
;       if (LB == 8) *(u32x2*)wp = (u32x2){v[m][0], v[m][1]};
;       else { *(u32x4*)wp = (u32x4){v[m][0], v[m][1], v[m][2], v[m][3]}; if (LB == 32) *(u32x4*)(wp + 16) = (u32x4){v[m][LB / 4 - 4], v[m][LB / 4 - 3], v[m][LB / 4 - 2], v[m][LB / 4 - 1]}; }
;     }
;     asm volatile("s_waitcnt lgkmcnt(0)" ::: "memory"); __builtin_amdgcn_s_barrier(); asm volatile("" ::: "memory");
; #pragma unroll
;     for (int k = 0; k < 2; ++k) { const int idx = k * 256 + t4, row = idx / LB, ch = idx % LB;
;       *(u32x4*)(dst + (long)(ps * ROWS + row) * row_stride + ch * 16) = *(const u32x4*)(stg + row * PITCH + ch * 16); }
;     asm volatile("s_waitcnt lgkmcnt(0)" ::: "memory"); __builtin_amdgcn_s_barrier(); asm volatile("" ::: "memory");
;   }
; }
; template <int KIND> DEV void EpiIn::run(const AccT& acc, int wr, int wc, int fr, int fq) const {
;     ...
; #pragma unroll
;   for (int ai = 0; ai < 2; ++ai)
; #pragma unroll
;     for (int bj = 0; bj < 2; ++bj) {
;       const long row = rowh + ai * HALF; const int cb = bj * HALF;
;       if (KIND == 4) {
;         unsigned vals[4][8];
; #pragma unroll
;         for (int m = 0; m < 4; ++m) pk_f32x8(vals[m], lbv[bj][0] + oml[bj][0] * sig4(acc[ai][bj][m][0]), lbv[bj][1] + oml[bj][1] * sig4(acc[ai][bj][m][1]));
;         stage_store_block<32>(vals, (unsigned char*)(((pn - 8) >> 2 ? P.gb : P.gf) + row * 1024 + ((pn - 8) & 3) * 256 + cb), 1024 * 4);
;       } else {
;         unsigned vals[4][4];
; #pragma unroll
;         for (int m = 0; m < 4; ++m) {
;           if (KIND == 3) pk_bf16x8(vals[m], acc[ai][bj][m][0] * sig4(acc[ai][bj][m][0]), acc[ai][bj][m][1] * sig4(acc[ai][bj][m][1]));
	v_cvt_pk_bf16_f32 v146, v94, v95
	v_lshrrev_b32_e32 v138, 8, v162
	v_and_b32_e32 v163, 15, v162
	v_mad_i32_i24 v164, v138, s72, v166
	v_and_b32_e32 v165, 0xf0, v162
	v_lshlrev_b32_e32 v138, 4, v162
	v_bfe_u32 v162, v162, 4, 4
	v_and_b32_e32 v138, 0xf0, v138
	v_mul_u32_u24_e32 v162, 0x110, v162
	v_add3_u32 v167, v164, v138, v162
	v_mul_u32_u24_e32 v162, 0x110, v163
	v_cvt_pk_bf16_f32 v147, v96, v97
	v_cvt_pk_bf16_f32 v149, v92, v93
	v_add3_u32 v168, v164, v165, v162
	v_cvt_pk_bf16_f32 v150, v86, v87
	v_cvt_pk_bf16_f32 v151, v88, v89
	v_cvt_pk_bf16_f32 v152, v82, v83
	v_cvt_pk_bf16_f32 v153, v84, v85
	ds_write_b128 v168, v[146:149]
	ds_write_b128 v168, v[150:153] offset:4352
	s_waitcnt lgkmcnt(0)
	s_barrier
	ds_read_b128 v[146:149], v167
	ds_read_b128 v[150:153], v167 offset:4352
	v_lshl_add_u64 v[162:163], s[34:35], 0, v[138:139]
	v_lshlrev_b32_e32 v138, 7, v165
	v_lshl_add_u64 v[164:165], v[162:163], 0, v[138:139]
	v_or_b32_e32 v138, 0x8000, v138
	s_waitcnt lgkmcnt(0)
	global_store_dwordx4 v[164:165], v[146:149], off offset:256
	v_cvt_pk_bf16_f32 v156, v74, v75
	v_cvt_pk_bf16_f32 v157, v76, v77
	v_lshl_add_u64 v[146:147], v[162:163], 0, v[138:139]
	global_store_dwordx4 v[146:147], v[150:153], off offset:256
	v_cvt_pk_bf16_f32 v158, v70, v71
	v_cvt_pk_bf16_f32 v159, v72, v73
	v_cvt_pk_bf16_f32 v160, v66, v67
	v_cvt_pk_bf16_f32 v161, v68, v69
	s_waitcnt lgkmcnt(0)
	s_barrier
	ds_write_b128 v168, v[154:157]
	ds_write_b128 v168, v[158:161] offset:4352
	s_waitcnt lgkmcnt(0)
	s_barrier
	ds_read_b128 v[146:149], v167
	ds_read_b128 v[150:153], v167 offset:4352
	v_add_co_u32_e32 v154, vcc, s58, v164
	v_mov_b32_e32 v162, v0
	s_nop 0
	v_addc_co_u32_e32 v155, vcc, 0, v165, vcc
	s_waitcnt lgkmcnt(0)
	global_store_dwordx4 v[154:155], v[146:149], off offset:256
	s_add_u32 s34, s34, 0x40000
	s_addc_u32 s35, s35, 0
	v_add_co_u32_e32 v146, vcc, s68, v164
	v_cvt_pk_bf16_f32 v148, v58, v59
	s_nop 0
	v_addc_co_u32_e32 v147, vcc, 0, v165, vcc
	global_store_dwordx4 v[146:147], v[150:153], off offset:256
	s_waitcnt lgkmcnt(0)
	s_barrier
	v_cvt_pk_bf16_f32 v146, v62, v63
	v_lshrrev_b32_e32 v138, 8, v162
	v_and_b32_e32 v163, 15, v162
	v_mad_i32_i24 v164, v138, s72, v166
	v_and_b32_e32 v165, 0xf0, v162
	v_lshlrev_b32_e32 v138, 4, v162
	v_bfe_u32 v162, v162, 4, 4
	v_and_b32_e32 v138, 0xf0, v138
	v_mul_u32_u24_e32 v162, 0x110, v162
	v_add3_u32 v167, v164, v138, v162
	v_mul_u32_u24_e32 v162, 0x110, v163
	v_cvt_pk_bf16_f32 v147, v64, v65
	v_cvt_pk_bf16_f32 v149, v60, v61
	v_add3_u32 v168, v164, v165, v162
	v_cvt_pk_bf16_f32 v150, v54, v55
	v_cvt_pk_bf16_f32 v151, v56, v57
	v_cvt_pk_bf16_f32 v152, v50, v51
	v_cvt_pk_bf16_f32 v153, v52, v53
	ds_write_b128 v168, v[146:149]
	ds_write_b128 v168, v[150:153] offset:4352
	s_waitcnt lgkmcnt(0)
	s_barrier
	ds_read_b128 v[146:149], v167
	ds_read_b128 v[150:153], v167 offset:4352
	v_lshl_add_u64 v[162:163], s[34:35], 0, v[138:139]
	v_lshlrev_b32_e32 v138, 7, v165
	v_lshl_add_u64 v[164:165], v[162:163], 0, v[138:139]
	v_or_b32_e32 v138, 0x8000, v138
	s_waitcnt lgkmcnt(0)
	global_store_dwordx4 v[164:165], v[146:149], off
	v_cvt_pk_bf16_f32 v154, v46, v47
	v_cvt_pk_bf16_f32 v155, v48, v49
	v_lshl_add_u64 v[146:147], v[162:163], 0, v[138:139]
	v_cvt_pk_bf16_f32 v156, v42, v43
	v_cvt_pk_bf16_f32 v157, v44, v45
	global_store_dwordx4 v[146:147], v[150:153], off
	v_cvt_pk_bf16_f32 v158, v38, v39
	v_cvt_pk_bf16_f32 v159, v40, v41
	v_cvt_pk_bf16_f32 v160, v34, v35
	v_cvt_pk_bf16_f32 v161, v36, v37
	s_waitcnt lgkmcnt(0)
	s_barrier
	ds_write_b128 v168, v[154:157]
	ds_write_b128 v168, v[158:161] offset:4352
	s_waitcnt lgkmcnt(0)
	s_barrier
	ds_read_b128 v[146:149], v167
	ds_read_b128 v[150:153], v167 offset:4352
	v_add_co_u32_e32 v154, vcc, s58, v164
	v_mov_b32_e32 v162, v0
	s_nop 0
	v_addc_co_u32_e32 v155, vcc, 0, v165, vcc
	s_waitcnt lgkmcnt(0)
	global_store_dwordx4 v[154:155], v[146:149], off
	v_cvt_pk_bf16_f32 v154, v14, v15
	v_cvt_pk_bf16_f32 v155, v16, v17
	v_add_co_u32_e32 v146, vcc, s68, v164
	v_cvt_pk_bf16_f32 v148, v26, v27
	s_nop 0
	v_addc_co_u32_e32 v147, vcc, 0, v165, vcc
	global_store_dwordx4 v[146:147], v[150:153], off
	s_waitcnt lgkmcnt(0)
	s_barrier
	v_cvt_pk_bf16_f32 v146, v30, v31
	v_lshrrev_b32_e32 v138, 8, v162
	v_and_b32_e32 v163, 15, v162
	v_mad_i32_i24 v164, v138, s72, v166
	v_and_b32_e32 v165, 0xf0, v162
	v_lshlrev_b32_e32 v138, 4, v162
	v_bfe_u32 v162, v162, 4, 4
	v_and_b32_e32 v138, 0xf0, v138
	v_mul_u32_u24_e32 v162, 0x110, v162
	v_add3_u32 v166, v164, v138, v162
	v_mul_u32_u24_e32 v162, 0x110, v163
	v_cvt_pk_bf16_f32 v147, v32, v33
	v_cvt_pk_bf16_f32 v149, v28, v29
	v_add3_u32 v167, v164, v165, v162
	v_cvt_pk_bf16_f32 v150, v22, v23
	v_cvt_pk_bf16_f32 v151, v24, v25
	v_cvt_pk_bf16_f32 v152, v18, v19
	v_cvt_pk_bf16_f32 v153, v20, v21
	ds_write_b128 v167, v[146:149]
	ds_write_b128 v167, v[150:153] offset:4352
	s_waitcnt lgkmcnt(0)
	s_barrier
	ds_read_b128 v[146:149], v166
	ds_read_b128 v[150:153], v166 offset:4352
	v_lshl_add_u64 v[162:163], s[34:35], 0, v[138:139]
	v_lshlrev_b32_e32 v138, 7, v165
	v_lshl_add_u64 v[164:165], v[162:163], 0, v[138:139]
	v_or_b32_e32 v138, 0x8000, v138
	s_waitcnt lgkmcnt(0)
	global_store_dwordx4 v[164:165], v[146:149], off offset:256
	v_cvt_pk_bf16_f32 v156, v10, v11
	v_cvt_pk_bf16_f32 v157, v12, v13
	v_lshl_add_u64 v[146:147], v[162:163], 0, v[138:139]
	global_store_dwordx4 v[146:147], v[150:153], off offset:256
	v_cvt_pk_bf16_f32 v158, v6, v7
	v_cvt_pk_bf16_f32 v159, v8, v9
	v_cvt_pk_bf16_f32 v160, v2, v3
	v_cvt_pk_bf16_f32 v161, v4, v5
	s_waitcnt lgkmcnt(0)
	s_barrier
	ds_write_b128 v167, v[154:157]
	ds_write_b128 v167, v[158:161] offset:4352
	s_waitcnt lgkmcnt(0)
	s_barrier
	ds_read_b128 v[146:149], v166
	ds_read_b128 v[150:153], v166 offset:4352
	v_add_co_u32_e32 v154, vcc, 0x10000, v164
	s_mov_b64 s[34:35], 0
	s_nop 0
	v_addc_co_u32_e32 v155, vcc, 0, v165, vcc
	s_waitcnt lgkmcnt(0)
	global_store_dwordx4 v[154:155], v[146:149], off offset:256
	s_nop 1
	v_add_co_u32_e32 v146, vcc, 0x18000, v164
	s_nop 1
	v_addc_co_u32_e32 v147, vcc, 0, v165, vcc
	global_store_dwordx4 v[146:147], v[150:153], off offset:256
	s_waitcnt lgkmcnt(0)
	s_barrier

; #define LAS __attribute__((address_space(3)))
; #define G_GATHER_OFFS(tab_, rv_) do { _Pragma("unroll") for (int i = 0; i < 2; ++i) { int R_, C_; G_SRC(i, R_, C_); const int ra_ = (tab_)[R_], rb_ = (tab_)[HALF + R_];        \
;     vAc[0][i] = (unsigned)((R_ < (rv_) ? ra_ : 0) * KB + C_); vAc[1][i] = (unsigned)((HALF + R_ < (rv_) ? rb_ : 0) * KB + C_); } } while (0)
; #define G_STAGE(bufoff, gbase, voff) do { _Pragma("unroll") for (int _i = 0; _i < 2; ++_i) \
;     __builtin_amdgcn_global_load_lds((const unsigned*)((const char*)(gbase) + (voff)[_i]), (LAS unsigned*)(lds + (bufoff) + ldsw + _i * 8192), 16, 0, 0); } while (0)
; #define G_LDA(dst, b, h) do { _Pragma("unroll") for (int m = 0; m < 4; ++m) dst[m] = G_LD2(G_SA(b, h) + aoff + m * 2048, G_SA(b, h) + (P::FP8 ? aoff1 : aoff + 1024) + m * 2048); } while (0)
; #define G_LDB(dst, b, h) do { _Pragma("unroll") for (int n = 0; n < 2; ++n) dst[n] = G_LD2(G_SB(b, h) + boff + n * 2048, G_SB(b, h) + (P::FP8 ? boff1 : boff + 1024) + n * 2048); } while (0)
; #define WAIT_V(n) asm volatile("s_waitcnt vmcnt(" #n ")" ::: "memory")
; #define WAIT_L(n) asm volatile("s_waitcnt lgkmcnt(" #n ")" ::: "memory")
; #define BAR __builtin_amdgcn_s_barrier()
; #define SCHED __builtin_amdgcn_sched_barrier(0)
; template <class P>
; DEV void gemm_stream(const P& pol) {
;     ...
;     for (int t = 0; t < nt; t += 2) {
;       const bool last = (t == nt - 2);
;       const size_t k1 = (size_t)(t + 1) * kstep, k2 = (size_t)(t + 2) * kstep;
;       const char* a20 = last ? nA0 : cA0 + k2; const char* a21 = last ? nA1 : cA1 + k2; const char* b2 = last ? nB : cB + k2;
;       G_LDB(B0, 0, 0); SCHED; G_LDA(At, 0, 0); G_STAGE(G_SA(1, 1), cA1 + k1, vAc[1]);
;       WAIT_L(8); BAR; WAIT_L(0); G_MMA(0, 0, At, B0); BAR; SCHED;
;       if (P::GATHER && last && has_next) { LAS int* tab = arow + ((ui + 1) & 1) * 256; G_GATHER_OFFS(tab, nxt.rv); }
;       G_LDB(B1, 0, 1); G_STAGE(G_SB(0, 0), b2, voffB);
;       BAR; WAIT_L(0); G_MMA(0, 1, At, B1); BAR;
;       G_LDA(At, 0, 1); G_STAGE(G_SA(0, 0), a20, vAc[0]);
;       BAR; WAIT_L(0); G_MMA(1, 0, At, B0); BAR; SCHED;
;       G_STAGE(G_SB(0, 1), b2 + hstep, voffB);
;       WAIT_V(6); BAR; G_MMA(1, 1, At, B1); BAR;
.LBB0_467:
	ds_read_b128 v[164:167], v1
	ds_read_b128 v[168:171], v148
	ds_read_b128 v[172:175], v155
	ds_read_b128 v[176:179], v156
	s_add_u32 s26, s20, s24
	s_addc_u32 s27, s21, s25
	s_add_u32 s28, s22, s24
	s_addc_u32 s29, s23, s25
	s_cmpk_eq_i32 s24, 0x1000
	s_cselect_b32 s29, s66, s29
	s_cselect_b32 s28, s67, s28
	v_lshl_add_u64 v[212:213], v[146:147], 0, s[24:25]
	s_mov_b32 m0, s58
	v_lshl_add_u64 v[212:213], v[212:213], 0, s[12:13]
	ds_read_b128 v[180:183], v163
	ds_read_b128 v[184:187], v163 offset:1024
	ds_read_b128 v[188:191], v163 offset:2048
	ds_read_b128 v[192:195], v163 offset:3072
	ds_read_b128 v[196:199], v163 offset:4096
	ds_read_b128 v[200:203], v163 offset:5120
	ds_read_b128 v[204:207], v163 offset:6144
	ds_read_b128 v[208:211], v163 offset:7168
	global_load_lds_dwordx4 v[212:213], off
	v_lshl_add_u64 v[212:213], v[144:145], 0, s[24:25]
	v_lshl_add_u64 v[212:213], v[212:213], 0, s[12:13]
	s_mov_b32 m0, s59
	s_cselect_b32 s71, s64, s27
	global_load_lds_dwordx4 v[212:213], off
	s_waitcnt lgkmcnt(8)
	s_barrier
	s_waitcnt lgkmcnt(0)
	s_cselect_b32 s70, s65, s26
	s_setprio 1
	v_mfma_f32_16x16x32_bf16 v[126:129], v[164:167], v[180:183], v[126:129]
	v_mfma_f32_16x16x32_bf16 v[122:125], v[172:175], v[180:183], v[122:125]
	v_mfma_f32_16x16x32_bf16 v[118:121], v[164:167], v[188:191], v[118:121]
	v_mfma_f32_16x16x32_bf16 v[114:117], v[172:175], v[188:191], v[114:117]
	v_mfma_f32_16x16x32_bf16 v[110:113], v[164:167], v[196:199], v[110:113]
	v_mfma_f32_16x16x32_bf16 v[106:109], v[172:175], v[196:199], v[106:109]
	v_mfma_f32_16x16x32_bf16 v[102:105], v[164:167], v[204:207], v[102:105]
	v_mfma_f32_16x16x32_bf16 v[98:101], v[172:175], v[204:207], v[98:101]
	v_mfma_f32_16x16x32_bf16 v[126:129], v[168:171], v[184:187], v[126:129]
	v_mfma_f32_16x16x32_bf16 v[122:125], v[176:179], v[184:187], v[122:125]
	v_mfma_f32_16x16x32_bf16 v[118:121], v[168:171], v[192:195], v[118:121]
	v_mfma_f32_16x16x32_bf16 v[114:117], v[176:179], v[192:195], v[114:117]
	v_mfma_f32_16x16x32_bf16 v[110:113], v[168:171], v[200:203], v[110:113]
	v_mfma_f32_16x16x32_bf16 v[106:109], v[176:179], v[200:203], v[106:109]
	v_mfma_f32_16x16x32_bf16 v[102:105], v[168:171], v[208:211], v[102:105]
	v_mfma_f32_16x16x32_bf16 v[98:101], v[176:179], v[208:211], v[98:101]
	s_setprio 0
	s_barrier
	s_cselect_b32 s26, 0, s24
	s_cselect_b32 s27, 0, s25
	s_add_u32 s26, s8, s26
	s_addc_u32 s27, s9, s27
	s_mov_b32 m0, s31
	v_lshl_add_u64 v[220:221], s[26:27], 0, v[130:131]
	ds_read_b128 v[212:215], v149
	ds_read_b128 v[216:219], v150
	ds_read_b128 v[224:227], v157
	ds_read_b128 v[228:231], v158
	global_load_lds_dwordx4 v[220:221], off
	v_lshl_add_u64 v[232:233], s[26:27], 0, v[132:133]
	s_mov_b32 m0, s34
	s_nop 0
	global_load_lds_dwordx4 v[232:233], off
	s_barrier
	s_waitcnt lgkmcnt(0)
	s_setprio 1
	v_mfma_f32_16x16x32_bf16 v[94:97], v[212:215], v[180:183], v[94:97]
	v_mfma_f32_16x16x32_bf16 v[90:93], v[224:227], v[180:183], v[90:93]
	v_mfma_f32_16x16x32_bf16 v[86:89], v[212:215], v[188:191], v[86:89]
	v_mfma_f32_16x16x32_bf16 v[82:85], v[224:227], v[188:191], v[82:85]
	v_mfma_f32_16x16x32_bf16 v[78:81], v[212:215], v[196:199], v[78:81]
	v_mfma_f32_16x16x32_bf16 v[74:77], v[224:227], v[196:199], v[74:77]
	v_mfma_f32_16x16x32_bf16 v[70:73], v[212:215], v[204:207], v[70:73]
	v_mfma_f32_16x16x32_bf16 v[66:69], v[224:227], v[204:207], v[66:69]
	v_mfma_f32_16x16x32_bf16 v[94:97], v[216:219], v[184:187], v[94:97]
	v_mfma_f32_16x16x32_bf16 v[90:93], v[228:231], v[184:187], v[90:93]
	v_mfma_f32_16x16x32_bf16 v[86:89], v[216:219], v[192:195], v[86:89]
	v_mfma_f32_16x16x32_bf16 v[82:85], v[228:231], v[192:195], v[82:85]
	v_mfma_f32_16x16x32_bf16 v[78:81], v[216:219], v[200:203], v[78:81]
	v_mfma_f32_16x16x32_bf16 v[74:77], v[228:231], v[200:203], v[74:77]
	v_mfma_f32_16x16x32_bf16 v[70:73], v[216:219], v[208:211], v[70:73]
	v_mfma_f32_16x16x32_bf16 v[66:69], v[228:231], v[208:211], v[66:69]
	s_setprio 0
	s_mov_b32 m0, s30
	v_lshl_add_u64 v[234:235], s[70:71], 0, v[134:135]
	s_barrier
	ds_read_b128 v[180:183], v163 offset:16384
	ds_read_b128 v[184:187], v163 offset:17408
	ds_read_b128 v[188:191], v163 offset:18432
	ds_read_b128 v[192:195], v163 offset:19456
	ds_read_b128 v[196:199], v163 offset:20480
	ds_read_b128 v[200:203], v163 offset:21504
	ds_read_b128 v[204:207], v163 offset:22528
	ds_read_b128 v[208:211], v163 offset:23552
	global_load_lds_dwordx4 v[234:235], off
	v_lshl_add_u64 v[236:237], s[70:71], 0, v[136:137]
	s_mov_b32 m0, s35
	s_nop 0
	global_load_lds_dwordx4 v[236:237], off
	s_barrier
	s_waitcnt lgkmcnt(0)
	s_setprio 1
	v_mfma_f32_16x16x32_bf16 v[62:65], v[164:167], v[180:183], v[62:65]
	v_mfma_f32_16x16x32_bf16 v[58:61], v[172:175], v[180:183], v[58:61]
	v_mfma_f32_16x16x32_bf16 v[54:57], v[164:167], v[188:191], v[54:57]
	v_mfma_f32_16x16x32_bf16 v[50:53], v[172:175], v[188:191], v[50:53]
	v_mfma_f32_16x16x32_bf16 v[46:49], v[164:167], v[196:199], v[46:49]
	v_mfma_f32_16x16x32_bf16 v[42:45], v[172:175], v[196:199], v[42:45]
	v_mfma_f32_16x16x32_bf16 v[38:41], v[164:167], v[204:207], v[38:41]
	v_mfma_f32_16x16x32_bf16 v[34:37], v[172:175], v[204:207], v[34:37]
	v_mfma_f32_16x16x32_bf16 v[62:65], v[168:171], v[184:187], v[62:65]
	v_mfma_f32_16x16x32_bf16 v[58:61], v[176:179], v[184:187], v[58:61]
	v_mfma_f32_16x16x32_bf16 v[54:57], v[168:171], v[192:195], v[54:57]
	v_mfma_f32_16x16x32_bf16 v[50:53], v[176:179], v[192:195], v[50:53]
	v_mfma_f32_16x16x32_bf16 v[46:49], v[168:171], v[200:203], v[46:49]
	v_mfma_f32_16x16x32_bf16 v[42:45], v[176:179], v[200:203], v[42:45]
	v_mfma_f32_16x16x32_bf16 v[38:41], v[168:171], v[208:211], v[38:41]
	v_mfma_f32_16x16x32_bf16 v[34:37], v[176:179], v[208:211], v[34:37]
	s_setprio 0
	s_barrier
; #define G_STAGE(bufoff, gbase, voff) do { _Pragma("unroll") for (int _i = 0; _i < 2; ++_i) \
;     __builtin_amdgcn_global_load_lds((const unsigned*)((const char*)(gbase) + (voff)[_i]), (LAS unsigned*)(lds + (bufoff) + ldsw + _i * 8192), 16, 0, 0); } while (0)
; #define G_LDA(dst, b, h) do { _Pragma("unroll") for (int m = 0; m < 4; ++m) dst[m] = G_LD2(G_SA(b, h) + aoff + m * 2048, G_SA(b, h) + (P::FP8 ? aoff1 : aoff + 1024) + m * 2048); } while (0)
; #define G_LDB(dst, b, h) do { _Pragma("unroll") for (int n = 0; n < 2; ++n) dst[n] = G_LD2(G_SB(b, h) + boff + n * 2048, G_SB(b, h) + (P::FP8 ? boff1 : boff + 1024) + n * 2048); } while (0)
; #define WAIT_V(n) asm volatile("s_waitcnt vmcnt(" #n ")" ::: "memory")
; #define WAIT_L(n) asm volatile("s_waitcnt lgkmcnt(" #n ")" ::: "memory")
; #define BAR __builtin_amdgcn_s_barrier()
; #define SCHED __builtin_amdgcn_sched_barrier(0)
; template <class P>
; DEV void gemm_stream(const P& pol) {
;     ...
;       WAIT_V(6); BAR; G_MMA(1, 1, At, B1); BAR;
;       G_LDB(B0, 1, 0); SCHED; G_LDA(At, 1, 0); G_STAGE(G_SA(0, 1), a21, vAc[1]);
;       WAIT_L(8); BAR; WAIT_L(0); G_MMA(0, 0, At, B0); BAR; SCHED;
;       G_LDB(B1, 1, 1); G_STAGE(G_SB(1, 0), b2 + kstep, voffB);
;       BAR; WAIT_L(0); G_MMA(0, 1, At, B1); BAR;
;       G_LDA(At, 1, 1); G_STAGE(G_SA(1, 0), a20 + kstep, vAc[0]);
;       BAR; WAIT_L(0); G_MMA(1, 0, At, B0); BAR; SCHED;
	s_add_u32 s70, s26, 0x80000
	s_addc_u32 s71, s27, 0
	s_mov_b32 m0, s36
	v_lshl_add_u64 v[164:165], s[70:71], 0, v[130:131]
	global_load_lds_dwordx4 v[164:165], off
	v_lshl_add_u64 v[164:165], s[70:71], 0, v[132:133]
	s_mov_b32 m0, s37
	s_nop 0
	global_load_lds_dwordx4 v[164:165], off
	s_waitcnt vmcnt(6)
	s_barrier
	s_setprio 1
	v_mfma_f32_16x16x32_bf16 v[30:33], v[212:215], v[180:183], v[30:33]
	v_mfma_f32_16x16x32_bf16 v[26:29], v[224:227], v[180:183], v[26:29]
	v_mfma_f32_16x16x32_bf16 v[22:25], v[212:215], v[188:191], v[22:25]
	v_mfma_f32_16x16x32_bf16 v[18:21], v[224:227], v[188:191], v[18:21]
	v_mfma_f32_16x16x32_bf16 v[14:17], v[212:215], v[196:199], v[14:17]
	v_mfma_f32_16x16x32_bf16 v[10:13], v[224:227], v[196:199], v[10:13]
	v_mfma_f32_16x16x32_bf16 v[6:9], v[212:215], v[204:207], v[6:9]
	v_mfma_f32_16x16x32_bf16 v[2:5], v[224:227], v[204:207], v[2:5]
	v_mfma_f32_16x16x32_bf16 v[30:33], v[216:219], v[184:187], v[30:33]
	v_mfma_f32_16x16x32_bf16 v[26:29], v[228:231], v[184:187], v[26:29]
	v_mfma_f32_16x16x32_bf16 v[22:25], v[216:219], v[192:195], v[22:25]
	v_mfma_f32_16x16x32_bf16 v[18:21], v[228:231], v[192:195], v[18:21]
	v_mfma_f32_16x16x32_bf16 v[14:17], v[216:219], v[200:203], v[14:17]
	v_mfma_f32_16x16x32_bf16 v[10:13], v[228:231], v[200:203], v[10:13]
	v_mfma_f32_16x16x32_bf16 v[6:9], v[216:219], v[208:211], v[6:9]
	v_mfma_f32_16x16x32_bf16 v[2:5], v[228:231], v[208:211], v[2:5]
	s_setprio 0
	s_barrier
	ds_read_b128 v[164:167], v151
	ds_read_b128 v[168:171], v152
	ds_read_b128 v[172:175], v159
	ds_read_b128 v[176:179], v160
	s_mov_b32 m0, s38
	v_lshl_add_u64 v[212:213], s[28:29], 0, v[134:135]
	ds_read_b128 v[180:183], v163 offset:32768
	ds_read_b128 v[184:187], v163 offset:33792
	ds_read_b128 v[188:191], v163 offset:34816
	ds_read_b128 v[192:195], v163 offset:35840
	ds_read_b128 v[196:199], v163 offset:36864
	ds_read_b128 v[200:203], v163 offset:37888
	ds_read_b128 v[204:207], v163 offset:38912
	ds_read_b128 v[208:211], v163 offset:39936
	global_load_lds_dwordx4 v[212:213], off
	v_lshl_add_u64 v[212:213], s[28:29], 0, v[136:137]
	s_mov_b32 m0, s39
	s_nop 0
	global_load_lds_dwordx4 v[212:213], off
	s_waitcnt lgkmcnt(8)
	s_barrier
	s_waitcnt lgkmcnt(0)
	s_setprio 1
	v_mfma_f32_16x16x32_bf16 v[126:129], v[164:167], v[180:183], v[126:129]
	v_mfma_f32_16x16x32_bf16 v[122:125], v[172:175], v[180:183], v[122:125]
	v_mfma_f32_16x16x32_bf16 v[118:121], v[164:167], v[188:191], v[118:121]
	v_mfma_f32_16x16x32_bf16 v[114:117], v[172:175], v[188:191], v[114:117]
	v_mfma_f32_16x16x32_bf16 v[110:113], v[164:167], v[196:199], v[110:113]
	v_mfma_f32_16x16x32_bf16 v[106:109], v[172:175], v[196:199], v[106:109]
	v_mfma_f32_16x16x32_bf16 v[102:105], v[164:167], v[204:207], v[102:105]
	v_mfma_f32_16x16x32_bf16 v[98:101], v[172:175], v[204:207], v[98:101]
	v_mfma_f32_16x16x32_bf16 v[126:129], v[168:171], v[184:187], v[126:129]
	v_mfma_f32_16x16x32_bf16 v[122:125], v[176:179], v[184:187], v[122:125]
	v_mfma_f32_16x16x32_bf16 v[118:121], v[168:171], v[192:195], v[118:121]
	v_mfma_f32_16x16x32_bf16 v[114:117], v[176:179], v[192:195], v[114:117]
	v_mfma_f32_16x16x32_bf16 v[110:113], v[168:171], v[200:203], v[110:113]
	v_mfma_f32_16x16x32_bf16 v[106:109], v[176:179], v[200:203], v[106:109]
	v_mfma_f32_16x16x32_bf16 v[102:105], v[168:171], v[208:211], v[102:105]
	v_mfma_f32_16x16x32_bf16 v[98:101], v[176:179], v[208:211], v[98:101]
	s_setprio 0
	s_barrier
	s_mov_b32 m0, s47
	v_lshl_add_u64 v[220:221], v[220:221], 0, s[10:11]
	ds_read_b128 v[212:215], v153
	ds_read_b128 v[216:219], v154
	ds_read_b128 v[224:227], v161
	ds_read_b128 v[228:231], v162
	global_load_lds_dwordx4 v[220:221], off
	v_lshl_add_u64 v[220:221], v[232:233], 0, s[10:11]
	s_mov_b32 m0, s52
	s_nop 0
	global_load_lds_dwordx4 v[220:221], off
	s_barrier
	s_waitcnt lgkmcnt(0)
	s_setprio 1
	v_mfma_f32_16x16x32_bf16 v[94:97], v[212:215], v[180:183], v[94:97]
	v_mfma_f32_16x16x32_bf16 v[90:93], v[224:227], v[180:183], v[90:93]
	v_mfma_f32_16x16x32_bf16 v[86:89], v[212:215], v[188:191], v[86:89]
	v_mfma_f32_16x16x32_bf16 v[82:85], v[224:227], v[188:191], v[82:85]
	v_mfma_f32_16x16x32_bf16 v[78:81], v[212:215], v[196:199], v[78:81]
	v_mfma_f32_16x16x32_bf16 v[74:77], v[224:227], v[196:199], v[74:77]
	v_mfma_f32_16x16x32_bf16 v[70:73], v[212:215], v[204:207], v[70:73]
	v_mfma_f32_16x16x32_bf16 v[66:69], v[224:227], v[204:207], v[66:69]
	v_mfma_f32_16x16x32_bf16 v[94:97], v[216:219], v[184:187], v[94:97]
	v_mfma_f32_16x16x32_bf16 v[90:93], v[228:231], v[184:187], v[90:93]
	v_mfma_f32_16x16x32_bf16 v[86:89], v[216:219], v[192:195], v[86:89]
	v_mfma_f32_16x16x32_bf16 v[82:85], v[228:231], v[192:195], v[82:85]
	v_mfma_f32_16x16x32_bf16 v[78:81], v[216:219], v[200:203], v[78:81]
	v_mfma_f32_16x16x32_bf16 v[74:77], v[228:231], v[200:203], v[74:77]
	v_mfma_f32_16x16x32_bf16 v[70:73], v[216:219], v[208:211], v[70:73]
	v_mfma_f32_16x16x32_bf16 v[66:69], v[228:231], v[208:211], v[66:69]
	s_setprio 0
	s_mov_b32 m0, s53
	v_lshl_add_u64 v[220:221], v[234:235], 0, s[10:11]
	s_barrier
	ds_read_b128 v[180:183], v163 offset:49152
	ds_read_b128 v[184:187], v163 offset:50176
	ds_read_b128 v[188:191], v163 offset:51200
	ds_read_b128 v[192:195], v163 offset:52224
	ds_read_b128 v[196:199], v163 offset:53248
	ds_read_b128 v[200:203], v163 offset:54272
	ds_read_b128 v[204:207], v163 offset:55296
	ds_read_b128 v[208:211], v163 offset:56320
	global_load_lds_dwordx4 v[220:221], off
	v_lshl_add_u64 v[220:221], v[236:237], 0, s[10:11]
	s_mov_b32 m0, s54
	s_nop 0
	global_load_lds_dwordx4 v[220:221], off
	s_barrier
; #define G_STAGE(bufoff, gbase, voff) do { _Pragma("unroll") for (int _i = 0; _i < 2; ++_i) \
;     __builtin_amdgcn_global_load_lds((const unsigned*)((const char*)(gbase) + (voff)[_i]), (LAS unsigned*)(lds + (bufoff) + ldsw + _i * 8192), 16, 0, 0); } while (0)
; #define WAIT_V(n) asm volatile("s_waitcnt vmcnt(" #n ")" ::: "memory")
; #define WAIT_L(n) asm volatile("s_waitcnt lgkmcnt(" #n ")" ::: "memory")
; #define BAR __builtin_amdgcn_s_barrier()
; #define SCHED __builtin_amdgcn_sched_barrier(0)
;   DEV void bias_dma(const Unit& u, LAS float* tabw) const { __builtin_amdgcn_global_load_lds((const unsigned*)bias_src(u, ltid() & 255), (LAS unsigned*)tabw, 4, 0, 0); }
;   DEV void bias_dma(const Unit& u, LAS float* tabw) const { __builtin_amdgcn_global_load_lds((const unsigned*)bias_src(u, ltid() & 255), (LAS unsigned*)tabw, 4, 0, 0); }
; template <class P>
; DEV void gemm_stream(const P& pol) {
;     ...
;       BAR; WAIT_L(0); G_MMA(1, 0, At, B0); BAR; SCHED;
;       G_STAGE(G_SB(1, 1), b2 + hstep + kstep, voffB);
;       WAIT_V(6); BAR; G_MMA(1, 1, At, B1); BAR;
;       if (P::HASBIAS && has_next && t == 0) pol.bias_dma(nxt, btab + ((ui + 1) & 1) * 256 + ((wid & 3) << 6));
;       if (P::GATHER && has_next && t == 0) pol.arow_dma(nxt, arow + ((ui + 1) & 1) * 256 + ((wid & 3) << 6));
;     }
; DEV f32x4 sig4(f32x4 v) {
;   const f32x4 t = v * -1.4426950408889634f; f32x4 e;
; #pragma unroll
;   for (int j = 0; j < 4; ++j) e[j] = __builtin_amdgcn_exp2f(t[j]);
;   e = e + 1.0f; f32x4 r;
; #pragma unroll
;   for (int j = 0; j < 4; ++j) r[j] = __builtin_amdgcn_rcpf(e[j]);
;   return r;
; }
	s_waitcnt lgkmcnt(0)
	s_setprio 1
	v_mfma_f32_16x16x32_bf16 v[62:65], v[164:167], v[180:183], v[62:65]
	v_mfma_f32_16x16x32_bf16 v[58:61], v[172:175], v[180:183], v[58:61]
	v_mfma_f32_16x16x32_bf16 v[54:57], v[164:167], v[188:191], v[54:57]
	v_mfma_f32_16x16x32_bf16 v[50:53], v[172:175], v[188:191], v[50:53]
	v_mfma_f32_16x16x32_bf16 v[46:49], v[164:167], v[196:199], v[46:49]
	v_mfma_f32_16x16x32_bf16 v[42:45], v[172:175], v[196:199], v[42:45]
	v_mfma_f32_16x16x32_bf16 v[38:41], v[164:167], v[204:207], v[38:41]
	v_mfma_f32_16x16x32_bf16 v[34:37], v[172:175], v[204:207], v[34:37]
	v_mfma_f32_16x16x32_bf16 v[62:65], v[168:171], v[184:187], v[62:65]
	v_mfma_f32_16x16x32_bf16 v[58:61], v[176:179], v[184:187], v[58:61]
	v_mfma_f32_16x16x32_bf16 v[54:57], v[168:171], v[192:195], v[54:57]
	v_mfma_f32_16x16x32_bf16 v[50:53], v[176:179], v[192:195], v[50:53]
	v_mfma_f32_16x16x32_bf16 v[46:49], v[168:171], v[200:203], v[46:49]
	v_mfma_f32_16x16x32_bf16 v[42:45], v[176:179], v[200:203], v[42:45]
	v_mfma_f32_16x16x32_bf16 v[38:41], v[168:171], v[208:211], v[38:41]
	v_mfma_f32_16x16x32_bf16 v[34:37], v[176:179], v[208:211], v[34:37]
	s_setprio 0
	s_barrier
	s_add_u32 s26, s26, 0x80080
	s_addc_u32 s27, s27, 0
	s_mov_b32 m0, s55
	v_lshl_add_u64 v[164:165], s[26:27], 0, v[130:131]
	global_load_lds_dwordx4 v[164:165], off
	v_lshl_add_u64 v[164:165], s[26:27], 0, v[132:133]
	s_mov_b32 m0, s56
	s_nop 0
	global_load_lds_dwordx4 v[164:165], off
	s_waitcnt vmcnt(6)
	s_barrier
	s_setprio 1
	v_mfma_f32_16x16x32_bf16 v[30:33], v[212:215], v[180:183], v[30:33]
	v_mfma_f32_16x16x32_bf16 v[26:29], v[224:227], v[180:183], v[26:29]
	v_mfma_f32_16x16x32_bf16 v[22:25], v[212:215], v[188:191], v[22:25]
	v_mfma_f32_16x16x32_bf16 v[18:21], v[224:227], v[188:191], v[18:21]
	v_mfma_f32_16x16x32_bf16 v[14:17], v[212:215], v[196:199], v[14:17]
	v_mfma_f32_16x16x32_bf16 v[10:13], v[224:227], v[196:199], v[10:13]
	v_mfma_f32_16x16x32_bf16 v[6:9], v[212:215], v[204:207], v[6:9]
	v_mfma_f32_16x16x32_bf16 v[2:5], v[224:227], v[204:207], v[2:5]
	v_mfma_f32_16x16x32_bf16 v[30:33], v[216:219], v[184:187], v[30:33]
	v_mfma_f32_16x16x32_bf16 v[26:29], v[228:231], v[184:187], v[26:29]
	v_mfma_f32_16x16x32_bf16 v[22:25], v[216:219], v[192:195], v[22:25]
	v_mfma_f32_16x16x32_bf16 v[18:21], v[228:231], v[192:195], v[18:21]
	v_mfma_f32_16x16x32_bf16 v[14:17], v[216:219], v[200:203], v[14:17]
	v_mfma_f32_16x16x32_bf16 v[10:13], v[228:231], v[200:203], v[10:13]
	v_mfma_f32_16x16x32_bf16 v[6:9], v[216:219], v[208:211], v[6:9]
	v_mfma_f32_16x16x32_bf16 v[2:5], v[228:231], v[208:211], v[2:5]
	s_setprio 0
	s_add_i32 s68, s68, 2
	s_add_u32 s24, s24, 0x100
	s_addc_u32 s25, s25, 0
	s_cmp_gt_u32 s68, 29
	s_barrier
	s_cbranch_scc0 .LBB0_467
	v_mul_f32_e32 v138, 0xbfb8aa3b, v126
	v_exp_f32_e32 v138, v138
	v_mul_f32_e32 v144, 0xbfb8aa3b, v127
	v_exp_f32_e32 v145, v144
	v_mul_f32_e32 v144, 0xbfb8aa3b, v128
	v_exp_f32_e32 v146, v144
	v_mul_f32_e32 v144, 0xbfb8aa3b, v129
	v_exp_f32_e32 v147, v144
	v_add_f32_e32 v138, 1.0, v138
	v_rcp_f32_e32 v144, v138
	v_add_f32_e32 v138, 1.0, v145
	v_rcp_f32_e32 v145, v138
	v_add_f32_e32 v138, 1.0, v146
	v_rcp_f32_e32 v146, v138
	v_add_f32_e32 v138, 1.0, v147
	v_rcp_f32_e32 v147, v138
	v_mul_f32_e32 v138, 0xbfb8aa3b, v122
	v_mul_f32_e32 v164, 0xbfb8aa3b, v123
	v_exp_f32_e32 v138, v138
	v_exp_f32_e32 v165, v164
	v_mul_f32_e32 v164, 0xbfb8aa3b, v124
	v_exp_f32_e32 v166, v164
	v_mul_f32_e32 v164, 0xbfb8aa3b, v125
	v_exp_f32_e32 v167, v164
	v_add_f32_e32 v138, 1.0, v138
	v_rcp_f32_e32 v164, v138
	v_add_f32_e32 v138, 1.0, v165
	v_add_f32_e32 v165, 1.0, v166
	v_rcp_f32_e32 v166, v165
	v_add_f32_e32 v165, 1.0, v167
	v_rcp_f32_e32 v167, v165
	v_rcp_f32_e32 v165, v138
	v_pk_mul_f32 v[126:127], v[126:127], v[144:145]
	v_mul_f32_e32 v138, 0xbfb8aa3b, v114
	v_pk_mul_f32 v[144:145], v[124:125], v[166:167]
	v_pk_mul_f32 v[124:125], v[122:123], v[164:165]
	v_exp_f32_e32 v138, v138
	v_cvt_pk_bf16_f32 v124, v124, v125
	v_cvt_pk_bf16_f32 v125, v144, v145
	v_mul_f32_e32 v144, 0xbfb8aa3b, v115
	v_exp_f32_e32 v145, v144
	v_mul_f32_e32 v144, 0xbfb8aa3b, v116
	v_pk_mul_f32 v[128:129], v[128:129], v[146:147]
	v_cvt_pk_bf16_f32 v122, v126, v127
	v_mul_f32_e32 v126, 0xbfb8aa3b, v118
	v_mul_f32_e32 v127, 0xbfb8aa3b, v119
	v_exp_f32_e32 v146, v144
	v_mul_f32_e32 v144, 0xbfb8aa3b, v117
	v_cvt_pk_bf16_f32 v123, v128, v129
	v_exp_f32_e32 v126, v126
	v_exp_f32_e32 v127, v127
	v_mul_f32_e32 v128, 0xbfb8aa3b, v120
	v_mul_f32_e32 v129, 0xbfb8aa3b, v121
	v_exp_f32_e32 v147, v144
	v_exp_f32_e32 v128, v128
	v_exp_f32_e32 v129, v129
	v_add_f32_e32 v138, 1.0, v138
	v_rcp_f32_e32 v144, v138
	v_add_f32_e32 v138, 1.0, v145
	v_add_f32_e32 v145, 1.0, v146
	v_add_f32_e32 v126, 1.0, v126
	v_add_f32_e32 v127, 1.0, v127
	v_rcp_f32_e32 v146, v145
	v_add_f32_e32 v145, 1.0, v147
	v_rcp_f32_e32 v126, v126
	v_rcp_f32_e32 v127, v127
	v_add_f32_e32 v128, 1.0, v128
	v_add_f32_e32 v129, 1.0, v129
	v_rcp_f32_e32 v147, v145
	v_rcp_f32_e32 v145, v138
	v_rcp_f32_e32 v128, v128
	v_rcp_f32_e32 v129, v129
	v_pk_mul_f32 v[118:119], v[118:119], v[126:127]
	v_pk_mul_f32 v[126:127], v[116:117], v[146:147]
	v_pk_mul_f32 v[116:117], v[114:115], v[144:145]
	v_pk_mul_f32 v[120:121], v[120:121], v[128:129]
	v_cvt_pk_bf16_f32 v114, v118, v119
	v_cvt_pk_bf16_f32 v116, v116, v117
	v_cvt_pk_bf16_f32 v117, v126, v127
	v_mul_f32_e32 v118, 0xbfb8aa3b, v110
	v_mul_f32_e32 v119, 0xbfb8aa3b, v111
	v_mul_f32_e32 v126, 0xbfb8aa3b, v106
	v_mul_f32_e32 v127, 0xbfb8aa3b, v107
	v_mul_f32_e32 v128, 0xbfb8aa3b, v108
	v_mul_f32_e32 v129, 0xbfb8aa3b, v109
	v_cvt_pk_bf16_f32 v115, v120, v121
	v_exp_f32_e32 v118, v118
	v_exp_f32_e32 v119, v119
; template <int LB> DEV void stage_store_block(const unsigned (&v)[4][LB / 4], unsigned char* dst, long row_stride) {
;   extern __shared__ __attribute__((aligned(16))) char shm[];
;   constexpr int MP = LB == 8 ? 4 : (LB == 16 ? 2 : 1), PITCH = 16 * LB + 16, ROWS = 16 * MP;
;   static_assert(ROWS * PITCH <= STG_HALF, "staging region");
;   const int tid = ltid(), wr = tid >> 8, wc = (tid >> 6) & 3, fr = tid & 15, fq = (tid >> 4) & 3;
;   char* stg = shm + STG_OFF + wr * STG_HALF;
;   const int t4 = tid & 255;
; #pragma unroll
;   for (int ps = 0; ps < 4 / MP; ++ps) {
; #pragma unroll
;     for (int mm = 0; mm < MP; ++mm) {
;       char* wp = stg + (16 * mm + fr) * PITCH + (4 * wc + fq) * LB; const int m = ps * MP + mm;
;       if (LB == 8) *(u32x2*)wp = (u32x2){v[m][0], v[m][1]};
;       else { *(u32x4*)wp = (u32x4){v[m][0], v[m][1], v[m][2], v[m][3]}; if (LB == 32) *(u32x4*)(wp + 16) = (u32x4){v[m][LB / 4 - 4], v[m][LB / 4 - 3], v[m][LB / 4 - 2], v[m][LB / 4 - 1]}; }
;     }
;     asm volatile("s_waitcnt lgkmcnt(0)" ::: "memory"); __builtin_amdgcn_s_barrier(); asm volatile("" ::: "memory");
; #pragma unroll
;     for (int k = 0; k < 2; ++k) { const int idx = k * 256 + t4, row = idx / LB, ch = idx % LB;
;       *(u32x4*)(dst + (long)(ps * ROWS + row) * row_stride + ch * 16) = *(const u32x4*)(stg + row * PITCH + ch * 16); }
;     asm volatile("s_waitcnt lgkmcnt(0)" ::: "memory"); __builtin_amdgcn_s_barrier(); asm volatile("" ::: "memory");
;   }
; }
; template <int KIND> DEV void EpiIn::run(const AccT& acc, int wr, int wc, int fr, int fq) const {
;     ...
;         unsigned vals[4][4];
; #pragma unroll
;         for (int m = 0; m < 4; ++m) {
;           if (KIND == 3) pk_bf16x8(vals[m], acc[ai][bj][m][0] * sig4(acc[ai][bj][m][0]), acc[ai][bj][m][1] * sig4(acc[ai][bj][m][1]));
;           else pk_bf16x8(vals[m], acc[ai][bj][m][0], acc[ai][bj][m][1]);
;         }
;         bf16_t* dst;
;         if (KIND == 0) dst = P.cq + (row - NCTX) * QRANK + pn * 256 + cb;
;         else if (KIND == 1) dst = P.ckv + row * KVRANK + cb;
;         else if (KIND == 3) dst = (pn < 8 ? P.qh + (pn - 4) * 256 : P.gate + (pn - 20) * 256) + row * 1024 + cb;
;         else dst = P.vh + row * 1024 + (pn - 16) * 256 + cb;
;         stage_store_block<16>(vals, (unsigned char*)dst, (KIND == 0 ? QRANK : (KIND == 1 ? KVRANK : 1024)) * 2);
	v_mul_f32_e32 v120, 0xbfb8aa3b, v112
	v_mul_f32_e32 v121, 0xbfb8aa3b, v113
	v_exp_f32_e32 v126, v126
	v_exp_f32_e32 v127, v127
	v_exp_f32_e32 v128, v128
	v_exp_f32_e32 v129, v129
	v_exp_f32_e32 v120, v120
	v_exp_f32_e32 v121, v121
	v_add_f32_e32 v118, 1.0, v118
	v_add_f32_e32 v119, 1.0, v119
	v_add_f32_e32 v126, 1.0, v126
	v_add_f32_e32 v127, 1.0, v127
	v_add_f32_e32 v128, 1.0, v128
	v_add_f32_e32 v129, 1.0, v129
	v_rcp_f32_e32 v118, v118
	v_rcp_f32_e32 v119, v119
	v_add_f32_e32 v120, 1.0, v120
	v_add_f32_e32 v121, 1.0, v121
	v_rcp_f32_e32 v126, v126
	v_rcp_f32_e32 v128, v128
	v_rcp_f32_e32 v129, v129
	v_rcp_f32_e32 v127, v127
	v_rcp_f32_e32 v120, v120
	v_rcp_f32_e32 v121, v121
	v_pk_mul_f32 v[110:111], v[110:111], v[118:119]
	v_pk_mul_f32 v[118:119], v[108:109], v[128:129]
	v_pk_mul_f32 v[108:109], v[106:107], v[126:127]
	v_pk_mul_f32 v[112:113], v[112:113], v[120:121]
	v_cvt_pk_bf16_f32 v106, v110, v111
	v_cvt_pk_bf16_f32 v108, v108, v109
	v_cvt_pk_bf16_f32 v109, v118, v119
	v_mul_f32_e32 v110, 0xbfb8aa3b, v102
	v_mul_f32_e32 v111, 0xbfb8aa3b, v103
	v_mul_f32_e32 v118, 0xbfb8aa3b, v98
	v_mul_f32_e32 v119, 0xbfb8aa3b, v99
	v_cvt_pk_bf16_f32 v107, v112, v113
	v_exp_f32_e32 v110, v110
	v_exp_f32_e32 v111, v111
	v_mul_f32_e32 v112, 0xbfb8aa3b, v104
	v_mul_f32_e32 v113, 0xbfb8aa3b, v105
	v_exp_f32_e32 v118, v118
	v_exp_f32_e32 v119, v119
	v_mul_f32_e32 v120, 0xbfb8aa3b, v100
	v_mul_f32_e32 v121, 0xbfb8aa3b, v101
	v_exp_f32_e32 v112, v112
	v_exp_f32_e32 v113, v113
	v_exp_f32_e32 v120, v120
	v_exp_f32_e32 v121, v121
	v_add_f32_e32 v110, 1.0, v110
	v_add_f32_e32 v111, 1.0, v111
	v_add_f32_e32 v118, 1.0, v118
	v_add_f32_e32 v119, 1.0, v119
	v_rcp_f32_e32 v110, v110
	v_rcp_f32_e32 v111, v111
	v_add_f32_e32 v112, 1.0, v112
	v_add_f32_e32 v113, 1.0, v113
	v_rcp_f32_e32 v118, v118
	v_add_f32_e32 v120, 1.0, v120
	v_add_f32_e32 v121, 1.0, v121
	v_rcp_f32_e32 v119, v119
	v_rcp_f32_e32 v112, v112
	v_rcp_f32_e32 v113, v113
	v_rcp_f32_e32 v120, v120
	v_rcp_f32_e32 v121, v121
	s_mov_b64 s[20:21], s[4:5]
	v_pk_mul_f32 v[102:103], v[102:103], v[110:111]
	v_pk_mul_f32 v[98:99], v[98:99], v[118:119]
	v_pk_mul_f32 v[104:105], v[104:105], v[112:113]
	v_pk_mul_f32 v[110:111], v[100:101], v[120:121]
	v_cvt_pk_bf16_f32 v100, v102, v103
	v_cvt_pk_bf16_f32 v102, v98, v99
	v_mov_b32_e32 v99, v0
	s_load_dwordx2 s[20:21], s[20:21], 0x168
	v_cvt_pk_bf16_f32 v101, v104, v105
	v_mov_b32_e32 v98, s60
	v_lshrrev_b32_e32 v104, 8, v99
	v_and_b32_e32 v105, 15, v99
	s_lshl_b32 s22, s63, 8
	v_mad_i32_i24 v104, v104, s61, v98
	v_and_b32_e32 v118, 0xf0, v99
	v_mul_u32_u24_e32 v105, 0x110, v105
	s_add_i32 s22, s22, s46
	v_cvt_pk_bf16_f32 v103, v110, v111
	v_lshlrev_b32_e32 v110, 4, v99
	v_bfe_u32 v99, v99, 4, 4
	v_add3_u32 v120, v104, v118, v105
	s_ashr_i32 s23, s22, 31
	v_and_b32_e32 v138, 0xf0, v110
	v_mul_u32_u24_e32 v99, 0x110, v99
	ds_write_b128 v120, v[122:125]
	ds_write_b128 v120, v[114:117] offset:4352
	s_lshl_b64 s[22:23], s[22:23], 11
	v_add3_u32 v99, v104, v138, v99
	s_waitcnt lgkmcnt(0)
	s_barrier
	s_waitcnt lgkmcnt(0)
	s_add_u32 s20, s20, s22
	ds_read_b128 v[110:113], v99
	ds_read_b128 v[114:117], v99 offset:4352
	s_addc_u32 s21, s21, s23
	v_lshl_add_u64 v[104:105], s[20:21], 0, v[138:139]
	v_lshlrev_b32_e32 v138, 7, v118
	v_lshl_add_u64 v[118:119], v[104:105], 0, v[138:139]
	v_or_b32_e32 v138, 0x8000, v138
	v_lshl_add_u64 v[104:105], v[104:105], 0, v[138:139]
	s_waitcnt lgkmcnt(0)
	global_store_dwordx4 v[118:119], v[110:113], off offset:1536
	global_store_dwordx4 v[104:105], v[114:117], off offset:1536
	s_waitcnt lgkmcnt(0)
	s_barrier
	ds_write_b128 v120, v[106:109]
	ds_write_b128 v120, v[100:103] offset:4352
	s_waitcnt lgkmcnt(0)
	s_barrier
	ds_read_b128 v[100:103], v99
	ds_read_b128 v[104:107], v99 offset:4352
	v_add_co_u32_e32 v108, vcc, s45, v118
	v_mul_f32_e32 v99, 0xbfb8aa3b, v94
	s_nop 0
	v_addc_co_u32_e32 v109, vcc, 0, v119, vcc
	s_waitcnt lgkmcnt(0)
	global_store_dwordx4 v[108:109], v[100:103], off offset:1536
	v_exp_f32_e32 v99, v99
	s_mov_b32 s63, s62
	v_add_co_u32_e32 v100, vcc, s57, v118
	v_add_f32_e32 v99, 1.0, v99
	s_nop 0
	v_addc_co_u32_e32 v101, vcc, 0, v119, vcc
	global_store_dwordx4 v[100:101], v[104:107], off offset:1536
	v_mul_f32_e32 v100, 0xbfb8aa3b, v95
	v_exp_f32_e32 v101, v100
	v_mul_f32_e32 v100, 0xbfb8aa3b, v96
	v_exp_f32_e32 v102, v100
	v_mul_f32_e32 v100, 0xbfb8aa3b, v97
	v_exp_f32_e32 v103, v100
	v_rcp_f32_e32 v100, v99
	v_add_f32_e32 v99, 1.0, v101
	v_rcp_f32_e32 v101, v99
	v_add_f32_e32 v99, 1.0, v102
	v_rcp_f32_e32 v102, v99
	v_add_f32_e32 v99, 1.0, v103
	v_rcp_f32_e32 v103, v99
	v_mul_f32_e32 v99, 0xbfb8aa3b, v90
	v_mul_f32_e32 v104, 0xbfb8aa3b, v91
	v_exp_f32_e32 v99, v99
	v_exp_f32_e32 v105, v104
	v_mul_f32_e32 v104, 0xbfb8aa3b, v92
	v_exp_f32_e32 v106, v104
	v_mul_f32_e32 v104, 0xbfb8aa3b, v93
	v_exp_f32_e32 v107, v104
	v_add_f32_e32 v99, 1.0, v99
	v_rcp_f32_e32 v104, v99
	v_add_f32_e32 v99, 1.0, v105
	v_add_f32_e32 v105, 1.0, v106
	v_rcp_f32_e32 v106, v105
	v_add_f32_e32 v105, 1.0, v107
	v_rcp_f32_e32 v107, v105
	v_rcp_f32_e32 v105, v99
	v_pk_mul_f32 v[94:95], v[94:95], v[100:101]
	v_mul_f32_e32 v99, 0xbfb8aa3b, v82
	v_pk_mul_f32 v[100:101], v[92:93], v[106:107]
	v_pk_mul_f32 v[92:93], v[90:91], v[104:105]
	v_cvt_pk_bf16_f32 v90, v94, v95
	v_cvt_pk_bf16_f32 v92, v92, v93
	v_cvt_pk_bf16_f32 v93, v100, v101
	v_mul_f32_e32 v100, 0xbfb8aa3b, v83
	v_mul_f32_e32 v94, 0xbfb8aa3b, v86
	v_mul_f32_e32 v95, 0xbfb8aa3b, v87
	v_exp_f32_e32 v99, v99
	v_exp_f32_e32 v101, v100
	v_mul_f32_e32 v100, 0xbfb8aa3b, v84
	v_pk_mul_f32 v[96:97], v[96:97], v[102:103]
	v_exp_f32_e32 v94, v94
	v_exp_f32_e32 v95, v95
	v_exp_f32_e32 v102, v100
; template <int LB> DEV void stage_store_block(const unsigned (&v)[4][LB / 4], unsigned char* dst, long row_stride) {
;   extern __shared__ __attribute__((aligned(16))) char shm[];
;   constexpr int MP = LB == 8 ? 4 : (LB == 16 ? 2 : 1), PITCH = 16 * LB + 16, ROWS = 16 * MP;
;   static_assert(ROWS * PITCH <= STG_HALF, "staging region");
;   const int tid = ltid(), wr = tid >> 8, wc = (tid >> 6) & 3, fr = tid & 15, fq = (tid >> 4) & 3;
;   char* stg = shm + STG_OFF + wr * STG_HALF;
;   const int t4 = tid & 255;
; #pragma unroll
;   for (int ps = 0; ps < 4 / MP; ++ps) {
; #pragma unroll
;     for (int mm = 0; mm < MP; ++mm) {
;       char* wp = stg + (16 * mm + fr) * PITCH + (4 * wc + fq) * LB; const int m = ps * MP + mm;
;       if (LB == 8) *(u32x2*)wp = (u32x2){v[m][0], v[m][1]};
;       else { *(u32x4*)wp = (u32x4){v[m][0], v[m][1], v[m][2], v[m][3]}; if (LB == 32) *(u32x4*)(wp + 16) = (u32x4){v[m][LB / 4 - 4], v[m][LB / 4 - 3], v[m][LB / 4 - 2], v[m][LB / 4 - 1]}; }
;     }
;     asm volatile("s_waitcnt lgkmcnt(0)" ::: "memory"); __builtin_amdgcn_s_barrier(); asm volatile("" ::: "memory");
; #pragma unroll
;     for (int k = 0; k < 2; ++k) { const int idx = k * 256 + t4, row = idx / LB, ch = idx % LB;
;       *(u32x4*)(dst + (long)(ps * ROWS + row) * row_stride + ch * 16) = *(const u32x4*)(stg + row * PITCH + ch * 16); }
;     asm volatile("s_waitcnt lgkmcnt(0)" ::: "memory"); __builtin_amdgcn_s_barrier(); asm volatile("" ::: "memory");
;   }
; }
; template <int KIND> DEV void EpiIn::run(const AccT& acc, int wr, int wc, int fr, int fq) const {
;     ...
;         unsigned vals[4][4];
; #pragma unroll
;         for (int m = 0; m < 4; ++m) {
;           if (KIND == 3) pk_bf16x8(vals[m], acc[ai][bj][m][0] * sig4(acc[ai][bj][m][0]), acc[ai][bj][m][1] * sig4(acc[ai][bj][m][1]));
;           else pk_bf16x8(vals[m], acc[ai][bj][m][0], acc[ai][bj][m][1]);
;         }
;         bf16_t* dst;
;         if (KIND == 0) dst = P.cq + (row - NCTX) * QRANK + pn * 256 + cb;
;         else if (KIND == 1) dst = P.ckv + row * KVRANK + cb;
;         else if (KIND == 3) dst = (pn < 8 ? P.qh + (pn - 4) * 256 : P.gate + (pn - 20) * 256) + row * 1024 + cb;
;         else dst = P.vh + row * 1024 + (pn - 16) * 256 + cb;
;         stage_store_block<16>(vals, (unsigned char*)dst, (KIND == 0 ? QRANK : (KIND == 1 ? KVRANK : 1024)) * 2);
	v_mul_f32_e32 v100, 0xbfb8aa3b, v85
	v_cvt_pk_bf16_f32 v91, v96, v97
	v_mul_f32_e32 v96, 0xbfb8aa3b, v88
	v_mul_f32_e32 v97, 0xbfb8aa3b, v89
	v_exp_f32_e32 v103, v100
	v_exp_f32_e32 v96, v96
	v_exp_f32_e32 v97, v97
	v_add_f32_e32 v99, 1.0, v99
	v_add_f32_e32 v94, 1.0, v94
	v_add_f32_e32 v95, 1.0, v95
	v_rcp_f32_e32 v100, v99
	v_add_f32_e32 v99, 1.0, v101
	v_add_f32_e32 v101, 1.0, v102
	v_rcp_f32_e32 v94, v94
	v_rcp_f32_e32 v95, v95
	v_rcp_f32_e32 v102, v101
	v_add_f32_e32 v101, 1.0, v103
	v_add_f32_e32 v96, 1.0, v96
	v_add_f32_e32 v97, 1.0, v97
	v_rcp_f32_e32 v103, v101
	v_rcp_f32_e32 v101, v99
	v_rcp_f32_e32 v96, v96
	v_rcp_f32_e32 v97, v97
	v_pk_mul_f32 v[86:87], v[86:87], v[94:95]
	v_pk_mul_f32 v[94:95], v[84:85], v[102:103]
	v_pk_mul_f32 v[84:85], v[82:83], v[100:101]
	v_cvt_pk_bf16_f32 v82, v86, v87
	v_mul_f32_e32 v86, 0xbfb8aa3b, v78
	v_mul_f32_e32 v87, 0xbfb8aa3b, v79
	v_pk_mul_f32 v[88:89], v[88:89], v[96:97]
	v_cvt_pk_bf16_f32 v84, v84, v85
	v_cvt_pk_bf16_f32 v85, v94, v95
	v_exp_f32_e32 v86, v86
	v_exp_f32_e32 v87, v87
	v_mul_f32_e32 v94, 0xbfb8aa3b, v74
	v_mul_f32_e32 v95, 0xbfb8aa3b, v75
	v_mul_f32_e32 v96, 0xbfb8aa3b, v76
	v_mul_f32_e32 v97, 0xbfb8aa3b, v77
	v_cvt_pk_bf16_f32 v83, v88, v89
	v_mul_f32_e32 v88, 0xbfb8aa3b, v80
	v_mul_f32_e32 v89, 0xbfb8aa3b, v81
	v_exp_f32_e32 v94, v94
	v_exp_f32_e32 v95, v95
	v_exp_f32_e32 v96, v96
	v_exp_f32_e32 v97, v97
	v_exp_f32_e32 v88, v88
	v_exp_f32_e32 v89, v89
	v_add_f32_e32 v86, 1.0, v86
	v_add_f32_e32 v87, 1.0, v87
	v_rcp_f32_e32 v86, v86
	v_rcp_f32_e32 v87, v87
	v_add_f32_e32 v94, 1.0, v94
	v_add_f32_e32 v95, 1.0, v95
	v_add_f32_e32 v96, 1.0, v96
	v_add_f32_e32 v97, 1.0, v97
	v_add_f32_e32 v88, 1.0, v88
	v_add_f32_e32 v89, 1.0, v89
	v_rcp_f32_e32 v94, v94
	v_rcp_f32_e32 v96, v96
	v_rcp_f32_e32 v97, v97
	v_rcp_f32_e32 v95, v95
	v_rcp_f32_e32 v88, v88
	v_rcp_f32_e32 v89, v89
	v_pk_mul_f32 v[78:79], v[78:79], v[86:87]
	v_pk_mul_f32 v[86:87], v[76:77], v[96:97]
	v_pk_mul_f32 v[76:77], v[74:75], v[94:95]
	v_cvt_pk_bf16_f32 v74, v78, v79
	v_mul_f32_e32 v78, 0xbfb8aa3b, v70
	v_mul_f32_e32 v79, 0xbfb8aa3b, v71
	v_pk_mul_f32 v[80:81], v[80:81], v[88:89]
	v_cvt_pk_bf16_f32 v76, v76, v77
	v_cvt_pk_bf16_f32 v77, v86, v87
	v_exp_f32_e32 v78, v78
	v_exp_f32_e32 v79, v79
	v_mul_f32_e32 v86, 0xbfb8aa3b, v66
	v_mul_f32_e32 v87, 0xbfb8aa3b, v67
	v_mul_f32_e32 v88, 0xbfb8aa3b, v68
	v_mul_f32_e32 v89, 0xbfb8aa3b, v69
	v_cvt_pk_bf16_f32 v75, v80, v81
	v_mul_f32_e32 v80, 0xbfb8aa3b, v72
	v_mul_f32_e32 v81, 0xbfb8aa3b, v73
	v_exp_f32_e32 v86, v86
	v_exp_f32_e32 v87, v87
	v_exp_f32_e32 v88, v88
	v_exp_f32_e32 v89, v89
	v_exp_f32_e32 v80, v80
	v_exp_f32_e32 v81, v81
	v_add_f32_e32 v78, 1.0, v78
	v_add_f32_e32 v79, 1.0, v79
	v_rcp_f32_e32 v78, v78
	v_rcp_f32_e32 v79, v79
	v_add_f32_e32 v86, 1.0, v86
	v_add_f32_e32 v87, 1.0, v87
	v_add_f32_e32 v88, 1.0, v88
	v_add_f32_e32 v89, 1.0, v89
	v_add_f32_e32 v80, 1.0, v80
	v_add_f32_e32 v81, 1.0, v81
	v_rcp_f32_e32 v86, v86
	v_rcp_f32_e32 v88, v88
	v_rcp_f32_e32 v89, v89
	v_rcp_f32_e32 v87, v87
	v_rcp_f32_e32 v80, v80
	v_rcp_f32_e32 v81, v81
	v_pk_mul_f32 v[70:71], v[70:71], v[78:79]
	v_pk_mul_f32 v[78:79], v[68:69], v[88:89]
	v_pk_mul_f32 v[68:69], v[66:67], v[86:87]
	v_cvt_pk_bf16_f32 v66, v70, v71
	v_mov_b32_e32 v70, v0
	s_waitcnt lgkmcnt(0)
	s_barrier
	v_pk_mul_f32 v[72:73], v[72:73], v[80:81]
	v_cvt_pk_bf16_f32 v68, v68, v69
	v_cvt_pk_bf16_f32 v67, v72, v73
	v_cvt_pk_bf16_f32 v69, v78, v79
	v_lshrrev_b32_e32 v71, 8, v70
	v_and_b32_e32 v72, 15, v70
	v_and_b32_e32 v78, 0xf0, v70
	v_lshlrev_b32_e32 v73, 4, v70
	v_bfe_u32 v70, v70, 4, 4
	v_mad_i32_i24 v71, v71, s61, v98
	v_and_b32_e32 v138, 0xf0, v73
	v_mul_u32_u24_e32 v70, 0x110, v70
	v_add3_u32 v86, v71, v138, v70
	v_mul_u32_u24_e32 v70, 0x110, v72
	v_add3_u32 v87, v71, v78, v70
	ds_write_b128 v87, v[90:93]
	ds_write_b128 v87, v[82:85] offset:4352
	s_waitcnt lgkmcnt(0)
	s_barrier
	ds_read_b128 v[70:73], v86
	v_lshl_add_u64 v[82:83], s[20:21], 0, v[138:139]
	v_lshlrev_b32_e32 v138, 7, v78
	ds_read_b128 v[78:81], v86 offset:4352
	v_lshl_add_u64 v[84:85], v[82:83], 0, v[138:139]
	v_or_b32_e32 v138, 0x8000, v138
	s_waitcnt lgkmcnt(0)
	global_store_dwordx4 v[84:85], v[70:73], off offset:1792
	s_add_u32 s20, s20, 0x40000
	s_addc_u32 s21, s21, 0
	v_lshl_add_u64 v[70:71], v[82:83], 0, v[138:139]
	global_store_dwordx4 v[70:71], v[78:81], off offset:1792
	s_waitcnt lgkmcnt(0)
	s_barrier
	ds_write_b128 v87, v[74:77]
	ds_write_b128 v87, v[66:69] offset:4352
	s_waitcnt lgkmcnt(0)
	s_barrier
; template <int LB> DEV void stage_store_block(const unsigned (&v)[4][LB / 4], unsigned char* dst, long row_stride) {
;   extern __shared__ __attribute__((aligned(16))) char shm[];
;   constexpr int MP = LB == 8 ? 4 : (LB == 16 ? 2 : 1), PITCH = 16 * LB + 16, ROWS = 16 * MP;
;   static_assert(ROWS * PITCH <= STG_HALF, "staging region");
;   const int tid = ltid(), wr = tid >> 8, wc = (tid >> 6) & 3, fr = tid & 15, fq = (tid >> 4) & 3;
;   char* stg = shm + STG_OFF + wr * STG_HALF;
;   const int t4 = tid & 255;
; #pragma unroll
;   for (int ps = 0; ps < 4 / MP; ++ps) {
; #pragma unroll
;     for (int mm = 0; mm < MP; ++mm) {
;       char* wp = stg + (16 * mm + fr) * PITCH + (4 * wc + fq) * LB; const int m = ps * MP + mm;
;       if (LB == 8) *(u32x2*)wp = (u32x2){v[m][0], v[m][1]};
;       else { *(u32x4*)wp = (u32x4){v[m][0], v[m][1], v[m][2], v[m][3]}; if (LB == 32) *(u32x4*)(wp + 16) = (u32x4){v[m][LB / 4 - 4], v[m][LB / 4 - 3], v[m][LB / 4 - 2], v[m][LB / 4 - 1]}; }
;     }
;     asm volatile("s_waitcnt lgkmcnt(0)" ::: "memory"); __builtin_amdgcn_s_barrier(); asm volatile("" ::: "memory");
; #pragma unroll
;     for (int k = 0; k < 2; ++k) { const int idx = k * 256 + t4, row = idx / LB, ch = idx % LB;
;       *(u32x4*)(dst + (long)(ps * ROWS + row) * row_stride + ch * 16) = *(const u32x4*)(stg + row * PITCH + ch * 16); }
;     asm volatile("s_waitcnt lgkmcnt(0)" ::: "memory"); __builtin_amdgcn_s_barrier(); asm volatile("" ::: "memory");
;   }
; }
; template <int KIND> DEV void EpiIn::run(const AccT& acc, int wr, int wc, int fr, int fq) const {
;     ...
;         unsigned vals[4][4];
; #pragma unroll
;         for (int m = 0; m < 4; ++m) {
;           if (KIND == 3) pk_bf16x8(vals[m], acc[ai][bj][m][0] * sig4(acc[ai][bj][m][0]), acc[ai][bj][m][1] * sig4(acc[ai][bj][m][1]));
;           else pk_bf16x8(vals[m], acc[ai][bj][m][0], acc[ai][bj][m][1]);
;         }
;         bf16_t* dst;
;         if (KIND == 0) dst = P.cq + (row - NCTX) * QRANK + pn * 256 + cb;
;         else if (KIND == 1) dst = P.ckv + row * KVRANK + cb;
;         else if (KIND == 3) dst = (pn < 8 ? P.qh + (pn - 4) * 256 : P.gate + (pn - 20) * 256) + row * 1024 + cb;
;         else dst = P.vh + row * 1024 + (pn - 16) * 256 + cb;
;         stage_store_block<16>(vals, (unsigned char*)dst, (KIND == 0 ? QRANK : (KIND == 1 ? KVRANK : 1024)) * 2);
	ds_read_b128 v[66:69], v86
	ds_read_b128 v[70:73], v86 offset:4352
	v_add_co_u32_e32 v74, vcc, s45, v84
	s_mov_b64 s[22:23], s[18:19]
	s_nop 0
	v_addc_co_u32_e32 v75, vcc, 0, v85, vcc
	s_waitcnt lgkmcnt(0)
	global_store_dwordx4 v[74:75], v[66:69], off offset:1792
	s_nop 1
	v_add_co_u32_e32 v66, vcc, s57, v84
	v_mul_f32_e32 v68, 0xbfb8aa3b, v64
	s_nop 0
	v_addc_co_u32_e32 v67, vcc, 0, v85, vcc
	global_store_dwordx4 v[66:67], v[70:73], off offset:1792
	v_mul_f32_e32 v66, 0xbfb8aa3b, v62
	v_mul_f32_e32 v67, 0xbfb8aa3b, v63
	v_exp_f32_e32 v66, v66
	v_exp_f32_e32 v67, v67
	v_mul_f32_e32 v70, 0xbfb8aa3b, v58
	v_mul_f32_e32 v71, 0xbfb8aa3b, v59
	v_mul_f32_e32 v72, 0xbfb8aa3b, v60
	v_mul_f32_e32 v73, 0xbfb8aa3b, v61
	v_mul_f32_e32 v69, 0xbfb8aa3b, v65
	v_exp_f32_e32 v70, v70
	v_exp_f32_e32 v71, v71
	v_exp_f32_e32 v72, v72
	v_exp_f32_e32 v73, v73
	v_exp_f32_e32 v68, v68
	v_exp_f32_e32 v69, v69
	v_add_f32_e32 v66, 1.0, v66
	v_add_f32_e32 v67, 1.0, v67
	v_rcp_f32_e32 v66, v66
	v_rcp_f32_e32 v67, v67
	v_add_f32_e32 v70, 1.0, v70
	v_add_f32_e32 v71, 1.0, v71
	v_add_f32_e32 v72, 1.0, v72
	v_add_f32_e32 v73, 1.0, v73
	v_add_f32_e32 v68, 1.0, v68
	v_add_f32_e32 v69, 1.0, v69
	v_rcp_f32_e32 v70, v70
	v_rcp_f32_e32 v72, v72
	v_rcp_f32_e32 v73, v73
	v_rcp_f32_e32 v71, v71
	v_rcp_f32_e32 v68, v68
	v_rcp_f32_e32 v69, v69
	v_pk_mul_f32 v[62:63], v[62:63], v[66:67]
	v_pk_mul_f32 v[66:67], v[60:61], v[72:73]
	v_pk_mul_f32 v[60:61], v[58:59], v[70:71]
	v_cvt_pk_bf16_f32 v58, v62, v63
	v_mul_f32_e32 v62, 0xbfb8aa3b, v54
	v_mul_f32_e32 v63, 0xbfb8aa3b, v55
	v_pk_mul_f32 v[64:65], v[64:65], v[68:69]
	v_cvt_pk_bf16_f32 v60, v60, v61
	v_cvt_pk_bf16_f32 v61, v66, v67
	v_exp_f32_e32 v62, v62
	v_exp_f32_e32 v63, v63
	v_mul_f32_e32 v66, 0xbfb8aa3b, v50
	v_mul_f32_e32 v67, 0xbfb8aa3b, v51
	v_mul_f32_e32 v68, 0xbfb8aa3b, v52
	v_mul_f32_e32 v69, 0xbfb8aa3b, v53
	v_cvt_pk_bf16_f32 v59, v64, v65
	v_mul_f32_e32 v64, 0xbfb8aa3b, v56
	v_mul_f32_e32 v65, 0xbfb8aa3b, v57
	v_exp_f32_e32 v66, v66
	v_exp_f32_e32 v67, v67
	v_exp_f32_e32 v68, v68
	v_exp_f32_e32 v69, v69
	v_exp_f32_e32 v64, v64
	v_exp_f32_e32 v65, v65
	v_add_f32_e32 v62, 1.0, v62
	v_add_f32_e32 v63, 1.0, v63
	v_rcp_f32_e32 v62, v62
	v_rcp_f32_e32 v63, v63
	v_add_f32_e32 v66, 1.0, v66
	v_add_f32_e32 v67, 1.0, v67
	v_add_f32_e32 v68, 1.0, v68
	v_add_f32_e32 v69, 1.0, v69
	v_add_f32_e32 v64, 1.0, v64
	v_add_f32_e32 v65, 1.0, v65
	v_rcp_f32_e32 v66, v66
	v_rcp_f32_e32 v68, v68
	v_rcp_f32_e32 v69, v69
	v_rcp_f32_e32 v67, v67
	v_rcp_f32_e32 v64, v64
	v_rcp_f32_e32 v65, v65
	v_pk_mul_f32 v[54:55], v[54:55], v[62:63]
	v_pk_mul_f32 v[62:63], v[52:53], v[68:69]
	v_pk_mul_f32 v[52:53], v[50:51], v[66:67]
	v_cvt_pk_bf16_f32 v50, v54, v55
	v_mul_f32_e32 v54, 0xbfb8aa3b, v46
	v_mul_f32_e32 v55, 0xbfb8aa3b, v47
	v_pk_mul_f32 v[56:57], v[56:57], v[64:65]
	v_cvt_pk_bf16_f32 v52, v52, v53
	v_cvt_pk_bf16_f32 v53, v62, v63
	v_exp_f32_e32 v54, v54
	v_exp_f32_e32 v55, v55
	v_mul_f32_e32 v62, 0xbfb8aa3b, v42
	v_mul_f32_e32 v63, 0xbfb8aa3b, v43
	v_mul_f32_e32 v64, 0xbfb8aa3b, v44
	v_mul_f32_e32 v65, 0xbfb8aa3b, v45
	v_cvt_pk_bf16_f32 v51, v56, v57
	v_mul_f32_e32 v56, 0xbfb8aa3b, v48
	v_mul_f32_e32 v57, 0xbfb8aa3b, v49
	v_exp_f32_e32 v62, v62
	v_exp_f32_e32 v63, v63
	v_exp_f32_e32 v64, v64
	v_exp_f32_e32 v65, v65
	v_exp_f32_e32 v56, v56
	v_exp_f32_e32 v57, v57
	v_add_f32_e32 v54, 1.0, v54
	v_add_f32_e32 v55, 1.0, v55
	v_rcp_f32_e32 v54, v54
	v_rcp_f32_e32 v55, v55
	v_add_f32_e32 v62, 1.0, v62
	v_add_f32_e32 v63, 1.0, v63
	v_add_f32_e32 v64, 1.0, v64
	v_add_f32_e32 v65, 1.0, v65
	v_add_f32_e32 v56, 1.0, v56
	v_add_f32_e32 v57, 1.0, v57
	v_rcp_f32_e32 v62, v62
	v_rcp_f32_e32 v64, v64
	v_rcp_f32_e32 v65, v65
	v_rcp_f32_e32 v63, v63
	v_rcp_f32_e32 v56, v56
	v_rcp_f32_e32 v57, v57
	v_pk_mul_f32 v[46:47], v[46:47], v[54:55]
	v_pk_mul_f32 v[54:55], v[44:45], v[64:65]
	v_pk_mul_f32 v[44:45], v[42:43], v[62:63]
	v_cvt_pk_bf16_f32 v42, v46, v47
	v_mul_f32_e32 v46, 0xbfb8aa3b, v38
	v_mul_f32_e32 v47, 0xbfb8aa3b, v39
	v_pk_mul_f32 v[48:49], v[48:49], v[56:57]
	v_cvt_pk_bf16_f32 v44, v44, v45
	v_cvt_pk_bf16_f32 v45, v54, v55
	v_exp_f32_e32 v46, v46
	v_exp_f32_e32 v47, v47
	v_mul_f32_e32 v54, 0xbfb8aa3b, v34
	v_mul_f32_e32 v55, 0xbfb8aa3b, v35
	v_mul_f32_e32 v56, 0xbfb8aa3b, v36
	v_mul_f32_e32 v57, 0xbfb8aa3b, v37
	v_cvt_pk_bf16_f32 v43, v48, v49
	v_mul_f32_e32 v48, 0xbfb8aa3b, v40
	v_mul_f32_e32 v49, 0xbfb8aa3b, v41
	v_exp_f32_e32 v54, v54
	v_exp_f32_e32 v55, v55
	v_exp_f32_e32 v56, v56
	v_exp_f32_e32 v57, v57
	v_exp_f32_e32 v48, v48
	v_exp_f32_e32 v49, v49
	v_add_f32_e32 v46, 1.0, v46
	v_add_f32_e32 v47, 1.0, v47
	v_rcp_f32_e32 v46, v46
	v_rcp_f32_e32 v47, v47
	v_add_f32_e32 v54, 1.0, v54
	v_add_f32_e32 v55, 1.0, v55
	v_add_f32_e32 v56, 1.0, v56
	v_add_f32_e32 v57, 1.0, v57
	v_add_f32_e32 v48, 1.0, v48
	v_add_f32_e32 v49, 1.0, v49
	v_rcp_f32_e32 v54, v54
	v_rcp_f32_e32 v56, v56
	v_rcp_f32_e32 v57, v57
	v_rcp_f32_e32 v55, v55
	v_rcp_f32_e32 v48, v48
	v_rcp_f32_e32 v49, v49
	v_pk_mul_f32 v[38:39], v[38:39], v[46:47]
	v_pk_mul_f32 v[46:47], v[36:37], v[56:57]
	v_pk_mul_f32 v[36:37], v[34:35], v[54:55]
	v_cvt_pk_bf16_f32 v34, v38, v39
	v_mov_b32_e32 v38, v0
	s_waitcnt lgkmcnt(0)
	s_barrier
	v_pk_mul_f32 v[40:41], v[40:41], v[48:49]
	v_cvt_pk_bf16_f32 v36, v36, v37
	v_cvt_pk_bf16_f32 v35, v40, v41
	v_cvt_pk_bf16_f32 v37, v46, v47
	v_lshrrev_b32_e32 v39, 8, v38
	v_and_b32_e32 v40, 15, v38
	v_and_b32_e32 v46, 0xf0, v38
	v_lshlrev_b32_e32 v41, 4, v38
	v_bfe_u32 v38, v38, 4, 4
	v_mad_i32_i24 v39, v39, s61, v98
	v_and_b32_e32 v138, 0xf0, v41
	v_mul_u32_u24_e32 v38, 0x110, v38
	v_add3_u32 v54, v39, v138, v38
	v_mul_u32_u24_e32 v38, 0x110, v40
	v_add3_u32 v55, v39, v46, v38
	ds_write_b128 v55, v[58:61]
	ds_write_b128 v55, v[50:53] offset:4352
	s_waitcnt lgkmcnt(0)
	s_barrier
; template <int LB> DEV void stage_store_block(const unsigned (&v)[4][LB / 4], unsigned char* dst, long row_stride) {
;   extern __shared__ __attribute__((aligned(16))) char shm[];
;   constexpr int MP = LB == 8 ? 4 : (LB == 16 ? 2 : 1), PITCH = 16 * LB + 16, ROWS = 16 * MP;
;   static_assert(ROWS * PITCH <= STG_HALF, "staging region");
;   const int tid = ltid(), wr = tid >> 8, wc = (tid >> 6) & 3, fr = tid & 15, fq = (tid >> 4) & 3;
;   char* stg = shm + STG_OFF + wr * STG_HALF;
;   const int t4 = tid & 255;
; #pragma unroll
;   for (int ps = 0; ps < 4 / MP; ++ps) {
; #pragma unroll
;     for (int mm = 0; mm < MP; ++mm) {
;       char* wp = stg + (16 * mm + fr) * PITCH + (4 * wc + fq) * LB; const int m = ps * MP + mm;
;       if (LB == 8) *(u32x2*)wp = (u32x2){v[m][0], v[m][1]};
;       else { *(u32x4*)wp = (u32x4){v[m][0], v[m][1], v[m][2], v[m][3]}; if (LB == 32) *(u32x4*)(wp + 16) = (u32x4){v[m][LB / 4 - 4], v[m][LB / 4 - 3], v[m][LB / 4 - 2], v[m][LB / 4 - 1]}; }
;     }
;     asm volatile("s_waitcnt lgkmcnt(0)" ::: "memory"); __builtin_amdgcn_s_barrier(); asm volatile("" ::: "memory");
; #pragma unroll
;     for (int k = 0; k < 2; ++k) { const int idx = k * 256 + t4, row = idx / LB, ch = idx % LB;
;       *(u32x4*)(dst + (long)(ps * ROWS + row) * row_stride + ch * 16) = *(const u32x4*)(stg + row * PITCH + ch * 16); }
;     asm volatile("s_waitcnt lgkmcnt(0)" ::: "memory"); __builtin_amdgcn_s_barrier(); asm volatile("" ::: "memory");
;   }
; }
; template <int KIND> DEV void EpiIn::run(const AccT& acc, int wr, int wc, int fr, int fq) const {
;     ...
;         unsigned vals[4][4];
; #pragma unroll
;         for (int m = 0; m < 4; ++m) {
;           if (KIND == 3) pk_bf16x8(vals[m], acc[ai][bj][m][0] * sig4(acc[ai][bj][m][0]), acc[ai][bj][m][1] * sig4(acc[ai][bj][m][1]));
;           else pk_bf16x8(vals[m], acc[ai][bj][m][0], acc[ai][bj][m][1]);
;         }
;         bf16_t* dst;
;         if (KIND == 0) dst = P.cq + (row - NCTX) * QRANK + pn * 256 + cb;
;         else if (KIND == 1) dst = P.ckv + row * KVRANK + cb;
;         else if (KIND == 3) dst = (pn < 8 ? P.qh + (pn - 4) * 256 : P.gate + (pn - 20) * 256) + row * 1024 + cb;
;         else dst = P.vh + row * 1024 + (pn - 16) * 256 + cb;
;         stage_store_block<16>(vals, (unsigned char*)dst, (KIND == 0 ? QRANK : (KIND == 1 ? KVRANK : 1024)) * 2);
	ds_read_b128 v[38:41], v54
	v_lshl_add_u64 v[50:51], s[20:21], 0, v[138:139]
	v_lshlrev_b32_e32 v138, 7, v46
	ds_read_b128 v[46:49], v54 offset:4352
	v_lshl_add_u64 v[52:53], v[50:51], 0, v[138:139]
	v_or_b32_e32 v138, 0x8000, v138
	s_waitcnt lgkmcnt(0)
	global_store_dwordx4 v[52:53], v[38:41], off offset:1536
	s_nop 1
	v_lshl_add_u64 v[38:39], v[50:51], 0, v[138:139]
	global_store_dwordx4 v[38:39], v[46:49], off offset:1536
	s_waitcnt lgkmcnt(0)
	s_barrier
	ds_write_b128 v55, v[42:45]
	ds_write_b128 v55, v[34:37] offset:4352
	s_waitcnt lgkmcnt(0)
	s_barrier
	ds_read_b128 v[34:37], v54
	ds_read_b128 v[38:41], v54 offset:4352
	v_add_co_u32_e32 v42, vcc, s45, v52
	s_nop 1
	v_addc_co_u32_e32 v43, vcc, 0, v53, vcc
	s_waitcnt lgkmcnt(0)
	global_store_dwordx4 v[42:43], v[34:37], off offset:1536
	s_nop 1
	v_add_co_u32_e32 v34, vcc, s57, v52
	v_mul_f32_e32 v36, 0xbfb8aa3b, v32
	s_nop 0
	v_addc_co_u32_e32 v35, vcc, 0, v53, vcc
	global_store_dwordx4 v[34:35], v[38:41], off offset:1536
	v_mul_f32_e32 v34, 0xbfb8aa3b, v30
	v_mul_f32_e32 v35, 0xbfb8aa3b, v31
	v_exp_f32_e32 v34, v34
	v_exp_f32_e32 v35, v35
	v_mul_f32_e32 v37, 0xbfb8aa3b, v33
	v_exp_f32_e32 v36, v36
	v_add_f32_e32 v34, 1.0, v34
	v_add_f32_e32 v35, 1.0, v35
	v_rcp_f32_e32 v34, v34
	v_rcp_f32_e32 v35, v35
	v_exp_f32_e32 v37, v37
	v_mul_f32_e32 v38, 0xbfb8aa3b, v26
	v_exp_f32_e32 v38, v38
	v_pk_mul_f32 v[30:31], v[30:31], v[34:35]
	v_mul_f32_e32 v35, 0xbfb8aa3b, v27
	v_exp_f32_e32 v35, v35
	v_add_f32_e32 v36, 1.0, v36
	v_add_f32_e32 v37, 1.0, v37
	v_rcp_f32_e32 v36, v36
	v_rcp_f32_e32 v37, v37
	v_add_f32_e32 v34, 1.0, v38
	v_add_f32_e32 v35, 1.0, v35
	v_rcp_f32_e32 v34, v34
	v_rcp_f32_e32 v35, v35
	v_pk_mul_f32 v[32:33], v[32:33], v[36:37]
	v_cvt_pk_bf16_f32 v30, v30, v31
	v_cvt_pk_bf16_f32 v31, v32, v33
	v_mul_f32_e32 v32, 0xbfb8aa3b, v22
	v_exp_f32_e32 v33, v32
	v_mul_f32_e32 v32, 0xbfb8aa3b, v23
	v_pk_mul_f32 v[26:27], v[26:27], v[34:35]
	v_exp_f32_e32 v34, v32
	v_mul_f32_e32 v36, 0xbfb8aa3b, v28
	v_mul_f32_e32 v37, 0xbfb8aa3b, v29
	v_exp_f32_e32 v36, v36
	v_exp_f32_e32 v37, v37
	v_cvt_pk_bf16_f32 v32, v26, v27
	v_add_f32_e32 v26, 1.0, v33
	v_mul_f32_e32 v33, 0xbfb8aa3b, v24
	v_add_f32_e32 v27, 1.0, v34
	v_exp_f32_e32 v33, v33
	v_mul_f32_e32 v34, 0xbfb8aa3b, v25
	v_exp_f32_e32 v35, v34
	v_add_f32_e32 v36, 1.0, v36
	v_add_f32_e32 v37, 1.0, v37
	v_rcp_f32_e32 v26, v26
	v_rcp_f32_e32 v27, v27
	v_rcp_f32_e32 v36, v36
	v_rcp_f32_e32 v37, v37
	v_add_f32_e32 v33, 1.0, v33
	v_rcp_f32_e32 v34, v33
	v_add_f32_e32 v33, 1.0, v35
	v_rcp_f32_e32 v35, v33
	v_mul_f32_e32 v33, 0xbfb8aa3b, v18
	v_pk_mul_f32 v[22:23], v[22:23], v[26:27]
	v_mul_f32_e32 v27, 0xbfb8aa3b, v19
	v_pk_mul_f32 v[28:29], v[28:29], v[36:37]
	v_exp_f32_e32 v36, v33
	v_exp_f32_e32 v27, v27
	v_pk_mul_f32 v[24:25], v[24:25], v[34:35]
	v_cvt_pk_bf16_f32 v22, v22, v23
	v_add_f32_e32 v26, 1.0, v36
	v_add_f32_e32 v27, 1.0, v27
	v_rcp_f32_e32 v26, v26
	v_rcp_f32_e32 v27, v27
	v_cvt_pk_bf16_f32 v23, v24, v25
	v_mul_f32_e32 v24, 0xbfb8aa3b, v14
	v_exp_f32_e32 v25, v24
	v_mul_f32_e32 v24, 0xbfb8aa3b, v15
	v_pk_mul_f32 v[18:19], v[18:19], v[26:27]
	v_exp_f32_e32 v26, v24
	v_cvt_pk_bf16_f32 v33, v28, v29
	v_mul_f32_e32 v28, 0xbfb8aa3b, v20
	v_mul_f32_e32 v29, 0xbfb8aa3b, v21
	v_exp_f32_e32 v28, v28
	v_exp_f32_e32 v29, v29
	v_cvt_pk_bf16_f32 v24, v18, v19
	v_add_f32_e32 v18, 1.0, v25
	v_mul_f32_e32 v25, 0xbfb8aa3b, v16
	v_add_f32_e32 v19, 1.0, v26
	v_exp_f32_e32 v25, v25
	v_mul_f32_e32 v26, 0xbfb8aa3b, v17
	v_exp_f32_e32 v27, v26
	v_add_f32_e32 v28, 1.0, v28
	v_add_f32_e32 v29, 1.0, v29
	v_rcp_f32_e32 v18, v18
	v_rcp_f32_e32 v19, v19
	v_rcp_f32_e32 v28, v28
	v_rcp_f32_e32 v29, v29
	v_add_f32_e32 v25, 1.0, v25
	v_rcp_f32_e32 v26, v25
	v_add_f32_e32 v25, 1.0, v27
	v_rcp_f32_e32 v27, v25
	v_mul_f32_e32 v25, 0xbfb8aa3b, v10
	v_pk_mul_f32 v[14:15], v[14:15], v[18:19]
	v_mul_f32_e32 v19, 0xbfb8aa3b, v11
	v_pk_mul_f32 v[20:21], v[20:21], v[28:29]
	v_exp_f32_e32 v28, v25
	v_exp_f32_e32 v19, v19
	v_pk_mul_f32 v[16:17], v[16:17], v[26:27]
	v_cvt_pk_bf16_f32 v14, v14, v15
	v_add_f32_e32 v18, 1.0, v28
	v_add_f32_e32 v19, 1.0, v19
	v_rcp_f32_e32 v18, v18
	v_rcp_f32_e32 v19, v19
	v_cvt_pk_bf16_f32 v15, v16, v17
	v_mul_f32_e32 v16, 0xbfb8aa3b, v6
	v_exp_f32_e32 v17, v16
	v_mul_f32_e32 v16, 0xbfb8aa3b, v7
	v_pk_mul_f32 v[10:11], v[10:11], v[18:19]
	v_exp_f32_e32 v18, v16
	v_cvt_pk_bf16_f32 v25, v20, v21
	v_mul_f32_e32 v20, 0xbfb8aa3b, v12
	v_mul_f32_e32 v21, 0xbfb8aa3b, v13
	v_exp_f32_e32 v20, v20
	v_exp_f32_e32 v21, v21
	v_cvt_pk_bf16_f32 v16, v10, v11
	v_add_f32_e32 v10, 1.0, v17
	v_mul_f32_e32 v17, 0xbfb8aa3b, v8
	v_add_f32_e32 v11, 1.0, v18
	v_exp_f32_e32 v17, v17
	v_mul_f32_e32 v18, 0xbfb8aa3b, v9
	v_exp_f32_e32 v19, v18
	v_add_f32_e32 v20, 1.0, v20
	v_add_f32_e32 v21, 1.0, v21
	v_rcp_f32_e32 v10, v10
	v_rcp_f32_e32 v11, v11
	v_rcp_f32_e32 v20, v20
	v_rcp_f32_e32 v21, v21
	v_add_f32_e32 v17, 1.0, v17
	v_rcp_f32_e32 v18, v17
	v_add_f32_e32 v17, 1.0, v19
	v_rcp_f32_e32 v19, v17
	v_mul_f32_e32 v17, 0xbfb8aa3b, v2
	v_pk_mul_f32 v[6:7], v[6:7], v[10:11]
	v_mul_f32_e32 v11, 0xbfb8aa3b, v3
	v_pk_mul_f32 v[12:13], v[12:13], v[20:21]
	v_exp_f32_e32 v20, v17
	v_exp_f32_e32 v11, v11
	v_cvt_pk_bf16_f32 v17, v12, v13
	v_mul_f32_e32 v12, 0xbfb8aa3b, v4
	v_mul_f32_e32 v13, 0xbfb8aa3b, v5
	v_exp_f32_e32 v12, v12
	v_exp_f32_e32 v13, v13
	v_add_f32_e32 v10, 1.0, v20
	v_add_f32_e32 v11, 1.0, v11
	v_rcp_f32_e32 v10, v10
	v_rcp_f32_e32 v11, v11
	v_add_f32_e32 v12, 1.0, v12
	v_add_f32_e32 v13, 1.0, v13
	v_rcp_f32_e32 v12, v12
	v_rcp_f32_e32 v13, v13
	v_pk_mul_f32 v[8:9], v[8:9], v[18:19]
	v_pk_mul_f32 v[2:3], v[2:3], v[10:11]
	v_cvt_pk_bf16_f32 v6, v6, v7
	v_cvt_pk_bf16_f32 v7, v8, v9
	v_cvt_pk_bf16_f32 v8, v2, v3
	v_mov_b32_e32 v2, v0
	s_waitcnt lgkmcnt(0)
	s_barrier
; DEV int ltid() { int t = threadIdx.x; asm volatile("" : "+v"(t)); return t; }
; #define WAIT_V(n) asm volatile("s_waitcnt vmcnt(" #n ")" ::: "memory")
; #define BAR __builtin_amdgcn_s_barrier()
; template <class P>
; DEV void gemm_stream(const P& pol) {
;     ...
;   }
;   WAIT_V(0);
;   if (wr == 0) BAR;
;   __syncthreads();
; template <int LB> DEV void stage_store_block(const unsigned (&v)[4][LB / 4], unsigned char* dst, long row_stride) {
;   extern __shared__ __attribute__((aligned(16))) char shm[];
;   constexpr int MP = LB == 8 ? 4 : (LB == 16 ? 2 : 1), PITCH = 16 * LB + 16, ROWS = 16 * MP;
;   static_assert(ROWS * PITCH <= STG_HALF, "staging region");
;   const int tid = ltid(), wr = tid >> 8, wc = (tid >> 6) & 3, fr = tid & 15, fq = (tid >> 4) & 3;
;   char* stg = shm + STG_OFF + wr * STG_HALF;
;   const int t4 = tid & 255;
; #pragma unroll
;   for (int ps = 0; ps < 4 / MP; ++ps) {
; #pragma unroll
;     for (int mm = 0; mm < MP; ++mm) {
;       char* wp = stg + (16 * mm + fr) * PITCH + (4 * wc + fq) * LB; const int m = ps * MP + mm;
;       if (LB == 8) *(u32x2*)wp = (u32x2){v[m][0], v[m][1]};
;       else { *(u32x4*)wp = (u32x4){v[m][0], v[m][1], v[m][2], v[m][3]}; if (LB == 32) *(u32x4*)(wp + 16) = (u32x4){v[m][LB / 4 - 4], v[m][LB / 4 - 3], v[m][LB / 4 - 2], v[m][LB / 4 - 1]}; }
;     }
;     asm volatile("s_waitcnt lgkmcnt(0)" ::: "memory"); __builtin_amdgcn_s_barrier(); asm volatile("" ::: "memory");
; #pragma unroll
;     for (int k = 0; k < 2; ++k) { const int idx = k * 256 + t4, row = idx / LB, ch = idx % LB;
;       *(u32x4*)(dst + (long)(ps * ROWS + row) * row_stride + ch * 16) = *(const u32x4*)(stg + row * PITCH + ch * 16); }
;     asm volatile("s_waitcnt lgkmcnt(0)" ::: "memory"); __builtin_amdgcn_s_barrier(); asm volatile("" ::: "memory");
;   }
; }
	v_pk_mul_f32 v[4:5], v[4:5], v[12:13]
	s_nop 0
	v_cvt_pk_bf16_f32 v9, v4, v5
	v_lshrrev_b32_e32 v3, 8, v2
	v_and_b32_e32 v4, 15, v2
	v_and_b32_e32 v10, 0xf0, v2
	v_lshlrev_b32_e32 v5, 4, v2
	v_bfe_u32 v2, v2, 4, 4
	v_mad_i32_i24 v3, v3, s61, v98
	v_and_b32_e32 v138, 0xf0, v5
	v_mul_u32_u24_e32 v2, 0x110, v2
	v_add3_u32 v26, v3, v138, v2
	v_mul_u32_u24_e32 v2, 0x110, v4
	v_add3_u32 v27, v3, v10, v2
	ds_write_b128 v27, v[30:33]
	ds_write_b128 v27, v[22:25] offset:4352
	s_waitcnt lgkmcnt(0)
	s_barrier
	ds_read_b128 v[2:5], v26
	v_lshl_add_u64 v[18:19], s[20:21], 0, v[138:139]
	v_lshlrev_b32_e32 v138, 7, v10
	ds_read_b128 v[10:13], v26 offset:4352
	v_lshl_add_u64 v[20:21], v[18:19], 0, v[138:139]
	v_or_b32_e32 v138, 0x8000, v138
	s_waitcnt lgkmcnt(0)
	global_store_dwordx4 v[20:21], v[2:5], off offset:1792
	s_mov_b64 s[20:21], s[16:17]
	s_nop 0
	v_lshl_add_u64 v[2:3], v[18:19], 0, v[138:139]
	global_store_dwordx4 v[2:3], v[10:13], off offset:1792
	s_waitcnt lgkmcnt(0)
	s_barrier
	ds_write_b128 v27, v[14:17]
	ds_write_b128 v27, v[6:9] offset:4352
	s_waitcnt lgkmcnt(0)
	s_barrier
	ds_read_b128 v[2:5], v26
	ds_read_b128 v[6:9], v26 offset:4352
	v_add_co_u32_e32 v10, vcc, 0x10000, v20
	s_nop 1
	v_addc_co_u32_e32 v11, vcc, 0, v21, vcc
	s_waitcnt lgkmcnt(0)
	global_store_dwordx4 v[10:11], v[2:5], off offset:1792
	s_nop 1
	v_add_co_u32_e32 v2, vcc, 0x18000, v20
	s_nop 1
	v_addc_co_u32_e32 v3, vcc, 0, v21, vcc
	global_store_dwordx4 v[2:3], v[6:9], off offset:1792
	s_waitcnt lgkmcnt(0)
	s_barrier
	s_and_b64 vcc, exec, s[14:15]
	s_cbranch_vccz .LBB0_466
	s_waitcnt vmcnt(0)
	s_cmpk_gt_u32 s3, 0xff
	s_cbranch_scc1 .LBB0_471
	s_barrier

; #define LAS __attribute__((address_space(3)))
; #define G_GATHER_OFFS(tab_, rv_) do { _Pragma("unroll") for (int i = 0; i < 2; ++i) { int R_, C_; G_SRC(i, R_, C_); const int ra_ = (tab_)[R_], rb_ = (tab_)[HALF + R_];        \
;     vAc[0][i] = (unsigned)((R_ < (rv_) ? ra_ : 0) * KB + C_); vAc[1][i] = (unsigned)((HALF + R_ < (rv_) ? rb_ : 0) * KB + C_); } } while (0)
; #define G_STAGE(bufoff, gbase, voff) do { _Pragma("unroll") for (int _i = 0; _i < 2; ++_i) \
;     __builtin_amdgcn_global_load_lds((const unsigned*)((const char*)(gbase) + (voff)[_i]), (LAS unsigned*)(lds + (bufoff) + ldsw + _i * 8192), 16, 0, 0); } while (0)
; #define G_LDA(dst, b, h) do { _Pragma("unroll") for (int m = 0; m < 4; ++m) dst[m] = G_LD2(G_SA(b, h) + aoff + m * 2048, G_SA(b, h) + (P::FP8 ? aoff1 : aoff + 1024) + m * 2048); } while (0)
; #define G_LDB(dst, b, h) do { _Pragma("unroll") for (int n = 0; n < 2; ++n) dst[n] = G_LD2(G_SB(b, h) + boff + n * 2048, G_SB(b, h) + (P::FP8 ? boff1 : boff + 1024) + n * 2048); } while (0)
; #define WAIT_V(n) asm volatile("s_waitcnt vmcnt(" #n ")" ::: "memory")
; #define WAIT_L(n) asm volatile("s_waitcnt lgkmcnt(" #n ")" ::: "memory")
; #define BAR __builtin_amdgcn_s_barrier()
; #define SCHED __builtin_amdgcn_sched_barrier(0)
; template <class P>
; DEV void gemm_stream(const P& pol) {
;     ...
;     for (int t = 0; t < nt; t += 2) {
;       const bool last = (t == nt - 2);
;       const size_t k1 = (size_t)(t + 1) * kstep, k2 = (size_t)(t + 2) * kstep;
;       const char* a20 = last ? nA0 : cA0 + k2; const char* a21 = last ? nA1 : cA1 + k2; const char* b2 = last ? nB : cB + k2;
;       G_LDB(B0, 0, 0); SCHED; G_LDA(At, 0, 0); G_STAGE(G_SA(1, 1), cA1 + k1, vAc[1]);
;       WAIT_L(8); BAR; WAIT_L(0); G_MMA(0, 0, At, B0); BAR; SCHED;
;       if (P::GATHER && last && has_next) { LAS int* tab = arow + ((ui + 1) & 1) * 256; G_GATHER_OFFS(tab, nxt.rv); }
;       G_LDB(B1, 0, 1); G_STAGE(G_SB(0, 0), b2, voffB);
;       BAR; WAIT_L(0); G_MMA(0, 1, At, B1); BAR;
;       G_LDA(At, 0, 1); G_STAGE(G_SA(0, 0), a20, vAc[0]);
;       BAR; WAIT_L(0); G_MMA(1, 0, At, B0); BAR; SCHED;
;       G_STAGE(G_SB(0, 1), b2 + hstep, voffB);
;       WAIT_V(6); BAR; G_MMA(1, 1, At, B1); BAR;
.LBB0_480:
	s_add_u32 s31, s22, s30
	s_addc_u32 s34, s23, 0
	s_add_u32 s35, s31, 0x100
	s_addc_u32 s34, s34, 0
	s_add_u32 s44, s24, s30
	s_addc_u32 s45, s25, 0
	s_add_u32 s36, s44, 0x100
	s_addc_u32 s37, s45, 0
	s_add_u32 s30, s20, s30
	s_addc_u32 s31, s21, 0
	s_add_u32 s38, s30, 0x100
	s_addc_u32 s39, s31, 0
	s_and_b64 s[30:31], s[28:29], exec
	ds_read_b128 v[142:145], v146
	ds_read_b128 v[168:171], v147
	ds_read_b128 v[172:175], v158
	ds_read_b128 v[176:179], v159
	s_cselect_b32 s30, s82, s36
	s_cselect_b32 s31, s81, s37
	s_cselect_b32 s36, s80, s35
	s_cselect_b32 s37, s79, s34
	s_add_i32 m0, s47, 0xc000
	s_add_i32 s85, s47, 0xe000
	s_and_b64 s[28:29], s[28:29], exec
	s_cselect_b32 s38, s84, s38
	s_cselect_b32 s39, s83, s39
	s_add_u32 s28, s38, 0x10000
	s_addc_u32 s29, s39, 0
	s_add_u32 s34, s38, 0x10080
	s_addc_u32 s35, s39, 0
	v_lshl_add_u64 v[212:213], s[44:45], 0, v[134:135]
	v_lshl_add_u64 v[212:213], v[212:213], 0, s[10:11]
	ds_read_b128 v[180:183], v166
	ds_read_b128 v[184:187], v166 offset:1024
	ds_read_b128 v[188:191], v166 offset:2048
	ds_read_b128 v[192:195], v166 offset:3072
	ds_read_b128 v[196:199], v166 offset:4096
	ds_read_b128 v[200:203], v166 offset:5120
	ds_read_b128 v[204:207], v166 offset:6144
	ds_read_b128 v[208:211], v166 offset:7168
	global_load_lds_dwordx4 v[212:213], off
	v_lshl_add_u64 v[212:213], s[44:45], 0, v[136:137]
	v_lshl_add_u64 v[212:213], v[212:213], 0, s[10:11]
	s_mov_b32 m0, s85
	s_nop 0
	global_load_lds_dwordx4 v[212:213], off
	s_waitcnt lgkmcnt(8)
	s_barrier
	s_waitcnt lgkmcnt(0)
	s_setprio 1
	v_mfma_f32_16x16x32_bf16 v[126:129], v[142:145], v[180:183], v[126:129]
	v_mfma_f32_16x16x32_bf16 v[122:125], v[172:175], v[180:183], v[122:125]
	v_mfma_f32_16x16x32_bf16 v[110:113], v[142:145], v[188:191], v[110:113]
	v_mfma_f32_16x16x32_bf16 v[106:109], v[172:175], v[188:191], v[106:109]
	v_mfma_f32_16x16x32_bf16 v[94:97], v[142:145], v[196:199], v[94:97]
	v_mfma_f32_16x16x32_bf16 v[90:93], v[172:175], v[196:199], v[90:93]
	v_mfma_f32_16x16x32_bf16 v[78:81], v[142:145], v[204:207], v[78:81]
	v_mfma_f32_16x16x32_bf16 v[74:77], v[172:175], v[204:207], v[74:77]
	v_mfma_f32_16x16x32_bf16 v[126:129], v[168:171], v[184:187], v[126:129]
	v_mfma_f32_16x16x32_bf16 v[122:125], v[176:179], v[184:187], v[122:125]
	v_mfma_f32_16x16x32_bf16 v[110:113], v[168:171], v[192:195], v[110:113]
	v_mfma_f32_16x16x32_bf16 v[106:109], v[176:179], v[192:195], v[106:109]
	v_mfma_f32_16x16x32_bf16 v[94:97], v[168:171], v[200:203], v[94:97]
	v_mfma_f32_16x16x32_bf16 v[90:93], v[176:179], v[200:203], v[90:93]
	v_mfma_f32_16x16x32_bf16 v[78:81], v[168:171], v[208:211], v[78:81]
	v_mfma_f32_16x16x32_bf16 v[74:77], v[176:179], v[208:211], v[74:77]
	s_setprio 0
	s_barrier
	s_mov_b32 m0, s52
	v_lshl_add_u64 v[220:221], s[38:39], 0, v[130:131]
	ds_read_b128 v[212:215], v148
	ds_read_b128 v[216:219], v149
	ds_read_b128 v[224:227], v160
	ds_read_b128 v[228:231], v161
	global_load_lds_dwordx4 v[220:221], off
	v_lshl_add_u64 v[232:233], s[38:39], 0, v[132:133]
	s_mov_b32 m0, s53
	s_nop 0
	global_load_lds_dwordx4 v[232:233], off
	s_barrier
	s_waitcnt lgkmcnt(0)
	s_setprio 1
	v_mfma_f32_16x16x32_bf16 v[118:121], v[212:215], v[180:183], v[118:121]
	v_mfma_f32_16x16x32_bf16 v[114:117], v[224:227], v[180:183], v[114:117]
	v_mfma_f32_16x16x32_bf16 v[102:105], v[212:215], v[188:191], v[102:105]
	v_mfma_f32_16x16x32_bf16 v[98:101], v[224:227], v[188:191], v[98:101]
	v_mfma_f32_16x16x32_bf16 v[86:89], v[212:215], v[196:199], v[86:89]
	v_mfma_f32_16x16x32_bf16 v[82:85], v[224:227], v[196:199], v[82:85]
	v_mfma_f32_16x16x32_bf16 v[70:73], v[212:215], v[204:207], v[70:73]
	v_mfma_f32_16x16x32_bf16 v[66:69], v[224:227], v[204:207], v[66:69]
	v_mfma_f32_16x16x32_bf16 v[118:121], v[216:219], v[184:187], v[118:121]
	v_mfma_f32_16x16x32_bf16 v[114:117], v[228:231], v[184:187], v[114:117]
	v_mfma_f32_16x16x32_bf16 v[102:105], v[216:219], v[192:195], v[102:105]
	v_mfma_f32_16x16x32_bf16 v[98:101], v[228:231], v[192:195], v[98:101]
	v_mfma_f32_16x16x32_bf16 v[86:89], v[216:219], v[200:203], v[86:89]
	v_mfma_f32_16x16x32_bf16 v[82:85], v[228:231], v[200:203], v[82:85]
	v_mfma_f32_16x16x32_bf16 v[70:73], v[216:219], v[208:211], v[70:73]
	v_mfma_f32_16x16x32_bf16 v[66:69], v[228:231], v[208:211], v[66:69]
	s_setprio 0
	s_mov_b32 m0, s47
	v_lshl_add_u64 v[234:235], s[36:37], 0, v[134:135]
	s_barrier
	ds_read_b128 v[180:183], v166 offset:16384
	ds_read_b128 v[184:187], v166 offset:17408
	ds_read_b128 v[188:191], v166 offset:18432
	ds_read_b128 v[192:195], v166 offset:19456
	ds_read_b128 v[196:199], v166 offset:20480
	ds_read_b128 v[200:203], v166 offset:21504
	ds_read_b128 v[204:207], v166 offset:22528
	ds_read_b128 v[208:211], v166 offset:23552
	global_load_lds_dwordx4 v[234:235], off
	v_lshl_add_u64 v[236:237], s[36:37], 0, v[136:137]
	s_mov_b32 m0, s54
	s_nop 0
	global_load_lds_dwordx4 v[236:237], off
	s_barrier
	s_waitcnt lgkmcnt(0)
	s_setprio 1
	v_mfma_f32_16x16x32_bf16 v[62:65], v[142:145], v[180:183], v[62:65]
	v_mfma_f32_16x16x32_bf16 v[58:61], v[172:175], v[180:183], v[58:61]
	v_mfma_f32_16x16x32_bf16 v[50:53], v[142:145], v[188:191], v[50:53]
	v_mfma_f32_16x16x32_bf16 v[42:45], v[172:175], v[188:191], v[42:45]
	v_mfma_f32_16x16x32_bf16 v[34:37], v[142:145], v[196:199], v[34:37]
	v_mfma_f32_16x16x32_bf16 v[26:29], v[172:175], v[196:199], v[26:29]
	v_mfma_f32_16x16x32_bf16 v[18:21], v[142:145], v[204:207], v[18:21]
	v_mfma_f32_16x16x32_bf16 v[10:13], v[172:175], v[204:207], v[10:13]
	v_mfma_f32_16x16x32_bf16 v[62:65], v[168:171], v[184:187], v[62:65]
	v_mfma_f32_16x16x32_bf16 v[58:61], v[176:179], v[184:187], v[58:61]
	v_mfma_f32_16x16x32_bf16 v[50:53], v[168:171], v[192:195], v[50:53]
	v_mfma_f32_16x16x32_bf16 v[42:45], v[176:179], v[192:195], v[42:45]
	v_mfma_f32_16x16x32_bf16 v[34:37], v[168:171], v[200:203], v[34:37]
	v_mfma_f32_16x16x32_bf16 v[26:29], v[176:179], v[200:203], v[26:29]
	v_mfma_f32_16x16x32_bf16 v[18:21], v[168:171], v[208:211], v[18:21]
	v_mfma_f32_16x16x32_bf16 v[10:13], v[176:179], v[208:211], v[10:13]
	s_setprio 0
	s_barrier
; #define G_STAGE(bufoff, gbase, voff) do { _Pragma("unroll") for (int _i = 0; _i < 2; ++_i) \
;     __builtin_amdgcn_global_load_lds((const unsigned*)((const char*)(gbase) + (voff)[_i]), (LAS unsigned*)(lds + (bufoff) + ldsw + _i * 8192), 16, 0, 0); } while (0)
; #define G_LDA(dst, b, h) do { _Pragma("unroll") for (int m = 0; m < 4; ++m) dst[m] = G_LD2(G_SA(b, h) + aoff + m * 2048, G_SA(b, h) + (P::FP8 ? aoff1 : aoff + 1024) + m * 2048); } while (0)
; #define G_LDB(dst, b, h) do { _Pragma("unroll") for (int n = 0; n < 2; ++n) dst[n] = G_LD2(G_SB(b, h) + boff + n * 2048, G_SB(b, h) + (P::FP8 ? boff1 : boff + 1024) + n * 2048); } while (0)
; #define WAIT_V(n) asm volatile("s_waitcnt vmcnt(" #n ")" ::: "memory")
; #define WAIT_L(n) asm volatile("s_waitcnt lgkmcnt(" #n ")" ::: "memory")
; #define BAR __builtin_amdgcn_s_barrier()
; #define SCHED __builtin_amdgcn_sched_barrier(0)
; template <class P>
; DEV void gemm_stream(const P& pol) {
;     ...
;       WAIT_V(6); BAR; G_MMA(1, 1, At, B1); BAR;
;       G_LDB(B0, 1, 0); SCHED; G_LDA(At, 1, 0); G_STAGE(G_SA(0, 1), a21, vAc[1]);
;       WAIT_L(8); BAR; WAIT_L(0); G_MMA(0, 0, At, B0); BAR; SCHED;
;       G_LDB(B1, 1, 1); G_STAGE(G_SB(1, 0), b2 + kstep, voffB);
;       BAR; WAIT_L(0); G_MMA(0, 1, At, B1); BAR;
;       G_LDA(At, 1, 1); G_STAGE(G_SA(1, 0), a20 + kstep, vAc[0]);
;       BAR; WAIT_L(0); G_MMA(1, 0, At, B0); BAR; SCHED;
	s_mov_b32 m0, s55
	v_lshl_add_u64 v[142:143], s[28:29], 0, v[130:131]
	global_load_lds_dwordx4 v[142:143], off
	v_lshl_add_u64 v[142:143], s[28:29], 0, v[132:133]
	s_mov_b32 m0, s56
	s_nop 0
	global_load_lds_dwordx4 v[142:143], off
	s_waitcnt vmcnt(6)
	s_barrier
	s_setprio 1
	v_mfma_f32_16x16x32_bf16 v[54:57], v[212:215], v[180:183], v[54:57]
	v_mfma_f32_16x16x32_bf16 v[46:49], v[224:227], v[180:183], v[46:49]
	v_mfma_f32_16x16x32_bf16 v[38:41], v[212:215], v[188:191], v[38:41]
	v_mfma_f32_16x16x32_bf16 v[30:33], v[224:227], v[188:191], v[30:33]
	v_mfma_f32_16x16x32_bf16 v[22:25], v[212:215], v[196:199], v[22:25]
	v_mfma_f32_16x16x32_bf16 v[14:17], v[224:227], v[196:199], v[14:17]
	v_mfma_f32_16x16x32_bf16 v[6:9], v[212:215], v[204:207], v[6:9]
	v_mfma_f32_16x16x32_bf16 v[2:5], v[224:227], v[204:207], v[2:5]
	v_mfma_f32_16x16x32_bf16 v[54:57], v[216:219], v[184:187], v[54:57]
	v_mfma_f32_16x16x32_bf16 v[46:49], v[228:231], v[184:187], v[46:49]
	v_mfma_f32_16x16x32_bf16 v[38:41], v[216:219], v[192:195], v[38:41]
	v_mfma_f32_16x16x32_bf16 v[30:33], v[228:231], v[192:195], v[30:33]
	v_mfma_f32_16x16x32_bf16 v[22:25], v[216:219], v[200:203], v[22:25]
	v_mfma_f32_16x16x32_bf16 v[14:17], v[228:231], v[200:203], v[14:17]
	v_mfma_f32_16x16x32_bf16 v[6:9], v[216:219], v[208:211], v[6:9]
	v_mfma_f32_16x16x32_bf16 v[2:5], v[228:231], v[208:211], v[2:5]
	s_setprio 0
	s_barrier
	ds_read_b128 v[142:145], v150
	ds_read_b128 v[168:171], v151
	ds_read_b128 v[172:175], v162
	ds_read_b128 v[176:179], v163
	s_mov_b32 m0, s57
	v_lshl_add_u64 v[212:213], s[30:31], 0, v[134:135]
	ds_read_b128 v[180:183], v166 offset:32768
	ds_read_b128 v[184:187], v166 offset:33792
	ds_read_b128 v[188:191], v166 offset:34816
	ds_read_b128 v[192:195], v166 offset:35840
	ds_read_b128 v[196:199], v166 offset:36864
	ds_read_b128 v[200:203], v166 offset:37888
	ds_read_b128 v[204:207], v166 offset:38912
	ds_read_b128 v[208:211], v166 offset:39936
	global_load_lds_dwordx4 v[212:213], off
	v_lshl_add_u64 v[212:213], s[30:31], 0, v[136:137]
	s_mov_b32 m0, s58
	s_nop 0
	global_load_lds_dwordx4 v[212:213], off
	s_waitcnt lgkmcnt(8)
	s_barrier
	s_waitcnt lgkmcnt(0)
	s_setprio 1
	v_mfma_f32_16x16x32_bf16 v[126:129], v[142:145], v[180:183], v[126:129]
	v_mfma_f32_16x16x32_bf16 v[122:125], v[172:175], v[180:183], v[122:125]
	v_mfma_f32_16x16x32_bf16 v[110:113], v[142:145], v[188:191], v[110:113]
	v_mfma_f32_16x16x32_bf16 v[106:109], v[172:175], v[188:191], v[106:109]
	v_mfma_f32_16x16x32_bf16 v[94:97], v[142:145], v[196:199], v[94:97]
	v_mfma_f32_16x16x32_bf16 v[90:93], v[172:175], v[196:199], v[90:93]
	v_mfma_f32_16x16x32_bf16 v[78:81], v[142:145], v[204:207], v[78:81]
	v_mfma_f32_16x16x32_bf16 v[74:77], v[172:175], v[204:207], v[74:77]
	v_mfma_f32_16x16x32_bf16 v[126:129], v[168:171], v[184:187], v[126:129]
	v_mfma_f32_16x16x32_bf16 v[122:125], v[176:179], v[184:187], v[122:125]
	v_mfma_f32_16x16x32_bf16 v[110:113], v[168:171], v[192:195], v[110:113]
	v_mfma_f32_16x16x32_bf16 v[106:109], v[176:179], v[192:195], v[106:109]
	v_mfma_f32_16x16x32_bf16 v[94:97], v[168:171], v[200:203], v[94:97]
	v_mfma_f32_16x16x32_bf16 v[90:93], v[176:179], v[200:203], v[90:93]
	v_mfma_f32_16x16x32_bf16 v[78:81], v[168:171], v[208:211], v[78:81]
	v_mfma_f32_16x16x32_bf16 v[74:77], v[176:179], v[208:211], v[74:77]
	s_setprio 0
	s_barrier
	s_mov_b32 m0, s61
	v_lshl_add_u64 v[220:221], v[220:221], 0, s[10:11]
	ds_read_b128 v[212:215], v152
	ds_read_b128 v[216:219], v153
	ds_read_b128 v[224:227], v164
	ds_read_b128 v[228:231], v165
	global_load_lds_dwordx4 v[220:221], off
	v_lshl_add_u64 v[220:221], v[232:233], 0, s[10:11]
	s_mov_b32 m0, s62
	s_nop 0
	global_load_lds_dwordx4 v[220:221], off
	s_barrier
	s_waitcnt lgkmcnt(0)
	s_setprio 1
	v_mfma_f32_16x16x32_bf16 v[118:121], v[212:215], v[180:183], v[118:121]
	v_mfma_f32_16x16x32_bf16 v[114:117], v[224:227], v[180:183], v[114:117]
	v_mfma_f32_16x16x32_bf16 v[102:105], v[212:215], v[188:191], v[102:105]
	v_mfma_f32_16x16x32_bf16 v[98:101], v[224:227], v[188:191], v[98:101]
	v_mfma_f32_16x16x32_bf16 v[86:89], v[212:215], v[196:199], v[86:89]
	v_mfma_f32_16x16x32_bf16 v[82:85], v[224:227], v[196:199], v[82:85]
	v_mfma_f32_16x16x32_bf16 v[70:73], v[212:215], v[204:207], v[70:73]
	v_mfma_f32_16x16x32_bf16 v[66:69], v[224:227], v[204:207], v[66:69]
	v_mfma_f32_16x16x32_bf16 v[118:121], v[216:219], v[184:187], v[118:121]
	v_mfma_f32_16x16x32_bf16 v[114:117], v[228:231], v[184:187], v[114:117]
	v_mfma_f32_16x16x32_bf16 v[102:105], v[216:219], v[192:195], v[102:105]
	v_mfma_f32_16x16x32_bf16 v[98:101], v[228:231], v[192:195], v[98:101]
	v_mfma_f32_16x16x32_bf16 v[86:89], v[216:219], v[200:203], v[86:89]
	v_mfma_f32_16x16x32_bf16 v[82:85], v[228:231], v[200:203], v[82:85]
	v_mfma_f32_16x16x32_bf16 v[70:73], v[216:219], v[208:211], v[70:73]
	v_mfma_f32_16x16x32_bf16 v[66:69], v[228:231], v[208:211], v[66:69]
	s_setprio 0
	s_mov_b32 m0, s63
	v_lshl_add_u64 v[220:221], v[234:235], 0, s[10:11]
	s_barrier
	ds_read_b128 v[180:183], v166 offset:49152
	ds_read_b128 v[184:187], v166 offset:50176
	ds_read_b128 v[188:191], v166 offset:51200
	ds_read_b128 v[192:195], v166 offset:52224
	ds_read_b128 v[196:199], v166 offset:53248
	ds_read_b128 v[200:203], v166 offset:54272
	ds_read_b128 v[204:207], v166 offset:55296
	ds_read_b128 v[208:211], v166 offset:56320
	global_load_lds_dwordx4 v[220:221], off
	v_lshl_add_u64 v[220:221], v[236:237], 0, s[10:11]
	s_mov_b32 m0, s64
	s_nop 0
	global_load_lds_dwordx4 v[220:221], off
	s_barrier
; #define G_STAGE(bufoff, gbase, voff) do { _Pragma("unroll") for (int _i = 0; _i < 2; ++_i) \
;     __builtin_amdgcn_global_load_lds((const unsigned*)((const char*)(gbase) + (voff)[_i]), (LAS unsigned*)(lds + (bufoff) + ldsw + _i * 8192), 16, 0, 0); } while (0)
; #define WAIT_V(n) asm volatile("s_waitcnt vmcnt(" #n ")" ::: "memory")
; #define WAIT_L(n) asm volatile("s_waitcnt lgkmcnt(" #n ")" ::: "memory")
; #define BAR __builtin_amdgcn_s_barrier()
; #define SCHED __builtin_amdgcn_sched_barrier(0)
;   DEV void bias_dma(const Unit& u, LAS float* tabw) const { __builtin_amdgcn_global_load_lds((const unsigned*)bias_src(u, ltid() & 255), (LAS unsigned*)tabw, 4, 0, 0); }
;   DEV void bias_dma(const Unit& u, LAS float* tabw) const { __builtin_amdgcn_global_load_lds((const unsigned*)bias_src(u, ltid() & 255), (LAS unsigned*)tabw, 4, 0, 0); }
; template <class P>
; DEV void gemm_stream(const P& pol) {
;     ...
;       BAR; WAIT_L(0); G_MMA(1, 0, At, B0); BAR; SCHED;
;       G_STAGE(G_SB(1, 1), b2 + hstep + kstep, voffB);
;       WAIT_V(6); BAR; G_MMA(1, 1, At, B1); BAR;
;       if (P::HASBIAS && has_next && t == 0) pol.bias_dma(nxt, btab + ((ui + 1) & 1) * 256 + ((wid & 3) << 6));
;       if (P::GATHER && has_next && t == 0) pol.arow_dma(nxt, arow + ((ui + 1) & 1) * 256 + ((wid & 3) << 6));
;     }
	s_waitcnt lgkmcnt(0)
	s_setprio 1
	v_mfma_f32_16x16x32_bf16 v[62:65], v[142:145], v[180:183], v[62:65]
	v_mfma_f32_16x16x32_bf16 v[58:61], v[172:175], v[180:183], v[58:61]
	v_mfma_f32_16x16x32_bf16 v[50:53], v[142:145], v[188:191], v[50:53]
	v_mfma_f32_16x16x32_bf16 v[42:45], v[172:175], v[188:191], v[42:45]
	v_mfma_f32_16x16x32_bf16 v[34:37], v[142:145], v[196:199], v[34:37]
	v_mfma_f32_16x16x32_bf16 v[26:29], v[172:175], v[196:199], v[26:29]
	v_mfma_f32_16x16x32_bf16 v[18:21], v[142:145], v[204:207], v[18:21]
	v_mfma_f32_16x16x32_bf16 v[10:13], v[172:175], v[204:207], v[10:13]
	v_mfma_f32_16x16x32_bf16 v[62:65], v[168:171], v[184:187], v[62:65]
	v_mfma_f32_16x16x32_bf16 v[58:61], v[176:179], v[184:187], v[58:61]
	v_mfma_f32_16x16x32_bf16 v[50:53], v[168:171], v[192:195], v[50:53]
	v_mfma_f32_16x16x32_bf16 v[42:45], v[176:179], v[192:195], v[42:45]
	v_mfma_f32_16x16x32_bf16 v[34:37], v[168:171], v[200:203], v[34:37]
	v_mfma_f32_16x16x32_bf16 v[26:29], v[176:179], v[200:203], v[26:29]
	v_mfma_f32_16x16x32_bf16 v[18:21], v[168:171], v[208:211], v[18:21]
	v_mfma_f32_16x16x32_bf16 v[10:13], v[176:179], v[208:211], v[10:13]
	s_setprio 0
	s_barrier
	s_mov_b32 m0, s65
	v_lshl_add_u64 v[142:143], s[34:35], 0, v[130:131]
	global_load_lds_dwordx4 v[142:143], off
	v_lshl_add_u64 v[142:143], s[34:35], 0, v[132:133]
	s_mov_b32 m0, s66
	s_nop 0
	global_load_lds_dwordx4 v[142:143], off
	s_waitcnt vmcnt(6)
	s_barrier
	s_setprio 1
	v_mfma_f32_16x16x32_bf16 v[54:57], v[212:215], v[180:183], v[54:57]
	v_mfma_f32_16x16x32_bf16 v[46:49], v[224:227], v[180:183], v[46:49]
	v_mfma_f32_16x16x32_bf16 v[38:41], v[212:215], v[188:191], v[38:41]
	v_mfma_f32_16x16x32_bf16 v[30:33], v[224:227], v[188:191], v[30:33]
	v_mfma_f32_16x16x32_bf16 v[22:25], v[212:215], v[196:199], v[22:25]
	v_mfma_f32_16x16x32_bf16 v[14:17], v[224:227], v[196:199], v[14:17]
	v_mfma_f32_16x16x32_bf16 v[6:9], v[212:215], v[204:207], v[6:9]
	v_mfma_f32_16x16x32_bf16 v[2:5], v[224:227], v[204:207], v[2:5]
	v_mfma_f32_16x16x32_bf16 v[54:57], v[216:219], v[184:187], v[54:57]
	v_mfma_f32_16x16x32_bf16 v[46:49], v[228:231], v[184:187], v[46:49]
	v_mfma_f32_16x16x32_bf16 v[38:41], v[216:219], v[192:195], v[38:41]
	v_mfma_f32_16x16x32_bf16 v[30:33], v[228:231], v[192:195], v[30:33]
	v_mfma_f32_16x16x32_bf16 v[22:25], v[216:219], v[200:203], v[22:25]
	v_mfma_f32_16x16x32_bf16 v[14:17], v[228:231], v[200:203], v[14:17]
	v_mfma_f32_16x16x32_bf16 v[6:9], v[216:219], v[208:211], v[6:9]
	v_mfma_f32_16x16x32_bf16 v[2:5], v[228:231], v[208:211], v[2:5]
	s_setprio 0
	s_movk_i32 s30, 0x100
	s_andn2_b64 vcc, exec, s[26:27]
	s_mov_b64 s[28:29], -1
	s_mov_b64 s[26:27], 0
	s_barrier
	s_cbranch_vccz .LBB0_480
; DEV CParams* launder(CParams* p) { asm volatile("" : "+s"(p)); return p; }
; DEV void st_bf16x8(bf16_t* p, f32x4 a, f32x4 b) { u32x4 o; o.x = cvt_pk_bf16(a[0], a[1]); o.y = cvt_pk_bf16(a[2], a[3]); o.z = cvt_pk_bf16(b[0], b[1]); o.w = cvt_pk_bf16(b[2], b[3]); *(u32x4*)p = o; }
; DEV void row_to_bkey(int row, int& b, int& key) { if (row < NCTX) { b = row >> 8; key = row & 255; } else { const int r = row - NCTX; b = r >> 12; key = CTX + (r & 4095); } }
;   DEV void operator()(const AccT& acc, int wr, int wc, int fr, int fq) const {
;     CParams& P = *launder(p); const int row0 = pm * BM + wr * 64 + fr;
; #pragma unroll
;     for (int ai = 0; ai < 2; ++ai)
; #pragma unroll
;       for (int m = 0; m < 4; ++m) {
;         const int row = row0 + ai * HALF + m * 16; int b, key; row_to_bkey(row, b, key);
;         const long bh = (long)(b * NH + pn) * KEYS + key; const int c = wc * 32 + 8 * fq;
;         st_bf16x8(P.kf + bh * QK + c, acc[ai][0][m][0], acc[ai][0][m][1]);
;         st_bf16x8(P.vf + bh * DV + c, acc[ai][1][m][0], acc[ai][1][m][1]);
;       }
;   }
	s_mov_b64 s[24:25], s[4:5]
	s_load_dwordx4 s[20:23], s[24:25], 0x178
	v_lshl_add_u32 v167, s78, 8, v1
	v_mov_b32_e32 v141, v139
	v_add_u32_e32 v138, 0xfffffc00, v167
	v_ashrrev_i32_e32 v168, 8, v167
	s_waitcnt lgkmcnt(0)
	v_lshl_add_u64 v[144:145], s[20:21], 0, v[140:141]
	v_lshl_add_u64 v[142:143], s[22:23], 0, v[140:141]
	v_lshrrev_b32_e32 v141, 12, v138
	v_and_b32_e32 v138, 0xfcf, v138
	v_cmp_gt_i32_e32 vcc, s59, v167
	v_add_u32_e32 v138, 0x100, v138
	v_cvt_pk_bf16_f32 v126, v126, v127
	v_cndmask_b32_e32 v141, v141, v168, vcc
	v_cndmask_b32_e32 v138, v138, v154, vcc
	v_lshl_add_u32 v141, v141, 3, s46
	v_mad_i64_i32 v[170:171], s[20:21], v141, s67, v[138:139]
	v_mad_u64_u32 v[172:173], s[20:21], v170, s68, v[144:145]
	v_cvt_pk_bf16_f32 v127, v128, v129
	v_cvt_pk_bf16_f32 v128, v122, v123
	v_lshlrev_b64 v[122:123], 8, v[170:171]
	v_cvt_pk_bf16_f32 v118, v118, v119
	v_cvt_pk_bf16_f32 v119, v120, v121
	v_cvt_pk_bf16_f32 v120, v114, v115
	v_or_b32_e32 v115, 16, v167
	v_mad_i32_i24 v173, v171, s68, v173
	v_cvt_pk_bf16_f32 v129, v124, v125
	v_lshl_add_u64 v[122:123], v[142:143], 0, v[122:123]
	v_cvt_pk_bf16_f32 v121, v116, v117
	v_cmp_lt_i32_e32 vcc, s69, v115
	global_store_dwordx4 v[172:173], v[126:129], off
	global_store_dwordx4 v[122:123], v[118:121], off
	s_and_saveexec_b64 s[20:21], vcc
	s_xor_b64 s[20:21], exec, s[20:21]
	v_add_u32_e32 v115, 0xfffffc10, v167
	v_lshrrev_b32_e32 v114, 12, v115
	v_and_b32_e32 v115, 0xfdf, v115
	v_add_u32_e32 v138, 0x100, v115
	s_andn2_saveexec_b64 s[20:21], s[20:21]
	v_and_b32_e32 v138, 0xdf, v115
	v_mov_b32_e32 v114, v168
	s_or_b64 exec, exec, s[20:21]
	v_lshl_add_u32 v114, v114, 3, s46
	v_mad_i64_i32 v[114:115], s[20:21], v114, s67, v[138:139]
	v_mad_u64_u32 v[116:117], s[20:21], v114, s68, v[144:145]
	v_cvt_pk_bf16_f32 v110, v110, v111
	v_cvt_pk_bf16_f32 v111, v112, v113
	v_cvt_pk_bf16_f32 v112, v106, v107
	v_lshlrev_b64 v[106:107], 8, v[114:115]
	v_cvt_pk_bf16_f32 v102, v102, v103
	v_cvt_pk_bf16_f32 v103, v104, v105
	v_cvt_pk_bf16_f32 v104, v98, v99
	v_or_b32_e32 v99, 32, v167
	v_mad_i32_i24 v117, v115, s68, v117
	v_cvt_pk_bf16_f32 v113, v108, v109
	v_lshl_add_u64 v[106:107], v[142:143], 0, v[106:107]
	v_cvt_pk_bf16_f32 v105, v100, v101
	v_cmp_lt_i32_e32 vcc, s69, v99
	global_store_dwordx4 v[116:117], v[110:113], off
	global_store_dwordx4 v[106:107], v[102:105], off
	s_and_saveexec_b64 s[20:21], vcc
	s_xor_b64 s[20:21], exec, s[20:21]
	v_add_u32_e32 v99, 0xfffffc20, v167
	v_lshrrev_b32_e32 v98, 12, v99
	v_and_b32_e32 v99, 0xfef, v99
	v_add_u32_e32 v138, 0x100, v99
	s_andn2_saveexec_b64 s[20:21], s[20:21]
	v_and_b32_e32 v138, 0xef, v99
	v_mov_b32_e32 v98, v168
	s_or_b64 exec, exec, s[20:21]
	v_lshl_add_u32 v98, v98, 3, s46
	v_mad_i64_i32 v[98:99], s[20:21], v98, s67, v[138:139]
	v_mad_u64_u32 v[100:101], s[20:21], v98, s68, v[144:145]
	v_cvt_pk_bf16_f32 v94, v94, v95
	v_cvt_pk_bf16_f32 v95, v96, v97
	v_cvt_pk_bf16_f32 v96, v90, v91
	v_lshlrev_b64 v[90:91], 8, v[98:99]
	v_cvt_pk_bf16_f32 v86, v86, v87
	v_cvt_pk_bf16_f32 v87, v88, v89
	v_cvt_pk_bf16_f32 v88, v82, v83
	v_or_b32_e32 v82, 48, v167
	v_mad_i32_i24 v101, v99, s68, v101
	v_cvt_pk_bf16_f32 v97, v92, v93
	v_lshl_add_u64 v[90:91], v[142:143], 0, v[90:91]
	v_cvt_pk_bf16_f32 v89, v84, v85
	v_cmp_lt_i32_e32 vcc, s69, v82
	global_store_dwordx4 v[100:101], v[94:97], off
	global_store_dwordx4 v[90:91], v[86:89], off
	s_and_saveexec_b64 s[20:21], vcc
	s_xor_b64 s[20:21], exec, s[20:21]
	v_add_u32_e32 v82, 0xfffffc30, v167
	v_lshrrev_b32_e32 v168, 12, v82
	v_and_b32_e32 v82, 0xfff, v82
	v_add_u32_e32 v138, 0x100, v82
	s_andn2_saveexec_b64 s[20:21], s[20:21]
	v_and_b32_e32 v138, 0xff, v82
	s_or_b64 exec, exec, s[20:21]
	v_lshl_add_u32 v82, v168, 3, s46
	v_mad_i64_i32 v[82:83], s[20:21], v82, s67, v[138:139]
	v_mad_u64_u32 v[84:85], s[20:21], v82, s68, v[144:145]
	v_cvt_pk_bf16_f32 v78, v78, v79
	v_cvt_pk_bf16_f32 v79, v80, v81
	v_cvt_pk_bf16_f32 v80, v74, v75
	v_lshlrev_b64 v[74:75], 8, v[82:83]
	v_mad_i32_i24 v85, v83, s68, v85
	v_cvt_pk_bf16_f32 v81, v76, v77
	v_lshl_add_u64 v[74:75], v[142:143], 0, v[74:75]
	v_cvt_pk_bf16_f32 v70, v70, v71
	v_cvt_pk_bf16_f32 v71, v72, v73
	v_cvt_pk_bf16_f32 v72, v66, v67
	v_cvt_pk_bf16_f32 v73, v68, v69
	v_cmp_lt_i32_e32 vcc, s70, v167
	global_store_dwordx4 v[84:85], v[78:81], off
	global_store_dwordx4 v[74:75], v[70:73], off
	s_and_saveexec_b64 s[20:21], vcc
	s_xor_b64 s[20:21], exec, s[20:21]
	v_add_u32_e32 v66, 0xfffffc80, v167
	v_lshrrev_b32_e32 v67, 12, v66
	v_and_b32_e32 v66, 0xfcf, v66
	v_add_u32_e32 v138, 0x100, v66
	s_or_saveexec_b64 s[20:21], s[20:21]
	v_add_u32_e32 v68, 0x80, v167
	v_ashrrev_i32_e32 v66, 8, v68
	s_xor_b64 exec, exec, s[20:21]
	s_cbranch_execz .LBB0_476
	v_and_b32_e32 v138, 0xcf, v68
	v_mov_b32_e32 v67, v66
	s_branch .LBB0_476

; #define LAS __attribute__((address_space(3)))
; #define G_GATHER_OFFS(tab_, rv_) do { _Pragma("unroll") for (int i = 0; i < 2; ++i) { int R_, C_; G_SRC(i, R_, C_); const int ra_ = (tab_)[R_], rb_ = (tab_)[HALF + R_];        \
;     vAc[0][i] = (unsigned)((R_ < (rv_) ? ra_ : 0) * KB + C_); vAc[1][i] = (unsigned)((HALF + R_ < (rv_) ? rb_ : 0) * KB + C_); } } while (0)
; #define G_STAGE(bufoff, gbase, voff) do { _Pragma("unroll") for (int _i = 0; _i < 2; ++_i) \
;     __builtin_amdgcn_global_load_lds((const unsigned*)((const char*)(gbase) + (voff)[_i]), (LAS unsigned*)(lds + (bufoff) + ldsw + _i * 8192), 16, 0, 0); } while (0)
; #define G_LDA(dst, b, h) do { _Pragma("unroll") for (int m = 0; m < 4; ++m) dst[m] = G_LD2(G_SA(b, h) + aoff + m * 2048, G_SA(b, h) + (P::FP8 ? aoff1 : aoff + 1024) + m * 2048); } while (0)
; #define G_LDB(dst, b, h) do { _Pragma("unroll") for (int n = 0; n < 2; ++n) dst[n] = G_LD2(G_SB(b, h) + boff + n * 2048, G_SB(b, h) + (P::FP8 ? boff1 : boff + 1024) + n * 2048); } while (0)
; #define WAIT_V(n) asm volatile("s_waitcnt vmcnt(" #n ")" ::: "memory")
; #define WAIT_L(n) asm volatile("s_waitcnt lgkmcnt(" #n ")" ::: "memory")
; #define BAR __builtin_amdgcn_s_barrier()
; #define SCHED __builtin_amdgcn_sched_barrier(0)
; template <class P>
; DEV void gemm_stream(const P& pol) {
;     ...
;     for (int t = 0; t < nt; t += 2) {
;       const bool last = (t == nt - 2);
;       const size_t k1 = (size_t)(t + 1) * kstep, k2 = (size_t)(t + 2) * kstep;
;       const char* a20 = last ? nA0 : cA0 + k2; const char* a21 = last ? nA1 : cA1 + k2; const char* b2 = last ? nB : cB + k2;
;       G_LDB(B0, 0, 0); SCHED; G_LDA(At, 0, 0); G_STAGE(G_SA(1, 1), cA1 + k1, vAc[1]);
;       WAIT_L(8); BAR; WAIT_L(0); G_MMA(0, 0, At, B0); BAR; SCHED;
;       if (P::GATHER && last && has_next) { LAS int* tab = arow + ((ui + 1) & 1) * 256; G_GATHER_OFFS(tab, nxt.rv); }
;       G_LDB(B1, 0, 1); G_STAGE(G_SB(0, 0), b2, voffB);
;       BAR; WAIT_L(0); G_MMA(0, 1, At, B1); BAR;
;       G_LDA(At, 0, 1); G_STAGE(G_SA(0, 0), a20, vAc[0]);
;       BAR; WAIT_L(0); G_MMA(1, 0, At, B0); BAR; SCHED;
;       G_STAGE(G_SB(0, 1), b2 + hstep, voffB);
;       WAIT_V(6); BAR; G_MMA(1, 1, At, B1); BAR;
.LBB0_506:
	s_add_u32 s26, s73, s24
	s_addc_u32 s27, s76, s25
	s_add_u32 s28, s22, s24
	ds_read_b128 v[166:169], v146
	ds_read_b128 v[170:173], v147
	ds_read_b128 v[174:177], v154
	ds_read_b128 v[178:181], v155
	s_addc_u32 s29, s23, s25
	s_add_u32 s28, s28, 0x100
	s_addc_u32 s29, s29, 0
	s_add_u32 s80, s71, s24
	s_addc_u32 s81, s72, s25
	s_cmpk_eq_i32 s24, 0x300
	s_cselect_b32 s29, s67, s29
	s_cselect_b32 s28, s68, s28
	s_mov_b32 m0, s61
	v_lshl_add_u64 v[214:215], v[144:145], 0, s[24:25]
	ds_read_b128 v[182:185], v163
	ds_read_b128 v[186:189], v163 offset:1024
	ds_read_b128 v[190:193], v163 offset:2048
	ds_read_b128 v[194:197], v163 offset:3072
	ds_read_b128 v[198:201], v163 offset:4096
	ds_read_b128 v[202:205], v163 offset:5120
	ds_read_b128 v[206:209], v163 offset:6144
	ds_read_b128 v[210:213], v163 offset:7168
	global_load_lds_dwordx4 v[214:215], off
	v_lshl_add_u64 v[214:215], v[142:143], 0, s[24:25]
	s_mov_b32 m0, s62
	s_cselect_b32 s79, s65, s27
	global_load_lds_dwordx4 v[214:215], off
	s_waitcnt lgkmcnt(8)
	s_barrier
	s_waitcnt lgkmcnt(0)
	s_cselect_b32 s78, s66, s26
	s_setprio 1
	v_mfma_f32_16x16x32_bf16 v[126:129], v[166:169], v[182:185], v[126:129]
	v_mfma_f32_16x16x32_bf16 v[122:125], v[174:177], v[182:185], v[122:125]
	v_mfma_f32_16x16x32_bf16 v[118:121], v[166:169], v[190:193], v[118:121]
	v_mfma_f32_16x16x32_bf16 v[114:117], v[174:177], v[190:193], v[114:117]
	v_mfma_f32_16x16x32_bf16 v[102:105], v[166:169], v[198:201], v[102:105]
	v_mfma_f32_16x16x32_bf16 v[98:101], v[174:177], v[198:201], v[98:101]
	v_mfma_f32_16x16x32_bf16 v[86:89], v[166:169], v[206:209], v[86:89]
	v_mfma_f32_16x16x32_bf16 v[82:85], v[174:177], v[206:209], v[82:85]
	v_mfma_f32_16x16x32_bf16 v[126:129], v[170:173], v[186:189], v[126:129]
	v_mfma_f32_16x16x32_bf16 v[122:125], v[178:181], v[186:189], v[122:125]
	v_mfma_f32_16x16x32_bf16 v[118:121], v[170:173], v[194:197], v[118:121]
	v_mfma_f32_16x16x32_bf16 v[114:117], v[178:181], v[194:197], v[114:117]
	v_mfma_f32_16x16x32_bf16 v[102:105], v[170:173], v[202:205], v[102:105]
	v_mfma_f32_16x16x32_bf16 v[98:101], v[178:181], v[202:205], v[98:101]
	v_mfma_f32_16x16x32_bf16 v[86:89], v[170:173], v[210:213], v[86:89]
	v_mfma_f32_16x16x32_bf16 v[82:85], v[178:181], v[210:213], v[82:85]
	s_setprio 0
	s_barrier
	s_cselect_b32 s27, s69, s81
	s_cselect_b32 s26, s70, s80
	s_mov_b32 m0, s31
	v_lshl_add_u64 v[232:233], s[26:27], 0, v[130:131]
	ds_read_b128 v[214:217], v148
	ds_read_b128 v[218:221], v149
	ds_read_b128 v[224:227], v156
	ds_read_b128 v[228:231], v157
	global_load_lds_dwordx4 v[232:233], off
	v_lshl_add_u64 v[234:235], s[26:27], 0, v[132:133]
	s_mov_b32 m0, s34
	s_nop 0
	global_load_lds_dwordx4 v[234:235], off
	s_barrier
	s_waitcnt lgkmcnt(0)
	s_setprio 1
	v_mfma_f32_16x16x32_bf16 v[110:113], v[214:217], v[182:185], v[110:113]
	v_mfma_f32_16x16x32_bf16 v[106:109], v[224:227], v[182:185], v[106:109]
	v_mfma_f32_16x16x32_bf16 v[94:97], v[214:217], v[190:193], v[94:97]
	v_mfma_f32_16x16x32_bf16 v[90:93], v[224:227], v[190:193], v[90:93]
	v_mfma_f32_16x16x32_bf16 v[78:81], v[214:217], v[198:201], v[78:81]
	v_mfma_f32_16x16x32_bf16 v[74:77], v[224:227], v[198:201], v[74:77]
	v_mfma_f32_16x16x32_bf16 v[70:73], v[214:217], v[206:209], v[70:73]
	v_mfma_f32_16x16x32_bf16 v[66:69], v[224:227], v[206:209], v[66:69]
	v_mfma_f32_16x16x32_bf16 v[110:113], v[218:221], v[186:189], v[110:113]
	v_mfma_f32_16x16x32_bf16 v[106:109], v[228:231], v[186:189], v[106:109]
	v_mfma_f32_16x16x32_bf16 v[94:97], v[218:221], v[194:197], v[94:97]
	v_mfma_f32_16x16x32_bf16 v[90:93], v[228:231], v[194:197], v[90:93]
	v_mfma_f32_16x16x32_bf16 v[78:81], v[218:221], v[202:205], v[78:81]
	v_mfma_f32_16x16x32_bf16 v[74:77], v[228:231], v[202:205], v[74:77]
	v_mfma_f32_16x16x32_bf16 v[70:73], v[218:221], v[210:213], v[70:73]
	v_mfma_f32_16x16x32_bf16 v[66:69], v[228:231], v[210:213], v[66:69]
	s_setprio 0
	s_mov_b32 m0, s30
	v_lshl_add_u64 v[236:237], s[78:79], 0, v[134:135]
	s_barrier
	ds_read_b128 v[182:185], v163 offset:16384
	ds_read_b128 v[186:189], v163 offset:17408
	ds_read_b128 v[190:193], v163 offset:18432
	ds_read_b128 v[194:197], v163 offset:19456
	ds_read_b128 v[198:201], v163 offset:20480
	ds_read_b128 v[202:205], v163 offset:21504
	ds_read_b128 v[206:209], v163 offset:22528
	ds_read_b128 v[210:213], v163 offset:23552
	global_load_lds_dwordx4 v[236:237], off
	v_lshl_add_u64 v[238:239], s[78:79], 0, v[136:137]
	s_mov_b32 m0, s35
	s_nop 0
	global_load_lds_dwordx4 v[238:239], off
	s_barrier
	s_waitcnt lgkmcnt(0)
	s_setprio 1
	v_mfma_f32_16x16x32_bf16 v[62:65], v[166:169], v[182:185], v[62:65]
	v_mfma_f32_16x16x32_bf16 v[58:61], v[174:177], v[182:185], v[58:61]
	v_mfma_f32_16x16x32_bf16 v[54:57], v[166:169], v[190:193], v[54:57]
	v_mfma_f32_16x16x32_bf16 v[50:53], v[174:177], v[190:193], v[50:53]
	v_mfma_f32_16x16x32_bf16 v[38:41], v[166:169], v[198:201], v[38:41]
	v_mfma_f32_16x16x32_bf16 v[34:37], v[174:177], v[198:201], v[34:37]
	v_mfma_f32_16x16x32_bf16 v[22:25], v[166:169], v[206:209], v[22:25]
	v_mfma_f32_16x16x32_bf16 v[18:21], v[174:177], v[206:209], v[18:21]
	v_mfma_f32_16x16x32_bf16 v[62:65], v[170:173], v[186:189], v[62:65]
	v_mfma_f32_16x16x32_bf16 v[58:61], v[178:181], v[186:189], v[58:61]
	v_mfma_f32_16x16x32_bf16 v[54:57], v[170:173], v[194:197], v[54:57]
	v_mfma_f32_16x16x32_bf16 v[50:53], v[178:181], v[194:197], v[50:53]
	v_mfma_f32_16x16x32_bf16 v[38:41], v[170:173], v[202:205], v[38:41]
	v_mfma_f32_16x16x32_bf16 v[34:37], v[178:181], v[202:205], v[34:37]
	v_mfma_f32_16x16x32_bf16 v[22:25], v[170:173], v[210:213], v[22:25]
	v_mfma_f32_16x16x32_bf16 v[18:21], v[178:181], v[210:213], v[18:21]
	s_setprio 0
	s_barrier
; #define G_STAGE(bufoff, gbase, voff) do { _Pragma("unroll") for (int _i = 0; _i < 2; ++_i) \
;     __builtin_amdgcn_global_load_lds((const unsigned*)((const char*)(gbase) + (voff)[_i]), (LAS unsigned*)(lds + (bufoff) + ldsw + _i * 8192), 16, 0, 0); } while (0)
; #define G_LDA(dst, b, h) do { _Pragma("unroll") for (int m = 0; m < 4; ++m) dst[m] = G_LD2(G_SA(b, h) + aoff + m * 2048, G_SA(b, h) + (P::FP8 ? aoff1 : aoff + 1024) + m * 2048); } while (0)
; #define G_LDB(dst, b, h) do { _Pragma("unroll") for (int n = 0; n < 2; ++n) dst[n] = G_LD2(G_SB(b, h) + boff + n * 2048, G_SB(b, h) + (P::FP8 ? boff1 : boff + 1024) + n * 2048); } while (0)
; #define WAIT_V(n) asm volatile("s_waitcnt vmcnt(" #n ")" ::: "memory")
; #define WAIT_L(n) asm volatile("s_waitcnt lgkmcnt(" #n ")" ::: "memory")
; #define BAR __builtin_amdgcn_s_barrier()
; #define SCHED __builtin_amdgcn_sched_barrier(0)
; template <class P>
; DEV void gemm_stream(const P& pol) {
;     ...
;       WAIT_V(6); BAR; G_MMA(1, 1, At, B1); BAR;
;       G_LDB(B0, 1, 0); SCHED; G_LDA(At, 1, 0); G_STAGE(G_SA(0, 1), a21, vAc[1]);
;       WAIT_L(8); BAR; WAIT_L(0); G_MMA(0, 0, At, B0); BAR; SCHED;
;       G_LDB(B1, 1, 1); G_STAGE(G_SB(1, 0), b2 + kstep, voffB);
;       BAR; WAIT_L(0); G_MMA(0, 1, At, B1); BAR;
;       G_LDA(At, 1, 1); G_STAGE(G_SA(1, 0), a20 + kstep, vAc[0]);
;       BAR; WAIT_L(0); G_MMA(1, 0, At, B0); BAR; SCHED;
	s_add_u32 s78, s26, 0x20000
	s_addc_u32 s79, s27, 0
	s_mov_b32 m0, s36
	v_lshl_add_u64 v[166:167], s[78:79], 0, v[130:131]
	global_load_lds_dwordx4 v[166:167], off
	v_lshl_add_u64 v[166:167], s[78:79], 0, v[132:133]
	s_mov_b32 m0, s37
	s_nop 0
	global_load_lds_dwordx4 v[166:167], off
	s_waitcnt vmcnt(6)
	s_barrier
	s_setprio 1
	v_mfma_f32_16x16x32_bf16 v[46:49], v[214:217], v[182:185], v[46:49]
	v_mfma_f32_16x16x32_bf16 v[42:45], v[224:227], v[182:185], v[42:45]
	v_mfma_f32_16x16x32_bf16 v[30:33], v[214:217], v[190:193], v[30:33]
	v_mfma_f32_16x16x32_bf16 v[26:29], v[224:227], v[190:193], v[26:29]
	v_mfma_f32_16x16x32_bf16 v[14:17], v[214:217], v[198:201], v[14:17]
	v_mfma_f32_16x16x32_bf16 v[10:13], v[224:227], v[198:201], v[10:13]
	v_mfma_f32_16x16x32_bf16 v[6:9], v[214:217], v[206:209], v[6:9]
	v_mfma_f32_16x16x32_bf16 v[2:5], v[224:227], v[206:209], v[2:5]
	v_mfma_f32_16x16x32_bf16 v[46:49], v[218:221], v[186:189], v[46:49]
	v_mfma_f32_16x16x32_bf16 v[42:45], v[228:231], v[186:189], v[42:45]
	v_mfma_f32_16x16x32_bf16 v[30:33], v[218:221], v[194:197], v[30:33]
	v_mfma_f32_16x16x32_bf16 v[26:29], v[228:231], v[194:197], v[26:29]
	v_mfma_f32_16x16x32_bf16 v[14:17], v[218:221], v[202:205], v[14:17]
	v_mfma_f32_16x16x32_bf16 v[10:13], v[228:231], v[202:205], v[10:13]
	v_mfma_f32_16x16x32_bf16 v[6:9], v[218:221], v[210:213], v[6:9]
	v_mfma_f32_16x16x32_bf16 v[2:5], v[228:231], v[210:213], v[2:5]
	s_setprio 0
	s_barrier
	ds_read_b128 v[166:169], v150
	ds_read_b128 v[170:173], v151
	ds_read_b128 v[174:177], v158
	ds_read_b128 v[178:181], v159
	s_mov_b32 m0, s38
	v_lshl_add_u64 v[214:215], s[28:29], 0, v[134:135]
	ds_read_b128 v[182:185], v163 offset:32768
	ds_read_b128 v[186:189], v163 offset:33792
	ds_read_b128 v[190:193], v163 offset:34816
	ds_read_b128 v[194:197], v163 offset:35840
	ds_read_b128 v[198:201], v163 offset:36864
	ds_read_b128 v[202:205], v163 offset:37888
	ds_read_b128 v[206:209], v163 offset:38912
	ds_read_b128 v[210:213], v163 offset:39936
	global_load_lds_dwordx4 v[214:215], off
	v_lshl_add_u64 v[214:215], s[28:29], 0, v[136:137]
	s_mov_b32 m0, s39
	s_nop 0
	global_load_lds_dwordx4 v[214:215], off
	s_waitcnt lgkmcnt(8)
	s_barrier
	s_waitcnt lgkmcnt(0)
	s_setprio 1
	v_mfma_f32_16x16x32_bf16 v[126:129], v[166:169], v[182:185], v[126:129]
	v_mfma_f32_16x16x32_bf16 v[122:125], v[174:177], v[182:185], v[122:125]
	v_mfma_f32_16x16x32_bf16 v[118:121], v[166:169], v[190:193], v[118:121]
	v_mfma_f32_16x16x32_bf16 v[114:117], v[174:177], v[190:193], v[114:117]
	v_mfma_f32_16x16x32_bf16 v[102:105], v[166:169], v[198:201], v[102:105]
	v_mfma_f32_16x16x32_bf16 v[98:101], v[174:177], v[198:201], v[98:101]
	v_mfma_f32_16x16x32_bf16 v[86:89], v[166:169], v[206:209], v[86:89]
	v_mfma_f32_16x16x32_bf16 v[82:85], v[174:177], v[206:209], v[82:85]
	v_mfma_f32_16x16x32_bf16 v[126:129], v[170:173], v[186:189], v[126:129]
	v_mfma_f32_16x16x32_bf16 v[122:125], v[178:181], v[186:189], v[122:125]
	v_mfma_f32_16x16x32_bf16 v[118:121], v[170:173], v[194:197], v[118:121]
	v_mfma_f32_16x16x32_bf16 v[114:117], v[178:181], v[194:197], v[114:117]
	v_mfma_f32_16x16x32_bf16 v[102:105], v[170:173], v[202:205], v[102:105]
	v_mfma_f32_16x16x32_bf16 v[98:101], v[178:181], v[202:205], v[98:101]
	v_mfma_f32_16x16x32_bf16 v[86:89], v[170:173], v[210:213], v[86:89]
	v_mfma_f32_16x16x32_bf16 v[82:85], v[178:181], v[210:213], v[82:85]
	s_setprio 0
	s_barrier
	s_mov_b32 m0, s46
	v_lshl_add_u64 v[232:233], v[232:233], 0, s[16:17]
	ds_read_b128 v[214:217], v152
	ds_read_b128 v[218:221], v153
	ds_read_b128 v[224:227], v160
	ds_read_b128 v[228:231], v161
	global_load_lds_dwordx4 v[232:233], off
	v_lshl_add_u64 v[232:233], v[234:235], 0, s[16:17]
	s_mov_b32 m0, s47
	s_nop 0
	global_load_lds_dwordx4 v[232:233], off
	s_barrier
	s_waitcnt lgkmcnt(0)
	s_setprio 1
	v_mfma_f32_16x16x32_bf16 v[110:113], v[214:217], v[182:185], v[110:113]
	v_mfma_f32_16x16x32_bf16 v[106:109], v[224:227], v[182:185], v[106:109]
	v_mfma_f32_16x16x32_bf16 v[94:97], v[214:217], v[190:193], v[94:97]
	v_mfma_f32_16x16x32_bf16 v[90:93], v[224:227], v[190:193], v[90:93]
	v_mfma_f32_16x16x32_bf16 v[78:81], v[214:217], v[198:201], v[78:81]
	v_mfma_f32_16x16x32_bf16 v[74:77], v[224:227], v[198:201], v[74:77]
	v_mfma_f32_16x16x32_bf16 v[70:73], v[214:217], v[206:209], v[70:73]
	v_mfma_f32_16x16x32_bf16 v[66:69], v[224:227], v[206:209], v[66:69]
	v_mfma_f32_16x16x32_bf16 v[110:113], v[218:221], v[186:189], v[110:113]
	v_mfma_f32_16x16x32_bf16 v[106:109], v[228:231], v[186:189], v[106:109]
	v_mfma_f32_16x16x32_bf16 v[94:97], v[218:221], v[194:197], v[94:97]
	v_mfma_f32_16x16x32_bf16 v[90:93], v[228:231], v[194:197], v[90:93]
	v_mfma_f32_16x16x32_bf16 v[78:81], v[218:221], v[202:205], v[78:81]
	v_mfma_f32_16x16x32_bf16 v[74:77], v[228:231], v[202:205], v[74:77]
	v_mfma_f32_16x16x32_bf16 v[70:73], v[218:221], v[210:213], v[70:73]
	v_mfma_f32_16x16x32_bf16 v[66:69], v[228:231], v[210:213], v[66:69]
	s_setprio 0
	s_mov_b32 m0, s52
	v_lshl_add_u64 v[232:233], v[236:237], 0, s[16:17]
	s_barrier
	ds_read_b128 v[182:185], v163 offset:49152
	ds_read_b128 v[186:189], v163 offset:50176
	ds_read_b128 v[190:193], v163 offset:51200
	ds_read_b128 v[194:197], v163 offset:52224
	ds_read_b128 v[198:201], v163 offset:53248
	ds_read_b128 v[202:205], v163 offset:54272
	ds_read_b128 v[206:209], v163 offset:55296
	ds_read_b128 v[210:213], v163 offset:56320
	global_load_lds_dwordx4 v[232:233], off
	v_lshl_add_u64 v[232:233], v[238:239], 0, s[16:17]
	s_mov_b32 m0, s53
	s_nop 0
	global_load_lds_dwordx4 v[232:233], off
	s_barrier
; DEV CParams* launder(CParams* p) { asm volatile("" : "+s"(p)); return p; }
; #define G_STAGE(bufoff, gbase, voff) do { _Pragma("unroll") for (int _i = 0; _i < 2; ++_i) \
;     __builtin_amdgcn_global_load_lds((const unsigned*)((const char*)(gbase) + (voff)[_i]), (LAS unsigned*)(lds + (bufoff) + ldsw + _i * 8192), 16, 0, 0); } while (0)
; #define WAIT_V(n) asm volatile("s_waitcnt vmcnt(" #n ")" ::: "memory")
; #define WAIT_L(n) asm volatile("s_waitcnt lgkmcnt(" #n ")" ::: "memory")
; #define BAR __builtin_amdgcn_s_barrier()
; #define SCHED __builtin_amdgcn_sched_barrier(0)
; DEV void st_bf16x8(bf16_t* p, f32x4 a, f32x4 b) { u32x4 o; o.x = cvt_pk_bf16(a[0], a[1]); o.y = cvt_pk_bf16(a[2], a[3]); o.z = cvt_pk_bf16(b[0], b[1]); o.w = cvt_pk_bf16(b[2], b[3]); *(u32x4*)p = o; }
;   DEV void bias_dma(const Unit& u, LAS float* tabw) const { __builtin_amdgcn_global_load_lds((const unsigned*)bias_src(u, ltid() & 255), (LAS unsigned*)tabw, 4, 0, 0); }
;   DEV void bias_dma(const Unit& u, LAS float* tabw) const { __builtin_amdgcn_global_load_lds((const unsigned*)bias_src(u, ltid() & 255), (LAS unsigned*)tabw, 4, 0, 0); }
; template <class P>
; DEV void gemm_stream(const P& pol) {
;     ...
;       BAR; WAIT_L(0); G_MMA(1, 0, At, B0); BAR; SCHED;
;       G_STAGE(G_SB(1, 1), b2 + hstep + kstep, voffB);
;       WAIT_V(6); BAR; G_MMA(1, 1, At, B1); BAR;
;       if (P::HASBIAS && has_next && t == 0) pol.bias_dma(nxt, btab + ((ui + 1) & 1) * 256 + ((wid & 3) << 6));
;       if (P::GATHER && has_next && t == 0) pol.arow_dma(nxt, arow + ((ui + 1) & 1) * 256 + ((wid & 3) << 6));
;     }
;   DEV void operator()(const AccT& acc, int wr, int wc, int fr, int fq) const {
;     CParams& P = *launder(p); const int row0 = pm * BM + wr * 64 + fr;
; #pragma unroll
;     for (int ai = 0; ai < 2; ++ai)
; #pragma unroll
;       for (int m = 0; m < 4; ++m) {
;         const int row = row0 + ai * HALF + m * 16, b = row >> 12, t = row & 4095;
; #pragma unroll
;         for (int bj = 0; bj < 2; ++bj) {
;           const int col = pn * 256 + bj * HALF + wc * 32 + 8 * fq, hh = col / QK, e = col - hh * QK;
;           st_bf16x8(P.qf + ((long)(b * NH + hh) * SEQ + t) * QK + e, acc[ai][bj][m][0], acc[ai][bj][m][1]);
;         }
;       }
;   }
	s_waitcnt lgkmcnt(0)
	s_setprio 1
	v_mfma_f32_16x16x32_bf16 v[62:65], v[166:169], v[182:185], v[62:65]
	v_mfma_f32_16x16x32_bf16 v[58:61], v[174:177], v[182:185], v[58:61]
	v_mfma_f32_16x16x32_bf16 v[54:57], v[166:169], v[190:193], v[54:57]
	v_mfma_f32_16x16x32_bf16 v[50:53], v[174:177], v[190:193], v[50:53]
	v_mfma_f32_16x16x32_bf16 v[38:41], v[166:169], v[198:201], v[38:41]
	v_mfma_f32_16x16x32_bf16 v[34:37], v[174:177], v[198:201], v[34:37]
	v_mfma_f32_16x16x32_bf16 v[22:25], v[166:169], v[206:209], v[22:25]
	v_mfma_f32_16x16x32_bf16 v[18:21], v[174:177], v[206:209], v[18:21]
	v_mfma_f32_16x16x32_bf16 v[62:65], v[170:173], v[186:189], v[62:65]
	v_mfma_f32_16x16x32_bf16 v[58:61], v[178:181], v[186:189], v[58:61]
	v_mfma_f32_16x16x32_bf16 v[54:57], v[170:173], v[194:197], v[54:57]
	v_mfma_f32_16x16x32_bf16 v[50:53], v[178:181], v[194:197], v[50:53]
	v_mfma_f32_16x16x32_bf16 v[38:41], v[170:173], v[202:205], v[38:41]
	v_mfma_f32_16x16x32_bf16 v[34:37], v[178:181], v[202:205], v[34:37]
	v_mfma_f32_16x16x32_bf16 v[22:25], v[170:173], v[210:213], v[22:25]
	v_mfma_f32_16x16x32_bf16 v[18:21], v[178:181], v[210:213], v[18:21]
	s_setprio 0
	s_barrier
	s_add_u32 s26, s26, 0x20080
	s_addc_u32 s27, s27, 0
	s_mov_b32 m0, s54
	v_lshl_add_u64 v[166:167], s[26:27], 0, v[130:131]
	global_load_lds_dwordx4 v[166:167], off
	v_lshl_add_u64 v[166:167], s[26:27], 0, v[132:133]
	s_mov_b32 m0, s55
	s_nop 0
	global_load_lds_dwordx4 v[166:167], off
	s_waitcnt vmcnt(6)
	s_barrier
	s_setprio 1
	v_mfma_f32_16x16x32_bf16 v[46:49], v[214:217], v[182:185], v[46:49]
	v_mfma_f32_16x16x32_bf16 v[42:45], v[224:227], v[182:185], v[42:45]
	v_mfma_f32_16x16x32_bf16 v[30:33], v[214:217], v[190:193], v[30:33]
	v_mfma_f32_16x16x32_bf16 v[26:29], v[224:227], v[190:193], v[26:29]
	v_mfma_f32_16x16x32_bf16 v[14:17], v[214:217], v[198:201], v[14:17]
	v_mfma_f32_16x16x32_bf16 v[10:13], v[224:227], v[198:201], v[10:13]
	v_mfma_f32_16x16x32_bf16 v[6:9], v[214:217], v[206:209], v[6:9]
	v_mfma_f32_16x16x32_bf16 v[2:5], v[224:227], v[206:209], v[2:5]
	v_mfma_f32_16x16x32_bf16 v[46:49], v[218:221], v[186:189], v[46:49]
	v_mfma_f32_16x16x32_bf16 v[42:45], v[228:231], v[186:189], v[42:45]
	v_mfma_f32_16x16x32_bf16 v[30:33], v[218:221], v[194:197], v[30:33]
	v_mfma_f32_16x16x32_bf16 v[26:29], v[228:231], v[194:197], v[26:29]
	v_mfma_f32_16x16x32_bf16 v[14:17], v[218:221], v[202:205], v[14:17]
	v_mfma_f32_16x16x32_bf16 v[10:13], v[228:231], v[202:205], v[10:13]
	v_mfma_f32_16x16x32_bf16 v[6:9], v[218:221], v[210:213], v[6:9]
	v_mfma_f32_16x16x32_bf16 v[2:5], v[228:231], v[210:213], v[2:5]
	s_setprio 0
	s_add_i32 s77, s77, 2
	s_add_u32 s24, s24, 0x100
	s_addc_u32 s25, s25, 0
	s_cmp_gt_u32 s77, 5
	s_barrier
	s_cbranch_scc0 .LBB0_506
	s_mov_b64 s[22:23], s[4:5]
	s_lshl_b32 s24, s57, 8
	v_lshl_or_b32 v144, s56, 8, v162
	s_add_i32 s24, s24, s45
	v_mul_hi_i32 v142, v144, s59
	v_or_b32_e32 v145, s24, v1
	s_load_dwordx2 s[22:23], s[22:23], 0x170
	v_bitop3_b32 v165, s24, v164, v1 bitop3:0xc8
	s_ashr_i32 s24, s24, 9
	v_lshrrev_b32_e32 v143, 31, v142
	v_ashrrev_i32_e32 v142, 5, v142
	s_and_b32 s26, s24, -8
	v_add_u32_e32 v172, v142, v143
	v_add_u32_e32 v142, s26, v172
	v_ashrrev_i32_e32 v143, 31, v142
	v_mad_u64_u32 v[166:167], s[24:25], v172, s60, v[144:145]
	v_lshlrev_b64 v[168:169], 12, v[142:143]
	v_or_b32_e32 v167, v168, v165
	s_waitcnt lgkmcnt(0)
; DEV CParams* launder(CParams* p) { asm volatile("" : "+s"(p)); return p; }
; DEV void st_bf16x8(bf16_t* p, f32x4 a, f32x4 b) { u32x4 o; o.x = cvt_pk_bf16(a[0], a[1]); o.y = cvt_pk_bf16(a[2], a[3]); o.z = cvt_pk_bf16(b[0], b[1]); o.w = cvt_pk_bf16(b[2], b[3]); *(u32x4*)p = o; }
;   DEV void operator()(const AccT& acc, int wr, int wc, int fr, int fq) const {
;     CParams& P = *launder(p); const int row0 = pm * BM + wr * 64 + fr;
; #pragma unroll
;     for (int ai = 0; ai < 2; ++ai)
; #pragma unroll
;       for (int m = 0; m < 4; ++m) {
;         const int row = row0 + ai * HALF + m * 16, b = row >> 12, t = row & 4095;
; #pragma unroll
;         for (int bj = 0; bj < 2; ++bj) {
;           const int col = pn * 256 + bj * HALF + wc * 32 + 8 * fq, hh = col / QK, e = col - hh * QK;
;           st_bf16x8(P.qf + ((long)(b * NH + hh) * SEQ + t) * QK + e, acc[ai][bj][m][0], acc[ai][bj][m][1]);
;         }
;       }
;   }
	v_mov_b64_e32 v[142:143], s[22:23]
	v_mad_u64_u32 v[170:171], s[22:23], v167, s58, v[142:143]
	v_ashrrev_i32_e32 v167, 31, v166
	v_cvt_pk_bf16_f32 v126, v126, v127
	v_cvt_pk_bf16_f32 v127, v128, v129
	v_cvt_pk_bf16_f32 v128, v122, v123
	v_or_b32_e32 v122, 0x80, v144
	v_mad_i32_i24 v171, v169, s58, v171
	v_lshlrev_b64 v[166:167], 1, v[166:167]
	v_mul_hi_i32 v123, v122, s59
	v_lshl_add_u64 v[170:171], v[170:171], 0, v[166:167]
	v_cvt_pk_bf16_f32 v129, v124, v125
	v_lshrrev_b32_e32 v124, 31, v123
	v_ashrrev_i32_e32 v123, 5, v123
	global_store_dwordx4 v[170:171], v[126:129], off
	v_cvt_pk_bf16_f32 v110, v110, v111
	v_cvt_pk_bf16_f32 v111, v112, v113
	v_add_u32_e32 v128, v123, v124
	v_add_u32_e32 v124, s26, v128
	v_ashrrev_i32_e32 v125, 31, v124
	v_mad_u64_u32 v[122:123], s[22:23], v128, s60, v[122:123]
	v_lshlrev_b64 v[124:125], 12, v[124:125]
	v_or_b32_e32 v123, v124, v165
	v_mad_u64_u32 v[126:127], s[22:23], v123, s58, v[142:143]
	v_ashrrev_i32_e32 v123, 31, v122
	v_mad_i32_i24 v127, v125, s58, v127
	v_lshlrev_b64 v[122:123], 1, v[122:123]
	v_lshl_add_u64 v[126:127], v[126:127], 0, v[122:123]
	v_cvt_pk_bf16_f32 v112, v106, v107
	v_cvt_pk_bf16_f32 v113, v108, v109
	global_store_dwordx4 v[126:127], v[110:113], off
	v_cvt_pk_bf16_f32 v108, v114, v115
	v_cvt_pk_bf16_f32 v109, v116, v117
	v_or_b32_e32 v112, 16, v165
	v_or_b32_e32 v106, v168, v112
	v_mad_u64_u32 v[106:107], s[22:23], v106, s58, v[142:143]
	v_mad_i32_i24 v107, v169, s58, v107
	v_lshl_add_u64 v[110:111], v[106:107], 0, v[166:167]
	v_cvt_pk_bf16_f32 v106, v118, v119
	v_cvt_pk_bf16_f32 v107, v120, v121
	global_store_dwordx4 v[110:111], v[106:109], off
	v_cvt_pk_bf16_f32 v94, v94, v95
	v_cvt_pk_bf16_f32 v95, v96, v97
	v_or_b32_e32 v106, v124, v112
	v_mad_u64_u32 v[106:107], s[22:23], v106, s58, v[142:143]
	v_mad_i32_i24 v107, v125, s58, v107
	v_lshl_add_u64 v[106:107], v[106:107], 0, v[122:123]
	v_cvt_pk_bf16_f32 v96, v90, v91
	v_cvt_pk_bf16_f32 v97, v92, v93
	global_store_dwordx4 v[106:107], v[94:97], off
	v_cvt_pk_bf16_f32 v92, v98, v99
	v_cvt_pk_bf16_f32 v93, v100, v101
	v_or_b32_e32 v96, 32, v165
	v_or_b32_e32 v90, v168, v96
	v_mad_u64_u32 v[90:91], s[22:23], v90, s58, v[142:143]
	v_mad_i32_i24 v91, v169, s58, v91
	v_lshl_add_u64 v[94:95], v[90:91], 0, v[166:167]
	v_cvt_pk_bf16_f32 v90, v102, v103
	v_cvt_pk_bf16_f32 v91, v104, v105
	global_store_dwordx4 v[94:95], v[90:93], off
	v_cvt_pk_bf16_f32 v78, v78, v79
	v_cvt_pk_bf16_f32 v79, v80, v81
	v_or_b32_e32 v90, v124, v96
	v_mad_u64_u32 v[90:91], s[22:23], v90, s58, v[142:143]
	v_mad_i32_i24 v91, v125, s58, v91
	v_lshl_add_u64 v[90:91], v[90:91], 0, v[122:123]
	v_cvt_pk_bf16_f32 v80, v74, v75
	v_cvt_pk_bf16_f32 v81, v76, v77
	global_store_dwordx4 v[90:91], v[78:81], off
	v_cvt_pk_bf16_f32 v76, v82, v83
	v_cvt_pk_bf16_f32 v77, v84, v85
	v_or_b32_e32 v80, 48, v165
	v_or_b32_e32 v74, v168, v80
	v_mad_u64_u32 v[74:75], s[22:23], v74, s58, v[142:143]
	v_mad_i32_i24 v75, v169, s58, v75
	v_lshl_add_u64 v[78:79], v[74:75], 0, v[166:167]
	v_cvt_pk_bf16_f32 v74, v86, v87
	v_cvt_pk_bf16_f32 v75, v88, v89
	global_store_dwordx4 v[78:79], v[74:77], off
	v_cvt_pk_bf16_f32 v70, v70, v71
	v_cvt_pk_bf16_f32 v71, v72, v73
	v_or_b32_e32 v74, v124, v80
	v_mad_u64_u32 v[74:75], s[22:23], v74, s58, v[142:143]
	v_mad_i32_i24 v75, v125, s58, v75
	v_lshl_add_u64 v[74:75], v[74:75], 0, v[122:123]
	v_cvt_pk_bf16_f32 v72, v66, v67
	v_cvt_pk_bf16_f32 v73, v68, v69
	v_add_u32_e32 v66, 0x80, v145
	global_store_dwordx4 v[74:75], v[70:73], off
	v_cvt_pk_bf16_f32 v62, v62, v63
	v_cvt_pk_bf16_f32 v63, v64, v65
	v_and_b32_e32 v70, 0xfcf, v66
	v_ashrrev_i32_e32 v66, 9, v66
	v_and_b32_e32 v71, -8, v66
	v_add_u32_e32 v66, v71, v172
	v_cvt_pk_bf16_f32 v64, v58, v59
	v_add_u32_e32 v58, v128, v71
	v_ashrrev_i32_e32 v67, 31, v66
	v_ashrrev_i32_e32 v59, 31, v58
	v_lshlrev_b64 v[66:67], 12, v[66:67]
	v_lshlrev_b64 v[58:59], 12, v[58:59]
	v_or_b32_e32 v68, v66, v70
	v_cvt_pk_bf16_f32 v65, v60, v61
	v_or_b32_e32 v60, v58, v70
	v_mad_u64_u32 v[68:69], s[22:23], v68, s58, v[142:143]
	v_mad_u64_u32 v[60:61], s[22:23], v60, s58, v[142:143]
	v_mad_i32_i24 v69, v67, s58, v69
	v_mad_i32_i24 v61, v59, s58, v61
	v_lshl_add_u64 v[68:69], v[68:69], 0, v[166:167]
	v_lshl_add_u64 v[60:61], v[60:61], 0, v[122:123]
	v_cvt_pk_bf16_f32 v46, v46, v47
	v_cvt_pk_bf16_f32 v47, v48, v49
	v_cvt_pk_bf16_f32 v48, v42, v43
	v_cvt_pk_bf16_f32 v49, v44, v45
	global_store_dwordx4 v[68:69], v[62:65], off
	global_store_dwordx4 v[60:61], v[46:49], off
	v_cvt_pk_bf16_f32 v44, v50, v51
	v_cvt_pk_bf16_f32 v45, v52, v53
	v_or_b32_e32 v48, 16, v70
	v_or_b32_e32 v42, v66, v48
	v_mad_u64_u32 v[42:43], s[22:23], v42, s58, v[142:143]
	v_mad_i32_i24 v43, v67, s58, v43
	v_lshl_add_u64 v[46:47], v[42:43], 0, v[166:167]
	v_cvt_pk_bf16_f32 v42, v54, v55
	v_cvt_pk_bf16_f32 v43, v56, v57
	global_store_dwordx4 v[46:47], v[42:45], off
	v_cvt_pk_bf16_f32 v30, v30, v31
	v_cvt_pk_bf16_f32 v31, v32, v33
	v_or_b32_e32 v42, v58, v48
	v_mad_u64_u32 v[42:43], s[22:23], v42, s58, v[142:143]
	v_mad_i32_i24 v43, v59, s58, v43
	v_lshl_add_u64 v[42:43], v[42:43], 0, v[122:123]
	v_cvt_pk_bf16_f32 v32, v26, v27
	v_cvt_pk_bf16_f32 v33, v28, v29
	global_store_dwordx4 v[42:43], v[30:33], off
	v_cvt_pk_bf16_f32 v28, v34, v35
	v_cvt_pk_bf16_f32 v29, v36, v37
	v_or_b32_e32 v32, 32, v70
	v_or_b32_e32 v26, v66, v32
	v_mad_u64_u32 v[26:27], s[22:23], v26, s58, v[142:143]
	v_mad_i32_i24 v27, v67, s58, v27
	v_lshl_add_u64 v[30:31], v[26:27], 0, v[166:167]
	v_cvt_pk_bf16_f32 v26, v38, v39
	v_cvt_pk_bf16_f32 v27, v40, v41
	global_store_dwordx4 v[30:31], v[26:29], off
	v_cvt_pk_bf16_f32 v14, v14, v15
	v_cvt_pk_bf16_f32 v15, v16, v17
	v_or_b32_e32 v26, v58, v32
	v_mad_u64_u32 v[26:27], s[22:23], v26, s58, v[142:143]
	v_mad_i32_i24 v27, v59, s58, v27
	v_lshl_add_u64 v[26:27], v[26:27], 0, v[122:123]
	v_cvt_pk_bf16_f32 v16, v10, v11
	v_cvt_pk_bf16_f32 v17, v12, v13
	global_store_dwordx4 v[26:27], v[14:17], off
	v_cvt_pk_bf16_f32 v12, v18, v19
	v_cvt_pk_bf16_f32 v13, v20, v21
	v_or_b32_e32 v16, 48, v70
	v_or_b32_e32 v10, v66, v16
	v_mad_u64_u32 v[10:11], s[22:23], v10, s58, v[142:143]
	v_mad_i32_i24 v11, v67, s58, v11
	v_lshl_add_u64 v[14:15], v[10:11], 0, v[166:167]
	v_cvt_pk_bf16_f32 v10, v22, v23
	v_cvt_pk_bf16_f32 v11, v24, v25
	global_store_dwordx4 v[14:15], v[10:13], off
	v_cvt_pk_bf16_f32 v6, v6, v7
	v_cvt_pk_bf16_f32 v7, v8, v9
	v_or_b32_e32 v10, v58, v16
	v_mad_u64_u32 v[10:11], s[22:23], v10, s58, v[142:143]
	v_mad_i32_i24 v11, v59, s58, v11
	v_lshl_add_u64 v[10:11], v[10:11], 0, v[122:123]
	v_cvt_pk_bf16_f32 v8, v2, v3
	v_cvt_pk_bf16_f32 v9, v4, v5
	s_and_b64 vcc, exec, s[18:19]
	s_mov_b32 s57, s64
	s_mov_b32 s56, s63
	s_mov_b64 s[22:23], s[20:21]
	global_store_dwordx4 v[10:11], v[6:9], off
	s_cbranch_vccz .LBB0_505
	s_waitcnt vmcnt(0)
	s_cmpk_gt_u32 s3, 0xff
	s_cbranch_scc1 .LBB0_510
	s_barrier

; #define LAS __attribute__((address_space(3)))
; #define G_GATHER_OFFS(tab_, rv_) do { _Pragma("unroll") for (int i = 0; i < 2; ++i) { int R_, C_; G_SRC(i, R_, C_); const int ra_ = (tab_)[R_], rb_ = (tab_)[HALF + R_];        \
;     vAc[0][i] = (unsigned)((R_ < (rv_) ? ra_ : 0) * KB + C_); vAc[1][i] = (unsigned)((HALF + R_ < (rv_) ? rb_ : 0) * KB + C_); } } while (0)
; #define G_STAGE(bufoff, gbase, voff) do { _Pragma("unroll") for (int _i = 0; _i < 2; ++_i) \
;     __builtin_amdgcn_global_load_lds((const unsigned*)((const char*)(gbase) + (voff)[_i]), (LAS unsigned*)(lds + (bufoff) + ldsw + _i * 8192), 16, 0, 0); } while (0)
; #define G_LDA(dst, b, h) do { _Pragma("unroll") for (int m = 0; m < 4; ++m) dst[m] = G_LD2(G_SA(b, h) + aoff + m * 2048, G_SA(b, h) + (P::FP8 ? aoff1 : aoff + 1024) + m * 2048); } while (0)
; #define G_LDB(dst, b, h) do { _Pragma("unroll") for (int n = 0; n < 2; ++n) dst[n] = G_LD2(G_SB(b, h) + boff + n * 2048, G_SB(b, h) + (P::FP8 ? boff1 : boff + 1024) + n * 2048); } while (0)
; #define WAIT_V(n) asm volatile("s_waitcnt vmcnt(" #n ")" ::: "memory")
; #define WAIT_L(n) asm volatile("s_waitcnt lgkmcnt(" #n ")" ::: "memory")
; #define BAR __builtin_amdgcn_s_barrier()
; #define SCHED __builtin_amdgcn_sched_barrier(0)
; template <class P>
; DEV void gemm_stream(const P& pol) {
;     ...
;     for (int t = 0; t < nt; t += 2) {
;       const bool last = (t == nt - 2);
;       const size_t k1 = (size_t)(t + 1) * kstep, k2 = (size_t)(t + 2) * kstep;
;       const char* a20 = last ? nA0 : cA0 + k2; const char* a21 = last ? nA1 : cA1 + k2; const char* b2 = last ? nB : cB + k2;
;       G_LDB(B0, 0, 0); SCHED; G_LDA(At, 0, 0); G_STAGE(G_SA(1, 1), cA1 + k1, vAc[1]);
;       WAIT_L(8); BAR; WAIT_L(0); G_MMA(0, 0, At, B0); BAR; SCHED;
;       if (P::GATHER && last && has_next) { LAS int* tab = arow + ((ui + 1) & 1) * 256; G_GATHER_OFFS(tab, nxt.rv); }
;       G_LDB(B1, 0, 1); G_STAGE(G_SB(0, 0), b2, voffB);
;       BAR; WAIT_L(0); G_MMA(0, 1, At, B1); BAR;
;       G_LDA(At, 0, 1); G_STAGE(G_SA(0, 0), a20, vAc[0]);
;       BAR; WAIT_L(0); G_MMA(1, 0, At, B0); BAR; SCHED;
;       G_STAGE(G_SB(0, 1), b2 + hstep, voffB);
;       WAIT_V(6); BAR; G_MMA(1, 1, At, B1); BAR;
.LBB0_521:
	s_add_u32 s35, s24, s34
	s_addc_u32 s36, s25, 0
	s_add_u32 s37, s35, 0x100
	s_addc_u32 s36, s36, 0
	s_add_u32 s46, s26, s34
	s_addc_u32 s47, s27, 0
	s_add_u32 s38, s46, 0x100
	s_addc_u32 s39, s47, 0
	s_add_u32 s34, s22, s34
	s_addc_u32 s35, s23, 0
	s_add_u32 s44, s34, 0x100
	s_addc_u32 s45, s35, 0
	s_and_b64 s[34:35], s[30:31], exec
	ds_read_b128 v[142:145], v146
	ds_read_b128 v[168:171], v147
	ds_read_b128 v[172:175], v158
	ds_read_b128 v[176:179], v159
	s_cselect_b32 s34, s86, s38
	s_cselect_b32 s35, s85, s39
	s_cselect_b32 s38, s84, s37
	s_cselect_b32 s39, s83, s36
	s_add_i32 m0, s55, 0xc000
	s_add_i32 s89, s55, 0xe000
	s_and_b64 s[30:31], s[30:31], exec
	s_cselect_b32 s44, s88, s44
	s_cselect_b32 s45, s87, s45
	s_add_u32 s30, s44, 0x10000
	s_addc_u32 s31, s45, 0
	s_add_u32 s36, s44, 0x10080
	s_addc_u32 s37, s45, 0
	v_lshl_add_u64 v[212:213], s[46:47], 0, v[134:135]
	v_lshl_add_u64 v[212:213], v[212:213], 0, s[12:13]
	ds_read_b128 v[180:183], v166
	ds_read_b128 v[184:187], v166 offset:1024
	ds_read_b128 v[188:191], v166 offset:2048
	ds_read_b128 v[192:195], v166 offset:3072
	ds_read_b128 v[196:199], v166 offset:4096
	ds_read_b128 v[200:203], v166 offset:5120
	ds_read_b128 v[204:207], v166 offset:6144
	ds_read_b128 v[208:211], v166 offset:7168
	global_load_lds_dwordx4 v[212:213], off
	v_lshl_add_u64 v[212:213], s[46:47], 0, v[136:137]
	v_lshl_add_u64 v[212:213], v[212:213], 0, s[12:13]
	s_mov_b32 m0, s89
	s_nop 0
	global_load_lds_dwordx4 v[212:213], off
	s_waitcnt lgkmcnt(8)
	s_barrier
	s_waitcnt lgkmcnt(0)
	s_setprio 1
	v_mfma_f32_16x16x32_bf16 v[126:129], v[142:145], v[180:183], v[126:129]
	v_mfma_f32_16x16x32_bf16 v[122:125], v[172:175], v[180:183], v[122:125]
	v_mfma_f32_16x16x32_bf16 v[110:113], v[142:145], v[188:191], v[110:113]
	v_mfma_f32_16x16x32_bf16 v[106:109], v[172:175], v[188:191], v[106:109]
	v_mfma_f32_16x16x32_bf16 v[94:97], v[142:145], v[196:199], v[94:97]
	v_mfma_f32_16x16x32_bf16 v[90:93], v[172:175], v[196:199], v[90:93]
	v_mfma_f32_16x16x32_bf16 v[78:81], v[142:145], v[204:207], v[78:81]
	v_mfma_f32_16x16x32_bf16 v[74:77], v[172:175], v[204:207], v[74:77]
	v_mfma_f32_16x16x32_bf16 v[126:129], v[168:171], v[184:187], v[126:129]
	v_mfma_f32_16x16x32_bf16 v[122:125], v[176:179], v[184:187], v[122:125]
	v_mfma_f32_16x16x32_bf16 v[110:113], v[168:171], v[192:195], v[110:113]
	v_mfma_f32_16x16x32_bf16 v[106:109], v[176:179], v[192:195], v[106:109]
	v_mfma_f32_16x16x32_bf16 v[94:97], v[168:171], v[200:203], v[94:97]
	v_mfma_f32_16x16x32_bf16 v[90:93], v[176:179], v[200:203], v[90:93]
	v_mfma_f32_16x16x32_bf16 v[78:81], v[168:171], v[208:211], v[78:81]
	v_mfma_f32_16x16x32_bf16 v[74:77], v[176:179], v[208:211], v[74:77]
	s_setprio 0
	s_barrier
	s_mov_b32 m0, s56
	v_lshl_add_u64 v[220:221], s[44:45], 0, v[130:131]
	ds_read_b128 v[212:215], v148
	ds_read_b128 v[216:219], v149
	ds_read_b128 v[224:227], v160
	ds_read_b128 v[228:231], v161
	global_load_lds_dwordx4 v[220:221], off
	v_lshl_add_u64 v[232:233], s[44:45], 0, v[132:133]
	s_mov_b32 m0, s57
	s_nop 0
	global_load_lds_dwordx4 v[232:233], off
	s_barrier
	s_waitcnt lgkmcnt(0)
	s_setprio 1
	v_mfma_f32_16x16x32_bf16 v[118:121], v[212:215], v[180:183], v[118:121]
	v_mfma_f32_16x16x32_bf16 v[114:117], v[224:227], v[180:183], v[114:117]
	v_mfma_f32_16x16x32_bf16 v[102:105], v[212:215], v[188:191], v[102:105]
	v_mfma_f32_16x16x32_bf16 v[98:101], v[224:227], v[188:191], v[98:101]
	v_mfma_f32_16x16x32_bf16 v[86:89], v[212:215], v[196:199], v[86:89]
	v_mfma_f32_16x16x32_bf16 v[82:85], v[224:227], v[196:199], v[82:85]
	v_mfma_f32_16x16x32_bf16 v[70:73], v[212:215], v[204:207], v[70:73]
	v_mfma_f32_16x16x32_bf16 v[66:69], v[224:227], v[204:207], v[66:69]
	v_mfma_f32_16x16x32_bf16 v[118:121], v[216:219], v[184:187], v[118:121]
	v_mfma_f32_16x16x32_bf16 v[114:117], v[228:231], v[184:187], v[114:117]
	v_mfma_f32_16x16x32_bf16 v[102:105], v[216:219], v[192:195], v[102:105]
	v_mfma_f32_16x16x32_bf16 v[98:101], v[228:231], v[192:195], v[98:101]
	v_mfma_f32_16x16x32_bf16 v[86:89], v[216:219], v[200:203], v[86:89]
	v_mfma_f32_16x16x32_bf16 v[82:85], v[228:231], v[200:203], v[82:85]
	v_mfma_f32_16x16x32_bf16 v[70:73], v[216:219], v[208:211], v[70:73]
	v_mfma_f32_16x16x32_bf16 v[66:69], v[228:231], v[208:211], v[66:69]
	s_setprio 0
	s_mov_b32 m0, s55
	v_lshl_add_u64 v[234:235], s[38:39], 0, v[134:135]
	s_barrier
	ds_read_b128 v[180:183], v166 offset:16384
	ds_read_b128 v[184:187], v166 offset:17408
	ds_read_b128 v[188:191], v166 offset:18432
	ds_read_b128 v[192:195], v166 offset:19456
	ds_read_b128 v[196:199], v166 offset:20480
	ds_read_b128 v[200:203], v166 offset:21504
	ds_read_b128 v[204:207], v166 offset:22528
	ds_read_b128 v[208:211], v166 offset:23552
	global_load_lds_dwordx4 v[234:235], off
	v_lshl_add_u64 v[236:237], s[38:39], 0, v[136:137]
	s_mov_b32 m0, s58
	s_nop 0
	global_load_lds_dwordx4 v[236:237], off
	s_barrier
	s_waitcnt lgkmcnt(0)
	s_setprio 1
	v_mfma_f32_16x16x32_bf16 v[62:65], v[142:145], v[180:183], v[62:65]
	v_mfma_f32_16x16x32_bf16 v[58:61], v[172:175], v[180:183], v[58:61]
	v_mfma_f32_16x16x32_bf16 v[50:53], v[142:145], v[188:191], v[50:53]
	v_mfma_f32_16x16x32_bf16 v[42:45], v[172:175], v[188:191], v[42:45]
	v_mfma_f32_16x16x32_bf16 v[34:37], v[142:145], v[196:199], v[34:37]
	v_mfma_f32_16x16x32_bf16 v[26:29], v[172:175], v[196:199], v[26:29]
	v_mfma_f32_16x16x32_bf16 v[18:21], v[142:145], v[204:207], v[18:21]
	v_mfma_f32_16x16x32_bf16 v[10:13], v[172:175], v[204:207], v[10:13]
	v_mfma_f32_16x16x32_bf16 v[62:65], v[168:171], v[184:187], v[62:65]
	v_mfma_f32_16x16x32_bf16 v[58:61], v[176:179], v[184:187], v[58:61]
	v_mfma_f32_16x16x32_bf16 v[50:53], v[168:171], v[192:195], v[50:53]
	v_mfma_f32_16x16x32_bf16 v[42:45], v[176:179], v[192:195], v[42:45]
	v_mfma_f32_16x16x32_bf16 v[34:37], v[168:171], v[200:203], v[34:37]
	v_mfma_f32_16x16x32_bf16 v[26:29], v[176:179], v[200:203], v[26:29]
	v_mfma_f32_16x16x32_bf16 v[18:21], v[168:171], v[208:211], v[18:21]
	v_mfma_f32_16x16x32_bf16 v[10:13], v[176:179], v[208:211], v[10:13]
	s_setprio 0
	s_barrier
; #define LAS __attribute__((address_space(3)))
; #define G_GATHER_OFFS(tab_, rv_) do { _Pragma("unroll") for (int i = 0; i < 2; ++i) { int R_, C_; G_SRC(i, R_, C_); const int ra_ = (tab_)[R_], rb_ = (tab_)[HALF + R_];        \
;     vAc[0][i] = (unsigned)((R_ < (rv_) ? ra_ : 0) * KB + C_); vAc[1][i] = (unsigned)((HALF + R_ < (rv_) ? rb_ : 0) * KB + C_); } } while (0)
; #define G_STAGE(bufoff, gbase, voff) do { _Pragma("unroll") for (int _i = 0; _i < 2; ++_i) \
;     __builtin_amdgcn_global_load_lds((const unsigned*)((const char*)(gbase) + (voff)[_i]), (LAS unsigned*)(lds + (bufoff) + ldsw + _i * 8192), 16, 0, 0); } while (0)
; #define G_LDA(dst, b, h) do { _Pragma("unroll") for (int m = 0; m < 4; ++m) dst[m] = G_LD2(G_SA(b, h) + aoff + m * 2048, G_SA(b, h) + (P::FP8 ? aoff1 : aoff + 1024) + m * 2048); } while (0)
; #define WAIT_V(n) asm volatile("s_waitcnt vmcnt(" #n ")" ::: "memory")
; #define BAR __builtin_amdgcn_s_barrier()
; template <class P>
; DEV void gemm_stream(const P& pol) {
;     ...
;     for (int t = 0; t < nt; t += 2) {
;       const bool last = (t == nt - 2);
;       const size_t k1 = (size_t)(t + 1) * kstep, k2 = (size_t)(t + 2) * kstep;
;       const char* a20 = last ? nA0 : cA0 + k2; const char* a21 = last ? nA1 : cA1 + k2; const char* b2 = last ? nB : cB + k2;
;       G_LDB(B0, 0, 0); SCHED; G_LDA(At, 0, 0); G_STAGE(G_SA(1, 1), cA1 + k1, vAc[1]);
;       WAIT_L(8); BAR; WAIT_L(0); G_MMA(0, 0, At, B0); BAR; SCHED;
;       if (P::GATHER && last && has_next) { LAS int* tab = arow + ((ui + 1) & 1) * 256; G_GATHER_OFFS(tab, nxt.rv); }
;       G_LDB(B1, 0, 1); G_STAGE(G_SB(0, 0), b2, voffB);
;       BAR; WAIT_L(0); G_MMA(0, 1, At, B1); BAR;
;       G_LDA(At, 0, 1); G_STAGE(G_SA(0, 0), a20, vAc[0]);
;       BAR; WAIT_L(0); G_MMA(1, 0, At, B0); BAR; SCHED;
;       G_STAGE(G_SB(0, 1), b2 + hstep, voffB);
;       WAIT_V(6); BAR; G_MMA(1, 1, At, B1); BAR;
;       G_LDB(B0, 1, 0); SCHED; G_LDA(At, 1, 0); G_STAGE(G_SA(0, 1), a21, vAc[1]);
;       WAIT_L(8); BAR; WAIT_L(0); G_MMA(0, 0, At, B0); BAR; SCHED;
;       G_LDB(B1, 1, 1); G_STAGE(G_SB(1, 0), b2 + kstep, voffB);
;       BAR; WAIT_L(0); G_MMA(0, 1, At, B1); BAR;
;       G_LDA(At, 1, 1); G_STAGE(G_SA(1, 0), a20 + kstep, vAc[0]);
;       BAR; WAIT_L(0); G_MMA(1, 0, At, B0); BAR; SCHED;
;       G_STAGE(G_SB(1, 1), b2 + hstep + kstep, voffB);
;       WAIT_V(6); BAR; G_MMA(1, 1, At, B1); BAR;
	s_mov_b32 m0, s59
	v_lshl_add_u64 v[142:143], s[30:31], 0, v[130:131]
	global_load_lds_dwordx4 v[142:143], off
	v_lshl_add_u64 v[142:143], s[30:31], 0, v[132:133]
	s_mov_b32 m0, s60
	s_nop 0
	global_load_lds_dwordx4 v[142:143], off
	s_waitcnt vmcnt(6)
	s_barrier
	s_setprio 1
	v_mfma_f32_16x16x32_bf16 v[54:57], v[212:215], v[180:183], v[54:57]
	v_mfma_f32_16x16x32_bf16 v[46:49], v[224:227], v[180:183], v[46:49]
	v_mfma_f32_16x16x32_bf16 v[38:41], v[212:215], v[188:191], v[38:41]
	v_mfma_f32_16x16x32_bf16 v[30:33], v[224:227], v[188:191], v[30:33]
	v_mfma_f32_16x16x32_bf16 v[22:25], v[212:215], v[196:199], v[22:25]
	v_mfma_f32_16x16x32_bf16 v[14:17], v[224:227], v[196:199], v[14:17]
	v_mfma_f32_16x16x32_bf16 v[6:9], v[212:215], v[204:207], v[6:9]
	v_mfma_f32_16x16x32_bf16 v[2:5], v[224:227], v[204:207], v[2:5]
	v_mfma_f32_16x16x32_bf16 v[54:57], v[216:219], v[184:187], v[54:57]
	v_mfma_f32_16x16x32_bf16 v[46:49], v[228:231], v[184:187], v[46:49]
	v_mfma_f32_16x16x32_bf16 v[38:41], v[216:219], v[192:195], v[38:41]
	v_mfma_f32_16x16x32_bf16 v[30:33], v[228:231], v[192:195], v[30:33]
	v_mfma_f32_16x16x32_bf16 v[22:25], v[216:219], v[200:203], v[22:25]
	v_mfma_f32_16x16x32_bf16 v[14:17], v[228:231], v[200:203], v[14:17]
	v_mfma_f32_16x16x32_bf16 v[6:9], v[216:219], v[208:211], v[6:9]
	v_mfma_f32_16x16x32_bf16 v[2:5], v[228:231], v[208:211], v[2:5]
	s_setprio 0
	s_barrier
	ds_read_b128 v[142:145], v150
	ds_read_b128 v[168:171], v151
	ds_read_b128 v[172:175], v162
	ds_read_b128 v[176:179], v163
	s_mov_b32 m0, s61
	v_lshl_add_u64 v[212:213], s[34:35], 0, v[134:135]
	ds_read_b128 v[180:183], v166 offset:32768
	ds_read_b128 v[184:187], v166 offset:33792
	ds_read_b128 v[188:191], v166 offset:34816
	ds_read_b128 v[192:195], v166 offset:35840
	ds_read_b128 v[196:199], v166 offset:36864
	ds_read_b128 v[200:203], v166 offset:37888
	ds_read_b128 v[204:207], v166 offset:38912
	ds_read_b128 v[208:211], v166 offset:39936
	global_load_lds_dwordx4 v[212:213], off
	v_lshl_add_u64 v[212:213], s[34:35], 0, v[136:137]
	s_mov_b32 m0, s62
	s_nop 0
	global_load_lds_dwordx4 v[212:213], off
	s_waitcnt lgkmcnt(8)
	s_barrier
	s_waitcnt lgkmcnt(0)
	s_setprio 1
	v_mfma_f32_16x16x32_bf16 v[126:129], v[142:145], v[180:183], v[126:129]
	v_mfma_f32_16x16x32_bf16 v[122:125], v[172:175], v[180:183], v[122:125]
	v_mfma_f32_16x16x32_bf16 v[110:113], v[142:145], v[188:191], v[110:113]
	v_mfma_f32_16x16x32_bf16 v[106:109], v[172:175], v[188:191], v[106:109]
	v_mfma_f32_16x16x32_bf16 v[94:97], v[142:145], v[196:199], v[94:97]
	v_mfma_f32_16x16x32_bf16 v[90:93], v[172:175], v[196:199], v[90:93]
	v_mfma_f32_16x16x32_bf16 v[78:81], v[142:145], v[204:207], v[78:81]
	v_mfma_f32_16x16x32_bf16 v[74:77], v[172:175], v[204:207], v[74:77]
	v_mfma_f32_16x16x32_bf16 v[126:129], v[168:171], v[184:187], v[126:129]
	v_mfma_f32_16x16x32_bf16 v[122:125], v[176:179], v[184:187], v[122:125]
	v_mfma_f32_16x16x32_bf16 v[110:113], v[168:171], v[192:195], v[110:113]
	v_mfma_f32_16x16x32_bf16 v[106:109], v[176:179], v[192:195], v[106:109]
	v_mfma_f32_16x16x32_bf16 v[94:97], v[168:171], v[200:203], v[94:97]
	v_mfma_f32_16x16x32_bf16 v[90:93], v[176:179], v[200:203], v[90:93]
	v_mfma_f32_16x16x32_bf16 v[78:81], v[168:171], v[208:211], v[78:81]
	v_mfma_f32_16x16x32_bf16 v[74:77], v[176:179], v[208:211], v[74:77]
	s_setprio 0
	s_barrier
	s_mov_b32 m0, s65
	v_lshl_add_u64 v[220:221], v[220:221], 0, s[12:13]
	ds_read_b128 v[212:215], v152
	ds_read_b128 v[216:219], v153
	ds_read_b128 v[224:227], v164
	ds_read_b128 v[228:231], v165
	global_load_lds_dwordx4 v[220:221], off
	v_lshl_add_u64 v[220:221], v[232:233], 0, s[12:13]
	s_mov_b32 m0, s66
	s_nop 0
	global_load_lds_dwordx4 v[220:221], off
	s_barrier
	s_waitcnt lgkmcnt(0)
	s_setprio 1
	v_mfma_f32_16x16x32_bf16 v[118:121], v[212:215], v[180:183], v[118:121]
	v_mfma_f32_16x16x32_bf16 v[114:117], v[224:227], v[180:183], v[114:117]
	v_mfma_f32_16x16x32_bf16 v[102:105], v[212:215], v[188:191], v[102:105]
	v_mfma_f32_16x16x32_bf16 v[98:101], v[224:227], v[188:191], v[98:101]
	v_mfma_f32_16x16x32_bf16 v[86:89], v[212:215], v[196:199], v[86:89]
	v_mfma_f32_16x16x32_bf16 v[82:85], v[224:227], v[196:199], v[82:85]
	v_mfma_f32_16x16x32_bf16 v[70:73], v[212:215], v[204:207], v[70:73]
	v_mfma_f32_16x16x32_bf16 v[66:69], v[224:227], v[204:207], v[66:69]
	v_mfma_f32_16x16x32_bf16 v[118:121], v[216:219], v[184:187], v[118:121]
	v_mfma_f32_16x16x32_bf16 v[114:117], v[228:231], v[184:187], v[114:117]
	v_mfma_f32_16x16x32_bf16 v[102:105], v[216:219], v[192:195], v[102:105]
	v_mfma_f32_16x16x32_bf16 v[98:101], v[228:231], v[192:195], v[98:101]
	v_mfma_f32_16x16x32_bf16 v[86:89], v[216:219], v[200:203], v[86:89]
	v_mfma_f32_16x16x32_bf16 v[82:85], v[228:231], v[200:203], v[82:85]
	v_mfma_f32_16x16x32_bf16 v[70:73], v[216:219], v[208:211], v[70:73]
	v_mfma_f32_16x16x32_bf16 v[66:69], v[228:231], v[208:211], v[66:69]
	s_setprio 0
	s_mov_b32 m0, s67
	v_lshl_add_u64 v[220:221], v[234:235], 0, s[12:13]
	s_barrier
	ds_read_b128 v[180:183], v166 offset:49152
	ds_read_b128 v[184:187], v166 offset:50176
	ds_read_b128 v[188:191], v166 offset:51200
	ds_read_b128 v[192:195], v166 offset:52224
	ds_read_b128 v[196:199], v166 offset:53248
	ds_read_b128 v[200:203], v166 offset:54272
	ds_read_b128 v[204:207], v166 offset:55296
	ds_read_b128 v[208:211], v166 offset:56320
	global_load_lds_dwordx4 v[220:221], off
	v_lshl_add_u64 v[220:221], v[236:237], 0, s[12:13]
	s_mov_b32 m0, s68
	s_nop 0
	global_load_lds_dwordx4 v[220:221], off
	s_barrier
; #define G_STAGE(bufoff, gbase, voff) do { _Pragma("unroll") for (int _i = 0; _i < 2; ++_i) \
;     __builtin_amdgcn_global_load_lds((const unsigned*)((const char*)(gbase) + (voff)[_i]), (LAS unsigned*)(lds + (bufoff) + ldsw + _i * 8192), 16, 0, 0); } while (0)
; #define G_LDA(dst, b, h) do { _Pragma("unroll") for (int m = 0; m < 4; ++m) dst[m] = G_LD2(G_SA(b, h) + aoff + m * 2048, G_SA(b, h) + (P::FP8 ? aoff1 : aoff + 1024) + m * 2048); } while (0)
; #define G_LDB(dst, b, h) do { _Pragma("unroll") for (int n = 0; n < 2; ++n) dst[n] = G_LD2(G_SB(b, h) + boff + n * 2048, G_SB(b, h) + (P::FP8 ? boff1 : boff + 1024) + n * 2048); } while (0)
; #define WAIT_V(n) asm volatile("s_waitcnt vmcnt(" #n ")" ::: "memory")
; #define WAIT_L(n) asm volatile("s_waitcnt lgkmcnt(" #n ")" ::: "memory")
; #define BAR __builtin_amdgcn_s_barrier()
; #define SCHED __builtin_amdgcn_sched_barrier(0)
; template <class P>
; DEV void gemm_stream(const P& pol) {
;     ...
;       BAR; WAIT_L(0); G_MMA(1, 0, At, B0); BAR; SCHED;
;       G_STAGE(G_SB(0, 1), b2 + hstep, voffB);
;       WAIT_V(6); BAR; G_MMA(1, 1, At, B1); BAR;
;       G_LDB(B0, 1, 0); SCHED; G_LDA(At, 1, 0); G_STAGE(G_SA(0, 1), a21, vAc[1]);
;       WAIT_L(8); BAR; WAIT_L(0); G_MMA(0, 0, At, B0); BAR; SCHED;
;       G_LDB(B1, 1, 1); G_STAGE(G_SB(1, 0), b2 + kstep, voffB);
;       BAR; WAIT_L(0); G_MMA(0, 1, At, B1); BAR;
;       G_LDA(At, 1, 1); G_STAGE(G_SA(1, 0), a20 + kstep, vAc[0]);
;       BAR; WAIT_L(0); G_MMA(1, 0, At, B0); BAR; SCHED;
;       G_STAGE(G_SB(1, 1), b2 + hstep + kstep, voffB);
;       WAIT_V(6); BAR; G_MMA(1, 1, At, B1); BAR;
	s_waitcnt lgkmcnt(0)
	s_setprio 1
	v_mfma_f32_16x16x32_bf16 v[62:65], v[142:145], v[180:183], v[62:65]
	v_mfma_f32_16x16x32_bf16 v[58:61], v[172:175], v[180:183], v[58:61]
	v_mfma_f32_16x16x32_bf16 v[50:53], v[142:145], v[188:191], v[50:53]
	v_mfma_f32_16x16x32_bf16 v[42:45], v[172:175], v[188:191], v[42:45]
	v_mfma_f32_16x16x32_bf16 v[34:37], v[142:145], v[196:199], v[34:37]
	v_mfma_f32_16x16x32_bf16 v[26:29], v[172:175], v[196:199], v[26:29]
	v_mfma_f32_16x16x32_bf16 v[18:21], v[142:145], v[204:207], v[18:21]
	v_mfma_f32_16x16x32_bf16 v[10:13], v[172:175], v[204:207], v[10:13]
	v_mfma_f32_16x16x32_bf16 v[62:65], v[168:171], v[184:187], v[62:65]
	v_mfma_f32_16x16x32_bf16 v[58:61], v[176:179], v[184:187], v[58:61]
	v_mfma_f32_16x16x32_bf16 v[50:53], v[168:171], v[192:195], v[50:53]
	v_mfma_f32_16x16x32_bf16 v[42:45], v[176:179], v[192:195], v[42:45]
	v_mfma_f32_16x16x32_bf16 v[34:37], v[168:171], v[200:203], v[34:37]
	v_mfma_f32_16x16x32_bf16 v[26:29], v[176:179], v[200:203], v[26:29]
	v_mfma_f32_16x16x32_bf16 v[18:21], v[168:171], v[208:211], v[18:21]
	v_mfma_f32_16x16x32_bf16 v[10:13], v[176:179], v[208:211], v[10:13]
	s_setprio 0
	s_barrier
	s_mov_b32 m0, s69
	v_lshl_add_u64 v[142:143], s[36:37], 0, v[130:131]
	global_load_lds_dwordx4 v[142:143], off
	v_lshl_add_u64 v[142:143], s[36:37], 0, v[132:133]
	s_mov_b32 m0, s70
	s_nop 0
	global_load_lds_dwordx4 v[142:143], off
	s_waitcnt vmcnt(6)
	s_barrier
	s_setprio 1
	v_mfma_f32_16x16x32_bf16 v[54:57], v[212:215], v[180:183], v[54:57]
	v_mfma_f32_16x16x32_bf16 v[46:49], v[224:227], v[180:183], v[46:49]
	v_mfma_f32_16x16x32_bf16 v[38:41], v[212:215], v[188:191], v[38:41]
	v_mfma_f32_16x16x32_bf16 v[30:33], v[224:227], v[188:191], v[30:33]
	v_mfma_f32_16x16x32_bf16 v[22:25], v[212:215], v[196:199], v[22:25]
	v_mfma_f32_16x16x32_bf16 v[14:17], v[224:227], v[196:199], v[14:17]
	v_mfma_f32_16x16x32_bf16 v[6:9], v[212:215], v[204:207], v[6:9]
	v_mfma_f32_16x16x32_bf16 v[2:5], v[224:227], v[204:207], v[2:5]
	v_mfma_f32_16x16x32_bf16 v[54:57], v[216:219], v[184:187], v[54:57]
	v_mfma_f32_16x16x32_bf16 v[46:49], v[228:231], v[184:187], v[46:49]
	v_mfma_f32_16x16x32_bf16 v[38:41], v[216:219], v[192:195], v[38:41]
	v_mfma_f32_16x16x32_bf16 v[30:33], v[228:231], v[192:195], v[30:33]
	v_mfma_f32_16x16x32_bf16 v[22:25], v[216:219], v[200:203], v[22:25]
	v_mfma_f32_16x16x32_bf16 v[14:17], v[228:231], v[200:203], v[14:17]
	v_mfma_f32_16x16x32_bf16 v[6:9], v[216:219], v[208:211], v[6:9]
	v_mfma_f32_16x16x32_bf16 v[2:5], v[228:231], v[208:211], v[2:5]
	s_setprio 0
	s_movk_i32 s34, 0x100
	s_andn2_b64 vcc, exec, s[28:29]
	s_mov_b64 s[30:31], -1
	s_mov_b64 s[28:29], 0
	s_barrier
	s_cbranch_vccz .LBB0_521
; DEV CParams* launder(CParams* p) { asm volatile("" : "+s"(p)); return p; }
; DEV void st_bf16x8(bf16_t* p, f32x4 a, f32x4 b) { u32x4 o; o.x = cvt_pk_bf16(a[0], a[1]); o.y = cvt_pk_bf16(a[2], a[3]); o.z = cvt_pk_bf16(b[0], b[1]); o.w = cvt_pk_bf16(b[2], b[3]); *(u32x4*)p = o; }
; DEV void row_to_bkey(int row, int& b, int& key) { if (row < NCTX) { b = row >> 8; key = row & 255; } else { const int r = row - NCTX; b = r >> 12; key = CTX + (r & 4095); } }
;   DEV void operator()(const AccT& acc, int wr, int wc, int fr, int fq) const {
;     CParams& P = *launder(p); const int row0 = pm * BM + wr * 64 + fr;
; #pragma unroll
;     for (int ai = 0; ai < 2; ++ai)
; #pragma unroll
;       for (int m = 0; m < 4; ++m) {
;         const int row = row0 + ai * HALF + m * 16; int b, key; row_to_bkey(row, b, key);
;         const long bh = (long)(b * NH + pn) * KEYS + key; const int c = wc * 32 + 8 * fq;
;         st_bf16x8(P.kf + bh * QK + c, acc[ai][0][m][0], acc[ai][0][m][1]);
;         st_bf16x8(P.vf + bh * DV + c, acc[ai][1][m][0], acc[ai][1][m][1]);
;       }
;   }
	s_mov_b64 s[22:23], s[4:5]
	s_load_dwordx4 s[24:27], s[22:23], 0x178
	v_lshl_add_u32 v167, s82, 8, v1
	v_mov_b32_e32 v141, v139
	v_add_u32_e32 v138, 0xfffffc00, v167
	v_ashrrev_i32_e32 v168, 8, v167
	s_waitcnt lgkmcnt(0)
	v_lshl_add_u64 v[144:145], s[24:25], 0, v[140:141]
	v_lshl_add_u64 v[142:143], s[26:27], 0, v[140:141]
	v_lshrrev_b32_e32 v141, 12, v138
	v_and_b32_e32 v138, 0xfcf, v138
	v_cmp_gt_i32_e32 vcc, s63, v167
	v_add_u32_e32 v138, 0x100, v138
	v_cvt_pk_bf16_f32 v126, v126, v127
	v_cndmask_b32_e32 v141, v141, v168, vcc
	v_cndmask_b32_e32 v138, v138, v154, vcc
	v_lshl_add_u32 v141, v141, 3, s54
	v_mad_i64_i32 v[170:171], s[22:23], v141, s71, v[138:139]
	v_mad_u64_u32 v[172:173], s[22:23], v170, s72, v[144:145]
	v_cvt_pk_bf16_f32 v127, v128, v129
	v_cvt_pk_bf16_f32 v128, v122, v123
	v_lshlrev_b64 v[122:123], 8, v[170:171]
	v_cvt_pk_bf16_f32 v118, v118, v119
	v_cvt_pk_bf16_f32 v119, v120, v121
	v_cvt_pk_bf16_f32 v120, v114, v115
	v_or_b32_e32 v115, 16, v167
	v_mad_i32_i24 v173, v171, s72, v173
	v_cvt_pk_bf16_f32 v129, v124, v125
	v_lshl_add_u64 v[122:123], v[142:143], 0, v[122:123]
	v_cvt_pk_bf16_f32 v121, v116, v117
	v_cmp_lt_i32_e32 vcc, s73, v115
	global_store_dwordx4 v[172:173], v[126:129], off
	global_store_dwordx4 v[122:123], v[118:121], off
	s_and_saveexec_b64 s[22:23], vcc
	s_xor_b64 s[22:23], exec, s[22:23]
	v_add_u32_e32 v115, 0xfffffc10, v167
	v_lshrrev_b32_e32 v114, 12, v115
	v_and_b32_e32 v115, 0xfdf, v115
	v_add_u32_e32 v138, 0x100, v115
	s_andn2_saveexec_b64 s[22:23], s[22:23]
	v_and_b32_e32 v138, 0xdf, v115
	v_mov_b32_e32 v114, v168
	s_or_b64 exec, exec, s[22:23]
	v_lshl_add_u32 v114, v114, 3, s54
	v_mad_i64_i32 v[114:115], s[22:23], v114, s71, v[138:139]
	v_mad_u64_u32 v[116:117], s[22:23], v114, s72, v[144:145]
	v_cvt_pk_bf16_f32 v110, v110, v111
	v_cvt_pk_bf16_f32 v111, v112, v113
	v_cvt_pk_bf16_f32 v112, v106, v107
	v_lshlrev_b64 v[106:107], 8, v[114:115]
	v_cvt_pk_bf16_f32 v102, v102, v103
	v_cvt_pk_bf16_f32 v103, v104, v105
	v_cvt_pk_bf16_f32 v104, v98, v99
	v_or_b32_e32 v99, 32, v167
	v_mad_i32_i24 v117, v115, s72, v117
	v_cvt_pk_bf16_f32 v113, v108, v109
	v_lshl_add_u64 v[106:107], v[142:143], 0, v[106:107]
	v_cvt_pk_bf16_f32 v105, v100, v101
	v_cmp_lt_i32_e32 vcc, s73, v99
	global_store_dwordx4 v[116:117], v[110:113], off
	global_store_dwordx4 v[106:107], v[102:105], off
	s_and_saveexec_b64 s[22:23], vcc
	s_xor_b64 s[22:23], exec, s[22:23]
	v_add_u32_e32 v99, 0xfffffc20, v167
	v_lshrrev_b32_e32 v98, 12, v99
	v_and_b32_e32 v99, 0xfef, v99
	v_add_u32_e32 v138, 0x100, v99
	s_andn2_saveexec_b64 s[22:23], s[22:23]
	v_and_b32_e32 v138, 0xef, v99
	v_mov_b32_e32 v98, v168
	s_or_b64 exec, exec, s[22:23]
	v_lshl_add_u32 v98, v98, 3, s54
	v_mad_i64_i32 v[98:99], s[22:23], v98, s71, v[138:139]
	v_mad_u64_u32 v[100:101], s[22:23], v98, s72, v[144:145]
	v_cvt_pk_bf16_f32 v94, v94, v95
	v_cvt_pk_bf16_f32 v95, v96, v97
	v_cvt_pk_bf16_f32 v96, v90, v91
	v_lshlrev_b64 v[90:91], 8, v[98:99]
	v_cvt_pk_bf16_f32 v86, v86, v87
	v_cvt_pk_bf16_f32 v87, v88, v89
	v_cvt_pk_bf16_f32 v88, v82, v83
	v_or_b32_e32 v82, 48, v167
	v_mad_i32_i24 v101, v99, s72, v101
	v_cvt_pk_bf16_f32 v97, v92, v93
	v_lshl_add_u64 v[90:91], v[142:143], 0, v[90:91]
	v_cvt_pk_bf16_f32 v89, v84, v85
	v_cmp_lt_i32_e32 vcc, s73, v82
	global_store_dwordx4 v[100:101], v[94:97], off
	global_store_dwordx4 v[90:91], v[86:89], off
	s_and_saveexec_b64 s[22:23], vcc
	s_xor_b64 s[22:23], exec, s[22:23]
	v_add_u32_e32 v82, 0xfffffc30, v167
	v_lshrrev_b32_e32 v168, 12, v82
	v_and_b32_e32 v82, 0xfff, v82
	v_add_u32_e32 v138, 0x100, v82
	s_andn2_saveexec_b64 s[22:23], s[22:23]
	v_and_b32_e32 v138, 0xff, v82
	s_or_b64 exec, exec, s[22:23]
	v_lshl_add_u32 v82, v168, 3, s54
	v_mad_i64_i32 v[82:83], s[22:23], v82, s71, v[138:139]
	v_mad_u64_u32 v[84:85], s[22:23], v82, s72, v[144:145]
	v_cvt_pk_bf16_f32 v78, v78, v79
	v_cvt_pk_bf16_f32 v79, v80, v81
	v_cvt_pk_bf16_f32 v80, v74, v75
	v_lshlrev_b64 v[74:75], 8, v[82:83]
	v_mad_i32_i24 v85, v83, s72, v85
	v_cvt_pk_bf16_f32 v81, v76, v77
	v_lshl_add_u64 v[74:75], v[142:143], 0, v[74:75]
	v_cvt_pk_bf16_f32 v70, v70, v71
	v_cvt_pk_bf16_f32 v71, v72, v73
	v_cvt_pk_bf16_f32 v72, v66, v67
	v_cvt_pk_bf16_f32 v73, v68, v69
	v_cmp_lt_i32_e32 vcc, s76, v167
	global_store_dwordx4 v[84:85], v[78:81], off
	global_store_dwordx4 v[74:75], v[70:73], off
	s_and_saveexec_b64 s[22:23], vcc
	s_xor_b64 s[22:23], exec, s[22:23]
	v_add_u32_e32 v66, 0xfffffc80, v167
	v_lshrrev_b32_e32 v67, 12, v66
	v_and_b32_e32 v66, 0xfcf, v66
	v_add_u32_e32 v138, 0x100, v66
	s_or_saveexec_b64 s[22:23], s[22:23]
	v_add_u32_e32 v68, 0x80, v167
	v_ashrrev_i32_e32 v66, 8, v68
	s_xor_b64 exec, exec, s[22:23]
	s_cbranch_execz .LBB0_517
	v_and_b32_e32 v138, 0xcf, v68
	v_mov_b32_e32 v67, v66
	s_branch .LBB0_517

; #define LAS __attribute__((address_space(3)))
; #define G_GATHER_OFFS(tab_, rv_) do { _Pragma("unroll") for (int i = 0; i < 2; ++i) { int R_, C_; G_SRC(i, R_, C_); const int ra_ = (tab_)[R_], rb_ = (tab_)[HALF + R_];        \
;     vAc[0][i] = (unsigned)((R_ < (rv_) ? ra_ : 0) * KB + C_); vAc[1][i] = (unsigned)((HALF + R_ < (rv_) ? rb_ : 0) * KB + C_); } } while (0)
; #define G_STAGE(bufoff, gbase, voff) do { _Pragma("unroll") for (int _i = 0; _i < 2; ++_i) \
;     __builtin_amdgcn_global_load_lds((const unsigned*)((const char*)(gbase) + (voff)[_i]), (LAS unsigned*)(lds + (bufoff) + ldsw + _i * 8192), 16, 0, 0); } while (0)
; #define G_LDA(dst, b, h) do { _Pragma("unroll") for (int m = 0; m < 4; ++m) dst[m] = G_LD2(G_SA(b, h) + aoff + m * 2048, G_SA(b, h) + (P::FP8 ? aoff1 : aoff + 1024) + m * 2048); } while (0)
; #define G_LDB(dst, b, h) do { _Pragma("unroll") for (int n = 0; n < 2; ++n) dst[n] = G_LD2(G_SB(b, h) + boff + n * 2048, G_SB(b, h) + (P::FP8 ? boff1 : boff + 1024) + n * 2048); } while (0)
; #define WAIT_V(n) asm volatile("s_waitcnt vmcnt(" #n ")" ::: "memory")
; #define WAIT_L(n) asm volatile("s_waitcnt lgkmcnt(" #n ")" ::: "memory")
; #define BAR __builtin_amdgcn_s_barrier()
; #define SCHED __builtin_amdgcn_sched_barrier(0)
; template <class P>
; DEV void gemm_stream(const P& pol) {
;     ...
;     for (int t = 0; t < nt; t += 2) {
;       const bool last = (t == nt - 2);
;       const size_t k1 = (size_t)(t + 1) * kstep, k2 = (size_t)(t + 2) * kstep;
;       const char* a20 = last ? nA0 : cA0 + k2; const char* a21 = last ? nA1 : cA1 + k2; const char* b2 = last ? nB : cB + k2;
;       G_LDB(B0, 0, 0); SCHED; G_LDA(At, 0, 0); G_STAGE(G_SA(1, 1), cA1 + k1, vAc[1]);
;       WAIT_L(8); BAR; WAIT_L(0); G_MMA(0, 0, At, B0); BAR; SCHED;
;       if (P::GATHER && last && has_next) { LAS int* tab = arow + ((ui + 1) & 1) * 256; G_GATHER_OFFS(tab, nxt.rv); }
;       G_LDB(B1, 0, 1); G_STAGE(G_SB(0, 0), b2, voffB);
;       BAR; WAIT_L(0); G_MMA(0, 1, At, B1); BAR;
;       G_LDA(At, 0, 1); G_STAGE(G_SA(0, 0), a20, vAc[0]);
;       BAR; WAIT_L(0); G_MMA(1, 0, At, B0); BAR; SCHED;
;       G_STAGE(G_SB(0, 1), b2 + hstep, voffB);
;       WAIT_V(6); BAR; G_MMA(1, 1, At, B1); BAR;
.LBB0_546:
	s_add_u32 s24, s73, s22
	s_addc_u32 s25, s76, s23
	s_add_u32 s26, s20, s22
	ds_read_b128 v[166:169], v146
	ds_read_b128 v[170:173], v147
	ds_read_b128 v[174:177], v154
	ds_read_b128 v[178:181], v155
	s_addc_u32 s27, s21, s23
	s_add_u32 s26, s26, 0x100
	s_addc_u32 s27, s27, 0
	s_add_u32 s80, s71, s22
	s_addc_u32 s81, s72, s23
	s_cmpk_eq_i32 s22, 0x300
	s_cselect_b32 s27, s67, s27
	s_cselect_b32 s26, s68, s26
	s_mov_b32 m0, s61
	v_lshl_add_u64 v[214:215], v[144:145], 0, s[22:23]
	ds_read_b128 v[182:185], v163
	ds_read_b128 v[186:189], v163 offset:1024
	ds_read_b128 v[190:193], v163 offset:2048
	ds_read_b128 v[194:197], v163 offset:3072
	ds_read_b128 v[198:201], v163 offset:4096
	ds_read_b128 v[202:205], v163 offset:5120
	ds_read_b128 v[206:209], v163 offset:6144
	ds_read_b128 v[210:213], v163 offset:7168
	global_load_lds_dwordx4 v[214:215], off
	v_lshl_add_u64 v[214:215], v[142:143], 0, s[22:23]
	s_mov_b32 m0, s62
	s_cselect_b32 s79, s65, s25
	global_load_lds_dwordx4 v[214:215], off
	s_waitcnt lgkmcnt(8)
	s_barrier
	s_waitcnt lgkmcnt(0)
	s_cselect_b32 s78, s66, s24
	s_setprio 1
	v_mfma_f32_16x16x32_bf16 v[126:129], v[166:169], v[182:185], v[126:129]
	v_mfma_f32_16x16x32_bf16 v[122:125], v[174:177], v[182:185], v[122:125]
	v_mfma_f32_16x16x32_bf16 v[118:121], v[166:169], v[190:193], v[118:121]
	v_mfma_f32_16x16x32_bf16 v[114:117], v[174:177], v[190:193], v[114:117]
	v_mfma_f32_16x16x32_bf16 v[102:105], v[166:169], v[198:201], v[102:105]
	v_mfma_f32_16x16x32_bf16 v[98:101], v[174:177], v[198:201], v[98:101]
	v_mfma_f32_16x16x32_bf16 v[86:89], v[166:169], v[206:209], v[86:89]
	v_mfma_f32_16x16x32_bf16 v[82:85], v[174:177], v[206:209], v[82:85]
	v_mfma_f32_16x16x32_bf16 v[126:129], v[170:173], v[186:189], v[126:129]
	v_mfma_f32_16x16x32_bf16 v[122:125], v[178:181], v[186:189], v[122:125]
	v_mfma_f32_16x16x32_bf16 v[118:121], v[170:173], v[194:197], v[118:121]
	v_mfma_f32_16x16x32_bf16 v[114:117], v[178:181], v[194:197], v[114:117]
	v_mfma_f32_16x16x32_bf16 v[102:105], v[170:173], v[202:205], v[102:105]
	v_mfma_f32_16x16x32_bf16 v[98:101], v[178:181], v[202:205], v[98:101]
	v_mfma_f32_16x16x32_bf16 v[86:89], v[170:173], v[210:213], v[86:89]
	v_mfma_f32_16x16x32_bf16 v[82:85], v[178:181], v[210:213], v[82:85]
	s_setprio 0
	s_barrier
	s_cselect_b32 s25, s69, s81
	s_cselect_b32 s24, s70, s80
	s_mov_b32 m0, s31
	v_lshl_add_u64 v[232:233], s[24:25], 0, v[130:131]
	ds_read_b128 v[214:217], v148
	ds_read_b128 v[218:221], v149
	ds_read_b128 v[224:227], v156
	ds_read_b128 v[228:231], v157
	global_load_lds_dwordx4 v[232:233], off
	v_lshl_add_u64 v[234:235], s[24:25], 0, v[132:133]
	s_mov_b32 m0, s34
	s_nop 0
	global_load_lds_dwordx4 v[234:235], off
	s_barrier
	s_waitcnt lgkmcnt(0)
	s_setprio 1
	v_mfma_f32_16x16x32_bf16 v[110:113], v[214:217], v[182:185], v[110:113]
	v_mfma_f32_16x16x32_bf16 v[106:109], v[224:227], v[182:185], v[106:109]
	v_mfma_f32_16x16x32_bf16 v[94:97], v[214:217], v[190:193], v[94:97]
	v_mfma_f32_16x16x32_bf16 v[90:93], v[224:227], v[190:193], v[90:93]
	v_mfma_f32_16x16x32_bf16 v[78:81], v[214:217], v[198:201], v[78:81]
	v_mfma_f32_16x16x32_bf16 v[74:77], v[224:227], v[198:201], v[74:77]
	v_mfma_f32_16x16x32_bf16 v[70:73], v[214:217], v[206:209], v[70:73]
	v_mfma_f32_16x16x32_bf16 v[66:69], v[224:227], v[206:209], v[66:69]
	v_mfma_f32_16x16x32_bf16 v[110:113], v[218:221], v[186:189], v[110:113]
	v_mfma_f32_16x16x32_bf16 v[106:109], v[228:231], v[186:189], v[106:109]
	v_mfma_f32_16x16x32_bf16 v[94:97], v[218:221], v[194:197], v[94:97]
	v_mfma_f32_16x16x32_bf16 v[90:93], v[228:231], v[194:197], v[90:93]
	v_mfma_f32_16x16x32_bf16 v[78:81], v[218:221], v[202:205], v[78:81]
	v_mfma_f32_16x16x32_bf16 v[74:77], v[228:231], v[202:205], v[74:77]
	v_mfma_f32_16x16x32_bf16 v[70:73], v[218:221], v[210:213], v[70:73]
	v_mfma_f32_16x16x32_bf16 v[66:69], v[228:231], v[210:213], v[66:69]
	s_setprio 0
	s_mov_b32 m0, s30
	v_lshl_add_u64 v[236:237], s[78:79], 0, v[134:135]
	s_barrier
	ds_read_b128 v[182:185], v163 offset:16384
	ds_read_b128 v[186:189], v163 offset:17408
	ds_read_b128 v[190:193], v163 offset:18432
	ds_read_b128 v[194:197], v163 offset:19456
	ds_read_b128 v[198:201], v163 offset:20480
	ds_read_b128 v[202:205], v163 offset:21504
	ds_read_b128 v[206:209], v163 offset:22528
	ds_read_b128 v[210:213], v163 offset:23552
	global_load_lds_dwordx4 v[236:237], off
	v_lshl_add_u64 v[238:239], s[78:79], 0, v[136:137]
	s_mov_b32 m0, s35
	s_nop 0
	global_load_lds_dwordx4 v[238:239], off
	s_barrier
	s_waitcnt lgkmcnt(0)
	s_setprio 1
	v_mfma_f32_16x16x32_bf16 v[62:65], v[166:169], v[182:185], v[62:65]
	v_mfma_f32_16x16x32_bf16 v[58:61], v[174:177], v[182:185], v[58:61]
	v_mfma_f32_16x16x32_bf16 v[54:57], v[166:169], v[190:193], v[54:57]
	v_mfma_f32_16x16x32_bf16 v[50:53], v[174:177], v[190:193], v[50:53]
	v_mfma_f32_16x16x32_bf16 v[38:41], v[166:169], v[198:201], v[38:41]
	v_mfma_f32_16x16x32_bf16 v[34:37], v[174:177], v[198:201], v[34:37]
	v_mfma_f32_16x16x32_bf16 v[22:25], v[166:169], v[206:209], v[22:25]
	v_mfma_f32_16x16x32_bf16 v[18:21], v[174:177], v[206:209], v[18:21]
	v_mfma_f32_16x16x32_bf16 v[62:65], v[170:173], v[186:189], v[62:65]
	v_mfma_f32_16x16x32_bf16 v[58:61], v[178:181], v[186:189], v[58:61]
	v_mfma_f32_16x16x32_bf16 v[54:57], v[170:173], v[194:197], v[54:57]
	v_mfma_f32_16x16x32_bf16 v[50:53], v[178:181], v[194:197], v[50:53]
	v_mfma_f32_16x16x32_bf16 v[38:41], v[170:173], v[202:205], v[38:41]
	v_mfma_f32_16x16x32_bf16 v[34:37], v[178:181], v[202:205], v[34:37]
	v_mfma_f32_16x16x32_bf16 v[22:25], v[170:173], v[210:213], v[22:25]
	v_mfma_f32_16x16x32_bf16 v[18:21], v[178:181], v[210:213], v[18:21]
	s_setprio 0
	s_barrier
; #define G_STAGE(bufoff, gbase, voff) do { _Pragma("unroll") for (int _i = 0; _i < 2; ++_i) \
;     __builtin_amdgcn_global_load_lds((const unsigned*)((const char*)(gbase) + (voff)[_i]), (LAS unsigned*)(lds + (bufoff) + ldsw + _i * 8192), 16, 0, 0); } while (0)
; #define G_LDA(dst, b, h) do { _Pragma("unroll") for (int m = 0; m < 4; ++m) dst[m] = G_LD2(G_SA(b, h) + aoff + m * 2048, G_SA(b, h) + (P::FP8 ? aoff1 : aoff + 1024) + m * 2048); } while (0)
; #define G_LDB(dst, b, h) do { _Pragma("unroll") for (int n = 0; n < 2; ++n) dst[n] = G_LD2(G_SB(b, h) + boff + n * 2048, G_SB(b, h) + (P::FP8 ? boff1 : boff + 1024) + n * 2048); } while (0)
; #define WAIT_V(n) asm volatile("s_waitcnt vmcnt(" #n ")" ::: "memory")
; #define WAIT_L(n) asm volatile("s_waitcnt lgkmcnt(" #n ")" ::: "memory")
; #define BAR __builtin_amdgcn_s_barrier()
; #define SCHED __builtin_amdgcn_sched_barrier(0)
; template <class P>
; DEV void gemm_stream(const P& pol) {
;     ...
;       WAIT_V(6); BAR; G_MMA(1, 1, At, B1); BAR;
;       G_LDB(B0, 1, 0); SCHED; G_LDA(At, 1, 0); G_STAGE(G_SA(0, 1), a21, vAc[1]);
;       WAIT_L(8); BAR; WAIT_L(0); G_MMA(0, 0, At, B0); BAR; SCHED;
;       G_LDB(B1, 1, 1); G_STAGE(G_SB(1, 0), b2 + kstep, voffB);
;       BAR; WAIT_L(0); G_MMA(0, 1, At, B1); BAR;
;       G_LDA(At, 1, 1); G_STAGE(G_SA(1, 0), a20 + kstep, vAc[0]);
;       BAR; WAIT_L(0); G_MMA(1, 0, At, B0); BAR; SCHED;
	s_add_u32 s78, s24, 0x20000
	s_addc_u32 s79, s25, 0
	s_mov_b32 m0, s36
	v_lshl_add_u64 v[166:167], s[78:79], 0, v[130:131]
	global_load_lds_dwordx4 v[166:167], off
	v_lshl_add_u64 v[166:167], s[78:79], 0, v[132:133]
	s_mov_b32 m0, s37
	s_nop 0
	global_load_lds_dwordx4 v[166:167], off
	s_waitcnt vmcnt(6)
	s_barrier
	s_setprio 1
	v_mfma_f32_16x16x32_bf16 v[46:49], v[214:217], v[182:185], v[46:49]
	v_mfma_f32_16x16x32_bf16 v[42:45], v[224:227], v[182:185], v[42:45]
	v_mfma_f32_16x16x32_bf16 v[30:33], v[214:217], v[190:193], v[30:33]
	v_mfma_f32_16x16x32_bf16 v[26:29], v[224:227], v[190:193], v[26:29]
	v_mfma_f32_16x16x32_bf16 v[14:17], v[214:217], v[198:201], v[14:17]
	v_mfma_f32_16x16x32_bf16 v[10:13], v[224:227], v[198:201], v[10:13]
	v_mfma_f32_16x16x32_bf16 v[6:9], v[214:217], v[206:209], v[6:9]
	v_mfma_f32_16x16x32_bf16 v[2:5], v[224:227], v[206:209], v[2:5]
	v_mfma_f32_16x16x32_bf16 v[46:49], v[218:221], v[186:189], v[46:49]
	v_mfma_f32_16x16x32_bf16 v[42:45], v[228:231], v[186:189], v[42:45]
	v_mfma_f32_16x16x32_bf16 v[30:33], v[218:221], v[194:197], v[30:33]
	v_mfma_f32_16x16x32_bf16 v[26:29], v[228:231], v[194:197], v[26:29]
	v_mfma_f32_16x16x32_bf16 v[14:17], v[218:221], v[202:205], v[14:17]
	v_mfma_f32_16x16x32_bf16 v[10:13], v[228:231], v[202:205], v[10:13]
	v_mfma_f32_16x16x32_bf16 v[6:9], v[218:221], v[210:213], v[6:9]
	v_mfma_f32_16x16x32_bf16 v[2:5], v[228:231], v[210:213], v[2:5]
	s_setprio 0
	s_barrier
	ds_read_b128 v[166:169], v150
	ds_read_b128 v[170:173], v151
	ds_read_b128 v[174:177], v158
	ds_read_b128 v[178:181], v159
	s_mov_b32 m0, s38
	v_lshl_add_u64 v[214:215], s[26:27], 0, v[134:135]
	ds_read_b128 v[182:185], v163 offset:32768
	ds_read_b128 v[186:189], v163 offset:33792
	ds_read_b128 v[190:193], v163 offset:34816
	ds_read_b128 v[194:197], v163 offset:35840
	ds_read_b128 v[198:201], v163 offset:36864
	ds_read_b128 v[202:205], v163 offset:37888
	ds_read_b128 v[206:209], v163 offset:38912
	ds_read_b128 v[210:213], v163 offset:39936
	global_load_lds_dwordx4 v[214:215], off
	v_lshl_add_u64 v[214:215], s[26:27], 0, v[136:137]
	s_mov_b32 m0, s39
	s_nop 0
	global_load_lds_dwordx4 v[214:215], off
	s_waitcnt lgkmcnt(8)
	s_barrier
	s_waitcnt lgkmcnt(0)
	s_setprio 1
	v_mfma_f32_16x16x32_bf16 v[126:129], v[166:169], v[182:185], v[126:129]
	v_mfma_f32_16x16x32_bf16 v[122:125], v[174:177], v[182:185], v[122:125]
	v_mfma_f32_16x16x32_bf16 v[118:121], v[166:169], v[190:193], v[118:121]
	v_mfma_f32_16x16x32_bf16 v[114:117], v[174:177], v[190:193], v[114:117]
	v_mfma_f32_16x16x32_bf16 v[102:105], v[166:169], v[198:201], v[102:105]
	v_mfma_f32_16x16x32_bf16 v[98:101], v[174:177], v[198:201], v[98:101]
	v_mfma_f32_16x16x32_bf16 v[86:89], v[166:169], v[206:209], v[86:89]
	v_mfma_f32_16x16x32_bf16 v[82:85], v[174:177], v[206:209], v[82:85]
	v_mfma_f32_16x16x32_bf16 v[126:129], v[170:173], v[186:189], v[126:129]
	v_mfma_f32_16x16x32_bf16 v[122:125], v[178:181], v[186:189], v[122:125]
	v_mfma_f32_16x16x32_bf16 v[118:121], v[170:173], v[194:197], v[118:121]
	v_mfma_f32_16x16x32_bf16 v[114:117], v[178:181], v[194:197], v[114:117]
	v_mfma_f32_16x16x32_bf16 v[102:105], v[170:173], v[202:205], v[102:105]
	v_mfma_f32_16x16x32_bf16 v[98:101], v[178:181], v[202:205], v[98:101]
	v_mfma_f32_16x16x32_bf16 v[86:89], v[170:173], v[210:213], v[86:89]
	v_mfma_f32_16x16x32_bf16 v[82:85], v[178:181], v[210:213], v[82:85]
	s_setprio 0
	s_barrier
	s_mov_b32 m0, s45
	v_lshl_add_u64 v[232:233], v[232:233], 0, s[14:15]
	ds_read_b128 v[214:217], v152
	ds_read_b128 v[218:221], v153
	ds_read_b128 v[224:227], v160
	ds_read_b128 v[228:231], v161
	global_load_lds_dwordx4 v[232:233], off
	v_lshl_add_u64 v[232:233], v[234:235], 0, s[14:15]
	s_mov_b32 m0, s46
	s_nop 0
	global_load_lds_dwordx4 v[232:233], off
	s_barrier
	s_waitcnt lgkmcnt(0)
	s_setprio 1
	v_mfma_f32_16x16x32_bf16 v[110:113], v[214:217], v[182:185], v[110:113]
	v_mfma_f32_16x16x32_bf16 v[106:109], v[224:227], v[182:185], v[106:109]
	v_mfma_f32_16x16x32_bf16 v[94:97], v[214:217], v[190:193], v[94:97]
	v_mfma_f32_16x16x32_bf16 v[90:93], v[224:227], v[190:193], v[90:93]
	v_mfma_f32_16x16x32_bf16 v[78:81], v[214:217], v[198:201], v[78:81]
	v_mfma_f32_16x16x32_bf16 v[74:77], v[224:227], v[198:201], v[74:77]
	v_mfma_f32_16x16x32_bf16 v[70:73], v[214:217], v[206:209], v[70:73]
	v_mfma_f32_16x16x32_bf16 v[66:69], v[224:227], v[206:209], v[66:69]
	v_mfma_f32_16x16x32_bf16 v[110:113], v[218:221], v[186:189], v[110:113]
	v_mfma_f32_16x16x32_bf16 v[106:109], v[228:231], v[186:189], v[106:109]
	v_mfma_f32_16x16x32_bf16 v[94:97], v[218:221], v[194:197], v[94:97]
	v_mfma_f32_16x16x32_bf16 v[90:93], v[228:231], v[194:197], v[90:93]
	v_mfma_f32_16x16x32_bf16 v[78:81], v[218:221], v[202:205], v[78:81]
	v_mfma_f32_16x16x32_bf16 v[74:77], v[228:231], v[202:205], v[74:77]
	v_mfma_f32_16x16x32_bf16 v[70:73], v[218:221], v[210:213], v[70:73]
	v_mfma_f32_16x16x32_bf16 v[66:69], v[228:231], v[210:213], v[66:69]
	s_setprio 0
	s_mov_b32 m0, s47
	v_lshl_add_u64 v[232:233], v[236:237], 0, s[14:15]
	s_barrier
	ds_read_b128 v[182:185], v163 offset:49152
	ds_read_b128 v[186:189], v163 offset:50176
	ds_read_b128 v[190:193], v163 offset:51200
	ds_read_b128 v[194:197], v163 offset:52224
	ds_read_b128 v[198:201], v163 offset:53248
	ds_read_b128 v[202:205], v163 offset:54272
	ds_read_b128 v[206:209], v163 offset:55296
	ds_read_b128 v[210:213], v163 offset:56320
	global_load_lds_dwordx4 v[232:233], off
	v_lshl_add_u64 v[232:233], v[238:239], 0, s[14:15]
	s_mov_b32 m0, s52
	s_nop 0
	global_load_lds_dwordx4 v[232:233], off
	s_barrier
; DEV CParams* launder(CParams* p) { asm volatile("" : "+s"(p)); return p; }
; #define G_STAGE(bufoff, gbase, voff) do { _Pragma("unroll") for (int _i = 0; _i < 2; ++_i) \
;     __builtin_amdgcn_global_load_lds((const unsigned*)((const char*)(gbase) + (voff)[_i]), (LAS unsigned*)(lds + (bufoff) + ldsw + _i * 8192), 16, 0, 0); } while (0)
; #define WAIT_V(n) asm volatile("s_waitcnt vmcnt(" #n ")" ::: "memory")
; #define WAIT_L(n) asm volatile("s_waitcnt lgkmcnt(" #n ")" ::: "memory")
; #define BAR __builtin_amdgcn_s_barrier()
; #define SCHED __builtin_amdgcn_sched_barrier(0)
; template <class P>
; DEV void gemm_stream(const P& pol) {
;     ...
;       BAR; WAIT_L(0); G_MMA(1, 0, At, B0); BAR; SCHED;
;       G_STAGE(G_SB(1, 1), b2 + hstep + kstep, voffB);
;       WAIT_V(6); BAR; G_MMA(1, 1, At, B1); BAR;
;   DEV void operator()(const AccT& acc, int wr, int wc, int fr, int fq) const {
;     CParams& P = *launder(p); const int row0 = pm * BM + wr * 64 + fr;
; #pragma unroll
;     for (int ai = 0; ai < 2; ++ai)
; #pragma unroll
;       for (int m = 0; m < 4; ++m) {
;         const int row = row0 + ai * HALF + m * 16, b = row >> 12, t = row & 4095;
; #pragma unroll
;         for (int bj = 0; bj < 2; ++bj) {
;           const int col = pn * 256 + bj * HALF + wc * 32 + 8 * fq, hh = col / QK, e = col - hh * QK;
	s_waitcnt lgkmcnt(0)
	s_setprio 1
	v_mfma_f32_16x16x32_bf16 v[62:65], v[166:169], v[182:185], v[62:65]
	v_mfma_f32_16x16x32_bf16 v[58:61], v[174:177], v[182:185], v[58:61]
	v_mfma_f32_16x16x32_bf16 v[54:57], v[166:169], v[190:193], v[54:57]
	v_mfma_f32_16x16x32_bf16 v[50:53], v[174:177], v[190:193], v[50:53]
	v_mfma_f32_16x16x32_bf16 v[38:41], v[166:169], v[198:201], v[38:41]
	v_mfma_f32_16x16x32_bf16 v[34:37], v[174:177], v[198:201], v[34:37]
	v_mfma_f32_16x16x32_bf16 v[22:25], v[166:169], v[206:209], v[22:25]
	v_mfma_f32_16x16x32_bf16 v[18:21], v[174:177], v[206:209], v[18:21]
	v_mfma_f32_16x16x32_bf16 v[62:65], v[170:173], v[186:189], v[62:65]
	v_mfma_f32_16x16x32_bf16 v[58:61], v[178:181], v[186:189], v[58:61]
	v_mfma_f32_16x16x32_bf16 v[54:57], v[170:173], v[194:197], v[54:57]
	v_mfma_f32_16x16x32_bf16 v[50:53], v[178:181], v[194:197], v[50:53]
	v_mfma_f32_16x16x32_bf16 v[38:41], v[170:173], v[202:205], v[38:41]
	v_mfma_f32_16x16x32_bf16 v[34:37], v[178:181], v[202:205], v[34:37]
	v_mfma_f32_16x16x32_bf16 v[22:25], v[170:173], v[210:213], v[22:25]
	v_mfma_f32_16x16x32_bf16 v[18:21], v[178:181], v[210:213], v[18:21]
	s_setprio 0
	s_barrier
	s_add_u32 s24, s24, 0x20080
	s_addc_u32 s25, s25, 0
	s_mov_b32 m0, s53
	v_lshl_add_u64 v[166:167], s[24:25], 0, v[130:131]
	global_load_lds_dwordx4 v[166:167], off
	v_lshl_add_u64 v[166:167], s[24:25], 0, v[132:133]
	s_mov_b32 m0, s54
	s_nop 0
	global_load_lds_dwordx4 v[166:167], off
	s_waitcnt vmcnt(6)
	s_barrier
	s_setprio 1
	v_mfma_f32_16x16x32_bf16 v[46:49], v[214:217], v[182:185], v[46:49]
	v_mfma_f32_16x16x32_bf16 v[42:45], v[224:227], v[182:185], v[42:45]
	v_mfma_f32_16x16x32_bf16 v[30:33], v[214:217], v[190:193], v[30:33]
	v_mfma_f32_16x16x32_bf16 v[26:29], v[224:227], v[190:193], v[26:29]
	v_mfma_f32_16x16x32_bf16 v[14:17], v[214:217], v[198:201], v[14:17]
	v_mfma_f32_16x16x32_bf16 v[10:13], v[224:227], v[198:201], v[10:13]
	v_mfma_f32_16x16x32_bf16 v[6:9], v[214:217], v[206:209], v[6:9]
	v_mfma_f32_16x16x32_bf16 v[2:5], v[224:227], v[206:209], v[2:5]
	v_mfma_f32_16x16x32_bf16 v[46:49], v[218:221], v[186:189], v[46:49]
	v_mfma_f32_16x16x32_bf16 v[42:45], v[228:231], v[186:189], v[42:45]
	v_mfma_f32_16x16x32_bf16 v[30:33], v[218:221], v[194:197], v[30:33]
	v_mfma_f32_16x16x32_bf16 v[26:29], v[228:231], v[194:197], v[26:29]
	v_mfma_f32_16x16x32_bf16 v[14:17], v[218:221], v[202:205], v[14:17]
	v_mfma_f32_16x16x32_bf16 v[10:13], v[228:231], v[202:205], v[10:13]
	v_mfma_f32_16x16x32_bf16 v[6:9], v[218:221], v[210:213], v[6:9]
	v_mfma_f32_16x16x32_bf16 v[2:5], v[228:231], v[210:213], v[2:5]
	s_setprio 0
	s_add_i32 s77, s77, 2
	s_add_u32 s22, s22, 0x100
	s_addc_u32 s23, s23, 0
	s_cmp_gt_u32 s77, 5
	s_barrier
	s_cbranch_scc0 .LBB0_546
	s_mov_b64 s[20:21], s[4:5]
	s_lshl_b32 s22, s58, 8
	v_lshl_or_b32 v144, s56, 8, v162
	s_add_i32 s22, s22, s44
	v_mul_hi_i32 v142, v144, s59
	v_or_b32_e32 v145, s22, v1
	s_load_dwordx2 s[20:21], s[20:21], 0x170
	v_bitop3_b32 v165, s22, v164, v1 bitop3:0xc8
	s_ashr_i32 s22, s22, 9
	v_lshrrev_b32_e32 v143, 31, v142
	v_ashrrev_i32_e32 v142, 5, v142
	s_and_b32 s24, s22, -8
	v_add_u32_e32 v172, v142, v143
	v_add_u32_e32 v142, s24, v172
	v_ashrrev_i32_e32 v143, 31, v142
	v_mad_u64_u32 v[166:167], s[22:23], v172, s60, v[144:145]
	v_lshlrev_b64 v[168:169], 12, v[142:143]
	v_or_b32_e32 v167, v168, v165
	s_waitcnt lgkmcnt(0)
; DEV CParams* launder(CParams* p) { asm volatile("" : "+s"(p)); return p; }
; #define G_ZERO() do { _Pragma("unroll") for (int a_ = 0; a_ < 2; ++a_) _Pragma("unroll") for (int b_ = 0; b_ < 2; ++b_) _Pragma("unroll") for (int m_ = 0; m_ < 4; ++m_) _Pragma("unroll") for (int n_ = 0; n_ < 2; ++n_) \
;     acc[a_][b_][m_][n_] = (f32x4){0.f, 0.f, 0.f, 0.f}; } while (0)
; #define WAIT_V(n) asm volatile("s_waitcnt vmcnt(" #n ")" ::: "memory")
; #define BAR __builtin_amdgcn_s_barrier()
; #define G_BIAS(tab_) do { _Pragma("unroll") for (int b_ = 0; b_ < 2; ++b_) _Pragma("unroll") for (int n_ = 0; n_ < 2; ++n_) { bv[b_][n_] = *(const LAS f32x4*)((tab_) + 128 * b_ + 32 * wc + 8 * fq + 4 * n_); \
;     if (b_ == 1 && P::BIAS_LIN1) bv[b_][n_] = bv[b_][n_] + 1.0f; } } while (0)
; #define G_INIT() do { _Pragma("unroll") for (int a_ = 0; a_ < 2; ++a_) _Pragma("unroll") for (int b_ = 0; b_ < 2; ++b_) _Pragma("unroll") for (int m_ = 0; m_ < 4; ++m_) _Pragma("unroll") for (int n_ = 0; n_ < 2; ++n_) \
;     acc[a_][b_][m_][n_] = bv[b_][n_]; } while (0)
; DEV void st_bf16x8(bf16_t* p, f32x4 a, f32x4 b) { u32x4 o; o.x = cvt_pk_bf16(a[0], a[1]); o.y = cvt_pk_bf16(a[2], a[3]); o.z = cvt_pk_bf16(b[0], b[1]); o.w = cvt_pk_bf16(b[2], b[3]); *(u32x4*)p = o; }
; template <class P>
; DEV void gemm_stream(const P& pol) {
;     ...
;     pol.epi(cur, acc, wr, wc, fr, fq);
;     if (!has_next) break;
;     if (P::HASBIAS) { G_BIAS(btab + ((ui + 1) & 1) * 256); G_INIT(); } else G_ZERO();
;     cur = nxt; cA0 = nA0; cA1 = nA1; cB = nB; ++ui;
;     if (P::ROWSKIP) rvw = cur.rv - 64 * wr;
;   }
;   WAIT_V(0);
;   if (wr == 0) BAR;
;   __syncthreads();
;   DEV void operator()(const AccT& acc, int wr, int wc, int fr, int fq) const {
;     CParams& P = *launder(p); const int row0 = pm * BM + wr * 64 + fr;
; #pragma unroll
;     for (int ai = 0; ai < 2; ++ai)
; #pragma unroll
;       for (int m = 0; m < 4; ++m) {
;         const int row = row0 + ai * HALF + m * 16, b = row >> 12, t = row & 4095;
; #pragma unroll
;         for (int bj = 0; bj < 2; ++bj) {
;           const int col = pn * 256 + bj * HALF + wc * 32 + 8 * fq, hh = col / QK, e = col - hh * QK;
;           st_bf16x8(P.qf + ((long)(b * NH + hh) * SEQ + t) * QK + e, acc[ai][bj][m][0], acc[ai][bj][m][1]);
;         }
;       }
;   }
	v_mov_b64_e32 v[142:143], s[20:21]
	v_mad_u64_u32 v[170:171], s[20:21], v167, s57, v[142:143]
	v_ashrrev_i32_e32 v167, 31, v166
	v_cvt_pk_bf16_f32 v126, v126, v127
	v_cvt_pk_bf16_f32 v127, v128, v129
	v_cvt_pk_bf16_f32 v128, v122, v123
	v_or_b32_e32 v122, 0x80, v144
	v_mad_i32_i24 v171, v169, s57, v171
	v_lshlrev_b64 v[166:167], 1, v[166:167]
	v_mul_hi_i32 v123, v122, s59
	v_lshl_add_u64 v[170:171], v[170:171], 0, v[166:167]
	v_cvt_pk_bf16_f32 v129, v124, v125
	v_lshrrev_b32_e32 v124, 31, v123
	v_ashrrev_i32_e32 v123, 5, v123
	global_store_dwordx4 v[170:171], v[126:129], off
	v_cvt_pk_bf16_f32 v110, v110, v111
	v_cvt_pk_bf16_f32 v111, v112, v113
	v_add_u32_e32 v128, v123, v124
	v_add_u32_e32 v124, s24, v128
	v_ashrrev_i32_e32 v125, 31, v124
	v_mad_u64_u32 v[122:123], s[20:21], v128, s60, v[122:123]
	v_lshlrev_b64 v[124:125], 12, v[124:125]
	v_or_b32_e32 v123, v124, v165
	v_mad_u64_u32 v[126:127], s[20:21], v123, s57, v[142:143]
	v_ashrrev_i32_e32 v123, 31, v122
	v_mad_i32_i24 v127, v125, s57, v127
	v_lshlrev_b64 v[122:123], 1, v[122:123]
	v_lshl_add_u64 v[126:127], v[126:127], 0, v[122:123]
	v_cvt_pk_bf16_f32 v112, v106, v107
	v_cvt_pk_bf16_f32 v113, v108, v109
	global_store_dwordx4 v[126:127], v[110:113], off
	v_cvt_pk_bf16_f32 v108, v114, v115
	v_cvt_pk_bf16_f32 v109, v116, v117
	v_or_b32_e32 v112, 16, v165
	v_or_b32_e32 v106, v168, v112
	v_mad_u64_u32 v[106:107], s[20:21], v106, s57, v[142:143]
	v_mad_i32_i24 v107, v169, s57, v107
	v_lshl_add_u64 v[110:111], v[106:107], 0, v[166:167]
	v_cvt_pk_bf16_f32 v106, v118, v119
	v_cvt_pk_bf16_f32 v107, v120, v121
	global_store_dwordx4 v[110:111], v[106:109], off
	v_cvt_pk_bf16_f32 v94, v94, v95
	v_cvt_pk_bf16_f32 v95, v96, v97
	v_or_b32_e32 v106, v124, v112
	v_mad_u64_u32 v[106:107], s[20:21], v106, s57, v[142:143]
	v_mad_i32_i24 v107, v125, s57, v107
	v_lshl_add_u64 v[106:107], v[106:107], 0, v[122:123]
	v_cvt_pk_bf16_f32 v96, v90, v91
	v_cvt_pk_bf16_f32 v97, v92, v93
	global_store_dwordx4 v[106:107], v[94:97], off
	v_cvt_pk_bf16_f32 v92, v98, v99
	v_cvt_pk_bf16_f32 v93, v100, v101
	v_or_b32_e32 v96, 32, v165
	v_or_b32_e32 v90, v168, v96
	v_mad_u64_u32 v[90:91], s[20:21], v90, s57, v[142:143]
	v_mad_i32_i24 v91, v169, s57, v91
	v_lshl_add_u64 v[94:95], v[90:91], 0, v[166:167]
	v_cvt_pk_bf16_f32 v90, v102, v103
	v_cvt_pk_bf16_f32 v91, v104, v105
	global_store_dwordx4 v[94:95], v[90:93], off
	v_cvt_pk_bf16_f32 v78, v78, v79
	v_cvt_pk_bf16_f32 v79, v80, v81
	v_or_b32_e32 v90, v124, v96
	v_mad_u64_u32 v[90:91], s[20:21], v90, s57, v[142:143]
	v_mad_i32_i24 v91, v125, s57, v91
	v_lshl_add_u64 v[90:91], v[90:91], 0, v[122:123]
	v_cvt_pk_bf16_f32 v80, v74, v75
	v_cvt_pk_bf16_f32 v81, v76, v77
	global_store_dwordx4 v[90:91], v[78:81], off
	v_cvt_pk_bf16_f32 v76, v82, v83
	v_cvt_pk_bf16_f32 v77, v84, v85
	v_or_b32_e32 v80, 48, v165
	v_or_b32_e32 v74, v168, v80
	v_mad_u64_u32 v[74:75], s[20:21], v74, s57, v[142:143]
	v_mad_i32_i24 v75, v169, s57, v75
	v_lshl_add_u64 v[78:79], v[74:75], 0, v[166:167]
	v_cvt_pk_bf16_f32 v74, v86, v87
	v_cvt_pk_bf16_f32 v75, v88, v89
	global_store_dwordx4 v[78:79], v[74:77], off
	v_cvt_pk_bf16_f32 v70, v70, v71
	v_cvt_pk_bf16_f32 v71, v72, v73
	v_or_b32_e32 v74, v124, v80
	v_mad_u64_u32 v[74:75], s[20:21], v74, s57, v[142:143]
	v_mad_i32_i24 v75, v125, s57, v75
	v_lshl_add_u64 v[74:75], v[74:75], 0, v[122:123]
	v_cvt_pk_bf16_f32 v72, v66, v67
	v_cvt_pk_bf16_f32 v73, v68, v69
	v_add_u32_e32 v66, 0x80, v145
	global_store_dwordx4 v[74:75], v[70:73], off
	v_cvt_pk_bf16_f32 v62, v62, v63
	v_cvt_pk_bf16_f32 v63, v64, v65
	v_and_b32_e32 v70, 0xfcf, v66
	v_ashrrev_i32_e32 v66, 9, v66
	v_and_b32_e32 v71, -8, v66
	v_add_u32_e32 v66, v71, v172
	v_cvt_pk_bf16_f32 v64, v58, v59
	v_add_u32_e32 v58, v128, v71
	v_ashrrev_i32_e32 v67, 31, v66
	v_ashrrev_i32_e32 v59, 31, v58
	v_lshlrev_b64 v[66:67], 12, v[66:67]
	v_lshlrev_b64 v[58:59], 12, v[58:59]
	v_or_b32_e32 v68, v66, v70
	v_cvt_pk_bf16_f32 v65, v60, v61
	v_or_b32_e32 v60, v58, v70
	v_mad_u64_u32 v[68:69], s[20:21], v68, s57, v[142:143]
	v_mad_u64_u32 v[60:61], s[20:21], v60, s57, v[142:143]
	v_mad_i32_i24 v69, v67, s57, v69
	v_mad_i32_i24 v61, v59, s57, v61
	v_lshl_add_u64 v[68:69], v[68:69], 0, v[166:167]
	v_lshl_add_u64 v[60:61], v[60:61], 0, v[122:123]
	v_cvt_pk_bf16_f32 v46, v46, v47
	v_cvt_pk_bf16_f32 v47, v48, v49
	v_cvt_pk_bf16_f32 v48, v42, v43
	v_cvt_pk_bf16_f32 v49, v44, v45
	global_store_dwordx4 v[68:69], v[62:65], off
	global_store_dwordx4 v[60:61], v[46:49], off
	v_cvt_pk_bf16_f32 v44, v50, v51
	v_cvt_pk_bf16_f32 v45, v52, v53
	v_or_b32_e32 v48, 16, v70
	v_or_b32_e32 v42, v66, v48
	v_mad_u64_u32 v[42:43], s[20:21], v42, s57, v[142:143]
	v_mad_i32_i24 v43, v67, s57, v43
	v_lshl_add_u64 v[46:47], v[42:43], 0, v[166:167]
	v_cvt_pk_bf16_f32 v42, v54, v55
	v_cvt_pk_bf16_f32 v43, v56, v57
	global_store_dwordx4 v[46:47], v[42:45], off
	v_cvt_pk_bf16_f32 v30, v30, v31
	v_cvt_pk_bf16_f32 v31, v32, v33
	v_or_b32_e32 v42, v58, v48
	v_mad_u64_u32 v[42:43], s[20:21], v42, s57, v[142:143]
	v_mad_i32_i24 v43, v59, s57, v43
	v_lshl_add_u64 v[42:43], v[42:43], 0, v[122:123]
	v_cvt_pk_bf16_f32 v32, v26, v27
	v_cvt_pk_bf16_f32 v33, v28, v29
	global_store_dwordx4 v[42:43], v[30:33], off
	v_cvt_pk_bf16_f32 v28, v34, v35
	v_cvt_pk_bf16_f32 v29, v36, v37
	v_or_b32_e32 v32, 32, v70
	v_or_b32_e32 v26, v66, v32
	v_mad_u64_u32 v[26:27], s[20:21], v26, s57, v[142:143]
	v_mad_i32_i24 v27, v67, s57, v27
	v_lshl_add_u64 v[30:31], v[26:27], 0, v[166:167]
	v_cvt_pk_bf16_f32 v26, v38, v39
	v_cvt_pk_bf16_f32 v27, v40, v41
	global_store_dwordx4 v[30:31], v[26:29], off
	v_cvt_pk_bf16_f32 v14, v14, v15
	v_cvt_pk_bf16_f32 v15, v16, v17
	v_or_b32_e32 v26, v58, v32
	v_mad_u64_u32 v[26:27], s[20:21], v26, s57, v[142:143]
	v_mad_i32_i24 v27, v59, s57, v27
	v_lshl_add_u64 v[26:27], v[26:27], 0, v[122:123]
	v_cvt_pk_bf16_f32 v16, v10, v11
	v_cvt_pk_bf16_f32 v17, v12, v13
	global_store_dwordx4 v[26:27], v[14:17], off
	v_cvt_pk_bf16_f32 v12, v18, v19
	v_cvt_pk_bf16_f32 v13, v20, v21
	v_or_b32_e32 v16, 48, v70
	v_or_b32_e32 v10, v66, v16
	v_mad_u64_u32 v[10:11], s[20:21], v10, s57, v[142:143]
	v_mad_i32_i24 v11, v67, s57, v11
	v_lshl_add_u64 v[14:15], v[10:11], 0, v[166:167]
	v_cvt_pk_bf16_f32 v10, v22, v23
	v_cvt_pk_bf16_f32 v11, v24, v25
	global_store_dwordx4 v[14:15], v[10:13], off
	v_cvt_pk_bf16_f32 v6, v6, v7
	v_cvt_pk_bf16_f32 v7, v8, v9
	v_or_b32_e32 v10, v58, v16
	v_mad_u64_u32 v[10:11], s[20:21], v10, s57, v[142:143]
	v_mad_i32_i24 v11, v59, s57, v11
	v_lshl_add_u64 v[10:11], v[10:11], 0, v[122:123]
	v_cvt_pk_bf16_f32 v8, v2, v3
	v_cvt_pk_bf16_f32 v9, v4, v5
	s_and_b64 vcc, exec, s[16:17]
	s_mov_b32 s58, s64
	s_mov_b32 s56, s63
	s_mov_b64 s[20:21], s[18:19]
	global_store_dwordx4 v[10:11], v[6:9], off
	s_cbranch_vccz .LBB0_545
	s_waitcnt vmcnt(0)
	s_cmpk_gt_u32 s29, 0xff
	s_cbranch_scc1 .LBB0_550
	s_barrier

; #define LAS __attribute__((address_space(3)))
; #define G_GATHER_OFFS(tab_, rv_) do { _Pragma("unroll") for (int i = 0; i < 2; ++i) { int R_, C_; G_SRC(i, R_, C_); const int ra_ = (tab_)[R_], rb_ = (tab_)[HALF + R_];        \
;     vAc[0][i] = (unsigned)((R_ < (rv_) ? ra_ : 0) * KB + C_); vAc[1][i] = (unsigned)((HALF + R_ < (rv_) ? rb_ : 0) * KB + C_); } } while (0)
; #define G_STAGE(bufoff, gbase, voff) do { _Pragma("unroll") for (int _i = 0; _i < 2; ++_i) \
;     __builtin_amdgcn_global_load_lds((const unsigned*)((const char*)(gbase) + (voff)[_i]), (LAS unsigned*)(lds + (bufoff) + ldsw + _i * 8192), 16, 0, 0); } while (0)
; #define G_LDA(dst, b, h) do { _Pragma("unroll") for (int m = 0; m < 4; ++m) dst[m] = G_LD2(G_SA(b, h) + aoff + m * 2048, G_SA(b, h) + (P::FP8 ? aoff1 : aoff + 1024) + m * 2048); } while (0)
; #define G_LDB(dst, b, h) do { _Pragma("unroll") for (int n = 0; n < 2; ++n) dst[n] = G_LD2(G_SB(b, h) + boff + n * 2048, G_SB(b, h) + (P::FP8 ? boff1 : boff + 1024) + n * 2048); } while (0)
; #define WAIT_V(n) asm volatile("s_waitcnt vmcnt(" #n ")" ::: "memory")
; #define WAIT_L(n) asm volatile("s_waitcnt lgkmcnt(" #n ")" ::: "memory")
; #define BAR __builtin_amdgcn_s_barrier()
; #define SCHED __builtin_amdgcn_sched_barrier(0)
; template <class P>
; DEV void gemm_stream(const P& pol) {
;     ...
;     for (int t = 0; t < nt; t += 2) {
;       const bool last = (t == nt - 2);
;       const size_t k1 = (size_t)(t + 1) * kstep, k2 = (size_t)(t + 2) * kstep;
;       const char* a20 = last ? nA0 : cA0 + k2; const char* a21 = last ? nA1 : cA1 + k2; const char* b2 = last ? nB : cB + k2;
;       G_LDB(B0, 0, 0); SCHED; G_LDA(At, 0, 0); G_STAGE(G_SA(1, 1), cA1 + k1, vAc[1]);
;       WAIT_L(8); BAR; WAIT_L(0); G_MMA(0, 0, At, B0); BAR; SCHED;
;       if (P::GATHER && last && has_next) { LAS int* tab = arow + ((ui + 1) & 1) * 256; G_GATHER_OFFS(tab, nxt.rv); }
;       G_LDB(B1, 0, 1); G_STAGE(G_SB(0, 0), b2, voffB);
;       BAR; WAIT_L(0); G_MMA(0, 1, At, B1); BAR;
;       G_LDA(At, 0, 1); G_STAGE(G_SA(0, 0), a20, vAc[0]);
;       BAR; WAIT_L(0); G_MMA(1, 0, At, B0); BAR; SCHED;
;       G_STAGE(G_SB(0, 1), b2 + hstep, voffB);
;       WAIT_V(6); BAR; G_MMA(1, 1, At, B1); BAR;
.LBB0_1243:
	s_add_u32 s24, s73, s22
	s_addc_u32 s25, s76, s23
	s_add_u32 s26, s20, s22
	ds_read_b128 v[164:167], v1
	ds_read_b128 v[168:171], v148
	ds_read_b128 v[172:175], v155
	ds_read_b128 v[176:179], v156
	s_addc_u32 s27, s21, s23
	s_add_u32 s26, s26, 0x100
	s_addc_u32 s27, s27, 0
	s_add_u32 s80, s71, s22
	s_addc_u32 s81, s72, s23
	s_cmpk_eq_i32 s22, 0xf00
	s_cselect_b32 s27, s67, s27
	s_cselect_b32 s26, s68, s26
	s_mov_b32 m0, s59
	v_lshl_add_u64 v[212:213], v[146:147], 0, s[22:23]
	ds_read_b128 v[180:183], v163
	ds_read_b128 v[184:187], v163 offset:1024
	ds_read_b128 v[188:191], v163 offset:2048
	ds_read_b128 v[192:195], v163 offset:3072
	ds_read_b128 v[196:199], v163 offset:4096
	ds_read_b128 v[200:203], v163 offset:5120
	ds_read_b128 v[204:207], v163 offset:6144
	ds_read_b128 v[208:211], v163 offset:7168
	global_load_lds_dwordx4 v[212:213], off
	v_lshl_add_u64 v[212:213], v[144:145], 0, s[22:23]
	s_mov_b32 m0, s60
	s_cselect_b32 s79, s65, s25
	global_load_lds_dwordx4 v[212:213], off
	s_waitcnt lgkmcnt(8)
	s_barrier
	s_waitcnt lgkmcnt(0)
	s_cselect_b32 s78, s66, s24
	s_setprio 1
	v_mfma_f32_16x16x32_bf16 v[126:129], v[164:167], v[180:183], v[126:129]
	v_mfma_f32_16x16x32_bf16 v[122:125], v[172:175], v[180:183], v[122:125]
	v_mfma_f32_16x16x32_bf16 v[118:121], v[164:167], v[188:191], v[118:121]
	v_mfma_f32_16x16x32_bf16 v[114:117], v[172:175], v[188:191], v[114:117]
	v_mfma_f32_16x16x32_bf16 v[110:113], v[164:167], v[196:199], v[110:113]
	v_mfma_f32_16x16x32_bf16 v[106:109], v[172:175], v[196:199], v[106:109]
	v_mfma_f32_16x16x32_bf16 v[102:105], v[164:167], v[204:207], v[102:105]
	v_mfma_f32_16x16x32_bf16 v[98:101], v[172:175], v[204:207], v[98:101]
	v_mfma_f32_16x16x32_bf16 v[126:129], v[168:171], v[184:187], v[126:129]
	v_mfma_f32_16x16x32_bf16 v[122:125], v[176:179], v[184:187], v[122:125]
	v_mfma_f32_16x16x32_bf16 v[118:121], v[168:171], v[192:195], v[118:121]
	v_mfma_f32_16x16x32_bf16 v[114:117], v[176:179], v[192:195], v[114:117]
	v_mfma_f32_16x16x32_bf16 v[110:113], v[168:171], v[200:203], v[110:113]
	v_mfma_f32_16x16x32_bf16 v[106:109], v[176:179], v[200:203], v[106:109]
	v_mfma_f32_16x16x32_bf16 v[102:105], v[168:171], v[208:211], v[102:105]
	v_mfma_f32_16x16x32_bf16 v[98:101], v[176:179], v[208:211], v[98:101]
	s_setprio 0
	s_barrier
	s_cselect_b32 s25, s69, s81
	s_cselect_b32 s24, s70, s80
	s_mov_b32 m0, s30
	v_lshl_add_u64 v[220:221], s[24:25], 0, v[130:131]
	ds_read_b128 v[212:215], v149
	ds_read_b128 v[216:219], v150
	ds_read_b128 v[224:227], v157
	ds_read_b128 v[228:231], v158
	global_load_lds_dwordx4 v[220:221], off
	v_lshl_add_u64 v[232:233], s[24:25], 0, v[132:133]
	s_mov_b32 m0, s31
	s_nop 0
	global_load_lds_dwordx4 v[232:233], off
	s_barrier
	s_waitcnt lgkmcnt(0)
	s_setprio 1
	v_mfma_f32_16x16x32_bf16 v[94:97], v[212:215], v[180:183], v[94:97]
	v_mfma_f32_16x16x32_bf16 v[90:93], v[224:227], v[180:183], v[90:93]
	v_mfma_f32_16x16x32_bf16 v[86:89], v[212:215], v[188:191], v[86:89]
	v_mfma_f32_16x16x32_bf16 v[82:85], v[224:227], v[188:191], v[82:85]
	v_mfma_f32_16x16x32_bf16 v[78:81], v[212:215], v[196:199], v[78:81]
	v_mfma_f32_16x16x32_bf16 v[74:77], v[224:227], v[196:199], v[74:77]
	v_mfma_f32_16x16x32_bf16 v[70:73], v[212:215], v[204:207], v[70:73]
	v_mfma_f32_16x16x32_bf16 v[66:69], v[224:227], v[204:207], v[66:69]
	v_mfma_f32_16x16x32_bf16 v[94:97], v[216:219], v[184:187], v[94:97]
	v_mfma_f32_16x16x32_bf16 v[90:93], v[228:231], v[184:187], v[90:93]
	v_mfma_f32_16x16x32_bf16 v[86:89], v[216:219], v[192:195], v[86:89]
	v_mfma_f32_16x16x32_bf16 v[82:85], v[228:231], v[192:195], v[82:85]
	v_mfma_f32_16x16x32_bf16 v[78:81], v[216:219], v[200:203], v[78:81]
	v_mfma_f32_16x16x32_bf16 v[74:77], v[228:231], v[200:203], v[74:77]
	v_mfma_f32_16x16x32_bf16 v[70:73], v[216:219], v[208:211], v[70:73]
	v_mfma_f32_16x16x32_bf16 v[66:69], v[228:231], v[208:211], v[66:69]
	s_setprio 0
	s_mov_b32 m0, s29
	v_lshl_add_u64 v[234:235], s[78:79], 0, v[134:135]
	s_barrier
	ds_read_b128 v[180:183], v163 offset:16384
	ds_read_b128 v[184:187], v163 offset:17408
	ds_read_b128 v[188:191], v163 offset:18432
	ds_read_b128 v[192:195], v163 offset:19456
	ds_read_b128 v[196:199], v163 offset:20480
	ds_read_b128 v[200:203], v163 offset:21504
	ds_read_b128 v[204:207], v163 offset:22528
	ds_read_b128 v[208:211], v163 offset:23552
	global_load_lds_dwordx4 v[234:235], off
	v_lshl_add_u64 v[236:237], s[78:79], 0, v[136:137]
	s_mov_b32 m0, s34
	s_nop 0
	global_load_lds_dwordx4 v[236:237], off
	s_barrier
	s_waitcnt lgkmcnt(0)
	s_setprio 1
	v_mfma_f32_16x16x32_bf16 v[62:65], v[164:167], v[180:183], v[62:65]
	v_mfma_f32_16x16x32_bf16 v[58:61], v[172:175], v[180:183], v[58:61]
	v_mfma_f32_16x16x32_bf16 v[54:57], v[164:167], v[188:191], v[54:57]
	v_mfma_f32_16x16x32_bf16 v[50:53], v[172:175], v[188:191], v[50:53]
	v_mfma_f32_16x16x32_bf16 v[46:49], v[164:167], v[196:199], v[46:49]
	v_mfma_f32_16x16x32_bf16 v[42:45], v[172:175], v[196:199], v[42:45]
	v_mfma_f32_16x16x32_bf16 v[38:41], v[164:167], v[204:207], v[38:41]
	v_mfma_f32_16x16x32_bf16 v[34:37], v[172:175], v[204:207], v[34:37]
	v_mfma_f32_16x16x32_bf16 v[62:65], v[168:171], v[184:187], v[62:65]
	v_mfma_f32_16x16x32_bf16 v[58:61], v[176:179], v[184:187], v[58:61]
	v_mfma_f32_16x16x32_bf16 v[54:57], v[168:171], v[192:195], v[54:57]
	v_mfma_f32_16x16x32_bf16 v[50:53], v[176:179], v[192:195], v[50:53]
	v_mfma_f32_16x16x32_bf16 v[46:49], v[168:171], v[200:203], v[46:49]
	v_mfma_f32_16x16x32_bf16 v[42:45], v[176:179], v[200:203], v[42:45]
	v_mfma_f32_16x16x32_bf16 v[38:41], v[168:171], v[208:211], v[38:41]
	v_mfma_f32_16x16x32_bf16 v[34:37], v[176:179], v[208:211], v[34:37]
	s_setprio 0
	s_barrier
; #define G_STAGE(bufoff, gbase, voff) do { _Pragma("unroll") for (int _i = 0; _i < 2; ++_i) \
;     __builtin_amdgcn_global_load_lds((const unsigned*)((const char*)(gbase) + (voff)[_i]), (LAS unsigned*)(lds + (bufoff) + ldsw + _i * 8192), 16, 0, 0); } while (0)
; #define G_LDA(dst, b, h) do { _Pragma("unroll") for (int m = 0; m < 4; ++m) dst[m] = G_LD2(G_SA(b, h) + aoff + m * 2048, G_SA(b, h) + (P::FP8 ? aoff1 : aoff + 1024) + m * 2048); } while (0)
; #define G_LDB(dst, b, h) do { _Pragma("unroll") for (int n = 0; n < 2; ++n) dst[n] = G_LD2(G_SB(b, h) + boff + n * 2048, G_SB(b, h) + (P::FP8 ? boff1 : boff + 1024) + n * 2048); } while (0)
; #define WAIT_V(n) asm volatile("s_waitcnt vmcnt(" #n ")" ::: "memory")
; #define WAIT_L(n) asm volatile("s_waitcnt lgkmcnt(" #n ")" ::: "memory")
; #define BAR __builtin_amdgcn_s_barrier()
; #define SCHED __builtin_amdgcn_sched_barrier(0)
; template <class P>
; DEV void gemm_stream(const P& pol) {
;     ...
;       WAIT_V(6); BAR; G_MMA(1, 1, At, B1); BAR;
;       G_LDB(B0, 1, 0); SCHED; G_LDA(At, 1, 0); G_STAGE(G_SA(0, 1), a21, vAc[1]);
;       WAIT_L(8); BAR; WAIT_L(0); G_MMA(0, 0, At, B0); BAR; SCHED;
;       G_LDB(B1, 1, 1); G_STAGE(G_SB(1, 0), b2 + kstep, voffB);
;       BAR; WAIT_L(0); G_MMA(0, 1, At, B1); BAR;
;       G_LDA(At, 1, 1); G_STAGE(G_SA(1, 0), a20 + kstep, vAc[0]);
;       BAR; WAIT_L(0); G_MMA(1, 0, At, B0); BAR; SCHED;
	s_add_u32 s78, s24, 0x80000
	s_addc_u32 s79, s25, 0
	s_mov_b32 m0, s35
	v_lshl_add_u64 v[164:165], s[78:79], 0, v[130:131]
	global_load_lds_dwordx4 v[164:165], off
	v_lshl_add_u64 v[164:165], s[78:79], 0, v[132:133]
	s_mov_b32 m0, s36
	s_nop 0
	global_load_lds_dwordx4 v[164:165], off
	s_waitcnt vmcnt(6)
	s_barrier
	s_setprio 1
	v_mfma_f32_16x16x32_bf16 v[30:33], v[212:215], v[180:183], v[30:33]
	v_mfma_f32_16x16x32_bf16 v[26:29], v[224:227], v[180:183], v[26:29]
	v_mfma_f32_16x16x32_bf16 v[22:25], v[212:215], v[188:191], v[22:25]
	v_mfma_f32_16x16x32_bf16 v[18:21], v[224:227], v[188:191], v[18:21]
	v_mfma_f32_16x16x32_bf16 v[14:17], v[212:215], v[196:199], v[14:17]
	v_mfma_f32_16x16x32_bf16 v[10:13], v[224:227], v[196:199], v[10:13]
	v_mfma_f32_16x16x32_bf16 v[6:9], v[212:215], v[204:207], v[6:9]
	v_mfma_f32_16x16x32_bf16 v[2:5], v[224:227], v[204:207], v[2:5]
	v_mfma_f32_16x16x32_bf16 v[30:33], v[216:219], v[184:187], v[30:33]
	v_mfma_f32_16x16x32_bf16 v[26:29], v[228:231], v[184:187], v[26:29]
	v_mfma_f32_16x16x32_bf16 v[22:25], v[216:219], v[192:195], v[22:25]
	v_mfma_f32_16x16x32_bf16 v[18:21], v[228:231], v[192:195], v[18:21]
	v_mfma_f32_16x16x32_bf16 v[14:17], v[216:219], v[200:203], v[14:17]
	v_mfma_f32_16x16x32_bf16 v[10:13], v[228:231], v[200:203], v[10:13]
	v_mfma_f32_16x16x32_bf16 v[6:9], v[216:219], v[208:211], v[6:9]
	v_mfma_f32_16x16x32_bf16 v[2:5], v[228:231], v[208:211], v[2:5]
	s_setprio 0
	s_barrier
	ds_read_b128 v[164:167], v151
	ds_read_b128 v[168:171], v152
	ds_read_b128 v[172:175], v159
	ds_read_b128 v[176:179], v160
	s_mov_b32 m0, s37
	v_lshl_add_u64 v[212:213], s[26:27], 0, v[134:135]
	ds_read_b128 v[180:183], v163 offset:32768
	ds_read_b128 v[184:187], v163 offset:33792
	ds_read_b128 v[188:191], v163 offset:34816
	ds_read_b128 v[192:195], v163 offset:35840
	ds_read_b128 v[196:199], v163 offset:36864
	ds_read_b128 v[200:203], v163 offset:37888
	ds_read_b128 v[204:207], v163 offset:38912
	ds_read_b128 v[208:211], v163 offset:39936
	global_load_lds_dwordx4 v[212:213], off
	v_lshl_add_u64 v[212:213], s[26:27], 0, v[136:137]
	s_mov_b32 m0, s38
	s_nop 0
	global_load_lds_dwordx4 v[212:213], off
	s_waitcnt lgkmcnt(8)
	s_barrier
	s_waitcnt lgkmcnt(0)
	s_setprio 1
	v_mfma_f32_16x16x32_bf16 v[126:129], v[164:167], v[180:183], v[126:129]
	v_mfma_f32_16x16x32_bf16 v[122:125], v[172:175], v[180:183], v[122:125]
	v_mfma_f32_16x16x32_bf16 v[118:121], v[164:167], v[188:191], v[118:121]
	v_mfma_f32_16x16x32_bf16 v[114:117], v[172:175], v[188:191], v[114:117]
	v_mfma_f32_16x16x32_bf16 v[110:113], v[164:167], v[196:199], v[110:113]
	v_mfma_f32_16x16x32_bf16 v[106:109], v[172:175], v[196:199], v[106:109]
	v_mfma_f32_16x16x32_bf16 v[102:105], v[164:167], v[204:207], v[102:105]
	v_mfma_f32_16x16x32_bf16 v[98:101], v[172:175], v[204:207], v[98:101]
	v_mfma_f32_16x16x32_bf16 v[126:129], v[168:171], v[184:187], v[126:129]
	v_mfma_f32_16x16x32_bf16 v[122:125], v[176:179], v[184:187], v[122:125]
	v_mfma_f32_16x16x32_bf16 v[118:121], v[168:171], v[192:195], v[118:121]
	v_mfma_f32_16x16x32_bf16 v[114:117], v[176:179], v[192:195], v[114:117]
	v_mfma_f32_16x16x32_bf16 v[110:113], v[168:171], v[200:203], v[110:113]
	v_mfma_f32_16x16x32_bf16 v[106:109], v[176:179], v[200:203], v[106:109]
	v_mfma_f32_16x16x32_bf16 v[102:105], v[168:171], v[208:211], v[102:105]
	v_mfma_f32_16x16x32_bf16 v[98:101], v[176:179], v[208:211], v[98:101]
	s_setprio 0
	s_barrier
	s_mov_b32 m0, s45
	v_lshl_add_u64 v[220:221], v[220:221], 0, s[14:15]
	ds_read_b128 v[212:215], v153
	ds_read_b128 v[216:219], v154
	ds_read_b128 v[224:227], v161
	ds_read_b128 v[228:231], v162
	global_load_lds_dwordx4 v[220:221], off
	v_lshl_add_u64 v[220:221], v[232:233], 0, s[14:15]
	s_mov_b32 m0, s46
	s_nop 0
	global_load_lds_dwordx4 v[220:221], off
	s_barrier
	s_waitcnt lgkmcnt(0)
	s_setprio 1
	v_mfma_f32_16x16x32_bf16 v[94:97], v[212:215], v[180:183], v[94:97]
	v_mfma_f32_16x16x32_bf16 v[90:93], v[224:227], v[180:183], v[90:93]
	v_mfma_f32_16x16x32_bf16 v[86:89], v[212:215], v[188:191], v[86:89]
	v_mfma_f32_16x16x32_bf16 v[82:85], v[224:227], v[188:191], v[82:85]
	v_mfma_f32_16x16x32_bf16 v[78:81], v[212:215], v[196:199], v[78:81]
	v_mfma_f32_16x16x32_bf16 v[74:77], v[224:227], v[196:199], v[74:77]
	v_mfma_f32_16x16x32_bf16 v[70:73], v[212:215], v[204:207], v[70:73]
	v_mfma_f32_16x16x32_bf16 v[66:69], v[224:227], v[204:207], v[66:69]
	v_mfma_f32_16x16x32_bf16 v[94:97], v[216:219], v[184:187], v[94:97]
	v_mfma_f32_16x16x32_bf16 v[90:93], v[228:231], v[184:187], v[90:93]
	v_mfma_f32_16x16x32_bf16 v[86:89], v[216:219], v[192:195], v[86:89]
	v_mfma_f32_16x16x32_bf16 v[82:85], v[228:231], v[192:195], v[82:85]
	v_mfma_f32_16x16x32_bf16 v[78:81], v[216:219], v[200:203], v[78:81]
	v_mfma_f32_16x16x32_bf16 v[74:77], v[228:231], v[200:203], v[74:77]
	v_mfma_f32_16x16x32_bf16 v[70:73], v[216:219], v[208:211], v[70:73]
	v_mfma_f32_16x16x32_bf16 v[66:69], v[228:231], v[208:211], v[66:69]
	s_setprio 0
	s_mov_b32 m0, s47
	v_lshl_add_u64 v[220:221], v[234:235], 0, s[14:15]
	s_barrier
	ds_read_b128 v[180:183], v163 offset:49152
	ds_read_b128 v[184:187], v163 offset:50176
	ds_read_b128 v[188:191], v163 offset:51200
	ds_read_b128 v[192:195], v163 offset:52224
	ds_read_b128 v[196:199], v163 offset:53248
	ds_read_b128 v[200:203], v163 offset:54272
	ds_read_b128 v[204:207], v163 offset:55296
	ds_read_b128 v[208:211], v163 offset:56320
	global_load_lds_dwordx4 v[220:221], off
	v_lshl_add_u64 v[220:221], v[236:237], 0, s[14:15]
	s_mov_b32 m0, s52
	s_nop 0
	global_load_lds_dwordx4 v[220:221], off
	s_barrier
; DEV int ltid() { int t = threadIdx.x; asm volatile("" : "+v"(t)); return t; }
; DEV CParams* launder(CParams* p) { asm volatile("" : "+s"(p)); return p; }
; template <class P>
; DEV void gemm_stream(const P& pol) {
;     ...
;       BAR; WAIT_L(0); G_MMA(1, 0, At, B0); BAR; SCHED;
;       G_STAGE(G_SB(1, 1), b2 + hstep + kstep, voffB);
;       WAIT_V(6); BAR; G_MMA(1, 1, At, B1); BAR;
; template <int LB> DEV void stage_store_block(const unsigned (&v)[4][LB / 4], unsigned char* dst, long row_stride) {
;   extern __shared__ __attribute__((aligned(16))) char shm[];
;   constexpr int MP = LB == 8 ? 4 : (LB == 16 ? 2 : 1), PITCH = 16 * LB + 16, ROWS = 16 * MP;
;   static_assert(ROWS * PITCH <= STG_HALF, "staging region");
;   const int tid = ltid(), wr = tid >> 8, wc = (tid >> 6) & 3, fr = tid & 15, fq = (tid >> 4) & 3;
;   char* stg = shm + STG_OFF + wr * STG_HALF;
;   const int t4 = tid & 255;
; #pragma unroll
;   for (int ps = 0; ps < 4 / MP; ++ps) {
; #pragma unroll
;     for (int mm = 0; mm < MP; ++mm) {
;       char* wp = stg + (16 * mm + fr) * PITCH + (4 * wc + fq) * LB; const int m = ps * MP + mm;
;       if (LB == 8) *(u32x2*)wp = (u32x2){v[m][0], v[m][1]};
;       else { *(u32x4*)wp = (u32x4){v[m][0], v[m][1], v[m][2], v[m][3]}; if (LB == 32) *(u32x4*)(wp + 16) = (u32x4){v[m][LB / 4 - 4], v[m][LB / 4 - 3], v[m][LB / 4 - 2], v[m][LB / 4 - 1]}; }
;     }
;     asm volatile("s_waitcnt lgkmcnt(0)" ::: "memory"); __builtin_amdgcn_s_barrier(); asm volatile("" ::: "memory");
; #pragma unroll
;     for (int k = 0; k < 2; ++k) { const int idx = k * 256 + t4, row = idx / LB, ch = idx % LB;
;       *(u32x4*)(dst + (long)(ps * ROWS + row) * row_stride + ch * 16) = *(const u32x4*)(stg + row * PITCH + ch * 16); }
;     asm volatile("s_waitcnt lgkmcnt(0)" ::: "memory"); __builtin_amdgcn_s_barrier(); asm volatile("" ::: "memory");
;   }
; DEV void EpiOut::operator()(const AccT& acc, int wr, int wc, int fr, int fq) const {
;   CParams& P = *launder(p);
; #pragma unroll
;   for (int ai = 0; ai < 2; ++ai)
; #pragma unroll
;     for (int bj = 0; bj < 2; ++bj) {
;       unsigned vals[4][4];
; #pragma unroll
;       for (int m = 0; m < 4; ++m) pk_bf16x8(vals[m], acc[ai][bj][m][0], acc[ai][bj][m][1]);
;       stage_store_block<16>(vals, (unsigned char*)(P.mix + (long)(pm * BM + ai * HALF + wr * 64) * DM + pn * 256 + bj * HALF), DM * 2);
;     }
	s_waitcnt lgkmcnt(0)
	s_setprio 1
	v_mfma_f32_16x16x32_bf16 v[62:65], v[164:167], v[180:183], v[62:65]
	v_mfma_f32_16x16x32_bf16 v[58:61], v[172:175], v[180:183], v[58:61]
	v_mfma_f32_16x16x32_bf16 v[54:57], v[164:167], v[188:191], v[54:57]
	v_mfma_f32_16x16x32_bf16 v[50:53], v[172:175], v[188:191], v[50:53]
	v_mfma_f32_16x16x32_bf16 v[46:49], v[164:167], v[196:199], v[46:49]
	v_mfma_f32_16x16x32_bf16 v[42:45], v[172:175], v[196:199], v[42:45]
	v_mfma_f32_16x16x32_bf16 v[38:41], v[164:167], v[204:207], v[38:41]
	v_mfma_f32_16x16x32_bf16 v[34:37], v[172:175], v[204:207], v[34:37]
	v_mfma_f32_16x16x32_bf16 v[62:65], v[168:171], v[184:187], v[62:65]
	v_mfma_f32_16x16x32_bf16 v[58:61], v[176:179], v[184:187], v[58:61]
	v_mfma_f32_16x16x32_bf16 v[54:57], v[168:171], v[192:195], v[54:57]
	v_mfma_f32_16x16x32_bf16 v[50:53], v[176:179], v[192:195], v[50:53]
	v_mfma_f32_16x16x32_bf16 v[46:49], v[168:171], v[200:203], v[46:49]
	v_mfma_f32_16x16x32_bf16 v[42:45], v[176:179], v[200:203], v[42:45]
	v_mfma_f32_16x16x32_bf16 v[38:41], v[168:171], v[208:211], v[38:41]
	v_mfma_f32_16x16x32_bf16 v[34:37], v[176:179], v[208:211], v[34:37]
	s_setprio 0
	s_barrier
	s_add_u32 s24, s24, 0x80080
	s_addc_u32 s25, s25, 0
	s_mov_b32 m0, s53
	v_lshl_add_u64 v[164:165], s[24:25], 0, v[130:131]
	global_load_lds_dwordx4 v[164:165], off
	v_lshl_add_u64 v[164:165], s[24:25], 0, v[132:133]
	s_mov_b32 m0, s54
	s_nop 0
	global_load_lds_dwordx4 v[164:165], off
	s_waitcnt vmcnt(6)
	s_barrier
	s_setprio 1
	v_mfma_f32_16x16x32_bf16 v[30:33], v[212:215], v[180:183], v[30:33]
	v_mfma_f32_16x16x32_bf16 v[26:29], v[224:227], v[180:183], v[26:29]
	v_mfma_f32_16x16x32_bf16 v[22:25], v[212:215], v[188:191], v[22:25]
	v_mfma_f32_16x16x32_bf16 v[18:21], v[224:227], v[188:191], v[18:21]
	v_mfma_f32_16x16x32_bf16 v[14:17], v[212:215], v[196:199], v[14:17]
	v_mfma_f32_16x16x32_bf16 v[10:13], v[224:227], v[196:199], v[10:13]
	v_mfma_f32_16x16x32_bf16 v[6:9], v[212:215], v[204:207], v[6:9]
	v_mfma_f32_16x16x32_bf16 v[2:5], v[224:227], v[204:207], v[2:5]
	v_mfma_f32_16x16x32_bf16 v[30:33], v[216:219], v[184:187], v[30:33]
	v_mfma_f32_16x16x32_bf16 v[26:29], v[228:231], v[184:187], v[26:29]
	v_mfma_f32_16x16x32_bf16 v[22:25], v[216:219], v[192:195], v[22:25]
	v_mfma_f32_16x16x32_bf16 v[18:21], v[228:231], v[192:195], v[18:21]
	v_mfma_f32_16x16x32_bf16 v[14:17], v[216:219], v[200:203], v[14:17]
	v_mfma_f32_16x16x32_bf16 v[10:13], v[228:231], v[200:203], v[10:13]
	v_mfma_f32_16x16x32_bf16 v[6:9], v[216:219], v[208:211], v[6:9]
	v_mfma_f32_16x16x32_bf16 v[2:5], v[228:231], v[208:211], v[2:5]
	s_setprio 0
	s_add_i32 s77, s77, 2
	s_add_u32 s22, s22, 0x100
	s_addc_u32 s23, s23, 0
	s_cmp_gt_u32 s77, 29
	s_barrier
	s_cbranch_scc0 .LBB0_1243
	s_mov_b64 s[20:21], s[4:5]
	s_load_dwordx2 s[20:21], s[20:21], 0x1a0
	s_lshl_b32 s22, s63, 8
	v_cvt_pk_bf16_f32 v102, v102, v103
	v_cvt_pk_bf16_f32 v103, v104, v105
	v_cvt_pk_bf16_f32 v104, v98, v99
	s_add_i32 s22, s22, s44
	v_mov_b32_e32 v98, v0
	s_ashr_i32 s23, s22, 31
	v_cvt_pk_bf16_f32 v126, v126, v127
	v_cvt_pk_bf16_f32 v127, v128, v129
	v_cvt_pk_bf16_f32 v128, v122, v123
	v_cvt_pk_bf16_f32 v110, v110, v111
	v_cvt_pk_bf16_f32 v111, v112, v113
	v_cvt_pk_bf16_f32 v112, v106, v107
	v_cvt_pk_bf16_f32 v105, v100, v101
	s_lshl_b64 s[22:23], s[22:23], 12
	v_lshrrev_b32_e32 v99, 8, v98
	v_and_b32_e32 v100, 15, v98
	v_mov_b32_e32 v122, s55
	v_and_b32_e32 v106, 0xf0, v98
	v_lshlrev_b32_e32 v101, 4, v98
	v_bfe_u32 v98, v98, 4, 4
	s_waitcnt lgkmcnt(0)
	s_add_u32 s22, s20, s22
	v_mad_i32_i24 v99, v99, s56, v122
	v_and_b32_e32 v138, 0xf0, v101
	v_mul_u32_u24_e32 v98, 0x110, v98
	s_addc_u32 s23, s21, s23
	s_lshl_b32 s20, s64, 8
	v_add3_u32 v123, v99, v138, v98
	v_mul_u32_u24_e32 v98, 0x110, v100
	v_cvt_pk_bf16_f32 v129, v124, v125
	s_ashr_i32 s21, s20, 31
	v_add3_u32 v124, v99, v106, v98
	v_cvt_pk_bf16_f32 v118, v118, v119
	v_cvt_pk_bf16_f32 v119, v120, v121
	v_cvt_pk_bf16_f32 v120, v114, v115
	v_cvt_pk_bf16_f32 v121, v116, v117
	s_lshl_b64 s[20:21], s[20:21], 1
	ds_write_b128 v124, v[126:129]
	ds_write_b128 v124, v[118:121] offset:4352
	s_add_u32 s20, s22, s20
	s_waitcnt lgkmcnt(0)
	s_barrier
	s_addc_u32 s21, s23, s21
	ds_read_b128 v[98:101], v123
	v_cvt_pk_bf16_f32 v113, v108, v109
	v_lshl_add_u64 v[114:115], s[20:21], 0, v[138:139]
	v_lshlrev_b32_e32 v138, 8, v106
	ds_read_b128 v[106:109], v123 offset:4352
	v_lshl_add_u64 v[116:117], v[114:115], 0, v[138:139]
	v_or_b32_e32 v138, 0x10000, v138
	s_waitcnt lgkmcnt(0)
	global_store_dwordx4 v[116:117], v[98:101], off
	v_cvt_pk_bf16_f32 v70, v70, v71
	v_cvt_pk_bf16_f32 v71, v72, v73
	v_lshl_add_u64 v[98:99], v[114:115], 0, v[138:139]
	global_store_dwordx4 v[98:99], v[106:109], off
	s_waitcnt lgkmcnt(0)
	s_barrier
	ds_write_b128 v124, v[110:113]
	ds_write_b128 v124, v[102:105] offset:4352
	s_waitcnt lgkmcnt(0)
	s_barrier
	ds_read_b128 v[98:101], v123
	ds_read_b128 v[102:105], v123 offset:4352
	v_add_co_u32_e32 v106, vcc, s57, v116
	v_cvt_pk_bf16_f32 v72, v66, v67
	s_nop 0
	v_addc_co_u32_e32 v107, vcc, 0, v117, vcc
	s_waitcnt lgkmcnt(0)
	global_store_dwordx4 v[106:107], v[98:101], off
	v_mov_b32_e32 v66, v0
	v_cvt_pk_bf16_f32 v78, v78, v79
	v_add_co_u32_e32 v98, vcc, s58, v116
	v_cvt_pk_bf16_f32 v79, v80, v81
	s_nop 0
	v_addc_co_u32_e32 v99, vcc, 0, v117, vcc
	global_store_dwordx4 v[98:99], v[102:105], off
	s_waitcnt lgkmcnt(0)
	s_barrier
; DEV int ltid() { int t = threadIdx.x; asm volatile("" : "+v"(t)); return t; }
; DEV CParams* launder(CParams* p) { asm volatile("" : "+s"(p)); return p; }
; DEV void pk_bf16x8(unsigned (&o)[4], f32x4 a, f32x4 b) { o[0] = cvt_pk_bf16(a[0], a[1]); o[1] = cvt_pk_bf16(a[2], a[3]); o[2] = cvt_pk_bf16(b[0], b[1]); o[3] = cvt_pk_bf16(b[2], b[3]); }
; template <int LB> DEV void stage_store_block(const unsigned (&v)[4][LB / 4], unsigned char* dst, long row_stride) {
;   extern __shared__ __attribute__((aligned(16))) char shm[];
;   constexpr int MP = LB == 8 ? 4 : (LB == 16 ? 2 : 1), PITCH = 16 * LB + 16, ROWS = 16 * MP;
;   static_assert(ROWS * PITCH <= STG_HALF, "staging region");
;   const int tid = ltid(), wr = tid >> 8, wc = (tid >> 6) & 3, fr = tid & 15, fq = (tid >> 4) & 3;
;   char* stg = shm + STG_OFF + wr * STG_HALF;
;   const int t4 = tid & 255;
; #pragma unroll
;   for (int ps = 0; ps < 4 / MP; ++ps) {
; #pragma unroll
;     for (int mm = 0; mm < MP; ++mm) {
;       char* wp = stg + (16 * mm + fr) * PITCH + (4 * wc + fq) * LB; const int m = ps * MP + mm;
;       if (LB == 8) *(u32x2*)wp = (u32x2){v[m][0], v[m][1]};
;       else { *(u32x4*)wp = (u32x4){v[m][0], v[m][1], v[m][2], v[m][3]}; if (LB == 32) *(u32x4*)(wp + 16) = (u32x4){v[m][LB / 4 - 4], v[m][LB / 4 - 3], v[m][LB / 4 - 2], v[m][LB / 4 - 1]}; }
;     }
;     asm volatile("s_waitcnt lgkmcnt(0)" ::: "memory"); __builtin_amdgcn_s_barrier(); asm volatile("" ::: "memory");
; #pragma unroll
;     for (int k = 0; k < 2; ++k) { const int idx = k * 256 + t4, row = idx / LB, ch = idx % LB;
;       *(u32x4*)(dst + (long)(ps * ROWS + row) * row_stride + ch * 16) = *(const u32x4*)(stg + row * PITCH + ch * 16); }
;     asm volatile("s_waitcnt lgkmcnt(0)" ::: "memory"); __builtin_amdgcn_s_barrier(); asm volatile("" ::: "memory");
;   }
; DEV void EpiOut::operator()(const AccT& acc, int wr, int wc, int fr, int fq) const {
;   CParams& P = *launder(p);
; #pragma unroll
;   for (int ai = 0; ai < 2; ++ai)
; #pragma unroll
;     for (int bj = 0; bj < 2; ++bj) {
;       unsigned vals[4][4];
; #pragma unroll
;       for (int m = 0; m < 4; ++m) pk_bf16x8(vals[m], acc[ai][bj][m][0], acc[ai][bj][m][1]);
;       stage_store_block<16>(vals, (unsigned char*)(P.mix + (long)(pm * BM + ai * HALF + wr * 64) * DM + pn * 256 + bj * HALF), DM * 2);
;     }
	v_cvt_pk_bf16_f32 v80, v74, v75
	v_cvt_pk_bf16_f32 v73, v68, v69
	v_lshrrev_b32_e32 v67, 8, v66
	v_and_b32_e32 v68, 15, v66
	v_and_b32_e32 v74, 0xf0, v66
	v_lshlrev_b32_e32 v69, 4, v66
	v_bfe_u32 v66, v66, 4, 4
	v_mad_i32_i24 v67, v67, s56, v122
	v_and_b32_e32 v138, 0xf0, v69
	v_mul_u32_u24_e32 v66, 0x110, v66
	v_cvt_pk_bf16_f32 v94, v94, v95
	v_cvt_pk_bf16_f32 v95, v96, v97
	v_cvt_pk_bf16_f32 v96, v90, v91
	v_add3_u32 v90, v67, v138, v66
	v_mul_u32_u24_e32 v66, 0x110, v68
	v_cvt_pk_bf16_f32 v97, v92, v93
	v_add3_u32 v91, v67, v74, v66
	v_cvt_pk_bf16_f32 v86, v86, v87
	v_cvt_pk_bf16_f32 v87, v88, v89
	v_cvt_pk_bf16_f32 v88, v82, v83
	v_cvt_pk_bf16_f32 v89, v84, v85
	ds_write_b128 v91, v[94:97]
	ds_write_b128 v91, v[86:89] offset:4352
	s_waitcnt lgkmcnt(0)
	s_barrier
	ds_read_b128 v[66:69], v90
	v_cvt_pk_bf16_f32 v81, v76, v77
	v_lshl_add_u64 v[82:83], s[20:21], 0, v[138:139]
	v_lshlrev_b32_e32 v138, 8, v74
	ds_read_b128 v[74:77], v90 offset:4352
	v_lshl_add_u64 v[84:85], v[82:83], 0, v[138:139]
	v_or_b32_e32 v138, 0x10000, v138
	s_waitcnt lgkmcnt(0)
	global_store_dwordx4 v[84:85], v[66:69], off offset:256
	v_cvt_pk_bf16_f32 v38, v38, v39
	v_cvt_pk_bf16_f32 v39, v40, v41
	v_lshl_add_u64 v[66:67], v[82:83], 0, v[138:139]
	global_store_dwordx4 v[66:67], v[74:77], off offset:256
	s_waitcnt lgkmcnt(0)
	s_barrier
	ds_write_b128 v91, v[78:81]
	ds_write_b128 v91, v[70:73] offset:4352
	s_waitcnt lgkmcnt(0)
	s_barrier
	ds_read_b128 v[66:69], v90
	ds_read_b128 v[70:73], v90 offset:4352
	v_add_co_u32_e32 v74, vcc, s57, v84
	v_cvt_pk_bf16_f32 v40, v34, v35
	s_nop 0
	v_addc_co_u32_e32 v75, vcc, 0, v85, vcc
	s_waitcnt lgkmcnt(0)
	global_store_dwordx4 v[74:75], v[66:69], off offset:256
	v_mov_b32_e32 v34, v0
	v_cvt_pk_bf16_f32 v46, v46, v47
	v_add_co_u32_e32 v66, vcc, s58, v84
	v_cvt_pk_bf16_f32 v47, v48, v49
	s_nop 0
	v_addc_co_u32_e32 v67, vcc, 0, v85, vcc
	global_store_dwordx4 v[66:67], v[70:73], off offset:256
	s_waitcnt lgkmcnt(0)
	s_barrier
	v_cvt_pk_bf16_f32 v48, v42, v43
	v_cvt_pk_bf16_f32 v41, v36, v37
	v_lshrrev_b32_e32 v35, 8, v34
	v_and_b32_e32 v36, 15, v34
	v_and_b32_e32 v42, 0xf0, v34
	v_lshlrev_b32_e32 v37, 4, v34
	v_bfe_u32 v34, v34, 4, 4
	v_mad_i32_i24 v35, v35, s56, v122
	v_and_b32_e32 v138, 0xf0, v37
	v_mul_u32_u24_e32 v34, 0x110, v34
	v_cvt_pk_bf16_f32 v62, v62, v63
	v_cvt_pk_bf16_f32 v63, v64, v65
	v_cvt_pk_bf16_f32 v64, v58, v59
	v_add3_u32 v58, v35, v138, v34
	v_mul_u32_u24_e32 v34, 0x110, v36
	v_cvt_pk_bf16_f32 v65, v60, v61
	v_add3_u32 v59, v35, v42, v34
	v_cvt_pk_bf16_f32 v54, v54, v55
	v_cvt_pk_bf16_f32 v55, v56, v57
	v_cvt_pk_bf16_f32 v56, v50, v51
	v_cvt_pk_bf16_f32 v57, v52, v53
	ds_write_b128 v59, v[62:65]
	ds_write_b128 v59, v[54:57] offset:4352
	s_add_u32 s20, s20, 0x80000
	s_waitcnt lgkmcnt(0)
	s_barrier
	s_addc_u32 s21, s21, 0
	ds_read_b128 v[34:37], v58
	v_cvt_pk_bf16_f32 v49, v44, v45
	v_lshl_add_u64 v[50:51], s[20:21], 0, v[138:139]
	v_lshlrev_b32_e32 v138, 8, v42
	ds_read_b128 v[42:45], v58 offset:4352
	v_lshl_add_u64 v[52:53], v[50:51], 0, v[138:139]
	v_or_b32_e32 v138, 0x10000, v138
	s_waitcnt lgkmcnt(0)
	global_store_dwordx4 v[52:53], v[34:37], off
	v_cvt_pk_bf16_f32 v6, v6, v7
	v_cvt_pk_bf16_f32 v7, v8, v9
	v_lshl_add_u64 v[34:35], v[50:51], 0, v[138:139]
	global_store_dwordx4 v[34:35], v[42:45], off
	s_waitcnt lgkmcnt(0)
	s_barrier
	ds_write_b128 v59, v[46:49]
	ds_write_b128 v59, v[38:41] offset:4352
	s_waitcnt lgkmcnt(0)
	s_barrier
	ds_read_b128 v[34:37], v58
	ds_read_b128 v[38:41], v58 offset:4352
	v_add_co_u32_e32 v42, vcc, s57, v52
	v_cvt_pk_bf16_f32 v8, v2, v3
	s_nop 0
	v_addc_co_u32_e32 v43, vcc, 0, v53, vcc
	s_waitcnt lgkmcnt(0)
	global_store_dwordx4 v[42:43], v[34:37], off
	v_mov_b32_e32 v2, v0
	v_cvt_pk_bf16_f32 v14, v14, v15
	v_add_co_u32_e32 v34, vcc, s58, v52
	v_cvt_pk_bf16_f32 v15, v16, v17
	s_nop 0
	v_addc_co_u32_e32 v35, vcc, 0, v53, vcc
	global_store_dwordx4 v[34:35], v[38:41], off
	s_waitcnt lgkmcnt(0)
	s_barrier
	v_cvt_pk_bf16_f32 v16, v10, v11
	v_cvt_pk_bf16_f32 v9, v4, v5
	v_lshrrev_b32_e32 v3, 8, v2
	v_and_b32_e32 v4, 15, v2
	v_and_b32_e32 v10, 0xf0, v2
	v_lshlrev_b32_e32 v5, 4, v2
	v_bfe_u32 v2, v2, 4, 4
	v_mad_i32_i24 v3, v3, s56, v122
	v_and_b32_e32 v138, 0xf0, v5
	v_mul_u32_u24_e32 v2, 0x110, v2
	v_cvt_pk_bf16_f32 v30, v30, v31
	v_cvt_pk_bf16_f32 v31, v32, v33
	v_cvt_pk_bf16_f32 v32, v26, v27
	v_add3_u32 v26, v3, v138, v2
	v_mul_u32_u24_e32 v2, 0x110, v4
	v_cvt_pk_bf16_f32 v33, v28, v29
	v_add3_u32 v27, v3, v10, v2
	v_cvt_pk_bf16_f32 v22, v22, v23
	v_cvt_pk_bf16_f32 v23, v24, v25
	v_cvt_pk_bf16_f32 v24, v18, v19
	v_cvt_pk_bf16_f32 v25, v20, v21
	ds_write_b128 v27, v[30:33]
	ds_write_b128 v27, v[22:25] offset:4352
	s_waitcnt lgkmcnt(0)
	s_barrier
	ds_read_b128 v[2:5], v26
	v_cvt_pk_bf16_f32 v17, v12, v13
	v_lshl_add_u64 v[18:19], s[20:21], 0, v[138:139]
	v_lshlrev_b32_e32 v138, 8, v10
	ds_read_b128 v[10:13], v26 offset:4352
	v_lshl_add_u64 v[20:21], v[18:19], 0, v[138:139]
	v_or_b32_e32 v138, 0x10000, v138
	s_waitcnt lgkmcnt(0)
	global_store_dwordx4 v[20:21], v[2:5], off offset:256
	s_mov_b32 s63, s62
	s_mov_b32 s64, s61
	v_lshl_add_u64 v[2:3], v[18:19], 0, v[138:139]
	global_store_dwordx4 v[2:3], v[10:13], off offset:256
	s_waitcnt lgkmcnt(0)
	s_barrier
	ds_write_b128 v27, v[14:17]
	ds_write_b128 v27, v[6:9] offset:4352
	s_waitcnt lgkmcnt(0)
	s_barrier
	ds_read_b128 v[2:5], v26
	ds_read_b128 v[6:9], v26 offset:4352
	v_add_co_u32_e32 v10, vcc, 0x20000, v20
	s_mov_b64 s[20:21], s[18:19]
	s_nop 0
	v_addc_co_u32_e32 v11, vcc, 0, v21, vcc
	s_waitcnt lgkmcnt(0)
	global_store_dwordx4 v[10:11], v[2:5], off offset:256
	s_nop 1
	v_add_co_u32_e32 v2, vcc, 0x30000, v20
	s_nop 1
	v_addc_co_u32_e32 v3, vcc, 0, v21, vcc
	global_store_dwordx4 v[2:3], v[6:9], off offset:256
	s_waitcnt lgkmcnt(0)
	s_barrier
	s_and_b64 vcc, exec, s[16:17]
	s_cbranch_vccz .LBB0_1242
	s_waitcnt vmcnt(0)
	s_cmpk_gt_u32 s28, 0xff
	s_cbranch_scc1 .LBB0_1247
	s_barrier

; #define LAS __attribute__((address_space(3)))
; #define G_GATHER_OFFS(tab_, rv_) do { _Pragma("unroll") for (int i = 0; i < 2; ++i) { int R_, C_; G_SRC(i, R_, C_); const int ra_ = (tab_)[R_], rb_ = (tab_)[HALF + R_];        \
;     vAc[0][i] = (unsigned)((R_ < (rv_) ? ra_ : 0) * KB + C_); vAc[1][i] = (unsigned)((HALF + R_ < (rv_) ? rb_ : 0) * KB + C_); } } while (0)
; #define G_STAGE(bufoff, gbase, voff) do { _Pragma("unroll") for (int _i = 0; _i < 2; ++_i) \
;     __builtin_amdgcn_global_load_lds((const unsigned*)((const char*)(gbase) + (voff)[_i]), (LAS unsigned*)(lds + (bufoff) + ldsw + _i * 8192), 16, 0, 0); } while (0)
; #define G_LDA(dst, b, h) do { _Pragma("unroll") for (int m = 0; m < 4; ++m) dst[m] = G_LD2(G_SA(b, h) + aoff + m * 2048, G_SA(b, h) + (P::FP8 ? aoff1 : aoff + 1024) + m * 2048); } while (0)
; #define G_LDB(dst, b, h) do { _Pragma("unroll") for (int n = 0; n < 2; ++n) dst[n] = G_LD2(G_SB(b, h) + boff + n * 2048, G_SB(b, h) + (P::FP8 ? boff1 : boff + 1024) + n * 2048); } while (0)
; #define WAIT_V(n) asm volatile("s_waitcnt vmcnt(" #n ")" ::: "memory")
; #define WAIT_L(n) asm volatile("s_waitcnt lgkmcnt(" #n ")" ::: "memory")
; #define BAR __builtin_amdgcn_s_barrier()
; #define SCHED __builtin_amdgcn_sched_barrier(0)
; template <class P>
; DEV void gemm_stream(const P& pol) {
;     ...
;     for (int t = 0; t < nt; t += 2) {
;       const bool last = (t == nt - 2);
;       const size_t k1 = (size_t)(t + 1) * kstep, k2 = (size_t)(t + 2) * kstep;
;       const char* a20 = last ? nA0 : cA0 + k2; const char* a21 = last ? nA1 : cA1 + k2; const char* b2 = last ? nB : cB + k2;
;       G_LDB(B0, 0, 0); SCHED; G_LDA(At, 0, 0); G_STAGE(G_SA(1, 1), cA1 + k1, vAc[1]);
;       WAIT_L(8); BAR; WAIT_L(0); G_MMA(0, 0, At, B0); BAR; SCHED;
;       if (P::GATHER && last && has_next) { LAS int* tab = arow + ((ui + 1) & 1) * 256; G_GATHER_OFFS(tab, nxt.rv); }
;       G_LDB(B1, 0, 1); G_STAGE(G_SB(0, 0), b2, voffB);
;       BAR; WAIT_L(0); G_MMA(0, 1, At, B1); BAR;
;       G_LDA(At, 0, 1); G_STAGE(G_SA(0, 0), a20, vAc[0]);
;       BAR; WAIT_L(0); G_MMA(1, 0, At, B0); BAR; SCHED;
;       G_STAGE(G_SB(0, 1), b2 + hstep, voffB);
;       WAIT_V(6); BAR; G_MMA(1, 1, At, B1); BAR;
.LBB0_1446:
	ds_read_b128 v[14:17], v209
	ds_read_b128 v[18:21], v205
	ds_read_b128 v[22:25], v210
	ds_read_b128 v[26:29], v211
	s_lshl_b32 s6, s67, 8
	s_waitcnt lgkmcnt(0)
	v_pk_add_f32 v[64:65], v[8:9], 1.0 op_sel_hi:[1,0]
	v_pk_add_f32 v[62:63], v[6:7], 1.0 op_sel_hi:[1,0]
	v_pk_add_f32 v[60:61], v[4:5], 1.0 op_sel_hi:[1,0]
	v_pk_add_f32 v[58:59], v[2:3], 1.0 op_sel_hi:[1,0]
	s_ashr_i32 s37, s36, 31
	s_and_b32 s93, s6, 0x100
	v_mov_b32_e32 v187, v179
	v_lshl_add_u64 v[2:3], s[10:11], 0, v[186:187]
	s_mov_b32 m0, s85
	v_lshl_add_u64 v[4:5], v[2:3], 0, s[14:15]
	v_mov_b32_e32 v189, v179
	v_add_u32_e32 v227, v204, v203
	ds_read_b128 v[30:33], v221
	ds_read_b128 v[38:41], v221 offset:2048
	ds_read_b128 v[34:37], v227
	ds_read_b128 v[42:45], v227 offset:2048
	ds_read_b128 v[66:69], v221 offset:4096
	ds_read_b128 v[74:77], v221 offset:6144
	ds_read_b128 v[70:73], v227 offset:4096
	ds_read_b128 v[78:81], v227 offset:6144
	global_load_lds_dwordx4 v[4:5], off
	v_lshl_add_u64 v[4:5], s[10:11], 0, v[188:189]
	v_lshl_add_u64 v[6:7], v[4:5], 0, s[14:15]
	s_mov_b32 m0, s86
	s_nop 0
	global_load_lds_dwordx4 v[6:7], off
	s_waitcnt lgkmcnt(8)
	s_barrier
	s_waitcnt lgkmcnt(0)
	s_setprio 1
	v_mov_b64_e32 v[172:173], v[56:57]
	v_mov_b64_e32 v[164:165], v[52:53]
	v_mov_b64_e32 v[156:157], v[56:57]
	v_mov_b64_e32 v[148:149], v[52:53]
	v_mov_b64_e32 v[140:141], v[56:57]
	v_mov_b64_e32 v[132:133], v[52:53]
	v_mov_b64_e32 v[124:125], v[56:57]
	v_mov_b64_e32 v[108:109], v[52:53]
	v_mov_b64_e32 v[170:171], v[54:55]
	v_mov_b64_e32 v[162:163], v[50:51]
	v_mov_b64_e32 v[154:155], v[54:55]
	v_mov_b64_e32 v[146:147], v[50:51]
	v_mov_b64_e32 v[138:139], v[54:55]
	v_mov_b64_e32 v[130:131], v[50:51]
	v_mov_b64_e32 v[122:123], v[54:55]
	v_mov_b64_e32 v[106:107], v[50:51]
	s_waitcnt lgkmcnt(0)
	v_mfma_scale_f32_16x16x128_f8f6f4 v[170:173], v[14:21], v[30:37], v[170:173], v222, v224 op_sel_hi:[0,0,0]
	v_mfma_scale_f32_16x16x128_f8f6f4 v[162:165], v[22:29], v[30:37], v[162:165], v222, v224 op_sel_hi:[0,0,0]
	v_mfma_scale_f32_16x16x128_f8f6f4 v[154:157], v[14:21], v[38:45], v[154:157], v222, v224 op_sel_hi:[0,0,0]
	v_mfma_scale_f32_16x16x128_f8f6f4 v[146:149], v[22:29], v[38:45], v[146:149], v222, v224 op_sel_hi:[0,0,0]
	v_mfma_scale_f32_16x16x128_f8f6f4 v[138:141], v[14:21], v[66:73], v[138:141], v222, v224 op_sel_hi:[0,0,0]
	v_mfma_scale_f32_16x16x128_f8f6f4 v[130:133], v[22:29], v[66:73], v[130:133], v222, v224 op_sel_hi:[0,0,0]
	v_mfma_scale_f32_16x16x128_f8f6f4 v[122:125], v[14:21], v[74:81], v[122:125], v222, v224 op_sel_hi:[0,0,0]
	v_mfma_scale_f32_16x16x128_f8f6f4 v[106:109], v[22:29], v[74:81], v[106:109], v222, v224 op_sel_hi:[0,0,0]
	s_setprio 0
	s_barrier
	v_lshl_add_u64 v[6:7], v[10:11], 0, v[180:181]
	s_mov_b32 m0, s59
	v_lshl_add_u64 v[8:9], v[6:7], 0, s[24:25]
	ds_read_b128 v[192:195], v212
	ds_read_b128 v[196:199], v206
	ds_read_b128 v[228:231], v213
	ds_read_b128 v[232:235], v214
	global_load_lds_dwordx4 v[8:9], off
	v_lshl_add_u64 v[8:9], v[10:11], 0, v[182:183]
	v_lshl_add_u64 v[12:13], v[8:9], 0, s[24:25]
	s_mov_b32 m0, s60
	s_nop 0
	global_load_lds_dwordx4 v[12:13], off
	s_barrier
	s_waitcnt lgkmcnt(0)
	s_setprio 1
	v_mov_b64_e32 v[176:177], v[64:65]
	v_mov_b64_e32 v[168:169], v[60:61]
	v_mov_b64_e32 v[160:161], v[64:65]
	v_mov_b64_e32 v[152:153], v[60:61]
	v_mov_b64_e32 v[144:145], v[64:65]
	v_mov_b64_e32 v[136:137], v[60:61]
	v_mov_b64_e32 v[128:129], v[64:65]
	v_mov_b64_e32 v[120:121], v[60:61]
	v_mov_b64_e32 v[174:175], v[62:63]
	v_mov_b64_e32 v[166:167], v[58:59]
	v_mov_b64_e32 v[158:159], v[62:63]
	v_mov_b64_e32 v[150:151], v[58:59]
	v_mov_b64_e32 v[142:143], v[62:63]
	v_mov_b64_e32 v[134:135], v[58:59]
	v_mov_b64_e32 v[126:127], v[62:63]
	v_mov_b64_e32 v[118:119], v[58:59]
	s_waitcnt lgkmcnt(0)
	v_mfma_scale_f32_16x16x128_f8f6f4 v[174:177], v[192:199], v[30:37], v[174:177], v222, v224 op_sel_hi:[0,0,0]
	v_mfma_scale_f32_16x16x128_f8f6f4 v[166:169], v[228:235], v[30:37], v[166:169], v222, v224 op_sel_hi:[0,0,0]
	v_mfma_scale_f32_16x16x128_f8f6f4 v[158:161], v[192:199], v[38:45], v[158:161], v222, v224 op_sel_hi:[0,0,0]
	v_mfma_scale_f32_16x16x128_f8f6f4 v[150:153], v[228:235], v[38:45], v[150:153], v222, v224 op_sel_hi:[0,0,0]
	v_mfma_scale_f32_16x16x128_f8f6f4 v[142:145], v[192:199], v[66:73], v[142:145], v222, v224 op_sel_hi:[0,0,0]
	v_mfma_scale_f32_16x16x128_f8f6f4 v[134:137], v[228:235], v[66:73], v[134:137], v222, v224 op_sel_hi:[0,0,0]
	v_mfma_scale_f32_16x16x128_f8f6f4 v[126:129], v[192:199], v[74:81], v[126:129], v222, v224 op_sel_hi:[0,0,0]
	v_mfma_scale_f32_16x16x128_f8f6f4 v[118:121], v[228:235], v[74:81], v[118:121], v222, v224 op_sel_hi:[0,0,0]
	s_setprio 0
	v_lshl_add_u64 v[12:13], s[10:11], 0, v[178:179]
	s_mov_b32 m0, s58
	v_lshl_add_u64 v[46:47], v[12:13], 0, s[24:25]
	v_mov_b32_e32 v185, v179
	s_barrier
	ds_read_b128 v[30:33], v221 offset:16384
	ds_read_b128 v[38:41], v221 offset:18432
	ds_read_b128 v[34:37], v227 offset:16384
	ds_read_b128 v[42:45], v227 offset:18432
	ds_read_b128 v[236:239], v221 offset:20480
	ds_read_b128 v[244:247], v221 offset:22528
	ds_read_b128 v[240:243], v227 offset:20480
	ds_read_b128 v[248:251], v227 offset:22528
	global_load_lds_dwordx4 v[46:47], off
	v_lshl_add_u64 v[46:47], s[10:11], 0, v[184:185]
	v_lshl_add_u64 v[48:49], v[46:47], 0, s[24:25]
	s_mov_b32 m0, s61
	s_nop 0
	global_load_lds_dwordx4 v[48:49], off
	s_barrier
; #define G_STAGE(bufoff, gbase, voff) do { _Pragma("unroll") for (int _i = 0; _i < 2; ++_i) \
;     __builtin_amdgcn_global_load_lds((const unsigned*)((const char*)(gbase) + (voff)[_i]), (LAS unsigned*)(lds + (bufoff) + ldsw + _i * 8192), 16, 0, 0); } while (0)
; #define G_LDA(dst, b, h) do { _Pragma("unroll") for (int m = 0; m < 4; ++m) dst[m] = G_LD2(G_SA(b, h) + aoff + m * 2048, G_SA(b, h) + (P::FP8 ? aoff1 : aoff + 1024) + m * 2048); } while (0)
; #define G_LDB(dst, b, h) do { _Pragma("unroll") for (int n = 0; n < 2; ++n) dst[n] = G_LD2(G_SB(b, h) + boff + n * 2048, G_SB(b, h) + (P::FP8 ? boff1 : boff + 1024) + n * 2048); } while (0)
; #define WAIT_V(n) asm volatile("s_waitcnt vmcnt(" #n ")" ::: "memory")
; #define WAIT_L(n) asm volatile("s_waitcnt lgkmcnt(" #n ")" ::: "memory")
; #define BAR __builtin_amdgcn_s_barrier()
; #define SCHED __builtin_amdgcn_sched_barrier(0)
; template <class P>
; DEV void gemm_stream(const P& pol) {
;     ...
;       BAR; WAIT_L(0); G_MMA(1, 0, At, B0); BAR; SCHED;
;       G_STAGE(G_SB(0, 1), b2 + hstep, voffB);
;       WAIT_V(6); BAR; G_MMA(1, 1, At, B1); BAR;
;       G_LDB(B0, 1, 0); SCHED; G_LDA(At, 1, 0); G_STAGE(G_SA(0, 1), a21, vAc[1]);
;       WAIT_L(8); BAR; WAIT_L(0); G_MMA(0, 0, At, B0); BAR; SCHED;
	s_waitcnt lgkmcnt(0)
	s_setprio 1
	v_mov_b64_e32 v[112:113], v[56:57]
	v_mov_b64_e32 v[100:101], v[52:53]
	v_mov_b64_e32 v[92:93], v[56:57]
	v_mov_b64_e32 v[84:85], v[52:53]
	v_mov_b64_e32 v[76:77], v[56:57]
	v_mov_b64_e32 v[68:69], v[52:53]
	v_mov_b64_e32 v[110:111], v[54:55]
	v_mov_b64_e32 v[98:99], v[50:51]
	v_mov_b64_e32 v[90:91], v[54:55]
	v_mov_b64_e32 v[82:83], v[50:51]
	v_mov_b64_e32 v[74:75], v[54:55]
	v_mov_b64_e32 v[66:67], v[50:51]
	s_waitcnt lgkmcnt(0)
	v_mfma_scale_f32_16x16x128_f8f6f4 v[110:113], v[14:21], v[30:37], v[110:113], v222, v224 op_sel_hi:[0,0,0]
	v_mfma_scale_f32_16x16x128_f8f6f4 v[98:101], v[22:29], v[30:37], v[98:101], v222, v224 op_sel_hi:[0,0,0]
	v_mfma_scale_f32_16x16x128_f8f6f4 v[90:93], v[14:21], v[38:45], v[90:93], v222, v224 op_sel_hi:[0,0,0]
	v_mfma_scale_f32_16x16x128_f8f6f4 v[82:85], v[22:29], v[38:45], v[82:85], v222, v224 op_sel_hi:[0,0,0]
	v_mfma_scale_f32_16x16x128_f8f6f4 v[74:77], v[14:21], v[236:243], v[74:77], v222, v224 op_sel_hi:[0,0,0]
	v_mfma_scale_f32_16x16x128_f8f6f4 v[66:69], v[22:29], v[236:243], v[66:69], v222, v224 op_sel_hi:[0,0,0]
	v_mfma_scale_f32_16x16x128_f8f6f4 v[54:57], v[14:21], v[244:251], v[54:57], v222, v224 op_sel_hi:[0,0,0]
	v_mfma_scale_f32_16x16x128_f8f6f4 v[50:53], v[22:29], v[244:251], v[50:53], v222, v224 op_sel_hi:[0,0,0]
	s_setprio 0
	s_barrier
	v_lshl_add_u64 v[14:15], v[10:11], 0, s[26:27]
	s_mov_b32 m0, s62
	v_lshl_add_u64 v[16:17], v[14:15], 0, v[180:181]
	global_load_lds_dwordx4 v[16:17], off
	v_lshl_add_u64 v[14:15], v[14:15], 0, v[182:183]
	s_mov_b32 m0, s63
	s_nop 0
	global_load_lds_dwordx4 v[14:15], off
	s_waitcnt vmcnt(6)
	s_barrier
	s_setprio 1
	v_mov_b64_e32 v[116:117], v[64:65]
	v_mov_b64_e32 v[104:105], v[60:61]
	v_mov_b64_e32 v[96:97], v[64:65]
	v_mov_b64_e32 v[88:89], v[60:61]
	v_mov_b64_e32 v[80:81], v[64:65]
	v_mov_b64_e32 v[72:73], v[60:61]
	v_mov_b64_e32 v[114:115], v[62:63]
	v_mov_b64_e32 v[102:103], v[58:59]
	v_mov_b64_e32 v[94:95], v[62:63]
	v_mov_b64_e32 v[86:87], v[58:59]
	v_mov_b64_e32 v[78:79], v[62:63]
	v_mov_b64_e32 v[70:71], v[58:59]
	v_mfma_scale_f32_16x16x128_f8f6f4 v[114:117], v[192:199], v[30:37], v[114:117], v222, v224 op_sel_hi:[0,0,0]
	v_mfma_scale_f32_16x16x128_f8f6f4 v[102:105], v[228:235], v[30:37], v[102:105], v222, v224 op_sel_hi:[0,0,0]
	v_mfma_scale_f32_16x16x128_f8f6f4 v[94:97], v[192:199], v[38:45], v[94:97], v222, v224 op_sel_hi:[0,0,0]
	v_mfma_scale_f32_16x16x128_f8f6f4 v[86:89], v[228:235], v[38:45], v[86:89], v222, v224 op_sel_hi:[0,0,0]
	v_mfma_scale_f32_16x16x128_f8f6f4 v[78:81], v[192:199], v[236:243], v[78:81], v222, v224 op_sel_hi:[0,0,0]
	v_mfma_scale_f32_16x16x128_f8f6f4 v[70:73], v[228:235], v[236:243], v[70:73], v222, v224 op_sel_hi:[0,0,0]
	v_mfma_scale_f32_16x16x128_f8f6f4 v[62:65], v[192:199], v[244:251], v[62:65], v222, v224 op_sel_hi:[0,0,0]
	v_mfma_scale_f32_16x16x128_f8f6f4 v[58:61], v[228:235], v[244:251], v[58:61], v222, v224 op_sel_hi:[0,0,0]
	s_setprio 0
	s_barrier
	ds_read_b128 v[14:17], v215
	ds_read_b128 v[18:21], v207
	ds_read_b128 v[22:25], v216
	ds_read_b128 v[26:29], v217
	s_mov_b32 m0, s64
	v_lshl_add_u64 v[2:3], v[2:3], 0, s[24:25]
	ds_read_b128 v[30:33], v221 offset:32768
	ds_read_b128 v[38:41], v221 offset:34816
	ds_read_b128 v[34:37], v227 offset:32768
	ds_read_b128 v[42:45], v227 offset:34816
	ds_read_b128 v[192:195], v221 offset:36864
	ds_read_b128 v[228:231], v221 offset:38912
	ds_read_b128 v[196:199], v227 offset:36864
	ds_read_b128 v[232:235], v227 offset:38912
	global_load_lds_dwordx4 v[2:3], off
	v_lshl_add_u64 v[2:3], v[4:5], 0, s[24:25]
	s_mov_b32 m0, s65
	s_nop 0
	global_load_lds_dwordx4 v[2:3], off
	s_waitcnt lgkmcnt(8)
	s_barrier
	s_waitcnt lgkmcnt(0)
	s_setprio 1
	v_mfma_scale_f32_16x16x128_f8f6f4 v[170:173], v[14:21], v[30:37], v[170:173], v222, v224 op_sel_hi:[0,0,0]
	v_mfma_scale_f32_16x16x128_f8f6f4 v[162:165], v[22:29], v[30:37], v[162:165], v222, v224 op_sel_hi:[0,0,0]
	v_mfma_scale_f32_16x16x128_f8f6f4 v[154:157], v[14:21], v[38:45], v[154:157], v222, v224 op_sel_hi:[0,0,0]
	v_mfma_scale_f32_16x16x128_f8f6f4 v[146:149], v[22:29], v[38:45], v[146:149], v222, v224 op_sel_hi:[0,0,0]
	v_mfma_scale_f32_16x16x128_f8f6f4 v[138:141], v[14:21], v[192:199], v[138:141], v222, v224 op_sel_hi:[0,0,0]
	v_mfma_scale_f32_16x16x128_f8f6f4 v[130:133], v[22:29], v[192:199], v[130:133], v222, v224 op_sel_hi:[0,0,0]
	v_mfma_scale_f32_16x16x128_f8f6f4 v[122:125], v[14:21], v[228:235], v[122:125], v222, v224 op_sel_hi:[0,0,0]
	v_mfma_scale_f32_16x16x128_f8f6f4 v[106:109], v[22:29], v[228:235], v[106:109], v222, v224 op_sel_hi:[0,0,0]
	s_setprio 0
	s_barrier
; #define G_STAGE(bufoff, gbase, voff) do { _Pragma("unroll") for (int _i = 0; _i < 2; ++_i) \
;     __builtin_amdgcn_global_load_lds((const unsigned*)((const char*)(gbase) + (voff)[_i]), (LAS unsigned*)(lds + (bufoff) + ldsw + _i * 8192), 16, 0, 0); } while (0)
; #define G_LDA(dst, b, h) do { _Pragma("unroll") for (int m = 0; m < 4; ++m) dst[m] = G_LD2(G_SA(b, h) + aoff + m * 2048, G_SA(b, h) + (P::FP8 ? aoff1 : aoff + 1024) + m * 2048); } while (0)
; #define G_LDB(dst, b, h) do { _Pragma("unroll") for (int n = 0; n < 2; ++n) dst[n] = G_LD2(G_SB(b, h) + boff + n * 2048, G_SB(b, h) + (P::FP8 ? boff1 : boff + 1024) + n * 2048); } while (0)
; #define WAIT_V(n) asm volatile("s_waitcnt vmcnt(" #n ")" ::: "memory")
; #define WAIT_L(n) asm volatile("s_waitcnt lgkmcnt(" #n ")" ::: "memory")
; #define BAR __builtin_amdgcn_s_barrier()
; #define SCHED __builtin_amdgcn_sched_barrier(0)
;   DEV void bias_dma(const Unit& u, LAS float* tabw) const { __builtin_amdgcn_global_load_lds((const unsigned*)bias_src(u, ltid() & 255), (LAS unsigned*)tabw, 4, 0, 0); }
;   DEV void bias_dma(const Unit& u, LAS float* tabw) const { __builtin_amdgcn_global_load_lds((const unsigned*)bias_src(u, ltid() & 255), (LAS unsigned*)tabw, 4, 0, 0); }
; template <class P>
; DEV void gemm_stream(const P& pol) {
;     ...
;       WAIT_V(6); BAR; G_MMA(1, 1, At, B1); BAR;
;       G_LDB(B0, 1, 0); SCHED; G_LDA(At, 1, 0); G_STAGE(G_SA(0, 1), a21, vAc[1]);
;       WAIT_L(8); BAR; WAIT_L(0); G_MMA(0, 0, At, B0); BAR; SCHED;
;       G_LDB(B1, 1, 1); G_STAGE(G_SB(1, 0), b2 + kstep, voffB);
;       BAR; WAIT_L(0); G_MMA(0, 1, At, B1); BAR;
;       G_LDA(At, 1, 1); G_STAGE(G_SA(1, 0), a20 + kstep, vAc[0]);
;       BAR; WAIT_L(0); G_MMA(1, 0, At, B0); BAR; SCHED;
;       G_STAGE(G_SB(1, 1), b2 + hstep + kstep, voffB);
;       WAIT_V(6); BAR; G_MMA(1, 1, At, B1); BAR;
;       if (P::HASBIAS && has_next && t == 0) pol.bias_dma(nxt, btab + ((ui + 1) & 1) * 256 + ((wid & 3) << 6));
;       if (P::GATHER && has_next && t == 0) pol.arow_dma(nxt, arow + ((ui + 1) & 1) * 256 + ((wid & 3) << 6));
	s_mov_b32 m0, s68
	v_lshl_add_u64 v[2:3], v[6:7], 0, s[22:23]
	ds_read_b128 v[236:239], v218
	ds_read_b128 v[240:243], v208
	ds_read_b128 v[244:247], v219
	ds_read_b128 v[248:251], v220
	global_load_lds_dwordx4 v[2:3], off
	v_lshl_add_u64 v[2:3], v[8:9], 0, s[22:23]
	s_mov_b32 m0, s69
	s_nop 0
	global_load_lds_dwordx4 v[2:3], off
	s_barrier
	s_waitcnt lgkmcnt(0)
	s_setprio 1
	v_mfma_scale_f32_16x16x128_f8f6f4 v[174:177], v[236:243], v[30:37], v[174:177], v222, v224 op_sel_hi:[0,0,0]
	v_mfma_scale_f32_16x16x128_f8f6f4 v[166:169], v[244:251], v[30:37], v[166:169], v222, v224 op_sel_hi:[0,0,0]
	v_mfma_scale_f32_16x16x128_f8f6f4 v[158:161], v[236:243], v[38:45], v[158:161], v222, v224 op_sel_hi:[0,0,0]
	v_mfma_scale_f32_16x16x128_f8f6f4 v[150:153], v[244:251], v[38:45], v[150:153], v222, v224 op_sel_hi:[0,0,0]
	v_mfma_scale_f32_16x16x128_f8f6f4 v[142:145], v[236:243], v[192:199], v[142:145], v222, v224 op_sel_hi:[0,0,0]
	v_mfma_scale_f32_16x16x128_f8f6f4 v[134:137], v[244:251], v[192:199], v[134:137], v222, v224 op_sel_hi:[0,0,0]
	v_mfma_scale_f32_16x16x128_f8f6f4 v[126:129], v[236:243], v[228:235], v[126:129], v222, v224 op_sel_hi:[0,0,0]
	v_mfma_scale_f32_16x16x128_f8f6f4 v[118:121], v[244:251], v[228:235], v[118:121], v222, v224 op_sel_hi:[0,0,0]
	s_setprio 0
	s_mov_b32 m0, s70
	v_lshl_add_u64 v[12:13], v[12:13], 0, s[22:23]
	s_barrier
	ds_read_b128 v[2:5], v221 offset:49152
	ds_read_b128 v[30:33], v221 offset:51200
	ds_read_b128 v[6:9], v227 offset:49152
	ds_read_b128 v[34:37], v227 offset:51200
	ds_read_b128 v[38:41], v221 offset:53248
	ds_read_b128 v[192:195], v221 offset:55296
	ds_read_b128 v[42:45], v227 offset:53248
	ds_read_b128 v[196:199], v227 offset:55296
	global_load_lds_dwordx4 v[12:13], off
	v_lshl_add_u64 v[12:13], v[46:47], 0, s[22:23]
	s_mov_b32 m0, s71
	s_nop 0
	global_load_lds_dwordx4 v[12:13], off
	s_barrier
	s_waitcnt lgkmcnt(0)
	s_setprio 1
	v_mfma_scale_f32_16x16x128_f8f6f4 v[110:113], v[14:21], v[2:9], v[110:113], v222, v224 op_sel_hi:[0,0,0]
	v_mfma_scale_f32_16x16x128_f8f6f4 v[98:101], v[22:29], v[2:9], v[98:101], v222, v224 op_sel_hi:[0,0,0]
	v_mfma_scale_f32_16x16x128_f8f6f4 v[90:93], v[14:21], v[30:37], v[90:93], v222, v224 op_sel_hi:[0,0,0]
	v_mfma_scale_f32_16x16x128_f8f6f4 v[82:85], v[22:29], v[30:37], v[82:85], v222, v224 op_sel_hi:[0,0,0]
	v_mfma_scale_f32_16x16x128_f8f6f4 v[74:77], v[14:21], v[38:45], v[74:77], v222, v224 op_sel_hi:[0,0,0]
	v_mfma_scale_f32_16x16x128_f8f6f4 v[66:69], v[22:29], v[38:45], v[66:69], v222, v224 op_sel_hi:[0,0,0]
	v_mfma_scale_f32_16x16x128_f8f6f4 v[54:57], v[14:21], v[192:199], v[54:57], v222, v224 op_sel_hi:[0,0,0]
	v_mfma_scale_f32_16x16x128_f8f6f4 v[50:53], v[22:29], v[192:199], v[50:53], v222, v224 op_sel_hi:[0,0,0]
	s_setprio 0
	s_barrier
	v_lshl_add_u64 v[12:13], v[10:11], 0, s[28:29]
	s_mov_b32 m0, s72
	v_lshl_add_u64 v[14:15], v[12:13], 0, v[180:181]
	global_load_lds_dwordx4 v[14:15], off
	v_lshl_add_u64 v[12:13], v[12:13], 0, v[182:183]
	s_mov_b32 m0, s73
	s_nop 0
	global_load_lds_dwordx4 v[12:13], off
	s_waitcnt vmcnt(6)
	s_barrier
	s_setprio 1
	v_mfma_scale_f32_16x16x128_f8f6f4 v[114:117], v[236:243], v[2:9], v[114:117], v222, v224 op_sel_hi:[0,0,0]
	v_mfma_scale_f32_16x16x128_f8f6f4 v[102:105], v[244:251], v[2:9], v[102:105], v222, v224 op_sel_hi:[0,0,0]
	v_mfma_scale_f32_16x16x128_f8f6f4 v[94:97], v[236:243], v[30:37], v[94:97], v222, v224 op_sel_hi:[0,0,0]
	v_mfma_scale_f32_16x16x128_f8f6f4 v[86:89], v[244:251], v[30:37], v[86:89], v222, v224 op_sel_hi:[0,0,0]
	v_mfma_scale_f32_16x16x128_f8f6f4 v[78:81], v[236:243], v[38:45], v[78:81], v222, v224 op_sel_hi:[0,0,0]
	v_mfma_scale_f32_16x16x128_f8f6f4 v[70:73], v[244:251], v[38:45], v[70:73], v222, v224 op_sel_hi:[0,0,0]
	v_mfma_scale_f32_16x16x128_f8f6f4 v[62:65], v[236:243], v[192:199], v[62:65], v222, v224 op_sel_hi:[0,0,0]
	v_mfma_scale_f32_16x16x128_f8f6f4 v[58:61], v[244:251], v[192:199], v[58:61], v222, v224 op_sel_hi:[0,0,0]
	s_setprio 0
	s_and_b64 vcc, exec, s[4:5]
	s_barrier
	s_cbranch_vccz .LBB0_1448
	v_mov_b32_e32 v1, v0
	s_lshl_b32 s6, s36, 14
	s_lshl_b32 s46, s93, 2
	v_and_b32_e32 v1, 0xff, v1
	s_ashr_i32 s39, s38, 31
	s_ashr_i32 s7, s6, 31
	s_add_i32 s47, s77, s46
	s_lshl_b64 s[44:45], s[36:37], 14
	s_add_i32 m0, s76, s46
	v_add_u32_e32 v2, 0x780, v1
	v_cmp_gt_u32_e32 vcc, s66, v1
	s_add_u32 s44, s81, s44
	s_addc_u32 s45, s82, s45
	v_cndmask_b32_e32 v1, v2, v1, vcc
	v_lshlrev_b32_e32 v1, 2, v1
	s_lshl_b64 s[6:7], s[6:7], 2
	global_load_lds_dword v1, s[44:45]
	s_add_u32 s44, s20, s6
	v_mov_b32_e32 v1, v0
	s_addc_u32 s45, s21, s7
	s_lshl_b64 s[6:7], s[38:39], 2
	s_add_u32 s6, s44, s6
	s_addc_u32 s7, s45, s7
	v_lshlrev_b32_sdwa v1, v225, v1 dst_sel:DWORD dst_unused:UNUSED_PAD src0_sel:DWORD src1_sel:BYTE_0
	s_mov_b32 m0, s47
	s_nop 0
	global_load_lds_dword v1, s[6:7]

; #define LAS __attribute__((address_space(3)))
; #define G_GATHER_OFFS(tab_, rv_) do { _Pragma("unroll") for (int i = 0; i < 2; ++i) { int R_, C_; G_SRC(i, R_, C_); const int ra_ = (tab_)[R_], rb_ = (tab_)[HALF + R_];        \
;     vAc[0][i] = (unsigned)((R_ < (rv_) ? ra_ : 0) * KB + C_); vAc[1][i] = (unsigned)((HALF + R_ < (rv_) ? rb_ : 0) * KB + C_); } } while (0)
; #define G_STAGE(bufoff, gbase, voff) do { _Pragma("unroll") for (int _i = 0; _i < 2; ++_i) \
;     __builtin_amdgcn_global_load_lds((const unsigned*)((const char*)(gbase) + (voff)[_i]), (LAS unsigned*)(lds + (bufoff) + ldsw + _i * 8192), 16, 0, 0); } while (0)
; #define G_LDA(dst, b, h) do { _Pragma("unroll") for (int m = 0; m < 4; ++m) dst[m] = G_LD2(G_SA(b, h) + aoff + m * 2048, G_SA(b, h) + (P::FP8 ? aoff1 : aoff + 1024) + m * 2048); } while (0)
; #define G_LDB(dst, b, h) do { _Pragma("unroll") for (int n = 0; n < 2; ++n) dst[n] = G_LD2(G_SB(b, h) + boff + n * 2048, G_SB(b, h) + (P::FP8 ? boff1 : boff + 1024) + n * 2048); } while (0)
; #define WAIT_V(n) asm volatile("s_waitcnt vmcnt(" #n ")" ::: "memory")
; #define WAIT_L(n) asm volatile("s_waitcnt lgkmcnt(" #n ")" ::: "memory")
; #define BAR __builtin_amdgcn_s_barrier()
; #define SCHED __builtin_amdgcn_sched_barrier(0)
; template <class P>
; DEV void gemm_stream(const P& pol) {
;     ...
;     for (int t = 0; t < nt; t += 2) {
;       const bool last = (t == nt - 2);
;       const size_t k1 = (size_t)(t + 1) * kstep, k2 = (size_t)(t + 2) * kstep;
;       const char* a20 = last ? nA0 : cA0 + k2; const char* a21 = last ? nA1 : cA1 + k2; const char* b2 = last ? nB : cB + k2;
;       G_LDB(B0, 0, 0); SCHED; G_LDA(At, 0, 0); G_STAGE(G_SA(1, 1), cA1 + k1, vAc[1]);
;       WAIT_L(8); BAR; WAIT_L(0); G_MMA(0, 0, At, B0); BAR; SCHED;
;       if (P::GATHER && last && has_next) { LAS int* tab = arow + ((ui + 1) & 1) * 256; G_GATHER_OFFS(tab, nxt.rv); }
;       G_LDB(B1, 0, 1); G_STAGE(G_SB(0, 0), b2, voffB);
;       BAR; WAIT_L(0); G_MMA(0, 1, At, B1); BAR;
;       G_LDA(At, 0, 1); G_STAGE(G_SA(0, 0), a20, vAc[0]);
;       BAR; WAIT_L(0); G_MMA(1, 0, At, B0); BAR; SCHED;
;       G_STAGE(G_SB(0, 1), b2 + hstep, voffB);
;       WAIT_V(6); BAR; G_MMA(1, 1, At, B1); BAR;
;       G_LDB(B0, 1, 0); SCHED; G_LDA(At, 1, 0); G_STAGE(G_SA(0, 1), a21, vAc[1]);
;       WAIT_L(8); BAR; WAIT_L(0); G_MMA(0, 0, At, B0); BAR; SCHED;
.LBB0_1450:
	v_lshl_add_u64 v[194:195], v[192:193], 0, s[46:47]
	v_cndmask_b32_e64 v195, v195, v1, s[6:7]
	v_cndmask_b32_e64 v194, v194, v190, s[6:7]
	s_mov_b32 m0, s59
	v_lshl_add_u64 v[196:197], v[194:195], 0, v[180:181]
	ds_read_b128 v[228:231], v212
	ds_read_b128 v[232:235], v206
	ds_read_b128 v[236:239], v213
	ds_read_b128 v[240:243], v214
	global_load_lds_dwordx4 v[196:197], off
	v_lshl_add_u64 v[198:199], v[194:195], 0, v[182:183]
	s_mov_b32 m0, s60
	s_add_u32 s95, s46, 0x200
	global_load_lds_dwordx4 v[198:199], off
	s_addc_u32 s96, s47, 0
	s_and_b64 s[6:7], s[6:7], exec
	s_barrier
	s_waitcnt lgkmcnt(0)
	s_cselect_b32 s6, 0, s95
	s_cselect_b32 s7, 0, s96
	s_add_u32 s6, s10, s6
	s_addc_u32 s7, s11, s7
	s_setprio 1
	v_mfma_scale_f32_16x16x128_f8f6f4 v[174:177], v[228:235], v[18:25], v[174:177], v222, v224 op_sel_hi:[0,0,0]
	v_mfma_scale_f32_16x16x128_f8f6f4 v[166:169], v[236:243], v[18:25], v[166:169], v222, v224 op_sel_hi:[0,0,0]
	v_mfma_scale_f32_16x16x128_f8f6f4 v[158:161], v[228:235], v[26:33], v[158:161], v222, v224 op_sel_hi:[0,0,0]
	v_mfma_scale_f32_16x16x128_f8f6f4 v[150:153], v[236:243], v[26:33], v[150:153], v222, v224 op_sel_hi:[0,0,0]
	v_mfma_scale_f32_16x16x128_f8f6f4 v[142:145], v[228:235], v[34:41], v[142:145], v222, v224 op_sel_hi:[0,0,0]
	v_mfma_scale_f32_16x16x128_f8f6f4 v[134:137], v[236:243], v[34:41], v[134:137], v222, v224 op_sel_hi:[0,0,0]
	v_mfma_scale_f32_16x16x128_f8f6f4 v[126:129], v[228:235], v[42:49], v[126:129], v222, v224 op_sel_hi:[0,0,0]
	v_mfma_scale_f32_16x16x128_f8f6f4 v[118:121], v[236:243], v[42:49], v[118:121], v222, v224 op_sel_hi:[0,0,0]
	s_setprio 0
	s_mov_b32 m0, s58
	s_barrier
	ds_read_b128 v[22:25], v221 offset:16384
	ds_read_b128 v[30:33], v221 offset:18432
	ds_read_b128 v[26:29], v227 offset:16384
	ds_read_b128 v[34:37], v227 offset:18432
	ds_read_b128 v[38:41], v221 offset:20480
	ds_read_b128 v[244:247], v221 offset:22528
	ds_read_b128 v[42:45], v227 offset:20480
	ds_read_b128 v[248:251], v227 offset:22528
	global_load_lds_dwordx4 v178, s[6:7]
	s_mov_b32 m0, s61
	v_mov_b32_e32 v185, v179
	global_load_lds_dwordx4 v184, s[6:7]
	s_barrier
	s_waitcnt lgkmcnt(0)
	v_lshl_add_u64 v[20:21], s[6:7], 0, v[178:179]
	v_lshl_add_u64 v[18:19], s[6:7], 0, v[184:185]
	s_setprio 1
	v_mfma_scale_f32_16x16x128_f8f6f4 v[110:113], v[2:9], v[22:29], v[110:113], v222, v224 op_sel_hi:[0,0,0]
	v_mfma_scale_f32_16x16x128_f8f6f4 v[98:101], v[10:17], v[22:29], v[98:101], v222, v224 op_sel_hi:[0,0,0]
	v_mfma_scale_f32_16x16x128_f8f6f4 v[90:93], v[2:9], v[30:37], v[90:93], v222, v224 op_sel_hi:[0,0,0]
	v_mfma_scale_f32_16x16x128_f8f6f4 v[82:85], v[10:17], v[30:37], v[82:85], v222, v224 op_sel_hi:[0,0,0]
	v_mfma_scale_f32_16x16x128_f8f6f4 v[74:77], v[2:9], v[38:45], v[74:77], v222, v224 op_sel_hi:[0,0,0]
	v_mfma_scale_f32_16x16x128_f8f6f4 v[66:69], v[10:17], v[38:45], v[66:69], v222, v224 op_sel_hi:[0,0,0]
	v_mfma_scale_f32_16x16x128_f8f6f4 v[54:57], v[2:9], v[244:251], v[54:57], v222, v224 op_sel_hi:[0,0,0]
	v_mfma_scale_f32_16x16x128_f8f6f4 v[50:53], v[10:17], v[244:251], v[50:53], v222, v224 op_sel_hi:[0,0,0]
	s_setprio 0
	s_barrier
	v_lshl_add_u64 v[2:3], v[194:195], 0, s[12:13]
	s_mov_b32 m0, s62
	v_lshl_add_u64 v[4:5], v[2:3], 0, v[180:181]
	global_load_lds_dwordx4 v[4:5], off
	v_lshl_add_u64 v[2:3], v[2:3], 0, v[182:183]
	s_mov_b32 m0, s63
	s_nop 0
	global_load_lds_dwordx4 v[2:3], off
	s_waitcnt vmcnt(6)
	s_barrier
	s_setprio 1
	v_mfma_scale_f32_16x16x128_f8f6f4 v[114:117], v[228:235], v[22:29], v[114:117], v222, v224 op_sel_hi:[0,0,0]
	v_mfma_scale_f32_16x16x128_f8f6f4 v[102:105], v[236:243], v[22:29], v[102:105], v222, v224 op_sel_hi:[0,0,0]
	v_mfma_scale_f32_16x16x128_f8f6f4 v[94:97], v[228:235], v[30:37], v[94:97], v222, v224 op_sel_hi:[0,0,0]
	v_mfma_scale_f32_16x16x128_f8f6f4 v[86:89], v[236:243], v[30:37], v[86:89], v222, v224 op_sel_hi:[0,0,0]
	v_mfma_scale_f32_16x16x128_f8f6f4 v[78:81], v[228:235], v[38:45], v[78:81], v222, v224 op_sel_hi:[0,0,0]
	v_mfma_scale_f32_16x16x128_f8f6f4 v[70:73], v[236:243], v[38:45], v[70:73], v222, v224 op_sel_hi:[0,0,0]
	v_mfma_scale_f32_16x16x128_f8f6f4 v[62:65], v[228:235], v[244:251], v[62:65], v222, v224 op_sel_hi:[0,0,0]
	v_mfma_scale_f32_16x16x128_f8f6f4 v[58:61], v[236:243], v[244:251], v[58:61], v222, v224 op_sel_hi:[0,0,0]
	s_setprio 0
	s_barrier
	ds_read_b128 v[2:5], v215
	ds_read_b128 v[6:9], v207
	ds_read_b128 v[10:13], v216
	ds_read_b128 v[14:17], v217
	s_mov_b32 m0, s64
	v_lshl_add_u64 v[46:47], s[6:7], 0, v[200:201]
	ds_read_b128 v[22:25], v221 offset:32768
	ds_read_b128 v[30:33], v221 offset:34816
	ds_read_b128 v[26:29], v227 offset:32768
	ds_read_b128 v[34:37], v227 offset:34816
	ds_read_b128 v[38:41], v221 offset:36864
	ds_read_b128 v[228:231], v221 offset:38912
	ds_read_b128 v[42:45], v227 offset:36864
	ds_read_b128 v[232:235], v227 offset:38912
	global_load_lds_dwordx4 v[46:47], off
	v_lshl_add_u64 v[46:47], s[6:7], 0, v[188:189]
	s_mov_b32 m0, s65
	s_nop 0
	global_load_lds_dwordx4 v[46:47], off
	s_waitcnt lgkmcnt(8)
	s_barrier
	s_waitcnt lgkmcnt(0)
	s_setprio 1
	v_mfma_scale_f32_16x16x128_f8f6f4 v[170:173], v[2:9], v[22:29], v[170:173], v222, v224 op_sel_hi:[0,0,0]
	v_mfma_scale_f32_16x16x128_f8f6f4 v[162:165], v[10:17], v[22:29], v[162:165], v222, v224 op_sel_hi:[0,0,0]
	v_mfma_scale_f32_16x16x128_f8f6f4 v[154:157], v[2:9], v[30:37], v[154:157], v222, v224 op_sel_hi:[0,0,0]
	v_mfma_scale_f32_16x16x128_f8f6f4 v[146:149], v[10:17], v[30:37], v[146:149], v222, v224 op_sel_hi:[0,0,0]
	v_mfma_scale_f32_16x16x128_f8f6f4 v[138:141], v[2:9], v[38:45], v[138:141], v222, v224 op_sel_hi:[0,0,0]
	v_mfma_scale_f32_16x16x128_f8f6f4 v[130:133], v[10:17], v[38:45], v[130:133], v222, v224 op_sel_hi:[0,0,0]
	v_mfma_scale_f32_16x16x128_f8f6f4 v[122:125], v[2:9], v[228:235], v[122:125], v222, v224 op_sel_hi:[0,0,0]
	v_mfma_scale_f32_16x16x128_f8f6f4 v[106:109], v[10:17], v[228:235], v[106:109], v222, v224 op_sel_hi:[0,0,0]
	s_setprio 0
	s_barrier
; #define LAS __attribute__((address_space(3)))
; #define G_GATHER_OFFS(tab_, rv_) do { _Pragma("unroll") for (int i = 0; i < 2; ++i) { int R_, C_; G_SRC(i, R_, C_); const int ra_ = (tab_)[R_], rb_ = (tab_)[HALF + R_];        \
;     vAc[0][i] = (unsigned)((R_ < (rv_) ? ra_ : 0) * KB + C_); vAc[1][i] = (unsigned)((HALF + R_ < (rv_) ? rb_ : 0) * KB + C_); } } while (0)
; #define G_STAGE(bufoff, gbase, voff) do { _Pragma("unroll") for (int _i = 0; _i < 2; ++_i) \
;     __builtin_amdgcn_global_load_lds((const unsigned*)((const char*)(gbase) + (voff)[_i]), (LAS unsigned*)(lds + (bufoff) + ldsw + _i * 8192), 16, 0, 0); } while (0)
; #define G_LDA(dst, b, h) do { _Pragma("unroll") for (int m = 0; m < 4; ++m) dst[m] = G_LD2(G_SA(b, h) + aoff + m * 2048, G_SA(b, h) + (P::FP8 ? aoff1 : aoff + 1024) + m * 2048); } while (0)
; #define G_LDB(dst, b, h) do { _Pragma("unroll") for (int n = 0; n < 2; ++n) dst[n] = G_LD2(G_SB(b, h) + boff + n * 2048, G_SB(b, h) + (P::FP8 ? boff1 : boff + 1024) + n * 2048); } while (0)
; #define WAIT_V(n) asm volatile("s_waitcnt vmcnt(" #n ")" ::: "memory")
; #define WAIT_L(n) asm volatile("s_waitcnt lgkmcnt(" #n ")" ::: "memory")
; #define BAR __builtin_amdgcn_s_barrier()
; template <class P>
; DEV void gemm_stream(const P& pol) {
;     ...
;     for (int t = 0; t < nt; t += 2) {
;       const bool last = (t == nt - 2);
;       const size_t k1 = (size_t)(t + 1) * kstep, k2 = (size_t)(t + 2) * kstep;
;       const char* a20 = last ? nA0 : cA0 + k2; const char* a21 = last ? nA1 : cA1 + k2; const char* b2 = last ? nB : cB + k2;
;       G_LDB(B0, 0, 0); SCHED; G_LDA(At, 0, 0); G_STAGE(G_SA(1, 1), cA1 + k1, vAc[1]);
;       WAIT_L(8); BAR; WAIT_L(0); G_MMA(0, 0, At, B0); BAR; SCHED;
;       if (P::GATHER && last && has_next) { LAS int* tab = arow + ((ui + 1) & 1) * 256; G_GATHER_OFFS(tab, nxt.rv); }
;     ...
;       WAIT_V(6); BAR; G_MMA(1, 1, At, B1); BAR;
;       G_LDB(B0, 1, 0); SCHED; G_LDA(At, 1, 0); G_STAGE(G_SA(0, 1), a21, vAc[1]);
;       WAIT_L(8); BAR; WAIT_L(0); G_MMA(0, 0, At, B0); BAR; SCHED;
;       G_LDB(B1, 1, 1); G_STAGE(G_SB(1, 0), b2 + kstep, voffB);
;       BAR; WAIT_L(0); G_MMA(0, 1, At, B1); BAR;
;       G_LDA(At, 1, 1); G_STAGE(G_SA(1, 0), a20 + kstep, vAc[0]);
;       BAR; WAIT_L(0); G_MMA(1, 0, At, B0); BAR; SCHED;
;       G_STAGE(G_SB(1, 1), b2 + hstep + kstep, voffB);
;       WAIT_V(6); BAR; G_MMA(1, 1, At, B1); BAR;
	s_mov_b32 m0, s68
	v_lshl_add_u64 v[46:47], v[196:197], 0, s[14:15]
	ds_read_b128 v[236:239], v218
	ds_read_b128 v[240:243], v208
	ds_read_b128 v[244:247], v219
	ds_read_b128 v[248:251], v220
	global_load_lds_dwordx4 v[46:47], off
	v_lshl_add_u64 v[46:47], v[198:199], 0, s[14:15]
	s_mov_b32 m0, s69
	s_nop 0
	global_load_lds_dwordx4 v[46:47], off
	s_barrier
	s_waitcnt lgkmcnt(0)
	s_setprio 1
	v_mfma_scale_f32_16x16x128_f8f6f4 v[174:177], v[236:243], v[22:29], v[174:177], v222, v224 op_sel_hi:[0,0,0]
	v_mfma_scale_f32_16x16x128_f8f6f4 v[166:169], v[244:251], v[22:29], v[166:169], v222, v224 op_sel_hi:[0,0,0]
	v_mfma_scale_f32_16x16x128_f8f6f4 v[158:161], v[236:243], v[30:37], v[158:161], v222, v224 op_sel_hi:[0,0,0]
	v_mfma_scale_f32_16x16x128_f8f6f4 v[150:153], v[244:251], v[30:37], v[150:153], v222, v224 op_sel_hi:[0,0,0]
	v_mfma_scale_f32_16x16x128_f8f6f4 v[142:145], v[236:243], v[38:45], v[142:145], v222, v224 op_sel_hi:[0,0,0]
	v_mfma_scale_f32_16x16x128_f8f6f4 v[134:137], v[244:251], v[38:45], v[134:137], v222, v224 op_sel_hi:[0,0,0]
	v_mfma_scale_f32_16x16x128_f8f6f4 v[126:129], v[236:243], v[228:235], v[126:129], v222, v224 op_sel_hi:[0,0,0]
	v_mfma_scale_f32_16x16x128_f8f6f4 v[118:121], v[244:251], v[228:235], v[118:121], v222, v224 op_sel_hi:[0,0,0]
	s_setprio 0
	s_mov_b32 m0, s70
	v_lshl_add_u64 v[20:21], v[20:21], 0, s[14:15]
	s_barrier
	ds_read_b128 v[22:25], v221 offset:49152
	ds_read_b128 v[30:33], v221 offset:51200
	ds_read_b128 v[26:29], v227 offset:49152
	ds_read_b128 v[34:37], v227 offset:51200
	ds_read_b128 v[38:41], v221 offset:53248
	ds_read_b128 v[228:231], v221 offset:55296
	ds_read_b128 v[42:45], v227 offset:53248
	ds_read_b128 v[232:235], v227 offset:55296
	global_load_lds_dwordx4 v[20:21], off
	v_lshl_add_u64 v[18:19], v[18:19], 0, s[14:15]
	s_mov_b32 m0, s71
	s_nop 0
	global_load_lds_dwordx4 v[18:19], off
	s_barrier
	s_waitcnt lgkmcnt(0)
	s_setprio 1
	v_mfma_scale_f32_16x16x128_f8f6f4 v[110:113], v[2:9], v[22:29], v[110:113], v222, v224 op_sel_hi:[0,0,0]
	v_mfma_scale_f32_16x16x128_f8f6f4 v[98:101], v[10:17], v[22:29], v[98:101], v222, v224 op_sel_hi:[0,0,0]
	v_mfma_scale_f32_16x16x128_f8f6f4 v[90:93], v[2:9], v[30:37], v[90:93], v222, v224 op_sel_hi:[0,0,0]
	v_mfma_scale_f32_16x16x128_f8f6f4 v[82:85], v[10:17], v[30:37], v[82:85], v222, v224 op_sel_hi:[0,0,0]
	v_mfma_scale_f32_16x16x128_f8f6f4 v[74:77], v[2:9], v[38:45], v[74:77], v222, v224 op_sel_hi:[0,0,0]
	v_mfma_scale_f32_16x16x128_f8f6f4 v[66:69], v[10:17], v[38:45], v[66:69], v222, v224 op_sel_hi:[0,0,0]
	v_mfma_scale_f32_16x16x128_f8f6f4 v[54:57], v[2:9], v[228:235], v[54:57], v222, v224 op_sel_hi:[0,0,0]
	v_mfma_scale_f32_16x16x128_f8f6f4 v[50:53], v[10:17], v[228:235], v[50:53], v222, v224 op_sel_hi:[0,0,0]
	s_setprio 0
	s_barrier
	v_lshl_add_u64 v[2:3], v[194:195], 0, s[16:17]
	s_mov_b32 m0, s72
	v_lshl_add_u64 v[4:5], v[2:3], 0, v[180:181]
	global_load_lds_dwordx4 v[4:5], off
	v_lshl_add_u64 v[2:3], v[2:3], 0, v[182:183]
	s_mov_b32 m0, s73
	s_nop 0
	global_load_lds_dwordx4 v[2:3], off
	s_waitcnt vmcnt(6)
	s_barrier
	s_setprio 1
	v_mfma_scale_f32_16x16x128_f8f6f4 v[114:117], v[236:243], v[22:29], v[114:117], v222, v224 op_sel_hi:[0,0,0]
	v_mfma_scale_f32_16x16x128_f8f6f4 v[102:105], v[244:251], v[22:29], v[102:105], v222, v224 op_sel_hi:[0,0,0]
	v_mfma_scale_f32_16x16x128_f8f6f4 v[94:97], v[236:243], v[30:37], v[94:97], v222, v224 op_sel_hi:[0,0,0]
	v_mfma_scale_f32_16x16x128_f8f6f4 v[86:89], v[244:251], v[30:37], v[86:89], v222, v224 op_sel_hi:[0,0,0]
	v_mfma_scale_f32_16x16x128_f8f6f4 v[78:81], v[236:243], v[38:45], v[78:81], v222, v224 op_sel_hi:[0,0,0]
	v_mfma_scale_f32_16x16x128_f8f6f4 v[70:73], v[244:251], v[38:45], v[70:73], v222, v224 op_sel_hi:[0,0,0]
	v_mfma_scale_f32_16x16x128_f8f6f4 v[62:65], v[236:243], v[228:235], v[62:65], v222, v224 op_sel_hi:[0,0,0]
	v_mfma_scale_f32_16x16x128_f8f6f4 v[58:61], v[244:251], v[228:235], v[58:61], v222, v224 op_sel_hi:[0,0,0]
	s_setprio 0
	s_add_i32 s39, s39, 2
	s_add_u32 s46, s46, 0x100
	s_addc_u32 s47, s47, 0
	s_cmp_gt_u32 s39, 13
	s_barrier
	s_cbranch_scc1 .LBB0_1453
.LBB0_1451:
	ds_read_b128 v[2:5], v209
	ds_read_b128 v[6:9], v205
	ds_read_b128 v[10:13], v210
	ds_read_b128 v[14:17], v211
	s_cmp_eq_u32 s39, 12
	s_cselect_b64 s[6:7], -1, 0
	s_add_u32 s96, s83, s46
	s_addc_u32 s97, s84, s47
	s_mov_b32 m0, s85
	ds_read_b128 v[18:21], v221
	ds_read_b128 v[26:29], v221 offset:2048
	ds_read_b128 v[22:25], v227
	ds_read_b128 v[30:33], v227 offset:2048
	ds_read_b128 v[34:37], v221 offset:4096
	ds_read_b128 v[42:45], v221 offset:6144
	ds_read_b128 v[38:41], v227 offset:4096
	ds_read_b128 v[46:49], v227 offset:6144
	global_load_lds_dwordx4 v186, s[96:97]
	s_mov_b32 m0, s86
	s_nop 0
	global_load_lds_dwordx4 v188, s[96:97]
	s_waitcnt lgkmcnt(8)
	s_barrier
	s_waitcnt lgkmcnt(0)
	s_setprio 1
	v_mfma_scale_f32_16x16x128_f8f6f4 v[170:173], v[2:9], v[18:25], v[170:173], v222, v224 op_sel_hi:[0,0,0]
	v_mfma_scale_f32_16x16x128_f8f6f4 v[162:165], v[10:17], v[18:25], v[162:165], v222, v224 op_sel_hi:[0,0,0]
	v_mfma_scale_f32_16x16x128_f8f6f4 v[154:157], v[2:9], v[26:33], v[154:157], v222, v224 op_sel_hi:[0,0,0]
	v_mfma_scale_f32_16x16x128_f8f6f4 v[146:149], v[10:17], v[26:33], v[146:149], v222, v224 op_sel_hi:[0,0,0]
	v_mfma_scale_f32_16x16x128_f8f6f4 v[138:141], v[2:9], v[34:41], v[138:141], v222, v224 op_sel_hi:[0,0,0]
	v_mfma_scale_f32_16x16x128_f8f6f4 v[130:133], v[10:17], v[34:41], v[130:133], v222, v224 op_sel_hi:[0,0,0]
	v_mfma_scale_f32_16x16x128_f8f6f4 v[122:125], v[2:9], v[42:49], v[122:125], v222, v224 op_sel_hi:[0,0,0]
	v_mfma_scale_f32_16x16x128_f8f6f4 v[106:109], v[10:17], v[42:49], v[106:109], v222, v224 op_sel_hi:[0,0,0]
	s_setprio 0
	s_barrier
	s_and_b64 s[96:97], s[4:5], s[6:7]
	s_andn2_b64 vcc, exec, s[96:97]
	s_cbranch_vccz .LBB0_1449
	v_mov_b32_e32 v187, v179
	v_mov_b32_e32 v189, v179
	v_mov_b64_e32 v[200:201], v[186:187]
	s_branch .LBB0_1450

; #define LAS __attribute__((address_space(3)))
; #define G_GATHER_OFFS(tab_, rv_) do { _Pragma("unroll") for (int i = 0; i < 2; ++i) { int R_, C_; G_SRC(i, R_, C_); const int ra_ = (tab_)[R_], rb_ = (tab_)[HALF + R_];        \
;     vAc[0][i] = (unsigned)((R_ < (rv_) ? ra_ : 0) * KB + C_); vAc[1][i] = (unsigned)((HALF + R_ < (rv_) ? rb_ : 0) * KB + C_); } } while (0)
; #define G_STAGE(bufoff, gbase, voff) do { _Pragma("unroll") for (int _i = 0; _i < 2; ++_i) \
;     __builtin_amdgcn_global_load_lds((const unsigned*)((const char*)(gbase) + (voff)[_i]), (LAS unsigned*)(lds + (bufoff) + ldsw + _i * 8192), 16, 0, 0); } while (0)
; #define G_LDA(dst, b, h) do { _Pragma("unroll") for (int m = 0; m < 4; ++m) dst[m] = G_LD2(G_SA(b, h) + aoff + m * 2048, G_SA(b, h) + (P::FP8 ? aoff1 : aoff + 1024) + m * 2048); } while (0)
; #define G_LDB(dst, b, h) do { _Pragma("unroll") for (int n = 0; n < 2; ++n) dst[n] = G_LD2(G_SB(b, h) + boff + n * 2048, G_SB(b, h) + (P::FP8 ? boff1 : boff + 1024) + n * 2048); } while (0)
; #define WAIT_V(n) asm volatile("s_waitcnt vmcnt(" #n ")" ::: "memory")
; #define WAIT_L(n) asm volatile("s_waitcnt lgkmcnt(" #n ")" ::: "memory")
; #define BAR __builtin_amdgcn_s_barrier()
; #define SCHED __builtin_amdgcn_sched_barrier(0)
; template <class P>
; DEV void gemm_stream(const P& pol) {
;     ...
;     for (int t = 0; t < nt; t += 2) {
;       const bool last = (t == nt - 2);
;       const size_t k1 = (size_t)(t + 1) * kstep, k2 = (size_t)(t + 2) * kstep;
;       const char* a20 = last ? nA0 : cA0 + k2; const char* a21 = last ? nA1 : cA1 + k2; const char* b2 = last ? nB : cB + k2;
;       G_LDB(B0, 0, 0); SCHED; G_LDA(At, 0, 0); G_STAGE(G_SA(1, 1), cA1 + k1, vAc[1]);
;       WAIT_L(8); BAR; WAIT_L(0); G_MMA(0, 0, At, B0); BAR; SCHED;
;       if (P::GATHER && last && has_next) { LAS int* tab = arow + ((ui + 1) & 1) * 256; G_GATHER_OFFS(tab, nxt.rv); }
;       G_LDB(B1, 0, 1); G_STAGE(G_SB(0, 0), b2, voffB);
;       BAR; WAIT_L(0); G_MMA(0, 1, At, B1); BAR;
;       G_LDA(At, 0, 1); G_STAGE(G_SA(0, 0), a20, vAc[0]);
;       BAR; WAIT_L(0); G_MMA(1, 0, At, B0); BAR; SCHED;
;       G_STAGE(G_SB(0, 1), b2 + hstep, voffB);
;       WAIT_V(6); BAR; G_MMA(1, 1, At, B1); BAR;
.LBB0_1543:
	ds_read_b128 v[38:41], v157
	ds_read_b128 v[42:45], v153
	ds_read_b128 v[58:61], v158
	ds_read_b128 v[62:65], v159
	s_ashr_i32 s27, s26, 31
	v_lshl_add_u64 v[142:143], s[38:39], 0, v[134:135]
	s_mov_b32 m0, s76
	v_lshl_add_u64 v[34:35], v[142:143], 0, s[10:11]
	v_lshl_add_u64 v[144:145], s[38:39], 0, v[136:137]
	ds_read_b128 v[18:21], v169
	ds_read_b128 v[26:29], v169 offset:2048
	ds_read_b128 v[22:25], v170
	ds_read_b128 v[30:33], v170 offset:2048
	ds_read_b128 v[66:69], v169 offset:4096
	ds_read_b128 v[106:109], v169 offset:6144
	ds_read_b128 v[70:73], v170 offset:4096
	ds_read_b128 v[110:113], v170 offset:6144
	global_load_lds_dwordx4 v[34:35], off
	v_lshl_add_u64 v[34:35], v[144:145], 0, s[10:11]
	s_mov_b32 m0, s77
	s_nop 0
	global_load_lds_dwordx4 v[34:35], off
	s_waitcnt lgkmcnt(8)
	s_barrier
	s_waitcnt lgkmcnt(0)
	s_setprio 1
	v_mov_b64_e32 v[92:93], v[16:17]
	v_mov_b64_e32 v[96:97], v[12:13]
	v_mov_b64_e32 v[104:105], v[16:17]
	v_mov_b64_e32 v[100:101], v[12:13]
	v_mov_b64_e32 v[76:77], v[16:17]
	v_mov_b64_e32 v[80:81], v[12:13]
	v_mov_b64_e32 v[88:89], v[16:17]
	v_mov_b64_e32 v[84:85], v[12:13]
	v_mov_b64_e32 v[90:91], v[14:15]
	v_mov_b64_e32 v[94:95], v[10:11]
	v_mov_b64_e32 v[102:103], v[14:15]
	v_mov_b64_e32 v[98:99], v[10:11]
	v_mov_b64_e32 v[74:75], v[14:15]
	v_mov_b64_e32 v[78:79], v[10:11]
	v_mov_b64_e32 v[86:87], v[14:15]
	v_mov_b64_e32 v[82:83], v[10:11]
	s_waitcnt lgkmcnt(0)
	v_mfma_scale_f32_16x16x128_f8f6f4 v[90:93], v[38:45], v[18:25], v[90:93], v171, v172 op_sel_hi:[0,0,0]
	v_mfma_scale_f32_16x16x128_f8f6f4 v[94:97], v[58:65], v[18:25], v[94:97], v171, v172 op_sel_hi:[0,0,0]
	v_mfma_scale_f32_16x16x128_f8f6f4 v[102:105], v[38:45], v[26:33], v[102:105], v171, v172 op_sel_hi:[0,0,0]
	v_mfma_scale_f32_16x16x128_f8f6f4 v[98:101], v[58:65], v[26:33], v[98:101], v171, v172 op_sel_hi:[0,0,0]
	v_mfma_scale_f32_16x16x128_f8f6f4 v[74:77], v[38:45], v[66:73], v[74:77], v171, v172 op_sel_hi:[0,0,0]
	v_mfma_scale_f32_16x16x128_f8f6f4 v[78:81], v[58:65], v[66:73], v[78:81], v171, v172 op_sel_hi:[0,0,0]
	v_mfma_scale_f32_16x16x128_f8f6f4 v[86:89], v[38:45], v[106:113], v[86:89], v171, v172 op_sel_hi:[0,0,0]
	v_mfma_scale_f32_16x16x128_f8f6f4 v[82:85], v[58:65], v[106:113], v[82:85], v171, v172 op_sel_hi:[0,0,0]
	s_setprio 0
	s_barrier
	v_lshl_add_u64 v[146:147], v[140:141], 0, v[130:131]
	s_mov_b32 m0, s54
	v_lshl_add_u64 v[34:35], v[146:147], 0, s[16:17]
	v_lshl_add_u64 v[148:149], v[140:141], 0, v[132:133]
	ds_read_b128 v[174:177], v160
	ds_read_b128 v[178:181], v154
	ds_read_b128 v[182:185], v161
	ds_read_b128 v[186:189], v162
	global_load_lds_dwordx4 v[34:35], off
	v_lshl_add_u64 v[34:35], v[148:149], 0, s[16:17]
	s_mov_b32 m0, s55
	s_nop 0
	global_load_lds_dwordx4 v[34:35], off
	s_barrier
	s_waitcnt lgkmcnt(0)
	s_setprio 1
	v_mov_b64_e32 v[36:37], v[8:9]
	v_mov_b64_e32 v[48:49], v[4:5]
	v_mov_b64_e32 v[56:57], v[8:9]
	v_mov_b64_e32 v[52:53], v[4:5]
	v_mov_b64_e32 v[34:35], v[6:7]
	v_mov_b64_e32 v[46:47], v[2:3]
	v_mov_b64_e32 v[54:55], v[6:7]
	v_mov_b64_e32 v[50:51], v[2:3]
	s_waitcnt lgkmcnt(0)
	v_mfma_scale_f32_16x16x128_f8f6f4 v[34:37], v[174:181], v[18:25], v[34:37], v171, v172 op_sel_hi:[0,0,0]
	v_mfma_scale_f32_16x16x128_f8f6f4 v[46:49], v[182:189], v[18:25], v[46:49], v171, v172 op_sel_hi:[0,0,0]
	v_mfma_scale_f32_16x16x128_f8f6f4 v[54:57], v[174:181], v[26:33], v[54:57], v171, v172 op_sel_hi:[0,0,0]
	v_mfma_scale_f32_16x16x128_f8f6f4 v[50:53], v[182:189], v[26:33], v[50:53], v171, v172 op_sel_hi:[0,0,0]
	v_mov_b64_e32 v[20:21], v[8:9]
	v_mov_b64_e32 v[24:25], v[4:5]
	v_mov_b64_e32 v[32:33], v[8:9]
	v_mov_b64_e32 v[28:29], v[4:5]
	v_mov_b64_e32 v[18:19], v[6:7]
	v_mov_b64_e32 v[22:23], v[2:3]
	v_mov_b64_e32 v[30:31], v[6:7]
	v_mov_b64_e32 v[26:27], v[2:3]
	v_mfma_scale_f32_16x16x128_f8f6f4 v[18:21], v[174:181], v[66:73], v[18:21], v171, v172 op_sel_hi:[0,0,0]
	v_mfma_scale_f32_16x16x128_f8f6f4 v[22:25], v[182:189], v[66:73], v[22:25], v171, v172 op_sel_hi:[0,0,0]
	v_mfma_scale_f32_16x16x128_f8f6f4 v[30:33], v[174:181], v[106:113], v[30:33], v171, v172 op_sel_hi:[0,0,0]
	v_mfma_scale_f32_16x16x128_f8f6f4 v[26:29], v[182:189], v[106:113], v[26:29], v171, v172 op_sel_hi:[0,0,0]
	s_setprio 0
	v_lshl_add_u64 v[150:151], s[36:37], 0, v[134:135]
	s_mov_b32 m0, s53
	v_lshl_add_u64 v[106:107], v[150:151], 0, s[16:17]
	v_lshl_add_u64 v[240:241], s[36:37], 0, v[136:137]
	s_barrier
	ds_read_b128 v[66:69], v169 offset:16384
	ds_read_b128 v[190:193], v169 offset:18432
	ds_read_b128 v[70:73], v170 offset:16384
	ds_read_b128 v[194:197], v170 offset:18432
	ds_read_b128 v[198:201], v169 offset:20480
	ds_read_b128 v[206:209], v169 offset:22528
	ds_read_b128 v[202:205], v170 offset:20480
	ds_read_b128 v[210:213], v170 offset:22528
	global_load_lds_dwordx4 v[106:107], off
	v_lshl_add_u64 v[106:107], v[240:241], 0, s[16:17]
	s_mov_b32 m0, s56
	s_nop 0
	global_load_lds_dwordx4 v[106:107], off
	s_barrier
	s_waitcnt lgkmcnt(0)
	s_setprio 1
	v_mov_b64_e32 v[116:117], v[16:17]
	v_mov_b64_e32 v[120:121], v[12:13]
	v_mov_b64_e32 v[128:129], v[16:17]
	v_mov_b64_e32 v[124:125], v[12:13]
	v_mov_b64_e32 v[108:109], v[16:17]
	v_mov_b64_e32 v[112:113], v[12:13]
	v_mov_b64_e32 v[114:115], v[14:15]
	v_mov_b64_e32 v[118:119], v[10:11]
	v_mov_b64_e32 v[126:127], v[14:15]
	v_mov_b64_e32 v[122:123], v[10:11]
	v_mov_b64_e32 v[106:107], v[14:15]
	v_mov_b64_e32 v[110:111], v[10:11]
	s_waitcnt lgkmcnt(0)
	v_mfma_scale_f32_16x16x128_f8f6f4 v[114:117], v[38:45], v[66:73], v[114:117], v171, v172 op_sel_hi:[0,0,0]
	v_mfma_scale_f32_16x16x128_f8f6f4 v[118:121], v[58:65], v[66:73], v[118:121], v171, v172 op_sel_hi:[0,0,0]
	v_mfma_scale_f32_16x16x128_f8f6f4 v[126:129], v[38:45], v[190:197], v[126:129], v171, v172 op_sel_hi:[0,0,0]
	v_mfma_scale_f32_16x16x128_f8f6f4 v[122:125], v[58:65], v[190:197], v[122:125], v171, v172 op_sel_hi:[0,0,0]
	v_mfma_scale_f32_16x16x128_f8f6f4 v[106:109], v[38:45], v[198:205], v[106:109], v171, v172 op_sel_hi:[0,0,0]
	v_mfma_scale_f32_16x16x128_f8f6f4 v[110:113], v[58:65], v[198:205], v[110:113], v171, v172 op_sel_hi:[0,0,0]
	v_mfma_scale_f32_16x16x128_f8f6f4 v[14:17], v[38:45], v[206:213], v[14:17], v171, v172 op_sel_hi:[0,0,0]
	v_mfma_scale_f32_16x16x128_f8f6f4 v[10:13], v[58:65], v[206:213], v[10:13], v171, v172 op_sel_hi:[0,0,0]
	s_setprio 0
	s_barrier
; #define G_STAGE(bufoff, gbase, voff) do { _Pragma("unroll") for (int _i = 0; _i < 2; ++_i) \
;     __builtin_amdgcn_global_load_lds((const unsigned*)((const char*)(gbase) + (voff)[_i]), (LAS unsigned*)(lds + (bufoff) + ldsw + _i * 8192), 16, 0, 0); } while (0)
; #define G_LDA(dst, b, h) do { _Pragma("unroll") for (int m = 0; m < 4; ++m) dst[m] = G_LD2(G_SA(b, h) + aoff + m * 2048, G_SA(b, h) + (P::FP8 ? aoff1 : aoff + 1024) + m * 2048); } while (0)
; #define G_LDB(dst, b, h) do { _Pragma("unroll") for (int n = 0; n < 2; ++n) dst[n] = G_LD2(G_SB(b, h) + boff + n * 2048, G_SB(b, h) + (P::FP8 ? boff1 : boff + 1024) + n * 2048); } while (0)
; #define WAIT_V(n) asm volatile("s_waitcnt vmcnt(" #n ")" ::: "memory")
; #define WAIT_L(n) asm volatile("s_waitcnt lgkmcnt(" #n ")" ::: "memory")
; #define BAR __builtin_amdgcn_s_barrier()
; #define SCHED __builtin_amdgcn_sched_barrier(0)
; template <class P>
; DEV void gemm_stream(const P& pol) {
;     ...
;       WAIT_V(6); BAR; G_MMA(1, 1, At, B1); BAR;
;       G_LDB(B0, 1, 0); SCHED; G_LDA(At, 1, 0); G_STAGE(G_SA(0, 1), a21, vAc[1]);
;       WAIT_L(8); BAR; WAIT_L(0); G_MMA(0, 0, At, B0); BAR; SCHED;
	v_lshl_add_u64 v[38:39], v[140:141], 0, s[18:19]
	s_mov_b32 m0, s57
	v_lshl_add_u64 v[40:41], v[38:39], 0, v[130:131]
	global_load_lds_dwordx4 v[40:41], off
	v_lshl_add_u64 v[38:39], v[38:39], 0, v[132:133]
	s_mov_b32 m0, s58
	s_nop 0
	global_load_lds_dwordx4 v[38:39], off
	s_waitcnt vmcnt(6)
	s_barrier
	s_setprio 1
	v_mov_b64_e32 v[60:61], v[8:9]
	v_mov_b64_e32 v[64:65], v[4:5]
	v_mov_b64_e32 v[58:59], v[6:7]
	v_mov_b64_e32 v[62:63], v[2:3]
	v_mfma_scale_f32_16x16x128_f8f6f4 v[58:61], v[174:181], v[66:73], v[58:61], v171, v172 op_sel_hi:[0,0,0]
	v_mfma_scale_f32_16x16x128_f8f6f4 v[62:65], v[182:189], v[66:73], v[62:65], v171, v172 op_sel_hi:[0,0,0]
	v_mov_b64_e32 v[72:73], v[8:9]
	v_mov_b64_e32 v[68:69], v[4:5]
	v_mov_b64_e32 v[40:41], v[8:9]
	v_mov_b64_e32 v[44:45], v[4:5]
	v_mov_b64_e32 v[70:71], v[6:7]
	v_mov_b64_e32 v[66:67], v[2:3]
	v_mov_b64_e32 v[38:39], v[6:7]
	v_mov_b64_e32 v[42:43], v[2:3]
	v_mfma_scale_f32_16x16x128_f8f6f4 v[70:73], v[174:181], v[190:197], v[70:73], v171, v172 op_sel_hi:[0,0,0]
	v_mfma_scale_f32_16x16x128_f8f6f4 v[66:69], v[182:189], v[190:197], v[66:69], v171, v172 op_sel_hi:[0,0,0]
	v_mfma_scale_f32_16x16x128_f8f6f4 v[38:41], v[174:181], v[198:205], v[38:41], v171, v172 op_sel_hi:[0,0,0]
	v_mfma_scale_f32_16x16x128_f8f6f4 v[42:45], v[182:189], v[198:205], v[42:45], v171, v172 op_sel_hi:[0,0,0]
	v_mfma_scale_f32_16x16x128_f8f6f4 v[6:9], v[174:181], v[206:213], v[6:9], v171, v172 op_sel_hi:[0,0,0]
	v_mfma_scale_f32_16x16x128_f8f6f4 v[2:5], v[182:189], v[206:213], v[2:5], v171, v172 op_sel_hi:[0,0,0]
	s_setprio 0
	s_barrier
	ds_read_b128 v[174:177], v163
	ds_read_b128 v[178:181], v155
	ds_read_b128 v[182:185], v164
	ds_read_b128 v[186:189], v165
	s_mov_b32 m0, s59
	v_lshl_add_u64 v[142:143], v[142:143], 0, s[16:17]
	ds_read_b128 v[190:193], v169 offset:32768
	ds_read_b128 v[198:201], v169 offset:34816
	ds_read_b128 v[194:197], v170 offset:32768
	ds_read_b128 v[202:205], v170 offset:34816
	ds_read_b128 v[206:209], v169 offset:36864
	ds_read_b128 v[214:217], v169 offset:38912
	ds_read_b128 v[210:213], v170 offset:36864
	ds_read_b128 v[218:221], v170 offset:38912
	global_load_lds_dwordx4 v[142:143], off
	v_lshl_add_u64 v[142:143], v[144:145], 0, s[16:17]
	s_mov_b32 m0, s60
	s_nop 0
	global_load_lds_dwordx4 v[142:143], off
	s_waitcnt lgkmcnt(8)
	s_barrier
	s_waitcnt lgkmcnt(0)
	s_setprio 1
	v_mfma_scale_f32_16x16x128_f8f6f4 v[90:93], v[174:181], v[190:197], v[90:93], v171, v172 op_sel_hi:[0,0,0]
	v_mfma_scale_f32_16x16x128_f8f6f4 v[94:97], v[182:189], v[190:197], v[94:97], v171, v172 op_sel_hi:[0,0,0]
	v_mfma_scale_f32_16x16x128_f8f6f4 v[102:105], v[174:181], v[198:205], v[102:105], v171, v172 op_sel_hi:[0,0,0]
	v_mfma_scale_f32_16x16x128_f8f6f4 v[98:101], v[182:189], v[198:205], v[98:101], v171, v172 op_sel_hi:[0,0,0]
	v_mfma_scale_f32_16x16x128_f8f6f4 v[74:77], v[174:181], v[206:213], v[74:77], v171, v172 op_sel_hi:[0,0,0]
	v_mfma_scale_f32_16x16x128_f8f6f4 v[78:81], v[182:189], v[206:213], v[78:81], v171, v172 op_sel_hi:[0,0,0]
	v_mfma_scale_f32_16x16x128_f8f6f4 v[86:89], v[174:181], v[214:221], v[86:89], v171, v172 op_sel_hi:[0,0,0]
	v_mfma_scale_f32_16x16x128_f8f6f4 v[82:85], v[182:189], v[214:221], v[82:85], v171, v172 op_sel_hi:[0,0,0]
	s_setprio 0
	s_barrier
	s_mov_b32 m0, s62
	v_lshl_add_u64 v[142:143], v[146:147], 0, s[20:21]
	ds_read_b128 v[224:227], v166
	ds_read_b128 v[228:231], v156
	ds_read_b128 v[232:235], v167
	ds_read_b128 v[236:239], v168
	global_load_lds_dwordx4 v[142:143], off
	v_lshl_add_u64 v[142:143], v[148:149], 0, s[20:21]
	s_mov_b32 m0, s63
	s_nop 0
	global_load_lds_dwordx4 v[142:143], off
	s_barrier
; #define G_STAGE(bufoff, gbase, voff) do { _Pragma("unroll") for (int _i = 0; _i < 2; ++_i) \
;     __builtin_amdgcn_global_load_lds((const unsigned*)((const char*)(gbase) + (voff)[_i]), (LAS unsigned*)(lds + (bufoff) + ldsw + _i * 8192), 16, 0, 0); } while (0)
; #define G_LDA(dst, b, h) do { _Pragma("unroll") for (int m = 0; m < 4; ++m) dst[m] = G_LD2(G_SA(b, h) + aoff + m * 2048, G_SA(b, h) + (P::FP8 ? aoff1 : aoff + 1024) + m * 2048); } while (0)
; #define WAIT_V(n) asm volatile("s_waitcnt vmcnt(" #n ")" ::: "memory")
; #define WAIT_L(n) asm volatile("s_waitcnt lgkmcnt(" #n ")" ::: "memory")
; #define BAR __builtin_amdgcn_s_barrier()
; #define SCHED __builtin_amdgcn_sched_barrier(0)
;   DEV void bias_dma(const Unit& u, LAS float* tabw) const { __builtin_amdgcn_global_load_lds((const unsigned*)bias_src(u, ltid() & 255), (LAS unsigned*)tabw, 4, 0, 0); }
;   DEV void bias_dma(const Unit& u, LAS float* tabw) const { __builtin_amdgcn_global_load_lds((const unsigned*)bias_src(u, ltid() & 255), (LAS unsigned*)tabw, 4, 0, 0); }
; template <class P>
; DEV void gemm_stream(const P& pol) {
;     ...
;       BAR; WAIT_L(0); G_MMA(0, 1, At, B1); BAR;
;       G_LDA(At, 1, 1); G_STAGE(G_SA(1, 0), a20 + kstep, vAc[0]);
;       BAR; WAIT_L(0); G_MMA(1, 0, At, B0); BAR; SCHED;
;       G_STAGE(G_SB(1, 1), b2 + hstep + kstep, voffB);
;       WAIT_V(6); BAR; G_MMA(1, 1, At, B1); BAR;
;       if (P::HASBIAS && has_next && t == 0) pol.bias_dma(nxt, btab + ((ui + 1) & 1) * 256 + ((wid & 3) << 6));
	s_waitcnt lgkmcnt(0)
	s_setprio 1
	v_mfma_scale_f32_16x16x128_f8f6f4 v[34:37], v[224:231], v[190:197], v[34:37], v171, v172 op_sel_hi:[0,0,0]
	v_mfma_scale_f32_16x16x128_f8f6f4 v[46:49], v[232:239], v[190:197], v[46:49], v171, v172 op_sel_hi:[0,0,0]
	v_mfma_scale_f32_16x16x128_f8f6f4 v[54:57], v[224:231], v[198:205], v[54:57], v171, v172 op_sel_hi:[0,0,0]
	v_mfma_scale_f32_16x16x128_f8f6f4 v[50:53], v[232:239], v[198:205], v[50:53], v171, v172 op_sel_hi:[0,0,0]
	v_mfma_scale_f32_16x16x128_f8f6f4 v[18:21], v[224:231], v[206:213], v[18:21], v171, v172 op_sel_hi:[0,0,0]
	v_mfma_scale_f32_16x16x128_f8f6f4 v[22:25], v[232:239], v[206:213], v[22:25], v171, v172 op_sel_hi:[0,0,0]
	v_mfma_scale_f32_16x16x128_f8f6f4 v[30:33], v[224:231], v[214:221], v[30:33], v171, v172 op_sel_hi:[0,0,0]
	v_mfma_scale_f32_16x16x128_f8f6f4 v[26:29], v[232:239], v[214:221], v[26:29], v171, v172 op_sel_hi:[0,0,0]
	s_setprio 0
	s_mov_b32 m0, s64
	v_lshl_add_u64 v[150:151], v[150:151], 0, s[20:21]
	s_barrier
	ds_read_b128 v[142:145], v169 offset:49152
	ds_read_b128 v[190:193], v169 offset:51200
	ds_read_b128 v[146:149], v170 offset:49152
	ds_read_b128 v[194:197], v170 offset:51200
	ds_read_b128 v[198:201], v169 offset:53248
	ds_read_b128 v[206:209], v169 offset:55296
	ds_read_b128 v[202:205], v170 offset:53248
	ds_read_b128 v[210:213], v170 offset:55296
	global_load_lds_dwordx4 v[150:151], off
	v_lshl_add_u64 v[150:151], v[240:241], 0, s[20:21]
	s_mov_b32 m0, s65
	s_nop 0
	global_load_lds_dwordx4 v[150:151], off
	s_barrier
	s_waitcnt lgkmcnt(0)
	s_setprio 1
	v_mfma_scale_f32_16x16x128_f8f6f4 v[114:117], v[174:181], v[142:149], v[114:117], v171, v172 op_sel_hi:[0,0,0]
	v_mfma_scale_f32_16x16x128_f8f6f4 v[118:121], v[182:189], v[142:149], v[118:121], v171, v172 op_sel_hi:[0,0,0]
	v_mfma_scale_f32_16x16x128_f8f6f4 v[126:129], v[174:181], v[190:197], v[126:129], v171, v172 op_sel_hi:[0,0,0]
	v_mfma_scale_f32_16x16x128_f8f6f4 v[122:125], v[182:189], v[190:197], v[122:125], v171, v172 op_sel_hi:[0,0,0]
	v_mfma_scale_f32_16x16x128_f8f6f4 v[106:109], v[174:181], v[198:205], v[106:109], v171, v172 op_sel_hi:[0,0,0]
	v_mfma_scale_f32_16x16x128_f8f6f4 v[110:113], v[182:189], v[198:205], v[110:113], v171, v172 op_sel_hi:[0,0,0]
	v_mfma_scale_f32_16x16x128_f8f6f4 v[14:17], v[174:181], v[206:213], v[14:17], v171, v172 op_sel_hi:[0,0,0]
	v_mfma_scale_f32_16x16x128_f8f6f4 v[10:13], v[182:189], v[206:213], v[10:13], v171, v172 op_sel_hi:[0,0,0]
	s_setprio 0
	s_barrier
	v_lshl_add_u64 v[150:151], v[140:141], 0, s[22:23]
	s_mov_b32 m0, s66
	v_lshl_add_u64 v[174:175], v[150:151], 0, v[130:131]
	global_load_lds_dwordx4 v[174:175], off
	v_lshl_add_u64 v[150:151], v[150:151], 0, v[132:133]
	s_mov_b32 m0, s67
	s_nop 0
	global_load_lds_dwordx4 v[150:151], off
	s_waitcnt vmcnt(6)
	s_barrier
	s_setprio 1
	v_mfma_scale_f32_16x16x128_f8f6f4 v[58:61], v[224:231], v[142:149], v[58:61], v171, v172 op_sel_hi:[0,0,0]
	v_mfma_scale_f32_16x16x128_f8f6f4 v[62:65], v[232:239], v[142:149], v[62:65], v171, v172 op_sel_hi:[0,0,0]
	v_mfma_scale_f32_16x16x128_f8f6f4 v[70:73], v[224:231], v[190:197], v[70:73], v171, v172 op_sel_hi:[0,0,0]
	v_mfma_scale_f32_16x16x128_f8f6f4 v[66:69], v[232:239], v[190:197], v[66:69], v171, v172 op_sel_hi:[0,0,0]
	v_mfma_scale_f32_16x16x128_f8f6f4 v[38:41], v[224:231], v[198:205], v[38:41], v171, v172 op_sel_hi:[0,0,0]
	v_mfma_scale_f32_16x16x128_f8f6f4 v[42:45], v[232:239], v[198:205], v[42:45], v171, v172 op_sel_hi:[0,0,0]
	v_mfma_scale_f32_16x16x128_f8f6f4 v[6:9], v[224:231], v[206:213], v[6:9], v171, v172 op_sel_hi:[0,0,0]
	v_mfma_scale_f32_16x16x128_f8f6f4 v[2:5], v[232:239], v[206:213], v[2:5], v171, v172 op_sel_hi:[0,0,0]
	s_setprio 0
	s_and_b64 vcc, exec, s[4:5]
	s_barrier
	s_cbranch_vccz .LBB0_1545
	s_lshl_b32 s30, s61, 10
	s_and_b32 s30, s30, 0x400
	s_lshl_b64 s[28:29], s[26:27], 13
	s_add_i32 m0, s68, s30
	v_mov_b32_e32 v1, v0
	s_add_u32 s28, s72, s28
	s_addc_u32 s29, s73, s29
	v_lshlrev_b32_sdwa v1, v173, v1 dst_sel:DWORD dst_unused:UNUSED_PAD src0_sel:DWORD src1_sel:BYTE_0
	global_load_lds_dword v1, s[28:29]

; #define LAS __attribute__((address_space(3)))
; #define G_GATHER_OFFS(tab_, rv_) do { _Pragma("unroll") for (int i = 0; i < 2; ++i) { int R_, C_; G_SRC(i, R_, C_); const int ra_ = (tab_)[R_], rb_ = (tab_)[HALF + R_];        \
;     vAc[0][i] = (unsigned)((R_ < (rv_) ? ra_ : 0) * KB + C_); vAc[1][i] = (unsigned)((HALF + R_ < (rv_) ? rb_ : 0) * KB + C_); } } while (0)
; #define G_STAGE(bufoff, gbase, voff) do { _Pragma("unroll") for (int _i = 0; _i < 2; ++_i) \
;     __builtin_amdgcn_global_load_lds((const unsigned*)((const char*)(gbase) + (voff)[_i]), (LAS unsigned*)(lds + (bufoff) + ldsw + _i * 8192), 16, 0, 0); } while (0)
; #define G_LDA(dst, b, h) do { _Pragma("unroll") for (int m = 0; m < 4; ++m) dst[m] = G_LD2(G_SA(b, h) + aoff + m * 2048, G_SA(b, h) + (P::FP8 ? aoff1 : aoff + 1024) + m * 2048); } while (0)
; #define G_LDB(dst, b, h) do { _Pragma("unroll") for (int n = 0; n < 2; ++n) dst[n] = G_LD2(G_SB(b, h) + boff + n * 2048, G_SB(b, h) + (P::FP8 ? boff1 : boff + 1024) + n * 2048); } while (0)
; #define WAIT_V(n) asm volatile("s_waitcnt vmcnt(" #n ")" ::: "memory")
; #define WAIT_L(n) asm volatile("s_waitcnt lgkmcnt(" #n ")" ::: "memory")
; #define BAR __builtin_amdgcn_s_barrier()
; #define SCHED __builtin_amdgcn_sched_barrier(0)
; template <class P>
; DEV void gemm_stream(const P& pol) {
;     ...
;     for (int t = 0; t < nt; t += 2) {
;       const bool last = (t == nt - 2);
;       const size_t k1 = (size_t)(t + 1) * kstep, k2 = (size_t)(t + 2) * kstep;
;       const char* a20 = last ? nA0 : cA0 + k2; const char* a21 = last ? nA1 : cA1 + k2; const char* b2 = last ? nB : cB + k2;
;       G_LDB(B0, 0, 0); SCHED; G_LDA(At, 0, 0); G_STAGE(G_SA(1, 1), cA1 + k1, vAc[1]);
;       WAIT_L(8); BAR; WAIT_L(0); G_MMA(0, 0, At, B0); BAR; SCHED;
;       if (P::GATHER && last && has_next) { LAS int* tab = arow + ((ui + 1) & 1) * 256; G_GATHER_OFFS(tab, nxt.rv); }
;       G_LDB(B1, 0, 1); G_STAGE(G_SB(0, 0), b2, voffB);
;       BAR; WAIT_L(0); G_MMA(0, 1, At, B1); BAR;
;       G_LDA(At, 0, 1); G_STAGE(G_SA(0, 0), a20, vAc[0]);
;       BAR; WAIT_L(0); G_MMA(1, 0, At, B0); BAR; SCHED;
;       G_STAGE(G_SB(0, 1), b2 + hstep, voffB);
;       WAIT_V(6); BAR; G_MMA(1, 1, At, B1); BAR;
;       G_LDB(B0, 1, 0); SCHED; G_LDA(At, 1, 0); G_STAGE(G_SA(0, 1), a21, vAc[1]);
;       WAIT_L(8); BAR; WAIT_L(0); G_MMA(0, 0, At, B0); BAR; SCHED;
.LBB0_1546:
	ds_read_b128 v[174:177], v157
	ds_read_b128 v[178:181], v153
	ds_read_b128 v[182:185], v158
	ds_read_b128 v[186:189], v159
	s_add_u32 s44, s38, 0x80
	s_addc_u32 s45, s39, 0
	s_cmp_eq_u32 s88, 12
	s_cselect_b64 vcc, -1, 0
	s_and_b64 s[36:37], vcc, exec
	s_cselect_b32 s37, s85, s45
	s_cselect_b32 s36, s86, s44
	s_mov_b32 m0, s76
	v_lshl_add_u64 v[142:143], s[38:39], 0, v[134:135]
	ds_read_b128 v[190:193], v169
	ds_read_b128 v[198:201], v169 offset:2048
	ds_read_b128 v[194:197], v170
	ds_read_b128 v[202:205], v170 offset:2048
	ds_read_b128 v[206:209], v169 offset:4096
	ds_read_b128 v[214:217], v169 offset:6144
	ds_read_b128 v[210:213], v170 offset:4096
	ds_read_b128 v[218:221], v170 offset:6144
	global_load_lds_dwordx4 v[142:143], off
	v_lshl_add_u64 v[142:143], s[38:39], 0, v[136:137]
	s_mov_b32 m0, s77
	s_cselect_b32 s45, s83, s87
	global_load_lds_dwordx4 v[142:143], off
	s_waitcnt lgkmcnt(8)
	s_barrier
	s_waitcnt lgkmcnt(0)
	s_cselect_b32 s44, s84, s27
	s_setprio 1
	v_mfma_scale_f32_16x16x128_f8f6f4 v[90:93], v[174:181], v[190:197], v[90:93], v171, v172 op_sel_hi:[0,0,0]
	v_mfma_scale_f32_16x16x128_f8f6f4 v[94:97], v[182:189], v[190:197], v[94:97], v171, v172 op_sel_hi:[0,0,0]
	v_mfma_scale_f32_16x16x128_f8f6f4 v[102:105], v[174:181], v[198:205], v[102:105], v171, v172 op_sel_hi:[0,0,0]
	v_mfma_scale_f32_16x16x128_f8f6f4 v[98:101], v[182:189], v[198:205], v[98:101], v171, v172 op_sel_hi:[0,0,0]
	v_mfma_scale_f32_16x16x128_f8f6f4 v[74:77], v[174:181], v[206:213], v[74:77], v171, v172 op_sel_hi:[0,0,0]
	v_mfma_scale_f32_16x16x128_f8f6f4 v[78:81], v[182:189], v[206:213], v[78:81], v171, v172 op_sel_hi:[0,0,0]
	v_mfma_scale_f32_16x16x128_f8f6f4 v[86:89], v[174:181], v[214:221], v[86:89], v171, v172 op_sel_hi:[0,0,0]
	v_mfma_scale_f32_16x16x128_f8f6f4 v[82:85], v[182:189], v[214:221], v[82:85], v171, v172 op_sel_hi:[0,0,0]
	s_setprio 0
	s_barrier
	v_cndmask_b32_e32 v143, v141, v1, vcc
	v_cndmask_b32_e32 v142, v140, v138, vcc
	s_mov_b32 m0, s54
	v_lshl_add_u64 v[148:149], v[142:143], 0, v[130:131]
	ds_read_b128 v[224:227], v160
	ds_read_b128 v[228:231], v154
	ds_read_b128 v[232:235], v161
	ds_read_b128 v[236:239], v162
	global_load_lds_dwordx4 v[148:149], off
	v_lshl_add_u64 v[150:151], v[142:143], 0, v[132:133]
	s_mov_b32 m0, s55
	s_nop 0
	global_load_lds_dwordx4 v[150:151], off
	s_barrier
	s_waitcnt lgkmcnt(0)
	s_setprio 1
	v_mfma_scale_f32_16x16x128_f8f6f4 v[34:37], v[224:231], v[190:197], v[34:37], v171, v172 op_sel_hi:[0,0,0]
	v_mfma_scale_f32_16x16x128_f8f6f4 v[46:49], v[232:239], v[190:197], v[46:49], v171, v172 op_sel_hi:[0,0,0]
	v_mfma_scale_f32_16x16x128_f8f6f4 v[54:57], v[224:231], v[198:205], v[54:57], v171, v172 op_sel_hi:[0,0,0]
	v_mfma_scale_f32_16x16x128_f8f6f4 v[50:53], v[232:239], v[198:205], v[50:53], v171, v172 op_sel_hi:[0,0,0]
	v_mfma_scale_f32_16x16x128_f8f6f4 v[18:21], v[224:231], v[206:213], v[18:21], v171, v172 op_sel_hi:[0,0,0]
	v_mfma_scale_f32_16x16x128_f8f6f4 v[22:25], v[232:239], v[206:213], v[22:25], v171, v172 op_sel_hi:[0,0,0]
	v_mfma_scale_f32_16x16x128_f8f6f4 v[30:33], v[224:231], v[214:221], v[30:33], v171, v172 op_sel_hi:[0,0,0]
	v_mfma_scale_f32_16x16x128_f8f6f4 v[26:29], v[232:239], v[214:221], v[26:29], v171, v172 op_sel_hi:[0,0,0]
	s_setprio 0
	s_mov_b32 m0, s53
	v_lshl_add_u64 v[144:145], s[44:45], 0, v[134:135]
	s_barrier
	ds_read_b128 v[190:193], v169 offset:16384
	ds_read_b128 v[198:201], v169 offset:18432
	ds_read_b128 v[194:197], v170 offset:16384
	ds_read_b128 v[202:205], v170 offset:18432
	ds_read_b128 v[206:209], v169 offset:20480
	ds_read_b128 v[214:217], v169 offset:22528
	ds_read_b128 v[210:213], v170 offset:20480
	ds_read_b128 v[218:221], v170 offset:22528
	global_load_lds_dwordx4 v[144:145], off
	v_lshl_add_u64 v[146:147], s[44:45], 0, v[136:137]
	s_mov_b32 m0, s56
	s_nop 0
	global_load_lds_dwordx4 v[146:147], off
	s_barrier
	s_waitcnt lgkmcnt(0)
	s_setprio 1
	v_mfma_scale_f32_16x16x128_f8f6f4 v[114:117], v[174:181], v[190:197], v[114:117], v171, v172 op_sel_hi:[0,0,0]
	v_mfma_scale_f32_16x16x128_f8f6f4 v[118:121], v[182:189], v[190:197], v[118:121], v171, v172 op_sel_hi:[0,0,0]
	v_mfma_scale_f32_16x16x128_f8f6f4 v[126:129], v[174:181], v[198:205], v[126:129], v171, v172 op_sel_hi:[0,0,0]
	v_mfma_scale_f32_16x16x128_f8f6f4 v[122:125], v[182:189], v[198:205], v[122:125], v171, v172 op_sel_hi:[0,0,0]
	v_mfma_scale_f32_16x16x128_f8f6f4 v[106:109], v[174:181], v[206:213], v[106:109], v171, v172 op_sel_hi:[0,0,0]
	v_mfma_scale_f32_16x16x128_f8f6f4 v[110:113], v[182:189], v[206:213], v[110:113], v171, v172 op_sel_hi:[0,0,0]
	v_mfma_scale_f32_16x16x128_f8f6f4 v[14:17], v[174:181], v[214:221], v[14:17], v171, v172 op_sel_hi:[0,0,0]
	v_mfma_scale_f32_16x16x128_f8f6f4 v[10:13], v[182:189], v[214:221], v[10:13], v171, v172 op_sel_hi:[0,0,0]
	s_setprio 0
	s_barrier
	v_lshl_add_u64 v[174:175], v[142:143], 0, s[8:9]
	s_mov_b32 m0, s57
	v_lshl_add_u64 v[176:177], v[174:175], 0, v[130:131]
	global_load_lds_dwordx4 v[176:177], off
	v_lshl_add_u64 v[174:175], v[174:175], 0, v[132:133]
	s_mov_b32 m0, s58
	s_nop 0
	global_load_lds_dwordx4 v[174:175], off
	s_waitcnt vmcnt(6)
	s_barrier
	s_setprio 1
	v_mfma_scale_f32_16x16x128_f8f6f4 v[58:61], v[224:231], v[190:197], v[58:61], v171, v172 op_sel_hi:[0,0,0]
	v_mfma_scale_f32_16x16x128_f8f6f4 v[62:65], v[232:239], v[190:197], v[62:65], v171, v172 op_sel_hi:[0,0,0]
	v_mfma_scale_f32_16x16x128_f8f6f4 v[70:73], v[224:231], v[198:205], v[70:73], v171, v172 op_sel_hi:[0,0,0]
	v_mfma_scale_f32_16x16x128_f8f6f4 v[66:69], v[232:239], v[198:205], v[66:69], v171, v172 op_sel_hi:[0,0,0]
	v_mfma_scale_f32_16x16x128_f8f6f4 v[38:41], v[224:231], v[206:213], v[38:41], v171, v172 op_sel_hi:[0,0,0]
	v_mfma_scale_f32_16x16x128_f8f6f4 v[42:45], v[232:239], v[206:213], v[42:45], v171, v172 op_sel_hi:[0,0,0]
	v_mfma_scale_f32_16x16x128_f8f6f4 v[6:9], v[224:231], v[214:221], v[6:9], v171, v172 op_sel_hi:[0,0,0]
	v_mfma_scale_f32_16x16x128_f8f6f4 v[2:5], v[232:239], v[214:221], v[2:5], v171, v172 op_sel_hi:[0,0,0]
	s_setprio 0
	s_barrier
; #define G_STAGE(bufoff, gbase, voff) do { _Pragma("unroll") for (int _i = 0; _i < 2; ++_i) \
;     __builtin_amdgcn_global_load_lds((const unsigned*)((const char*)(gbase) + (voff)[_i]), (LAS unsigned*)(lds + (bufoff) + ldsw + _i * 8192), 16, 0, 0); } while (0)
; #define G_LDA(dst, b, h) do { _Pragma("unroll") for (int m = 0; m < 4; ++m) dst[m] = G_LD2(G_SA(b, h) + aoff + m * 2048, G_SA(b, h) + (P::FP8 ? aoff1 : aoff + 1024) + m * 2048); } while (0)
; #define G_LDB(dst, b, h) do { _Pragma("unroll") for (int n = 0; n < 2; ++n) dst[n] = G_LD2(G_SB(b, h) + boff + n * 2048, G_SB(b, h) + (P::FP8 ? boff1 : boff + 1024) + n * 2048); } while (0)
; #define WAIT_V(n) asm volatile("s_waitcnt vmcnt(" #n ")" ::: "memory")
; #define WAIT_L(n) asm volatile("s_waitcnt lgkmcnt(" #n ")" ::: "memory")
; #define BAR __builtin_amdgcn_s_barrier()
; #define SCHED __builtin_amdgcn_sched_barrier(0)
; template <class P>
; DEV void gemm_stream(const P& pol) {
;     ...
;       G_LDB(B0, 1, 0); SCHED; G_LDA(At, 1, 0); G_STAGE(G_SA(0, 1), a21, vAc[1]);
;       WAIT_L(8); BAR; WAIT_L(0); G_MMA(0, 0, At, B0); BAR; SCHED;
;       G_LDB(B1, 1, 1); G_STAGE(G_SB(1, 0), b2 + kstep, voffB);
;       BAR; WAIT_L(0); G_MMA(0, 1, At, B1); BAR;
;       G_LDA(At, 1, 1); G_STAGE(G_SA(1, 0), a20 + kstep, vAc[0]);
;       BAR; WAIT_L(0); G_MMA(1, 0, At, B0); BAR; SCHED;
;       G_STAGE(G_SB(1, 1), b2 + hstep + kstep, voffB);
;       WAIT_V(6); BAR; G_MMA(1, 1, At, B1); BAR;
	ds_read_b128 v[174:177], v163
	ds_read_b128 v[178:181], v155
	ds_read_b128 v[182:185], v164
	ds_read_b128 v[186:189], v165
	s_mov_b32 m0, s59
	v_lshl_add_u64 v[224:225], s[36:37], 0, v[134:135]
	ds_read_b128 v[190:193], v169 offset:32768
	ds_read_b128 v[198:201], v169 offset:34816
	ds_read_b128 v[194:197], v170 offset:32768
	ds_read_b128 v[202:205], v170 offset:34816
	ds_read_b128 v[206:209], v169 offset:36864
	ds_read_b128 v[214:217], v169 offset:38912
	ds_read_b128 v[210:213], v170 offset:36864
	ds_read_b128 v[218:221], v170 offset:38912
	global_load_lds_dwordx4 v[224:225], off
	v_lshl_add_u64 v[224:225], s[36:37], 0, v[136:137]
	s_mov_b32 m0, s60
	s_nop 0
	global_load_lds_dwordx4 v[224:225], off
	s_waitcnt lgkmcnt(8)
	s_barrier
	s_waitcnt lgkmcnt(0)
	s_setprio 1
	v_mfma_scale_f32_16x16x128_f8f6f4 v[90:93], v[174:181], v[190:197], v[90:93], v171, v172 op_sel_hi:[0,0,0]
	v_mfma_scale_f32_16x16x128_f8f6f4 v[94:97], v[182:189], v[190:197], v[94:97], v171, v172 op_sel_hi:[0,0,0]
	v_mfma_scale_f32_16x16x128_f8f6f4 v[102:105], v[174:181], v[198:205], v[102:105], v171, v172 op_sel_hi:[0,0,0]
	v_mfma_scale_f32_16x16x128_f8f6f4 v[98:101], v[182:189], v[198:205], v[98:101], v171, v172 op_sel_hi:[0,0,0]
	v_mfma_scale_f32_16x16x128_f8f6f4 v[74:77], v[174:181], v[206:213], v[74:77], v171, v172 op_sel_hi:[0,0,0]
	v_mfma_scale_f32_16x16x128_f8f6f4 v[78:81], v[182:189], v[206:213], v[78:81], v171, v172 op_sel_hi:[0,0,0]
	v_mfma_scale_f32_16x16x128_f8f6f4 v[86:89], v[174:181], v[214:221], v[86:89], v171, v172 op_sel_hi:[0,0,0]
	v_mfma_scale_f32_16x16x128_f8f6f4 v[82:85], v[182:189], v[214:221], v[82:85], v171, v172 op_sel_hi:[0,0,0]
	s_setprio 0
	s_barrier
	s_mov_b32 m0, s62
	v_lshl_add_u64 v[148:149], v[148:149], 0, s[10:11]
	ds_read_b128 v[224:227], v166
	ds_read_b128 v[228:231], v156
	ds_read_b128 v[232:235], v167
	ds_read_b128 v[236:239], v168
	global_load_lds_dwordx4 v[148:149], off
	v_lshl_add_u64 v[148:149], v[150:151], 0, s[10:11]
	s_mov_b32 m0, s63
	s_nop 0
	global_load_lds_dwordx4 v[148:149], off
	s_barrier
	s_waitcnt lgkmcnt(0)
	s_setprio 1
	v_mfma_scale_f32_16x16x128_f8f6f4 v[34:37], v[224:231], v[190:197], v[34:37], v171, v172 op_sel_hi:[0,0,0]
	v_mfma_scale_f32_16x16x128_f8f6f4 v[46:49], v[232:239], v[190:197], v[46:49], v171, v172 op_sel_hi:[0,0,0]
	v_mfma_scale_f32_16x16x128_f8f6f4 v[54:57], v[224:231], v[198:205], v[54:57], v171, v172 op_sel_hi:[0,0,0]
	v_mfma_scale_f32_16x16x128_f8f6f4 v[50:53], v[232:239], v[198:205], v[50:53], v171, v172 op_sel_hi:[0,0,0]
	v_mfma_scale_f32_16x16x128_f8f6f4 v[18:21], v[224:231], v[206:213], v[18:21], v171, v172 op_sel_hi:[0,0,0]
	v_mfma_scale_f32_16x16x128_f8f6f4 v[22:25], v[232:239], v[206:213], v[22:25], v171, v172 op_sel_hi:[0,0,0]
	v_mfma_scale_f32_16x16x128_f8f6f4 v[30:33], v[224:231], v[214:221], v[30:33], v171, v172 op_sel_hi:[0,0,0]
	v_mfma_scale_f32_16x16x128_f8f6f4 v[26:29], v[232:239], v[214:221], v[26:29], v171, v172 op_sel_hi:[0,0,0]
	s_setprio 0
	s_mov_b32 m0, s64
	v_lshl_add_u64 v[144:145], v[144:145], 0, s[10:11]
	s_barrier
	ds_read_b128 v[190:193], v169 offset:49152
	ds_read_b128 v[198:201], v169 offset:51200
	ds_read_b128 v[194:197], v170 offset:49152
	ds_read_b128 v[202:205], v170 offset:51200
	ds_read_b128 v[206:209], v169 offset:53248
	ds_read_b128 v[214:217], v169 offset:55296
	ds_read_b128 v[210:213], v170 offset:53248
	ds_read_b128 v[218:221], v170 offset:55296
	global_load_lds_dwordx4 v[144:145], off
	v_lshl_add_u64 v[144:145], v[146:147], 0, s[10:11]
	s_mov_b32 m0, s65
	s_nop 0
	global_load_lds_dwordx4 v[144:145], off
	s_barrier
	s_waitcnt lgkmcnt(0)
	s_setprio 1
	v_mfma_scale_f32_16x16x128_f8f6f4 v[114:117], v[174:181], v[190:197], v[114:117], v171, v172 op_sel_hi:[0,0,0]
	v_mfma_scale_f32_16x16x128_f8f6f4 v[118:121], v[182:189], v[190:197], v[118:121], v171, v172 op_sel_hi:[0,0,0]
	v_mfma_scale_f32_16x16x128_f8f6f4 v[126:129], v[174:181], v[198:205], v[126:129], v171, v172 op_sel_hi:[0,0,0]
	v_mfma_scale_f32_16x16x128_f8f6f4 v[122:125], v[182:189], v[198:205], v[122:125], v171, v172 op_sel_hi:[0,0,0]
	v_mfma_scale_f32_16x16x128_f8f6f4 v[106:109], v[174:181], v[206:213], v[106:109], v171, v172 op_sel_hi:[0,0,0]
	v_mfma_scale_f32_16x16x128_f8f6f4 v[110:113], v[182:189], v[206:213], v[110:113], v171, v172 op_sel_hi:[0,0,0]
	v_mfma_scale_f32_16x16x128_f8f6f4 v[14:17], v[174:181], v[214:221], v[14:17], v171, v172 op_sel_hi:[0,0,0]
	v_mfma_scale_f32_16x16x128_f8f6f4 v[10:13], v[182:189], v[214:221], v[10:13], v171, v172 op_sel_hi:[0,0,0]
	s_setprio 0
	s_barrier
	v_lshl_add_u64 v[142:143], v[142:143], 0, s[12:13]
	s_mov_b32 m0, s66
	v_lshl_add_u64 v[144:145], v[142:143], 0, v[130:131]
	global_load_lds_dwordx4 v[144:145], off
	v_lshl_add_u64 v[142:143], v[142:143], 0, v[132:133]
	s_mov_b32 m0, s67
	s_nop 0
	global_load_lds_dwordx4 v[142:143], off
	s_waitcnt vmcnt(6)
	s_barrier
	s_setprio 1
	v_mfma_scale_f32_16x16x128_f8f6f4 v[58:61], v[224:231], v[190:197], v[58:61], v171, v172 op_sel_hi:[0,0,0]
	v_mfma_scale_f32_16x16x128_f8f6f4 v[62:65], v[232:239], v[190:197], v[62:65], v171, v172 op_sel_hi:[0,0,0]
	v_mfma_scale_f32_16x16x128_f8f6f4 v[70:73], v[224:231], v[198:205], v[70:73], v171, v172 op_sel_hi:[0,0,0]
	v_mfma_scale_f32_16x16x128_f8f6f4 v[66:69], v[232:239], v[198:205], v[66:69], v171, v172 op_sel_hi:[0,0,0]
	v_mfma_scale_f32_16x16x128_f8f6f4 v[38:41], v[224:231], v[206:213], v[38:41], v171, v172 op_sel_hi:[0,0,0]
	v_mfma_scale_f32_16x16x128_f8f6f4 v[42:45], v[232:239], v[206:213], v[42:45], v171, v172 op_sel_hi:[0,0,0]
	v_mfma_scale_f32_16x16x128_f8f6f4 v[6:9], v[224:231], v[214:221], v[6:9], v171, v172 op_sel_hi:[0,0,0]
	v_mfma_scale_f32_16x16x128_f8f6f4 v[2:5], v[232:239], v[214:221], v[2:5], v171, v172 op_sel_hi:[0,0,0]
	s_setprio 0
	s_add_i32 s88, s88, 2
	s_add_u32 s38, s38, 0x100
	s_addc_u32 s39, s39, 0
	s_add_u32 s27, s27, 0x100
	s_addc_u32 s87, s87, 0
	s_cmp_gt_u32 s88, 13
	v_lshl_add_u64 v[140:141], v[140:141], 0, s[16:17]
	s_barrier
; DEV int ltid() { int t = threadIdx.x; asm volatile("" : "+v"(t)); return t; }
; DEV CParams* launder(CParams* p) { asm volatile("" : "+s"(p)); return p; }
; DEV unsigned cvt_pk4_fp8(f32x4 v) { unsigned r = 0; r = __builtin_amdgcn_cvt_pk_fp8_f32(v[0], v[1], r, false); r = __builtin_amdgcn_cvt_pk_fp8_f32(v[2], v[3], r, true); return r; }
; template <int LB> DEV void stage_store_block(const unsigned (&v)[4][LB / 4], unsigned char* dst, long row_stride) {
;   extern __shared__ __attribute__((aligned(16))) char shm[];
;   constexpr int MP = LB == 8 ? 4 : (LB == 16 ? 2 : 1), PITCH = 16 * LB + 16, ROWS = 16 * MP;
;   static_assert(ROWS * PITCH <= STG_HALF, "staging region");
;   const int tid = ltid(), wr = tid >> 8, wc = (tid >> 6) & 3, fr = tid & 15, fq = (tid >> 4) & 3;
;   char* stg = shm + STG_OFF + wr * STG_HALF;
;   const int t4 = tid & 255;
; #pragma unroll
;   for (int ps = 0; ps < 4 / MP; ++ps) {
; #pragma unroll
;     for (int mm = 0; mm < MP; ++mm) {
;       char* wp = stg + (16 * mm + fr) * PITCH + (4 * wc + fq) * LB; const int m = ps * MP + mm;
;       if (LB == 8) *(u32x2*)wp = (u32x2){v[m][0], v[m][1]};
;       else { *(u32x4*)wp = (u32x4){v[m][0], v[m][1], v[m][2], v[m][3]}; if (LB == 32) *(u32x4*)(wp + 16) = (u32x4){v[m][LB / 4 - 4], v[m][LB / 4 - 3], v[m][LB / 4 - 2], v[m][LB / 4 - 1]}; }
;     }
;     asm volatile("s_waitcnt lgkmcnt(0)" ::: "memory"); __builtin_amdgcn_s_barrier(); asm volatile("" ::: "memory");
; #pragma unroll
;     for (int k = 0; k < 2; ++k) { const int idx = k * 256 + t4, row = idx / LB, ch = idx % LB;
;       *(u32x4*)(dst + (long)(ps * ROWS + row) * row_stride + ch * 16) = *(const u32x4*)(stg + row * PITCH + ch * 16); }
;     asm volatile("s_waitcnt lgkmcnt(0)" ::: "memory"); __builtin_amdgcn_s_barrier(); asm volatile("" ::: "memory");
;   }
;   DEV void operator()(const AccT& acc, int wr, int wc, int fr, int fq) const {
;     CParams& P = *launder(p); const int row0 = srow0 + wr * 64 + fr;
; #pragma unroll
;     for (int bj = 0; bj < 2; ++bj)
; #pragma unroll
;       for (int ai = 0; ai < 2; ++ai) {
;         unsigned vals[4][2];
; #pragma unroll
;         for (int m = 0; m < 4; ++m) { vals[m][0] = cvt_pk4_fp8(acc[ai][bj][m][0]); vals[m][1] = cvt_pk4_fp8(acc[ai][bj][m][1]); }
;         stage_store_block<8>(vals, P.ys8 + (long)(srow0 + ai * HALF + wr * 64) * DM + pn * 256 + bj * HALF, DM);
;       }
;   }
	s_cbranch_scc0 .LBB0_1546
	v_mov_b32_e32 v140, 0
	v_cvt_pk_fp8_f32 v140, v90, v91
	v_mov_b32_e32 v141, 0
	v_cvt_pk_fp8_f32 v141, v94, v95
	v_mov_b32_e32 v90, 0
	v_mov_b32_e32 v91, 0
	v_cvt_pk_fp8_f32 v140, v92, v93 op_sel:[0,0,1]
	v_mov_b32_e32 v92, 0
	s_mov_b64 s[36:37], s[6:7]
	v_cvt_pk_fp8_f32 v90, v102, v103
	v_cvt_pk_fp8_f32 v91, v98, v99
	v_cvt_pk_fp8_f32 v92, v74, v75
	v_mov_b32_e32 v93, 0
	s_nop 7
	s_nop 7
	s_load_dwordx2 s[38:39], s[36:37], 0x1d8
	v_cvt_pk_fp8_f32 v93, v78, v79
	v_mov_b32_e32 v74, 0
	v_mov_b32_e32 v75, 0
	s_lshl_b32 s27, s82, 8
	v_cvt_pk_fp8_f32 v74, v86, v87
	v_cvt_pk_fp8_f32 v75, v82, v83
	v_cvt_pk_fp8_f32 v141, v96, v97 op_sel:[0,0,1]
	s_add_i32 s44, s27, s69
	v_mov_b32_e32 v1, v0
	v_cvt_pk_fp8_f32 v90, v104, v105 op_sel:[0,0,1]
	v_cvt_pk_fp8_f32 v91, v100, v101 op_sel:[0,0,1]
	v_cvt_pk_fp8_f32 v92, v76, v77 op_sel:[0,0,1]
	s_ashr_i32 s45, s44, 31
	v_mov_b32_e32 v86, s78
	v_lshrrev_b32_e32 v76, 8, v1
	v_and_b32_e32 v77, 15, v1
	v_lshrrev_b32_e32 v78, 1, v1
	v_lshlrev_b32_e32 v79, 4, v1
	v_cvt_pk_fp8_f32 v93, v80, v81 op_sel:[0,0,1]
	s_lshl_b64 s[36:37], s[44:45], 11
	v_mad_i32_i24 v76, v76, s79, v86
	v_and_b32_e32 v78, 0x78, v78
	v_and_b32_e32 v138, 0x70, v79
	v_mul_u32_u24_e32 v77, 0x90, v77
	v_cvt_pk_fp8_f32 v74, v88, v89 op_sel:[0,0,1]
	v_cvt_pk_fp8_f32 v75, v84, v85 op_sel:[0,0,1]
	s_waitcnt lgkmcnt(0)
	s_add_u32 s27, s38, s36
	v_add_u32_e32 v79, v76, v138
	v_add3_u32 v76, v76, v78, v77
	s_addc_u32 s37, s39, s37
	ds_write_b64 v76, v[140:141]
	ds_write_b64 v76, v[90:91] offset:2304
	ds_write_b64 v76, v[92:93] offset:4608
	ds_write_b64 v76, v[74:75] offset:6912
	v_and_b32_e32 v78, 0xf8, v1
	v_bfe_u32 v1, v1, 3, 5
	s_add_u32 s36, s27, s14
	s_waitcnt lgkmcnt(0)
	s_barrier
	v_mad_u32_u24 v1, v1, s80, v79
	s_addc_u32 s37, s37, s15
	ds_read_b128 v[74:77], v1
	v_or_b32_e32 v1, 0x100, v78
	v_lshl_add_u64 v[82:83], s[36:37], 0, v[138:139]
	v_lshlrev_b32_e32 v138, 8, v78
	v_lshrrev_b32_e32 v78, 3, v1
	v_mad_u32_u24 v78, v78, s80, v79
	ds_read_b128 v[78:81], v78
	v_lshl_add_u64 v[84:85], v[82:83], 0, v[138:139]
	v_lshlrev_b32_e32 v138, 8, v1
	s_waitcnt lgkmcnt(0)
	global_store_dwordx4 v[84:85], v[74:77], off
	s_addk_i32 s44, 0x80
	v_mov_b32_e32 v1, v0
	v_lshl_add_u64 v[74:75], v[82:83], 0, v[138:139]
	global_store_dwordx4 v[74:75], v[78:81], off
	v_mov_b32_e32 v74, v139
	v_mov_b32_e32 v75, v139
	v_cvt_pk_fp8_f32 v74, v114, v115
	v_cvt_pk_fp8_f32 v75, v118, v119
	v_mov_b32_e32 v76, v139
	v_mov_b32_e32 v77, v139
	v_mov_b32_e32 v81, v139
	v_cvt_pk_fp8_f32 v76, v126, v127
	v_cvt_pk_fp8_f32 v77, v122, v123
	v_mov_b32_e32 v78, v139
	v_mov_b32_e32 v79, v139
	v_cvt_pk_fp8_f32 v81, v10, v11
	v_cvt_pk_fp8_f32 v78, v106, v107
	v_cvt_pk_fp8_f32 v79, v110, v111
	v_mov_b32_e32 v80, v139
	v_cvt_pk_fp8_f32 v80, v14, v15
	v_cvt_pk_fp8_f32 v74, v116, v117 op_sel:[0,0,1]
	v_cvt_pk_fp8_f32 v75, v120, v121 op_sel:[0,0,1]
	s_waitcnt lgkmcnt(0)
	s_barrier
	v_cvt_pk_fp8_f32 v76, v128, v129 op_sel:[0,0,1]
	v_cvt_pk_fp8_f32 v77, v124, v125 op_sel:[0,0,1]
	v_cvt_pk_fp8_f32 v81, v12, v13 op_sel:[0,0,1]
	s_ashr_i32 s45, s44, 31
	v_cvt_pk_fp8_f32 v78, v108, v109 op_sel:[0,0,1]
	v_lshrrev_b32_e32 v10, 8, v1
	v_and_b32_e32 v11, 15, v1
	v_lshrrev_b32_e32 v12, 1, v1
	v_lshlrev_b32_e32 v13, 4, v1
	v_cvt_pk_fp8_f32 v79, v112, v113 op_sel:[0,0,1]
	s_lshl_b64 s[44:45], s[44:45], 11
	v_mad_i32_i24 v10, v10, s79, v86
	v_and_b32_e32 v12, 0x78, v12
	v_and_b32_e32 v138, 0x70, v13
	v_mul_u32_u24_e32 v11, 0x90, v11
	v_cvt_pk_fp8_f32 v80, v16, v17 op_sel:[0,0,1]
	s_add_u32 s27, s38, s44
	v_add_u32_e32 v14, v10, v138
	v_add3_u32 v10, v10, v12, v11
	s_addc_u32 s39, s39, s45
	ds_write_b64 v10, v[74:75]
	ds_write_b64 v10, v[76:77] offset:2304
	ds_write_b64 v10, v[78:79] offset:4608
	ds_write_b64 v10, v[80:81] offset:6912
	v_and_b32_e32 v15, 0xf8, v1
	v_bfe_u32 v1, v1, 3, 5
	s_add_u32 s38, s27, s14
	s_waitcnt lgkmcnt(0)
	s_barrier
; DEV CParams* launder(CParams* p) { asm volatile("" : "+s"(p)); return p; }
; DEV unsigned cvt_pk4_fp8(f32x4 v) { unsigned r = 0; r = __builtin_amdgcn_cvt_pk_fp8_f32(v[0], v[1], r, false); r = __builtin_amdgcn_cvt_pk_fp8_f32(v[2], v[3], r, true); return r; }
; #define G_ZERO() do { _Pragma("unroll") for (int a_ = 0; a_ < 2; ++a_) _Pragma("unroll") for (int b_ = 0; b_ < 2; ++b_) _Pragma("unroll") for (int m_ = 0; m_ < 4; ++m_) _Pragma("unroll") for (int n_ = 0; n_ < 2; ++n_) \
;     acc[a_][b_][m_][n_] = (f32x4){0.f, 0.f, 0.f, 0.f}; } while (0)
; #define G_BIAS(tab_) do { _Pragma("unroll") for (int b_ = 0; b_ < 2; ++b_) _Pragma("unroll") for (int n_ = 0; n_ < 2; ++n_) { bv[b_][n_] = *(const LAS f32x4*)((tab_) + 128 * b_ + 32 * wc + 8 * fq + 4 * n_); \
;     if (b_ == 1 && P::BIAS_LIN1) bv[b_][n_] = bv[b_][n_] + 1.0f; } } while (0)
; #define G_INIT() do { _Pragma("unroll") for (int a_ = 0; a_ < 2; ++a_) _Pragma("unroll") for (int b_ = 0; b_ < 2; ++b_) _Pragma("unroll") for (int m_ = 0; m_ < 4; ++m_) _Pragma("unroll") for (int n_ = 0; n_ < 2; ++n_) \
;     acc[a_][b_][m_][n_] = bv[b_][n_]; } while (0)
;   DEV void epi(const Unit& u, const AccT& acc, int wr, int wc, int fr, int fq) const { EpiIn e{p, u.pm, u.pn}; e(acc, wr, wc, fr, fq); }
;   DEV void epi(const Unit& u, const AccT& acc, int wr, int wc, int fr, int fq) const { EpiKV e{p, u.pm, u.pn}; e(acc, wr, wc, fr, fq); }
; template <class P>
; DEV void gemm_stream(const P& pol) {
;     ...
;     pol.epi(cur, acc, wr, wc, fr, fq);
;     if (!has_next) break;
;     if (P::HASBIAS) { G_BIAS(btab + ((ui + 1) & 1) * 256); G_INIT(); } else G_ZERO();
;     cur = nxt; cA0 = nA0; cA1 = nA1; cB = nB; ++ui;
;     if (P::ROWSKIP) rvw = cur.rv - 64 * wr;
;   DEV void operator()(const AccT& acc, int wr, int wc, int fr, int fq) const {
;     CParams& P = *launder(p); const int row0 = srow0 + wr * 64 + fr;
; #pragma unroll
;     for (int bj = 0; bj < 2; ++bj)
; #pragma unroll
;       for (int ai = 0; ai < 2; ++ai) {
;         unsigned vals[4][2];
; #pragma unroll
;         for (int m = 0; m < 4; ++m) { vals[m][0] = cvt_pk4_fp8(acc[ai][bj][m][0]); vals[m][1] = cvt_pk4_fp8(acc[ai][bj][m][1]); }
;         stage_store_block<8>(vals, P.ys8 + (long)(srow0 + ai * HALF + wr * 64) * DM + pn * 256 + bj * HALF, DM);
;       }
;   }
	v_mad_u32_u24 v1, v1, s80, v14
	s_addc_u32 s39, s39, s15
	ds_read_b128 v[10:13], v1
	v_or_b32_e32 v1, 0x100, v15
	v_lshl_add_u64 v[74:75], s[38:39], 0, v[138:139]
	v_lshlrev_b32_e32 v138, 8, v15
	v_lshrrev_b32_e32 v15, 3, v1
	v_mad_u32_u24 v14, v15, s80, v14
	ds_read_b128 v[14:17], v14
	v_lshl_add_u64 v[76:77], v[74:75], 0, v[138:139]
	v_lshlrev_b32_e32 v138, 8, v1
	s_waitcnt lgkmcnt(0)
	global_store_dwordx4 v[76:77], v[10:13], off
	v_mov_b32_e32 v1, v0
	s_andn2_b64 vcc, exec, s[4:5]
	v_lshl_add_u64 v[10:11], v[74:75], 0, v[138:139]
	global_store_dwordx4 v[10:11], v[14:17], off
	v_mov_b32_e32 v10, v139
	v_mov_b32_e32 v11, v139
	v_cvt_pk_fp8_f32 v10, v34, v35
	v_cvt_pk_fp8_f32 v11, v46, v47
	v_mov_b32_e32 v12, v139
	v_mov_b32_e32 v13, v139
	v_mov_b32_e32 v14, v139
	v_cvt_pk_fp8_f32 v12, v54, v55
	v_cvt_pk_fp8_f32 v13, v50, v51
	v_cvt_pk_fp8_f32 v14, v18, v19
	v_mov_b32_e32 v15, v139
	v_cvt_pk_fp8_f32 v15, v22, v23
	v_mov_b32_e32 v16, v139
	v_mov_b32_e32 v17, v139
	v_cvt_pk_fp8_f32 v16, v30, v31
	v_cvt_pk_fp8_f32 v17, v26, v27
	v_cvt_pk_fp8_f32 v10, v36, v37 op_sel:[0,0,1]
	v_cvt_pk_fp8_f32 v11, v48, v49 op_sel:[0,0,1]
	s_waitcnt lgkmcnt(0)
	s_barrier
	v_cvt_pk_fp8_f32 v12, v56, v57 op_sel:[0,0,1]
	v_cvt_pk_fp8_f32 v13, v52, v53 op_sel:[0,0,1]
	v_cvt_pk_fp8_f32 v14, v20, v21 op_sel:[0,0,1]
	v_cvt_pk_fp8_f32 v15, v24, v25 op_sel:[0,0,1]
	v_lshrrev_b32_e32 v18, 8, v1
	v_and_b32_e32 v19, 15, v1
	v_lshrrev_b32_e32 v20, 1, v1
	v_lshlrev_b32_e32 v21, 4, v1
	v_mad_i32_i24 v18, v18, s79, v86
	v_and_b32_e32 v20, 0x78, v20
	v_and_b32_e32 v138, 0x70, v21
	v_mul_u32_u24_e32 v19, 0x90, v19
	v_cvt_pk_fp8_f32 v16, v32, v33 op_sel:[0,0,1]
	v_cvt_pk_fp8_f32 v17, v28, v29 op_sel:[0,0,1]
	v_add_u32_e32 v21, v18, v138
	v_add3_u32 v18, v18, v20, v19
	ds_write_b64 v18, v[10:11]
	ds_write_b64 v18, v[12:13] offset:2304
	ds_write_b64 v18, v[14:15] offset:4608
	ds_write_b64 v18, v[16:17] offset:6912
	v_and_b32_e32 v14, 0xf8, v1
	v_bfe_u32 v1, v1, 3, 5
	s_waitcnt lgkmcnt(0)
	s_barrier
	v_mad_u32_u24 v1, v1, s80, v21
	ds_read_b128 v[10:13], v1
	v_or_b32_e32 v1, 0x100, v14
	v_lshl_add_u64 v[18:19], s[36:37], 0, v[138:139]
	v_lshlrev_b32_e32 v138, 8, v14
	v_lshrrev_b32_e32 v14, 3, v1
	v_mad_u32_u24 v14, v14, s80, v21
	ds_read_b128 v[14:17], v14
	v_lshl_add_u64 v[20:21], v[18:19], 0, v[138:139]
	v_lshlrev_b32_e32 v138, 8, v1
	s_waitcnt lgkmcnt(0)
	global_store_dwordx4 v[20:21], v[10:13], off offset:128
	v_mov_b32_e32 v1, v0
	s_mov_b64 s[4:5], -1
	v_lshl_add_u64 v[10:11], v[18:19], 0, v[138:139]
	global_store_dwordx4 v[10:11], v[14:17], off offset:128
	v_mov_b32_e32 v10, v139
	v_mov_b32_e32 v11, v139
	v_cvt_pk_fp8_f32 v10, v58, v59
	v_cvt_pk_fp8_f32 v11, v62, v63
	v_mov_b32_e32 v12, v139
	v_mov_b32_e32 v13, v139
	v_mov_b32_e32 v17, v139
	v_cvt_pk_fp8_f32 v12, v70, v71
	v_cvt_pk_fp8_f32 v13, v66, v67
	v_mov_b32_e32 v14, v139
	v_mov_b32_e32 v15, v139
	v_cvt_pk_fp8_f32 v17, v2, v3
	v_cvt_pk_fp8_f32 v14, v38, v39
	v_cvt_pk_fp8_f32 v15, v42, v43
	v_mov_b32_e32 v16, v139
	v_cvt_pk_fp8_f32 v16, v6, v7
	v_cvt_pk_fp8_f32 v10, v60, v61 op_sel:[0,0,1]
	v_cvt_pk_fp8_f32 v11, v64, v65 op_sel:[0,0,1]
	s_waitcnt lgkmcnt(0)
	s_barrier
	v_cvt_pk_fp8_f32 v12, v72, v73 op_sel:[0,0,1]
	v_cvt_pk_fp8_f32 v13, v68, v69 op_sel:[0,0,1]
	v_cvt_pk_fp8_f32 v17, v4, v5 op_sel:[0,0,1]
	v_cvt_pk_fp8_f32 v14, v40, v41 op_sel:[0,0,1]
	v_lshrrev_b32_e32 v2, 8, v1
	v_and_b32_e32 v3, 15, v1
	v_lshrrev_b32_e32 v4, 1, v1
	v_lshlrev_b32_e32 v5, 4, v1
	v_cvt_pk_fp8_f32 v15, v44, v45 op_sel:[0,0,1]
	v_mad_i32_i24 v2, v2, s79, v86
	v_and_b32_e32 v4, 0x78, v4
	v_and_b32_e32 v138, 0x70, v5
	v_mul_u32_u24_e32 v3, 0x90, v3
	v_cvt_pk_fp8_f32 v16, v8, v9 op_sel:[0,0,1]
	v_add_u32_e32 v6, v2, v138
	v_add3_u32 v2, v2, v4, v3
	ds_write_b64 v2, v[10:11]
	ds_write_b64 v2, v[12:13] offset:2304
	ds_write_b64 v2, v[14:15] offset:4608
	ds_write_b64 v2, v[16:17] offset:6912
	v_and_b32_e32 v7, 0xf8, v1
	v_bfe_u32 v1, v1, 3, 5
	s_waitcnt lgkmcnt(0)
	s_barrier
	v_mad_u32_u24 v1, v1, s80, v6
	ds_read_b128 v[2:5], v1
	v_or_b32_e32 v1, 0x100, v7
	v_lshl_add_u64 v[10:11], s[38:39], 0, v[138:139]
	v_lshlrev_b32_e32 v138, 8, v7
	v_lshrrev_b32_e32 v7, 3, v1
	v_mad_u32_u24 v6, v7, s80, v6
	ds_read_b128 v[6:9], v6
	v_lshl_add_u64 v[12:13], v[10:11], 0, v[138:139]
	v_lshlrev_b32_e32 v138, 8, v1
	s_waitcnt lgkmcnt(0)
	global_store_dwordx4 v[12:13], v[2:5], off offset:128
	s_nop 1
	v_lshl_add_u64 v[2:3], v[10:11], 0, v[138:139]
	global_store_dwordx4 v[2:3], v[6:9], off offset:128
	s_waitcnt lgkmcnt(0)
	s_barrier
	s_cbranch_vccnz .LBB0_1540
	s_lshl_b32 s4, s61, 10
	s_and_b32 s4, s4, 0x400
	v_add_u32_e32 v1, s4, v152
	ds_read_b128 v[14:17], v1
	ds_read_b128 v[10:13], v1 offset:16
	ds_read_b128 v[6:9], v1 offset:512
	ds_read_b128 v[2:5], v1 offset:528
	s_mov_b64 s[4:5], 0
	s_branch .LBB0_1540
